# unit queues of the mixer phases: the returning atomic that pops the next unit stays in flight across the unit body (waited for only when its value is stored)
# baseline (speedup 1.0000x reference)
.LBB0_562:
	v_mov_b32_e32 v1, 0
	s_and_saveexec_b64 s[6:7], s[36:37]
	s_cbranch_execz .LBB0_566
	s_mov_b64 s[12:13], exec
	v_mbcnt_lo_u32_b32 v1, s12, 0
	v_mbcnt_hi_u32_b32 v1, s13, v1
	v_cmp_eq_u32_e32 vcc, 0, v1
	s_and_saveexec_b64 s[10:11], vcc
	s_cbranch_execz .LBB0_565
	s_bcnt1_i32_b64 s12, s[12:13]
	v_mov_b32_e32 v2, s12
	global_atomic_add v255, v131, v2, s[4:5] sc0

.LBB0_566:
	s_or_b64 exec, exec, s[6:7]
	v_mov_b32 v132, v0
	s_lshl_b32 s6, s46, 6
	v_readfirstlane_b32 s13, v132
	s_ashr_i32 s11, s13, 6
	s_ashr_i32 s12, s46, 8
	s_and_b32 s48, s6, 0x3c00
	s_cmp_eq_u32 s12, 1
	s_cselect_b32 s6, s19, 0xd8
	s_cmpk_lt_u32 s46, 0x100
	s_cselect_b32 s7, 16, 0x90
	s_cselect_b32 s10, 0xc8, s6
	s_add_u32 s6, s15, s7
	s_addc_u32 s7, s16, 0
	s_lshr_b32 s47, s48, 8
	v_mov_b32_e32 v2, s47
	global_load_dword v4, v2, s[6:7] sc1
	s_add_u32 s6, s0, s10
	s_addc_u32 s7, s1, 0
	s_load_dwordx2 s[6:7], s[6:7], 0x0
	s_lshl_b32 s10, s46, 7
	s_mul_i32 s46, s11, 0x4400
	s_and_b32 s10, s10, 0x780
	s_add_i32 s49, s46, 0
	s_lshl_b32 s46, s48, 13
	v_bfe_u32 v133, v132, 3, 3
	s_waitcnt lgkmcnt(0)
	s_add_u32 s6, s6, s46
	v_or_b32_e32 v2, s10, v133
	s_addc_u32 s7, s7, 0
	v_lshlrev_b32_e32 v130, 12, v2
	v_lshlrev_b32_e32 v5, 4, v132
	s_waitcnt vmcnt(1)
	v_lshl_add_u64 v[2:3], s[6:7], 0, v[130:131]
	v_and_b32_e32 v130, 0x70, v5
	s_lshl_b32 s6, s11, 5
	v_lshl_add_u64 v[2:3], v[2:3], 0, v[130:131]
	s_ashr_i32 s7, s6, 31
	v_lshl_add_u64 v[142:143], s[6:7], 2, v[2:3]
	v_add_co_u32_e32 v140, vcc, s21, v142
	global_load_dwordx4 v[66:69], v[142:143], off nt
	s_nop 0
	v_addc_co_u32_e32 v141, vcc, 0, v143, vcc
	v_add_co_u32_e32 v144, vcc, s22, v142
	global_load_dwordx4 v[70:73], v[140:141], off nt
	s_nop 0
	v_addc_co_u32_e32 v145, vcc, 0, v143, vcc
	v_add_co_u32_e32 v146, vcc, s23, v142
	global_load_dwordx4 v[74:77], v[144:145], off nt
	s_nop 0
	v_addc_co_u32_e32 v147, vcc, 0, v143, vcc
	v_add_co_u32_e32 v148, vcc, s24, v142
	global_load_dwordx4 v[78:81], v[146:147], off nt
	s_nop 0
	v_addc_co_u32_e32 v149, vcc, 0, v143, vcc
	v_add_co_u32_e32 v150, vcc, s25, v142
	global_load_dwordx4 v[82:85], v[148:149], off nt
	s_nop 0
	v_addc_co_u32_e32 v151, vcc, 0, v143, vcc
	v_add_co_u32_e32 v152, vcc, s26, v142
	global_load_dwordx4 v[86:89], v[150:151], off nt
	s_nop 0
	v_addc_co_u32_e32 v153, vcc, 0, v143, vcc
	v_add_co_u32_e32 v154, vcc, s27, v142
	global_load_dwordx4 v[90:93], v[152:153], off nt
	s_nop 0
	v_addc_co_u32_e32 v155, vcc, 0, v143, vcc
	v_add_co_u32_e32 v156, vcc, s28, v142
	global_load_dwordx4 v[94:97], v[154:155], off nt
	s_nop 0
	v_addc_co_u32_e32 v157, vcc, 0, v143, vcc
	v_add_co_u32_e32 v158, vcc, s29, v142
	global_load_dwordx4 v[98:101], v[156:157], off nt
	s_nop 0
	v_addc_co_u32_e32 v159, vcc, 0, v143, vcc
	v_add_co_u32_e32 v160, vcc, s30, v142
	global_load_dwordx4 v[102:105], v[158:159], off nt
	s_nop 0
	v_addc_co_u32_e32 v161, vcc, 0, v143, vcc
	v_add_co_u32_e32 v162, vcc, s31, v142
	global_load_dwordx4 v[106:109], v[160:161], off nt
	s_nop 0
	v_addc_co_u32_e32 v163, vcc, 0, v143, vcc
	v_add_co_u32_e32 v164, vcc, s33, v142
	global_load_dwordx4 v[110:113], v[162:163], off nt
	s_nop 0
	v_addc_co_u32_e32 v165, vcc, 0, v143, vcc
	v_add_co_u32_e32 v166, vcc, s34, v142
	global_load_dwordx4 v[114:117], v[164:165], off nt
	s_nop 0
	v_addc_co_u32_e32 v167, vcc, 0, v143, vcc
	v_add_co_u32_e32 v168, vcc, s35, v142
	global_load_dwordx4 v[118:121], v[166:167], off nt
	s_nop 0
	v_addc_co_u32_e32 v169, vcc, 0, v143, vcc
	v_add_co_u32_e32 v170, vcc, s38, v142
	global_load_dwordx4 v[122:125], v[168:169], off nt
	s_nop 0
	v_addc_co_u32_e32 v171, vcc, 0, v143, vcc
	global_load_dwordx4 v[126:129], v[170:171], off nt
	s_waitcnt vmcnt(16)
	v_div_scale_f32 v2, s[46:47], v4, v4, s20
	v_rcp_f32_e32 v3, v2
	v_and_b32_e32 v130, 7, v132
	v_mul_u32_u24_e32 v132, 0x840, v130
	v_lshlrev_b32_e32 v134, 2, v133
	v_fma_f32 v5, -v2, v3, 1.0
	v_fmac_f32_e32 v3, v5, v3
	v_div_scale_f32 v5, vcc, s20, v4, s20
	v_mul_f32_e32 v6, v5, v3
	v_fma_f32 v7, -v2, v6, v5
	v_fmac_f32_e32 v6, v7, v3
	v_fma_f32 v2, -v2, v6, v5
	v_div_fmas_f32 v2, v2, v3, v6
	v_add3_u32 v174, s49, v132, v134
	v_div_fixup_f32 v2, v2, v4, s20
	v_cmp_lt_f32_e32 vcc, 0, v4
	v_add_u32_e32 v175, 0x400, v174
	v_add_u32_e32 v176, 0x600, v174
	v_cndmask_b32_e32 v172, 0, v2, vcc
	global_load_dwordx4 v[50:53], v[142:143], off offset:1024 nt
	global_load_dwordx4 v[54:57], v[140:141], off offset:1024 nt
	global_load_dwordx4 v[58:61], v[144:145], off offset:1024 nt
	global_load_dwordx4 v[62:65], v[146:147], off offset:1024 nt
	global_load_dwordx4 v[34:37], v[148:149], off offset:1024 nt
	global_load_dwordx4 v[38:41], v[150:151], off offset:1024 nt
	global_load_dwordx4 v[42:45], v[152:153], off offset:1024 nt
	global_load_dwordx4 v[46:49], v[154:155], off offset:1024 nt
	global_load_dwordx4 v[18:21], v[156:157], off offset:1024 nt
	global_load_dwordx4 v[22:25], v[158:159], off offset:1024 nt
	global_load_dwordx4 v[26:29], v[160:161], off offset:1024 nt
	global_load_dwordx4 v[30:33], v[162:163], off offset:1024 nt
	global_load_dwordx4 v[2:5], v[164:165], off offset:1024 nt
	global_load_dwordx4 v[6:9], v[166:167], off offset:1024 nt
	global_load_dwordx4 v[10:13], v[168:169], off offset:1024 nt
	global_load_dwordx4 v[14:17], v[170:171], off offset:1024 nt
	s_waitcnt vmcnt(29)
	ds_write2_b32 v174, v66, v74 offset1:8
	s_waitcnt vmcnt(28)
	ds_write2_b32 v174, v70, v78 offset0:64 offset1:72
	ds_write2_b32 v174, v67, v75 offset0:132 offset1:140
	ds_write2_b32 v174, v71, v79 offset0:196 offset1:204
	ds_write2_b32 v175, v68, v76 offset0:8 offset1:16
	ds_write2_b32 v175, v72, v80 offset0:72 offset1:80
	ds_write2_b32 v175, v69, v77 offset0:140 offset1:148
	ds_write2_b32 v175, v73, v81 offset0:204 offset1:212
	s_waitcnt vmcnt(25)
	ds_write2_b32 v174, v82, v90 offset0:16 offset1:24
	s_waitcnt vmcnt(24)
	ds_write2_b32 v174, v86, v94 offset0:80 offset1:88
	ds_write2_b32 v174, v83, v91 offset0:148 offset1:156
	ds_write2_b32 v174, v87, v95 offset0:212 offset1:220
	ds_write2_b32 v175, v84, v92 offset0:24 offset1:32
	ds_write2_b32 v175, v88, v96 offset0:88 offset1:96
	ds_write2_b32 v175, v85, v93 offset0:156 offset1:164
	ds_write2_b32 v175, v89, v97 offset0:220 offset1:228
	s_waitcnt vmcnt(21)
	ds_write2_b32 v174, v98, v106 offset0:32 offset1:40
	s_waitcnt vmcnt(20)
	ds_write2_b32 v174, v102, v110 offset0:96 offset1:104
	ds_write2_b32 v174, v99, v107 offset0:164 offset1:172
	ds_write2_b32 v174, v103, v111 offset0:228 offset1:236
	ds_write2_b32 v175, v100, v108 offset0:40 offset1:48
	ds_write2_b32 v175, v104, v112 offset0:104 offset1:112
	ds_write2_b32 v175, v101, v109 offset0:172 offset1:180
	ds_write2_b32 v175, v105, v113 offset0:236 offset1:244
	s_waitcnt vmcnt(17)
	ds_write2_b32 v174, v114, v122 offset0:48 offset1:56
	s_waitcnt vmcnt(16)
	ds_write2_b32 v174, v118, v126 offset0:112 offset1:120
	ds_write2_b32 v174, v115, v123 offset0:180 offset1:188
	ds_write2_b32 v174, v119, v127 offset0:244 offset1:252
	ds_write2_b32 v175, v116, v124 offset0:56 offset1:64
	ds_write2_b32 v175, v120, v128 offset0:120 offset1:128
	ds_write2_b32 v175, v117, v125 offset0:188 offset1:196
	v_lshlrev_b32_e32 v66, 6, v130
	v_mul_u32_u24_e32 v67, 0x210, v133
	v_add3_u32 v173, s49, v66, v67
	s_lshl_b32 s7, s48, 12
	s_add_u32 s11, s17, s7
	s_addc_u32 s7, s18, 0
	s_and_b32 s46, s13, 0xffffff00
	s_lshl_b32 s12, s12, 7
	s_add_i32 s46, s46, s12
	s_and_b32 s6, s6, 0x60
	s_or_b32 s46, s6, s46
	s_ashr_i32 s47, s46, 31
	s_lshl_b64 s[46:47], s[46:47], 11
	s_add_u32 s46, s11, s46
	s_addc_u32 s47, s7, s47
	s_add_u32 s46, s46, s10
	v_lshlrev_b32_e32 v130, 4, v130
	s_addc_u32 s47, s47, 0
	v_lshlrev_b32_e32 v134, 11, v133
	v_mov_b32_e32 v135, v131
	ds_write2_b32 v176, v121, v129 offset0:124 offset1:132
	s_waitcnt lgkmcnt(0)
	ds_read_b128 v[66:69], v173
	ds_read_b128 v[70:73], v173 offset:16
	ds_read_b128 v[74:77], v173 offset:32
	ds_read_b128 v[78:81], v173 offset:48
	v_or_b32_e32 v136, 0x4000, v134
	v_mov_b32_e32 v137, v131
	s_waitcnt lgkmcnt(2)
	v_mul_f32_e32 v70, v172, v70
	v_mul_f32_e32 v82, v172, v66
	v_mul_f32_e32 v67, v172, v67
	v_mov_b32_e32 v66, 0
	v_cvt_pk_fp8_f32 v66, v82, v67
	v_mul_f32_e32 v71, v172, v71
	v_mov_b32_e32 v67, 0
	v_cvt_pk_fp8_f32 v67, v70, v71
	v_mul_f32_e32 v68, v172, v68
	v_mul_f32_e32 v69, v172, v69
	v_cvt_pk_fp8_f32 v66, v68, v69 op_sel:[0,0,1]
	v_mul_f32_e32 v68, v172, v72
	v_mul_f32_e32 v69, v172, v73
	v_cvt_pk_fp8_f32 v67, v68, v69 op_sel:[0,0,1]
	s_waitcnt lgkmcnt(1)
	v_mul_f32_e32 v69, v172, v74
	v_mul_f32_e32 v70, v172, v75
	v_mov_b32_e32 v68, 0
	v_cvt_pk_fp8_f32 v68, v69, v70
	s_waitcnt lgkmcnt(0)
	v_mul_f32_e32 v72, v172, v78
	v_mul_f32_e32 v73, v172, v79
	v_mov_b32_e32 v69, 0
	v_cvt_pk_fp8_f32 v69, v72, v73
	v_mul_f32_e32 v70, v172, v76
	v_mul_f32_e32 v71, v172, v77
	v_cvt_pk_fp8_f32 v68, v70, v71 op_sel:[0,0,1]
	v_mul_f32_e32 v70, v172, v80
	v_mul_f32_e32 v71, v172, v81
	v_cvt_pk_fp8_f32 v69, v70, v71 op_sel:[0,0,1]
	ds_read_b128 v[70:73], v173 offset:4224
	ds_read_b128 v[74:77], v173 offset:4240
	v_lshl_add_u64 v[78:79], s[46:47], 0, v[130:131]
	v_lshl_add_u64 v[80:81], v[78:79], 0, v[134:135]
	global_store_dwordx4 v[80:81], v[66:69], off nt
	s_waitcnt lgkmcnt(1)
	v_mul_f32_e32 v82, v172, v70
	v_mul_f32_e32 v71, v172, v71
	v_mov_b32_e32 v70, 0
	v_cvt_pk_fp8_f32 v70, v82, v71
	v_mul_f32_e32 v66, v172, v72
	v_mul_f32_e32 v67, v172, v73
	v_mov_b32_e32 v71, 0
	v_cvt_pk_fp8_f32 v70, v66, v67 op_sel:[0,0,1]
	s_waitcnt lgkmcnt(0)
	v_mul_f32_e32 v66, v172, v74
	v_mul_f32_e32 v67, v172, v75
	v_cvt_pk_fp8_f32 v71, v66, v67
	ds_read_b128 v[66:69], v173 offset:4256
	v_mul_f32_e32 v72, v172, v76
	v_mul_f32_e32 v73, v172, v77
	ds_read_b128 v[74:77], v173 offset:4272
	v_cvt_pk_fp8_f32 v71, v72, v73 op_sel:[0,0,1]
	s_waitcnt lgkmcnt(1)
	v_mul_f32_e32 v66, v172, v66
	v_mul_f32_e32 v67, v172, v67
	v_mov_b32_e32 v72, 0
	v_cvt_pk_fp8_f32 v72, v66, v67
	v_mul_f32_e32 v66, v172, v68
	v_mul_f32_e32 v67, v172, v69
	s_waitcnt lgkmcnt(0)
	v_mul_f32_e32 v68, v172, v74
	v_mul_f32_e32 v69, v172, v75
	v_mov_b32_e32 v73, 0
	v_cvt_pk_fp8_f32 v73, v68, v69
	v_cvt_pk_fp8_f32 v72, v66, v67 op_sel:[0,0,1]
	v_mul_f32_e32 v66, v172, v76
	v_mul_f32_e32 v67, v172, v77
	v_cvt_pk_fp8_f32 v73, v66, v67 op_sel:[0,0,1]
	ds_read_b128 v[66:69], v173 offset:8448
	ds_read_b128 v[74:77], v173 offset:8464
	v_lshl_add_u64 v[80:81], v[78:79], 0, v[136:137]
	global_store_dwordx4 v[80:81], v[70:73], off nt
	v_or_b32_e32 v132, 0x8000, v134
	s_waitcnt lgkmcnt(1)
	v_mul_f32_e32 v82, v172, v66
	v_mul_f32_e32 v67, v172, v67
	v_mov_b32_e32 v66, 0
	v_cvt_pk_fp8_f32 v66, v82, v67
	v_mul_f32_e32 v67, v172, v68
	v_mul_f32_e32 v68, v172, v69
	s_waitcnt lgkmcnt(0)
	v_mul_f32_e32 v69, v172, v75
	v_cvt_pk_fp8_f32 v66, v67, v68 op_sel:[0,0,1]
	v_mul_f32_e32 v68, v172, v74
	v_mov_b32_e32 v67, 0
	v_cvt_pk_fp8_f32 v67, v68, v69
	ds_read_b128 v[68:71], v173 offset:8480
	v_mul_f32_e32 v72, v172, v76
	v_mul_f32_e32 v73, v172, v77
	v_cvt_pk_fp8_f32 v67, v72, v73 op_sel:[0,0,1]
	ds_read_b128 v[72:75], v173 offset:8496
	s_waitcnt lgkmcnt(1)
	v_mul_f32_e32 v76, v172, v68
	v_mul_f32_e32 v69, v172, v69
	v_mov_b32_e32 v68, 0
	v_cvt_pk_fp8_f32 v68, v76, v69
	s_waitcnt lgkmcnt(0)
	v_mul_f32_e32 v72, v172, v72
	v_mul_f32_e32 v73, v172, v73
	v_mov_b32_e32 v69, 0
	v_cvt_pk_fp8_f32 v69, v72, v73
	v_mul_f32_e32 v70, v172, v70
	v_mul_f32_e32 v71, v172, v71
	v_cvt_pk_fp8_f32 v68, v70, v71 op_sel:[0,0,1]
	v_mul_f32_e32 v70, v172, v74
	v_mul_f32_e32 v71, v172, v75
	v_cvt_pk_fp8_f32 v69, v70, v71 op_sel:[0,0,1]
	ds_read_b128 v[70:73], v173 offset:12672
	ds_read_b128 v[74:77], v173 offset:12688
	v_mov_b32_e32 v133, v131
	v_lshl_add_u64 v[80:81], v[78:79], 0, v[132:133]
	global_store_dwordx4 v[80:81], v[66:69], off nt
	s_waitcnt lgkmcnt(1)
	v_mul_f32_e32 v82, v172, v70
	v_mul_f32_e32 v71, v172, v71
	v_mov_b32_e32 v70, 0
	v_cvt_pk_fp8_f32 v70, v82, v71
	v_mul_f32_e32 v66, v172, v72
	v_mul_f32_e32 v67, v172, v73
	v_mov_b32_e32 v71, 0
	v_cvt_pk_fp8_f32 v70, v66, v67 op_sel:[0,0,1]
	s_waitcnt lgkmcnt(0)
	v_mul_f32_e32 v66, v172, v74
	v_mul_f32_e32 v67, v172, v75
	v_cvt_pk_fp8_f32 v71, v66, v67
	ds_read_b128 v[66:69], v173 offset:12704
	v_mul_f32_e32 v72, v172, v76
	v_mul_f32_e32 v73, v172, v77
	ds_read_b128 v[74:77], v173 offset:12720
	v_cvt_pk_fp8_f32 v71, v72, v73 op_sel:[0,0,1]
	s_waitcnt lgkmcnt(1)
	v_mul_f32_e32 v66, v172, v66
	v_mul_f32_e32 v67, v172, v67
	v_mov_b32_e32 v72, 0
	v_cvt_pk_fp8_f32 v72, v66, v67
	v_mul_f32_e32 v66, v172, v68
	v_mul_f32_e32 v67, v172, v69
	s_waitcnt lgkmcnt(0)
	v_mul_f32_e32 v68, v172, v74
	v_mul_f32_e32 v69, v172, v75
	v_mov_b32_e32 v73, 0
	v_cvt_pk_fp8_f32 v73, v68, v69
	v_cvt_pk_fp8_f32 v72, v66, v67 op_sel:[0,0,1]
	v_mul_f32_e32 v66, v172, v76
	v_mul_f32_e32 v67, v172, v77
	v_cvt_pk_fp8_f32 v73, v66, v67 op_sel:[0,0,1]
	v_or_b32_e32 v138, 0xc000, v134
	v_mov_b32_e32 v139, v131
	v_lshl_add_u64 v[66:67], v[78:79], 0, v[138:139]
	global_store_dwordx4 v[66:67], v[70:73], off nt
	s_waitcnt lgkmcnt(0)
	global_load_dwordx4 v[114:117], v[142:143], off offset:2048 nt
	global_load_dwordx4 v[118:121], v[140:141], off offset:2048 nt
	global_load_dwordx4 v[122:125], v[144:145], off offset:2048 nt
	global_load_dwordx4 v[126:129], v[146:147], off offset:2048 nt
	global_load_dwordx4 v[98:101], v[148:149], off offset:2048 nt
	global_load_dwordx4 v[102:105], v[150:151], off offset:2048 nt
	global_load_dwordx4 v[106:109], v[152:153], off offset:2048 nt
	global_load_dwordx4 v[110:113], v[154:155], off offset:2048 nt
	global_load_dwordx4 v[82:85], v[156:157], off offset:2048 nt
	global_load_dwordx4 v[86:89], v[158:159], off offset:2048 nt
	global_load_dwordx4 v[90:93], v[160:161], off offset:2048 nt
	global_load_dwordx4 v[94:97], v[162:163], off offset:2048 nt
	global_load_dwordx4 v[66:69], v[164:165], off offset:2048 nt
	global_load_dwordx4 v[70:73], v[166:167], off offset:2048 nt
	global_load_dwordx4 v[74:77], v[168:169], off offset:2048 nt
	global_load_dwordx4 v[78:81], v[170:171], off offset:2048 nt
	s_waitcnt vmcnt(33)
	ds_write2_b32 v174, v50, v58 offset1:8
	s_waitcnt vmcnt(32)
	ds_write2_b32 v174, v54, v62 offset0:64 offset1:72
	ds_write2_b32 v174, v51, v59 offset0:132 offset1:140
	ds_write2_b32 v174, v55, v63 offset0:196 offset1:204
	ds_write2_b32 v175, v52, v60 offset0:8 offset1:16
	ds_write2_b32 v175, v56, v64 offset0:72 offset1:80
	ds_write2_b32 v175, v53, v61 offset0:140 offset1:148
	ds_write2_b32 v175, v57, v65 offset0:204 offset1:212
	s_waitcnt vmcnt(29)
	ds_write2_b32 v174, v34, v42 offset0:16 offset1:24
	s_waitcnt vmcnt(28)
	ds_write2_b32 v174, v38, v46 offset0:80 offset1:88
	ds_write2_b32 v174, v35, v43 offset0:148 offset1:156
	ds_write2_b32 v174, v39, v47 offset0:212 offset1:220
	ds_write2_b32 v175, v36, v44 offset0:24 offset1:32
	ds_write2_b32 v175, v40, v48 offset0:88 offset1:96
	ds_write2_b32 v175, v37, v45 offset0:156 offset1:164
	ds_write2_b32 v175, v41, v49 offset0:220 offset1:228
	s_waitcnt vmcnt(25)
	ds_write2_b32 v174, v18, v26 offset0:32 offset1:40
	s_waitcnt vmcnt(24)
	ds_write2_b32 v174, v22, v30 offset0:96 offset1:104
	ds_write2_b32 v174, v19, v27 offset0:164 offset1:172
	ds_write2_b32 v174, v23, v31 offset0:228 offset1:236
	ds_write2_b32 v175, v20, v28 offset0:40 offset1:48
	ds_write2_b32 v175, v24, v32 offset0:104 offset1:112
	ds_write2_b32 v175, v21, v29 offset0:172 offset1:180
	ds_write2_b32 v175, v25, v33 offset0:236 offset1:244
	s_waitcnt vmcnt(21)
	ds_write2_b32 v174, v2, v10 offset0:48 offset1:56
	s_waitcnt vmcnt(20)
	ds_write2_b32 v174, v6, v14 offset0:112 offset1:120
	ds_write2_b32 v174, v3, v11 offset0:180 offset1:188
	ds_write2_b32 v174, v7, v15 offset0:244 offset1:252
	ds_write2_b32 v175, v4, v12 offset0:56 offset1:64
	ds_write2_b32 v175, v8, v16 offset0:120 offset1:128
	ds_write2_b32 v175, v5, v13 offset0:188 offset1:196
	ds_write2_b32 v176, v9, v17 offset0:124 offset1:132
	s_waitcnt lgkmcnt(0)
	ds_read_b128 v[2:5], v173
	ds_read_b128 v[6:9], v173 offset:16
	ds_read_b128 v[10:13], v173 offset:32
	ds_read_b128 v[14:17], v173 offset:48
	s_andn2_b32 s13, s13, 63
	s_add_i32 s46, s13, 0x200
	s_waitcnt lgkmcnt(2)
	v_mul_f32_e32 v6, v172, v6
	v_mul_f32_e32 v18, v172, v2
	v_mul_f32_e32 v3, v172, v3
	v_mov_b32_e32 v2, 0
	v_cvt_pk_fp8_f32 v2, v18, v3
	v_mul_f32_e32 v7, v172, v7
	v_mov_b32_e32 v3, 0
	v_cvt_pk_fp8_f32 v3, v6, v7
	v_mul_f32_e32 v4, v172, v4
	v_mul_f32_e32 v5, v172, v5
	v_cvt_pk_fp8_f32 v2, v4, v5 op_sel:[0,0,1]
	v_mul_f32_e32 v4, v172, v8
	v_mul_f32_e32 v5, v172, v9
	v_cvt_pk_fp8_f32 v3, v4, v5 op_sel:[0,0,1]
	s_waitcnt lgkmcnt(1)
	v_mul_f32_e32 v5, v172, v10
	v_mul_f32_e32 v6, v172, v11
	v_mov_b32_e32 v4, 0
	v_cvt_pk_fp8_f32 v4, v5, v6
	s_waitcnt lgkmcnt(0)
	v_mul_f32_e32 v8, v172, v14
	v_mul_f32_e32 v9, v172, v15
	v_mov_b32_e32 v5, 0
	v_cvt_pk_fp8_f32 v5, v8, v9
	s_and_b32 s46, s46, 0xffffff00
	v_mul_f32_e32 v6, v172, v12
	v_mul_f32_e32 v7, v172, v13
	s_add_i32 s46, s46, s12
	v_cvt_pk_fp8_f32 v4, v6, v7 op_sel:[0,0,1]
	v_mul_f32_e32 v6, v172, v16
	v_mul_f32_e32 v7, v172, v17
	s_or_b32 s46, s46, s6
	v_cvt_pk_fp8_f32 v5, v6, v7 op_sel:[0,0,1]
	ds_read_b128 v[6:9], v173 offset:4224
	ds_read_b128 v[10:13], v173 offset:4240
	s_ashr_i32 s47, s46, 31
	s_lshl_b64 s[46:47], s[46:47], 11
	s_add_u32 s46, s11, s46
	s_addc_u32 s47, s7, s47
	s_add_u32 s46, s46, s10
	s_waitcnt lgkmcnt(1)
	v_mul_f32_e32 v18, v172, v6
	v_mul_f32_e32 v7, v172, v7
	v_mov_b32_e32 v6, 0
	s_addc_u32 s47, s47, 0
	v_cvt_pk_fp8_f32 v6, v18, v7
	v_lshl_add_u64 v[16:17], s[46:47], 0, v[130:131]
	v_lshl_add_u64 v[14:15], v[16:17], 0, v[134:135]
	global_store_dwordx4 v[14:15], v[2:5], off nt
	v_mov_b32_e32 v7, 0
	s_waitcnt lgkmcnt(0)
	v_mul_f32_e32 v14, v172, v13
	v_mul_f32_e32 v2, v172, v8
	v_mul_f32_e32 v3, v172, v9
	v_cvt_pk_fp8_f32 v6, v2, v3 op_sel:[0,0,1]
	ds_read_b128 v[2:5], v173 offset:4256
	v_mul_f32_e32 v8, v172, v10
	v_mul_f32_e32 v9, v172, v11
	v_cvt_pk_fp8_f32 v7, v8, v9
	v_mul_f32_e32 v9, v172, v12
	ds_read_b128 v[10:13], v173 offset:4272
	s_waitcnt lgkmcnt(1)
	v_mul_f32_e32 v2, v172, v2
	v_mul_f32_e32 v3, v172, v3
	v_mov_b32_e32 v8, 0
	v_cvt_pk_fp8_f32 v8, v2, v3
	v_mul_f32_e32 v2, v172, v4
	v_mul_f32_e32 v3, v172, v5
	v_cvt_pk_fp8_f32 v7, v9, v14 op_sel:[0,0,1]
	v_cvt_pk_fp8_f32 v8, v2, v3 op_sel:[0,0,1]
	s_waitcnt lgkmcnt(0)
	v_mul_f32_e32 v2, v172, v10
	v_mul_f32_e32 v3, v172, v11
	v_mov_b32_e32 v9, 0
	v_cvt_pk_fp8_f32 v9, v2, v3
	ds_read_b128 v[2:5], v173 offset:8448
	v_mul_f32_e32 v10, v172, v12
	v_mul_f32_e32 v11, v172, v13
	v_cvt_pk_fp8_f32 v9, v10, v11 op_sel:[0,0,1]
	ds_read_b128 v[10:13], v173 offset:8464
	s_waitcnt lgkmcnt(1)
	v_mul_f32_e32 v18, v172, v2
	v_mul_f32_e32 v3, v172, v3
	v_mov_b32_e32 v2, 0
	v_cvt_pk_fp8_f32 v2, v18, v3
	v_lshl_add_u64 v[14:15], v[16:17], 0, v[136:137]
	v_mul_f32_e32 v3, v172, v4
	v_mul_f32_e32 v4, v172, v5
	global_store_dwordx4 v[14:15], v[6:9], off nt
	v_cvt_pk_fp8_f32 v2, v3, v4 op_sel:[0,0,1]
	ds_read_b128 v[4:7], v173 offset:8480
	s_waitcnt lgkmcnt(1)
	v_mul_f32_e32 v8, v172, v10
	v_mul_f32_e32 v9, v172, v11
	v_mov_b32_e32 v3, 0
	v_cvt_pk_fp8_f32 v3, v8, v9
	ds_read_b128 v[8:11], v173 offset:8496
	s_waitcnt lgkmcnt(1)
	v_mul_f32_e32 v14, v172, v4
	v_mul_f32_e32 v5, v172, v5
	v_mov_b32_e32 v4, 0
	v_cvt_pk_fp8_f32 v4, v14, v5
	v_mul_f32_e32 v12, v172, v12
	v_mul_f32_e32 v13, v172, v13
	v_mul_f32_e32 v5, v172, v6
	v_mul_f32_e32 v6, v172, v7
	v_cvt_pk_fp8_f32 v3, v12, v13 op_sel:[0,0,1]
	v_cvt_pk_fp8_f32 v4, v5, v6 op_sel:[0,0,1]
	s_waitcnt lgkmcnt(0)
	v_mul_f32_e32 v12, v172, v8
	v_mul_f32_e32 v13, v172, v9
	ds_read_b128 v[6:9], v173 offset:12672
	v_mov_b32_e32 v5, 0
	v_cvt_pk_fp8_f32 v5, v12, v13
	v_mul_f32_e32 v14, v172, v10
	v_mul_f32_e32 v15, v172, v11
	ds_read_b128 v[10:13], v173 offset:12688
	s_waitcnt lgkmcnt(1)
	v_mul_f32_e32 v18, v172, v6
	v_mul_f32_e32 v7, v172, v7
	v_mov_b32_e32 v6, 0
	v_cvt_pk_fp8_f32 v6, v18, v7
	v_mul_f32_e32 v7, v172, v8
	v_mul_f32_e32 v8, v172, v9
	s_waitcnt lgkmcnt(0)
	v_mul_f32_e32 v9, v172, v11
	v_cvt_pk_fp8_f32 v6, v7, v8 op_sel:[0,0,1]
	v_mul_f32_e32 v8, v172, v10
	v_mov_b32_e32 v7, 0
	v_cvt_pk_fp8_f32 v7, v8, v9
	ds_read_b128 v[8:11], v173 offset:12704
	v_mul_f32_e32 v12, v172, v12
	v_mul_f32_e32 v13, v172, v13
	v_cvt_pk_fp8_f32 v5, v14, v15 op_sel:[0,0,1]
	v_cvt_pk_fp8_f32 v7, v12, v13 op_sel:[0,0,1]
	ds_read_b128 v[12:15], v173 offset:12720
	s_waitcnt lgkmcnt(1)
	v_mul_f32_e32 v18, v172, v8
	v_mul_f32_e32 v9, v172, v9
	v_mov_b32_e32 v8, 0
	v_cvt_pk_fp8_f32 v8, v18, v9
	s_waitcnt lgkmcnt(0)
	v_mul_f32_e32 v12, v172, v12
	v_mul_f32_e32 v13, v172, v13
	v_mov_b32_e32 v9, 0
	v_cvt_pk_fp8_f32 v9, v12, v13
	v_mul_f32_e32 v10, v172, v10
	v_mul_f32_e32 v11, v172, v11
	v_cvt_pk_fp8_f32 v8, v10, v11 op_sel:[0,0,1]
	v_mul_f32_e32 v10, v172, v14
	v_mul_f32_e32 v11, v172, v15
	v_cvt_pk_fp8_f32 v9, v10, v11 op_sel:[0,0,1]
	v_lshl_add_u64 v[10:11], v[16:17], 0, v[132:133]
	global_store_dwordx4 v[10:11], v[2:5], off nt
	s_add_i32 s46, s13, 0x400
	s_and_b32 s46, s46, 0xffffff00
	v_lshl_add_u64 v[2:3], v[16:17], 0, v[138:139]
	global_store_dwordx4 v[2:3], v[6:9], off nt
	s_waitcnt lgkmcnt(0)
	global_load_dwordx4 v[42:45], v[142:143], off offset:3072 nt
	global_load_dwordx4 v[46:49], v[140:141], off offset:3072 nt
	global_load_dwordx4 v[58:61], v[144:145], off offset:3072 nt
	global_load_dwordx4 v[62:65], v[146:147], off offset:3072 nt
	global_load_dwordx4 v[34:37], v[148:149], off offset:3072 nt
	global_load_dwordx4 v[38:41], v[150:151], off offset:3072 nt
	global_load_dwordx4 v[50:53], v[152:153], off offset:3072 nt
	global_load_dwordx4 v[54:57], v[154:155], off offset:3072 nt
	global_load_dwordx4 v[18:21], v[156:157], off offset:3072 nt
	global_load_dwordx4 v[22:25], v[158:159], off offset:3072 nt
	global_load_dwordx4 v[26:29], v[160:161], off offset:3072 nt
	global_load_dwordx4 v[30:33], v[162:163], off offset:3072 nt
	global_load_dwordx4 v[2:5], v[164:165], off offset:3072 nt
	global_load_dwordx4 v[6:9], v[166:167], off offset:3072 nt
	global_load_dwordx4 v[10:13], v[168:169], off offset:3072 nt
	global_load_dwordx4 v[14:17], v[170:171], off offset:3072 nt
	s_waitcnt vmcnt(33)
	ds_write2_b32 v174, v114, v122 offset1:8
	s_waitcnt vmcnt(32)
	ds_write2_b32 v174, v118, v126 offset0:64 offset1:72
	ds_write2_b32 v174, v115, v123 offset0:132 offset1:140
	ds_write2_b32 v174, v119, v127 offset0:196 offset1:204
	ds_write2_b32 v175, v116, v124 offset0:8 offset1:16
	ds_write2_b32 v175, v120, v128 offset0:72 offset1:80
	ds_write2_b32 v175, v117, v125 offset0:140 offset1:148
	ds_write2_b32 v175, v121, v129 offset0:204 offset1:212
	s_waitcnt vmcnt(29)
	ds_write2_b32 v174, v98, v106 offset0:16 offset1:24
	s_waitcnt vmcnt(28)
	ds_write2_b32 v174, v102, v110 offset0:80 offset1:88
	ds_write2_b32 v174, v99, v107 offset0:148 offset1:156
	ds_write2_b32 v174, v103, v111 offset0:212 offset1:220
	ds_write2_b32 v175, v100, v108 offset0:24 offset1:32
	ds_write2_b32 v175, v104, v112 offset0:88 offset1:96
	ds_write2_b32 v175, v101, v109 offset0:156 offset1:164
	ds_write2_b32 v175, v105, v113 offset0:220 offset1:228
	s_waitcnt vmcnt(25)
	ds_write2_b32 v174, v82, v90 offset0:32 offset1:40
	s_waitcnt vmcnt(24)
	ds_write2_b32 v174, v86, v94 offset0:96 offset1:104
	ds_write2_b32 v174, v83, v91 offset0:164 offset1:172
	ds_write2_b32 v174, v87, v95 offset0:228 offset1:236
	ds_write2_b32 v175, v84, v92 offset0:40 offset1:48
	ds_write2_b32 v175, v88, v96 offset0:104 offset1:112
	ds_write2_b32 v175, v85, v93 offset0:172 offset1:180
	ds_write2_b32 v175, v89, v97 offset0:236 offset1:244
	s_waitcnt vmcnt(21)
	ds_write2_b32 v174, v66, v74 offset0:48 offset1:56
	s_waitcnt vmcnt(20)
	ds_write2_b32 v174, v70, v78 offset0:112 offset1:120
	ds_write2_b32 v174, v67, v75 offset0:180 offset1:188
	ds_write2_b32 v174, v71, v79 offset0:244 offset1:252
	ds_write2_b32 v175, v68, v76 offset0:56 offset1:64
	ds_write2_b32 v175, v72, v80 offset0:120 offset1:128
	ds_write2_b32 v175, v69, v77 offset0:188 offset1:196
	ds_write2_b32 v176, v73, v81 offset0:124 offset1:132
	s_waitcnt lgkmcnt(0)
	ds_read_b128 v[66:69], v173
	ds_read_b128 v[70:73], v173 offset:16
	ds_read_b128 v[74:77], v173 offset:32
	ds_read_b128 v[78:81], v173 offset:48
	s_add_i32 s46, s46, s12
	s_or_b32 s46, s46, s6
	s_waitcnt lgkmcnt(2)
	v_mul_f32_e32 v70, v172, v70
	v_mul_f32_e32 v82, v172, v66
	v_mul_f32_e32 v67, v172, v67
	v_mov_b32_e32 v66, 0
	v_cvt_pk_fp8_f32 v66, v82, v67
	v_mul_f32_e32 v71, v172, v71
	v_mov_b32_e32 v67, 0
	v_cvt_pk_fp8_f32 v67, v70, v71
	v_mul_f32_e32 v68, v172, v68
	v_mul_f32_e32 v69, v172, v69
	v_cvt_pk_fp8_f32 v66, v68, v69 op_sel:[0,0,1]
	v_mul_f32_e32 v68, v172, v72
	v_mul_f32_e32 v69, v172, v73
	v_cvt_pk_fp8_f32 v67, v68, v69 op_sel:[0,0,1]
	s_waitcnt lgkmcnt(1)
	v_mul_f32_e32 v69, v172, v74
	v_mul_f32_e32 v70, v172, v75
	v_mov_b32_e32 v68, 0
	v_cvt_pk_fp8_f32 v68, v69, v70
	s_waitcnt lgkmcnt(0)
	v_mul_f32_e32 v72, v172, v78
	v_mul_f32_e32 v73, v172, v79
	v_mov_b32_e32 v69, 0
	v_cvt_pk_fp8_f32 v69, v72, v73
	v_mul_f32_e32 v70, v172, v76
	v_mul_f32_e32 v71, v172, v77
	v_cvt_pk_fp8_f32 v68, v70, v71 op_sel:[0,0,1]
	v_mul_f32_e32 v70, v172, v80
	v_mul_f32_e32 v71, v172, v81
	v_cvt_pk_fp8_f32 v69, v70, v71 op_sel:[0,0,1]
	ds_read_b128 v[70:73], v173 offset:4224
	ds_read_b128 v[74:77], v173 offset:4240
	s_ashr_i32 s47, s46, 31
	s_lshl_b64 s[46:47], s[46:47], 11
	s_add_u32 s46, s11, s46
	s_addc_u32 s47, s7, s47
	s_add_u32 s46, s46, s10
	s_waitcnt lgkmcnt(1)
	v_mul_f32_e32 v82, v172, v70
	v_mul_f32_e32 v71, v172, v71
	v_mov_b32_e32 v70, 0
	s_addc_u32 s47, s47, 0
	v_cvt_pk_fp8_f32 v70, v82, v71
	v_lshl_add_u64 v[80:81], s[46:47], 0, v[130:131]
	v_lshl_add_u64 v[78:79], v[80:81], 0, v[134:135]
	global_store_dwordx4 v[78:79], v[66:69], off nt
	v_mov_b32_e32 v71, 0
	s_waitcnt lgkmcnt(0)
	v_mul_f32_e32 v78, v172, v77
	v_mul_f32_e32 v66, v172, v72
	v_mul_f32_e32 v67, v172, v73
	v_cvt_pk_fp8_f32 v70, v66, v67 op_sel:[0,0,1]
	ds_read_b128 v[66:69], v173 offset:4256
	v_mul_f32_e32 v72, v172, v74
	v_mul_f32_e32 v73, v172, v75
	v_cvt_pk_fp8_f32 v71, v72, v73
	v_mul_f32_e32 v73, v172, v76
	ds_read_b128 v[74:77], v173 offset:4272
	s_waitcnt lgkmcnt(1)
	v_mul_f32_e32 v66, v172, v66
	v_mul_f32_e32 v67, v172, v67
	v_mov_b32_e32 v72, 0
	v_cvt_pk_fp8_f32 v72, v66, v67
	v_mul_f32_e32 v66, v172, v68
	v_mul_f32_e32 v67, v172, v69
	v_cvt_pk_fp8_f32 v71, v73, v78 op_sel:[0,0,1]
	v_cvt_pk_fp8_f32 v72, v66, v67 op_sel:[0,0,1]
	s_waitcnt lgkmcnt(0)
	v_mul_f32_e32 v66, v172, v74
	v_mul_f32_e32 v67, v172, v75
	v_mov_b32_e32 v73, 0
	v_cvt_pk_fp8_f32 v73, v66, v67
	ds_read_b128 v[66:69], v173 offset:8448
	v_mul_f32_e32 v74, v172, v76
	v_mul_f32_e32 v75, v172, v77
	v_cvt_pk_fp8_f32 v73, v74, v75 op_sel:[0,0,1]
	ds_read_b128 v[74:77], v173 offset:8464
	s_waitcnt lgkmcnt(1)
	v_mul_f32_e32 v82, v172, v66
	v_mul_f32_e32 v67, v172, v67
	v_mov_b32_e32 v66, 0
	v_cvt_pk_fp8_f32 v66, v82, v67
	v_lshl_add_u64 v[78:79], v[80:81], 0, v[136:137]
	v_mul_f32_e32 v67, v172, v68
	v_mul_f32_e32 v68, v172, v69
	global_store_dwordx4 v[78:79], v[70:73], off nt
	v_cvt_pk_fp8_f32 v66, v67, v68 op_sel:[0,0,1]
	ds_read_b128 v[68:71], v173 offset:8480
	s_waitcnt lgkmcnt(1)
	v_mul_f32_e32 v72, v172, v74
	v_mul_f32_e32 v73, v172, v75
	v_mov_b32_e32 v67, 0
	v_cvt_pk_fp8_f32 v67, v72, v73
	ds_read_b128 v[72:75], v173 offset:8496
	s_waitcnt lgkmcnt(1)
	v_mul_f32_e32 v78, v172, v68
	v_mul_f32_e32 v69, v172, v69
	v_mov_b32_e32 v68, 0
	v_cvt_pk_fp8_f32 v68, v78, v69
	v_mul_f32_e32 v76, v172, v76
	v_mul_f32_e32 v77, v172, v77
	v_mul_f32_e32 v69, v172, v70
	v_mul_f32_e32 v70, v172, v71
	v_cvt_pk_fp8_f32 v67, v76, v77 op_sel:[0,0,1]
	v_cvt_pk_fp8_f32 v68, v69, v70 op_sel:[0,0,1]
	s_waitcnt lgkmcnt(0)
	v_mul_f32_e32 v76, v172, v72
	v_mul_f32_e32 v77, v172, v73
	ds_read_b128 v[70:73], v173 offset:12672
	v_mov_b32_e32 v69, 0
	v_cvt_pk_fp8_f32 v69, v76, v77
	v_mul_f32_e32 v78, v172, v74
	v_mul_f32_e32 v79, v172, v75
	ds_read_b128 v[74:77], v173 offset:12688
	s_waitcnt lgkmcnt(1)
	v_mul_f32_e32 v82, v172, v70
	v_mul_f32_e32 v71, v172, v71
	v_mov_b32_e32 v70, 0
	v_cvt_pk_fp8_f32 v70, v82, v71
	v_mul_f32_e32 v71, v172, v72
	v_mul_f32_e32 v72, v172, v73
	s_waitcnt lgkmcnt(0)
	v_mul_f32_e32 v73, v172, v75
	v_cvt_pk_fp8_f32 v70, v71, v72 op_sel:[0,0,1]
	v_mul_f32_e32 v72, v172, v74
	v_mov_b32_e32 v71, 0
	v_cvt_pk_fp8_f32 v71, v72, v73
	ds_read_b128 v[72:75], v173 offset:12704
	v_mul_f32_e32 v76, v172, v76
	v_mul_f32_e32 v77, v172, v77
	v_cvt_pk_fp8_f32 v69, v78, v79 op_sel:[0,0,1]
	v_cvt_pk_fp8_f32 v71, v76, v77 op_sel:[0,0,1]
	ds_read_b128 v[76:79], v173 offset:12720
	s_waitcnt lgkmcnt(1)
	v_mul_f32_e32 v82, v172, v72
	v_mul_f32_e32 v73, v172, v73
	v_mov_b32_e32 v72, 0
	v_cvt_pk_fp8_f32 v72, v82, v73
	s_waitcnt lgkmcnt(0)
	v_mul_f32_e32 v76, v172, v76
	v_mul_f32_e32 v77, v172, v77
	v_mov_b32_e32 v73, 0
	v_cvt_pk_fp8_f32 v73, v76, v77
	v_mul_f32_e32 v74, v172, v74
	v_mul_f32_e32 v75, v172, v75
	v_cvt_pk_fp8_f32 v72, v74, v75 op_sel:[0,0,1]
	v_mul_f32_e32 v74, v172, v78
	v_mul_f32_e32 v75, v172, v79
	v_cvt_pk_fp8_f32 v73, v74, v75 op_sel:[0,0,1]
	v_lshl_add_u64 v[74:75], v[80:81], 0, v[132:133]
	global_store_dwordx4 v[74:75], v[66:69], off nt
	s_addk_i32 s13, 0x600
	s_and_b32 s13, s13, 0xffffff00
	v_lshl_add_u64 v[66:67], v[80:81], 0, v[138:139]
	global_store_dwordx4 v[66:67], v[70:73], off nt
	s_waitcnt lgkmcnt(0)
	s_waitcnt vmcnt(17)
	ds_write2_b32 v174, v42, v58 offset1:8
	s_waitcnt vmcnt(16)
	ds_write2_b32 v174, v46, v62 offset0:64 offset1:72
	ds_write2_b32 v174, v43, v59 offset0:132 offset1:140
	ds_write2_b32 v174, v47, v63 offset0:196 offset1:204
	ds_write2_b32 v175, v44, v60 offset0:8 offset1:16
	ds_write2_b32 v175, v48, v64 offset0:72 offset1:80
	ds_write2_b32 v175, v45, v61 offset0:140 offset1:148
	ds_write2_b32 v175, v49, v65 offset0:204 offset1:212
	s_waitcnt vmcnt(13)
	ds_write2_b32 v174, v34, v50 offset0:16 offset1:24
	s_waitcnt vmcnt(12)
	ds_write2_b32 v174, v38, v54 offset0:80 offset1:88
	ds_write2_b32 v174, v35, v51 offset0:148 offset1:156
	ds_write2_b32 v174, v39, v55 offset0:212 offset1:220
	ds_write2_b32 v175, v36, v52 offset0:24 offset1:32
	ds_write2_b32 v175, v40, v56 offset0:88 offset1:96
	ds_write2_b32 v175, v37, v53 offset0:156 offset1:164
	ds_write2_b32 v175, v41, v57 offset0:220 offset1:228
	s_waitcnt vmcnt(9)
	ds_write2_b32 v174, v18, v26 offset0:32 offset1:40
	s_waitcnt vmcnt(8)
	ds_write2_b32 v174, v22, v30 offset0:96 offset1:104
	ds_write2_b32 v174, v19, v27 offset0:164 offset1:172
	ds_write2_b32 v174, v23, v31 offset0:228 offset1:236
	ds_write2_b32 v175, v20, v28 offset0:40 offset1:48
	ds_write2_b32 v175, v24, v32 offset0:104 offset1:112
	ds_write2_b32 v175, v21, v29 offset0:172 offset1:180
	ds_write2_b32 v175, v25, v33 offset0:236 offset1:244
	s_waitcnt vmcnt(5)
	ds_write2_b32 v174, v2, v10 offset0:48 offset1:56
	s_waitcnt vmcnt(4)
	ds_write2_b32 v174, v6, v14 offset0:112 offset1:120
	ds_write2_b32 v174, v3, v11 offset0:180 offset1:188
	ds_write2_b32 v174, v7, v15 offset0:244 offset1:252
	ds_write2_b32 v175, v4, v12 offset0:56 offset1:64
	ds_write2_b32 v175, v8, v16 offset0:120 offset1:128
	ds_write2_b32 v175, v5, v13 offset0:188 offset1:196
	ds_write2_b32 v176, v9, v17 offset0:124 offset1:132
	s_waitcnt lgkmcnt(0)
	ds_read_b128 v[2:5], v173
	ds_read_b128 v[6:9], v173 offset:16
	ds_read_b128 v[10:13], v173 offset:32
	ds_read_b128 v[14:17], v173 offset:48
	s_add_i32 s13, s13, s12
	s_or_b32 s12, s13, s6
	s_waitcnt lgkmcnt(2)
	v_mul_f32_e32 v6, v172, v6
	v_mul_f32_e32 v18, v172, v2
	v_mul_f32_e32 v3, v172, v3
	v_mov_b32_e32 v2, 0
	v_cvt_pk_fp8_f32 v2, v18, v3
	v_mul_f32_e32 v7, v172, v7
	v_mov_b32_e32 v3, 0
	v_cvt_pk_fp8_f32 v3, v6, v7
	v_mul_f32_e32 v4, v172, v4
	v_mul_f32_e32 v5, v172, v5
	v_cvt_pk_fp8_f32 v2, v4, v5 op_sel:[0,0,1]
	v_mul_f32_e32 v4, v172, v8
	v_mul_f32_e32 v5, v172, v9
	v_cvt_pk_fp8_f32 v3, v4, v5 op_sel:[0,0,1]
	s_waitcnt lgkmcnt(1)
	v_mul_f32_e32 v5, v172, v10
	v_mul_f32_e32 v6, v172, v11
	v_mov_b32_e32 v4, 0
	v_cvt_pk_fp8_f32 v4, v5, v6
	s_waitcnt lgkmcnt(0)
	v_mul_f32_e32 v8, v172, v14
	v_mul_f32_e32 v9, v172, v15
	v_mov_b32_e32 v5, 0
	v_cvt_pk_fp8_f32 v5, v8, v9
	v_mul_f32_e32 v6, v172, v12
	v_mul_f32_e32 v7, v172, v13
	v_cvt_pk_fp8_f32 v4, v6, v7 op_sel:[0,0,1]
	v_mul_f32_e32 v6, v172, v16
	v_mul_f32_e32 v7, v172, v17
	v_cvt_pk_fp8_f32 v5, v6, v7 op_sel:[0,0,1]
	ds_read_b128 v[6:9], v173 offset:4224
	ds_read_b128 v[10:13], v173 offset:4240
	s_ashr_i32 s13, s12, 31
	s_lshl_b64 s[12:13], s[12:13], 11
	s_add_u32 s6, s11, s12
	s_addc_u32 s7, s7, s13
	s_add_u32 s6, s6, s10
	s_waitcnt lgkmcnt(1)
	v_mul_f32_e32 v18, v172, v6
	v_mul_f32_e32 v7, v172, v7
	v_mov_b32_e32 v6, 0
	s_addc_u32 s7, s7, 0
	v_cvt_pk_fp8_f32 v6, v18, v7
	v_lshl_add_u64 v[16:17], s[6:7], 0, v[130:131]
	v_lshl_add_u64 v[14:15], v[16:17], 0, v[134:135]
	global_store_dwordx4 v[14:15], v[2:5], off nt
	v_mov_b32_e32 v7, 0
	s_waitcnt lgkmcnt(0)
	v_mul_f32_e32 v14, v172, v13
	v_mul_f32_e32 v2, v172, v8
	v_mul_f32_e32 v3, v172, v9
	v_cvt_pk_fp8_f32 v6, v2, v3 op_sel:[0,0,1]
	ds_read_b128 v[2:5], v173 offset:4256
	v_mul_f32_e32 v8, v172, v10
	v_mul_f32_e32 v9, v172, v11
	v_cvt_pk_fp8_f32 v7, v8, v9
	v_mul_f32_e32 v9, v172, v12
	ds_read_b128 v[10:13], v173 offset:4272
	s_waitcnt lgkmcnt(1)
	v_mul_f32_e32 v2, v172, v2
	v_mul_f32_e32 v3, v172, v3
	v_mov_b32_e32 v8, 0
	v_cvt_pk_fp8_f32 v8, v2, v3
	v_mul_f32_e32 v2, v172, v4
	v_mul_f32_e32 v3, v172, v5
	v_cvt_pk_fp8_f32 v7, v9, v14 op_sel:[0,0,1]
	v_cvt_pk_fp8_f32 v8, v2, v3 op_sel:[0,0,1]
	s_waitcnt lgkmcnt(0)
	v_mul_f32_e32 v2, v172, v10
	v_mul_f32_e32 v3, v172, v11
	v_mov_b32_e32 v9, 0
	v_cvt_pk_fp8_f32 v9, v2, v3
	ds_read_b128 v[2:5], v173 offset:8448
	v_mul_f32_e32 v10, v172, v12
	v_mul_f32_e32 v11, v172, v13
	v_cvt_pk_fp8_f32 v9, v10, v11 op_sel:[0,0,1]
	ds_read_b128 v[10:13], v173 offset:8464
	s_waitcnt lgkmcnt(1)
	v_mul_f32_e32 v18, v172, v2
	v_mul_f32_e32 v3, v172, v3
	v_mov_b32_e32 v2, 0
	v_cvt_pk_fp8_f32 v2, v18, v3
	v_lshl_add_u64 v[14:15], v[16:17], 0, v[136:137]
	v_mul_f32_e32 v3, v172, v4
	v_mul_f32_e32 v4, v172, v5
	global_store_dwordx4 v[14:15], v[6:9], off nt
	v_cvt_pk_fp8_f32 v2, v3, v4 op_sel:[0,0,1]
	ds_read_b128 v[4:7], v173 offset:8480
	s_waitcnt lgkmcnt(1)
	v_mul_f32_e32 v8, v172, v10
	v_mul_f32_e32 v9, v172, v11
	v_mov_b32_e32 v3, 0
	v_cvt_pk_fp8_f32 v3, v8, v9
	ds_read_b128 v[8:11], v173 offset:8496
	s_waitcnt lgkmcnt(1)
	v_mul_f32_e32 v14, v172, v4
	v_mul_f32_e32 v5, v172, v5
	v_mov_b32_e32 v4, 0
	v_cvt_pk_fp8_f32 v4, v14, v5
	v_mul_f32_e32 v12, v172, v12
	v_mul_f32_e32 v13, v172, v13
	v_mul_f32_e32 v5, v172, v6
	v_mul_f32_e32 v6, v172, v7
	v_cvt_pk_fp8_f32 v3, v12, v13 op_sel:[0,0,1]
	v_cvt_pk_fp8_f32 v4, v5, v6 op_sel:[0,0,1]
	s_waitcnt lgkmcnt(0)
	v_mul_f32_e32 v12, v172, v8
	v_mul_f32_e32 v13, v172, v9
	ds_read_b128 v[6:9], v173 offset:12672
	v_mov_b32_e32 v5, 0
	v_cvt_pk_fp8_f32 v5, v12, v13
	v_mul_f32_e32 v14, v172, v10
	v_mul_f32_e32 v15, v172, v11
	ds_read_b128 v[10:13], v173 offset:12688
	s_waitcnt lgkmcnt(1)
	v_mul_f32_e32 v18, v172, v6
	v_mul_f32_e32 v7, v172, v7
	v_mov_b32_e32 v6, 0
	v_cvt_pk_fp8_f32 v6, v18, v7
	v_mul_f32_e32 v7, v172, v8
	v_mul_f32_e32 v8, v172, v9
	s_waitcnt lgkmcnt(0)
	v_mul_f32_e32 v9, v172, v11
	v_cvt_pk_fp8_f32 v6, v7, v8 op_sel:[0,0,1]
	v_mul_f32_e32 v8, v172, v10
	v_mov_b32_e32 v7, 0
	v_cvt_pk_fp8_f32 v7, v8, v9
	ds_read_b128 v[8:11], v173 offset:12704
	v_mul_f32_e32 v12, v172, v12
	v_mul_f32_e32 v13, v172, v13
	v_cvt_pk_fp8_f32 v5, v14, v15 op_sel:[0,0,1]
	v_cvt_pk_fp8_f32 v7, v12, v13 op_sel:[0,0,1]
	ds_read_b128 v[12:15], v173 offset:12720
	s_waitcnt lgkmcnt(1)
	v_mul_f32_e32 v18, v172, v8
	v_mul_f32_e32 v9, v172, v9
	v_mov_b32_e32 v8, 0
	v_cvt_pk_fp8_f32 v8, v18, v9
	s_waitcnt lgkmcnt(0)
	v_mul_f32_e32 v12, v172, v12
	v_mul_f32_e32 v13, v172, v13
	v_mov_b32_e32 v9, 0
	v_cvt_pk_fp8_f32 v9, v12, v13
	v_mul_f32_e32 v10, v172, v10
	v_mul_f32_e32 v11, v172, v11
	v_cvt_pk_fp8_f32 v8, v10, v11 op_sel:[0,0,1]
	v_mul_f32_e32 v10, v172, v14
	v_mul_f32_e32 v11, v172, v15
	v_cvt_pk_fp8_f32 v9, v10, v11 op_sel:[0,0,1]
	v_lshl_add_u64 v[10:11], v[16:17], 0, v[132:133]
	global_store_dwordx4 v[10:11], v[2:5], off nt
	s_nop 1
	v_lshl_add_u64 v[2:3], v[16:17], 0, v[138:139]
	global_store_dwordx4 v[2:3], v[6:9], off nt
	s_waitcnt lgkmcnt(0)
	s_barrier
	s_and_saveexec_b64 s[6:7], s[36:37]
	s_cbranch_execz .LBB0_561
	v_mov_b32_e32 v2, s14
	s_waitcnt vmcnt(0)
	ds_write_b32 v2, v255
	s_branch .LBB0_561

.LBB0_576:
	v_mov_b32_e32 v182, v3
	s_and_saveexec_b64 s[4:5], s[36:37]
	s_cbranch_execz .LBB0_580
	s_mov_b64 s[28:29], exec
	v_mbcnt_lo_u32_b32 v2, s28, 0
	v_mbcnt_hi_u32_b32 v2, s29, v2
	v_cmp_eq_u32_e32 vcc, 0, v2
	s_and_saveexec_b64 s[6:7], vcc
	s_cbranch_execz .LBB0_579
	s_bcnt1_i32_b64 s12, s[28:29]
	v_mov_b32_e32 v4, s12
	global_atomic_add v255, v3, v4, s[10:11] sc0
.LBB0_579:
	s_or_b64 exec, exec, s[6:7]
.LBB0_580:
	s_or_b64 exec, exec, s[4:5]
	v_mov_b32 v68, v0
	s_ashr_i32 s6, s52, 7
	v_lshlrev_b32_e32 v2, 3, v68
	v_and_b32_e32 v10, 8, v2
	s_and_b32 s46, s52, 63
	s_bfe_u32 s39, s52, 0x10006
	s_ashr_i32 s7, s6, 31
	v_bfe_u32 v6, v68, 1, 1
	v_lshlrev_b32_e32 v2, 2, v10
	s_add_i32 s66, s46, -1
	s_lshl_b64 s[28:29], s[6:7], 13
	v_ashrrev_i32_e32 v168, 2, v68
	s_lshl_b32 s34, s39, 6
	v_lshlrev_b32_e32 v7, 5, v6
	v_cmp_eq_u32_e64 s[4:5], 0, v6
	v_lshl_add_u64 v[4:5], s[18:19], 0, v[2:3]
	v_lshl_add_u64 v[8:9], s[20:21], 0, v[2:3]
	v_lshlrev_b32_e32 v2, 6, v6
	v_lshlrev_b32_e32 v6, 1, v10
	v_readfirstlane_b32 s38, v68
	v_ashrrev_i32_e32 v169, 31, v168
	v_and_b32_e32 v11, 63, v168
	v_add3_u32 v10, 0, v2, v6
	s_mov_b64 s[30:31], -1
	s_cmp_lt_u32 s66, 64
	v_lshlrev_b32_e32 v2, 1, v7
	v_mul_lo_u32 v13, v168, s57
	s_barrier
	s_cbranch_scc0 .LBB0_582
	s_lshl_b32 s7, s66, 7
	s_or_b32 s30, s28, s7
	s_mov_b32 s31, s29
	v_lshl_add_u64 v[14:15], s[30:31], 0, v[168:169]
	v_mov_b64_e32 v[16:17], s[14:15]
	v_mad_u64_u32 v[16:17], s[30:31], v14, s56, v[16:17]
	v_mad_i32_i24 v17, v15, s56, v17
	s_lshl_b32 s12, s34, 1
	v_lshl_add_u64 v[14:15], v[16:17], 0, s[12:13]
	v_lshl_add_u64 v[14:15], v[14:15], 0, v[2:3]
	v_mov_b32_e32 v7, v3
	v_lshl_add_u64 v[18:19], v[14:15], 0, v[6:7]
	v_add_u32_e32 v7, s7, v168
	v_ashrrev_i32_e32 v7, 6, v7
	v_cndmask_b32_e64 v7, v11, v7, s[4:5]
	v_lshlrev_b32_e32 v22, 4, v7
	v_ashrrev_i32_e32 v23, 31, v22
	v_lshlrev_b64 v[30:31], 2, v[22:23]
	global_load_dwordx4 v[14:17], v[18:19], off offset:1024
	s_nop 0
	global_load_dwordx4 v[18:21], v[18:19], off offset:1056
	v_lshl_add_u64 v[26:27], v[8:9], 0, v[30:31]
	global_load_dwordx4 v[22:25], v[26:27], off
	s_nop 0
	global_load_dwordx4 v[26:29], v[26:27], off offset:16
	v_lshl_add_u64 v[34:35], v[4:5], 0, v[30:31]
	global_load_dwordx4 v[30:33], v[34:35], off
	s_nop 0
	global_load_dwordx4 v[34:37], v[34:35], off offset:16
	v_mul_lo_u32 v12, v168, s57
	v_add_u32_e32 v7, v10, v12
	s_mov_b64 s[30:31], 0
	s_waitcnt vmcnt(5)
	v_lshlrev_b32_e32 v38, 16, v14
	v_and_b32_e32 v39, 0xffff0000, v14
	s_waitcnt vmcnt(4)
	v_lshlrev_b32_e32 v40, 16, v18
	v_and_b32_e32 v41, 0xffff0000, v18
	v_lshlrev_b32_e32 v14, 16, v15
	v_and_b32_e32 v15, 0xffff0000, v15
	v_lshlrev_b32_e32 v18, 16, v19
	v_and_b32_e32 v19, 0xffff0000, v19
	v_lshlrev_b32_e32 v42, 16, v16
	v_and_b32_e32 v43, 0xffff0000, v16
	v_lshlrev_b32_e32 v44, 16, v20
	v_and_b32_e32 v45, 0xffff0000, v20
	v_lshlrev_b32_e32 v16, 16, v17
	v_and_b32_e32 v17, 0xffff0000, v17
	v_lshlrev_b32_e32 v20, 16, v21
	v_and_b32_e32 v21, 0xffff0000, v21
	s_waitcnt vmcnt(3)
	v_pk_mul_f32 v[46:47], v[22:23], v[38:39]
	v_pk_mul_f32 v[22:23], v[22:23], v[40:41]
	v_pk_mul_f32 v[48:49], v[24:25], v[14:15]
	v_pk_mul_f32 v[24:25], v[24:25], v[18:19]
	s_waitcnt vmcnt(2)
	v_pk_mul_f32 v[50:51], v[26:27], v[42:43]
	v_pk_mul_f32 v[26:27], v[26:27], v[44:45]
	v_pk_mul_f32 v[52:53], v[28:29], v[16:17]
	v_pk_mul_f32 v[28:29], v[28:29], v[20:21]
	s_waitcnt vmcnt(1)
	v_pk_fma_f32 v[40:41], v[30:31], v[40:41], v[46:47]
	v_pk_fma_f32 v[22:23], v[30:31], v[38:39], v[22:23] neg_lo:[0,0,1] neg_hi:[0,0,1]
	v_pk_fma_f32 v[30:31], v[32:33], v[18:19], v[48:49]
	v_pk_fma_f32 v[18:19], v[32:33], v[14:15], v[24:25] neg_lo:[0,0,1] neg_hi:[0,0,1]
	s_waitcnt vmcnt(0)
	v_pk_fma_f32 v[26:27], v[34:35], v[42:43], v[26:27] neg_lo:[0,0,1] neg_hi:[0,0,1]
	v_pk_fma_f32 v[32:33], v[36:37], v[20:21], v[52:53]
	v_pk_fma_f32 v[20:21], v[36:37], v[16:17], v[28:29] neg_lo:[0,0,1] neg_hi:[0,0,1]
	v_pk_fma_f32 v[24:25], v[34:35], v[44:45], v[50:51]
	v_cvt_pk_bf16_f32 v14, v22, v23
	v_cvt_pk_bf16_f32 v15, v18, v19
	v_cvt_pk_bf16_f32 v16, v26, v27
	v_cvt_pk_bf16_f32 v17, v20, v21
	v_cvt_pk_bf16_f32 v18, v40, v41
	v_cvt_pk_bf16_f32 v19, v30, v31
	v_cvt_pk_bf16_f32 v20, v24, v25
	v_cvt_pk_bf16_f32 v21, v32, v33
	ds_write_b128 v7, v[14:17]
	ds_write_b128 v7, v[18:21] offset:32

.LBB0_747:
	v_mov_b32_e32 v2, s25
	s_waitcnt vmcnt(0)
	ds_write_b32 v2, v255
	s_branch .LBB0_575

.LBB0_751:
	v_mov_b32_e32 v37, 0
	s_and_saveexec_b64 s[4:5], s[36:37]
	s_cbranch_execz .LBB0_755
	s_mov_b64 s[20:21], exec
	v_mbcnt_lo_u32_b32 v2, s20, 0
	v_mbcnt_hi_u32_b32 v2, s21, v2
	v_cmp_eq_u32_e32 vcc, 0, v2
	s_and_saveexec_b64 s[6:7], vcc
	s_cbranch_execz .LBB0_754
	s_bcnt1_i32_b64 s16, s[20:21]
	s_waitcnt vmcnt(0)
	v_mov_b32_e32 v3, s16
	global_atomic_add v255, v15, v3, s[10:11] sc0
.LBB0_754:
	s_or_b64 exec, exec, s[6:7]
.LBB0_755:
	s_or_b64 exec, exec, s[4:5]
	s_add_i32 s4, s52, 0xffffff00
	s_mul_hi_i32 s5, s4, 0x3e0f83e1
	s_lshr_b32 s6, s5, 31
	s_ashr_i32 s54, s5, 5
	s_add_i32 s54, s54, s6
	s_mul_i32 s5, s54, 0x84
	s_sub_i32 s52, s4, s5
	s_ashr_i32 s4, s54, 2
	s_cmp_gt_i32 s52, 3
	s_cselect_b64 s[20:21], -1, 0
	v_mov_b32 v39, v0
	s_mov_b64 s[6:7], -1
	v_readfirstlane_b32 s53, v39
	s_and_b64 vcc, exec, s[20:21]
	s_cbranch_vccz .LBB0_757
	s_ashr_i32 s5, s4, 31
	s_lshl_b64 s[6:7], s[4:5], 13
	s_lshl_b32 s5, s52, 6
	s_addk_i32 s5, 0xff00
	s_add_u32 s22, s6, s5
	s_addc_u32 s23, s7, 0
	s_mov_b64 s[6:7], 0

.LBB0_789:
	s_ashr_i32 s4, s52, 31
	v_mad_u32_u24 v18, v20, s48, 0
	v_lshlrev_b32_e32 v54, 1, v14
	v_add_u32_e32 v12, s7, v21
	v_mov_b32_e32 v10, s52
	v_mov_b32_e32 v11, s4
	v_add_u32_e32 v21, v18, v54
	v_mad_i64_i32 v[22:23], s[4:5], v12, s26, v[10:11]
	ds_read_b128 v[10:13], v21 offset:61440
	v_lshlrev_b64 v[22:23], 14, v[22:23]
	v_lshl_add_u64 v[26:27], s[14:15], 0, v[22:23]
	ds_read_b128 v[22:25], v21 offset:61504
	s_waitcnt lgkmcnt(1)
	v_mfma_f32_16x16x32_bf16 v[10:13], v[6:9], v[10:13], 0
	v_lshlrev_b32_e32 v28, 7, v20
	v_add_u32_e32 v20, 40, v14
	v_and_b32_e32 v20, 56, v20
	s_waitcnt lgkmcnt(0)
	v_mfma_f32_16x16x32_bf16 v[10:13], v[2:5], v[22:25], v[10:13]
	v_lshlrev_b32_e32 v47, 1, v20
	v_add_u32_e32 v46, 0xf000, v18
	v_add_u32_e32 v18, v18, v47
	s_lshl_b32 s16, s6, 1
	v_lshl_add_u64 v[26:27], v[26:27], 0, s[16:17]
	s_nop 2
	v_cvt_pk_bf16_f32 v24, v10, v11
	v_cvt_pk_bf16_f32 v25, v12, v13
	ds_read_b128 v[10:13], v21 offset:63760
	ds_read_b128 v[20:23], v18 offset:63744
	s_waitcnt lgkmcnt(1)
	v_mfma_f32_16x16x32_bf16 v[10:13], v[6:9], v[10:13], 0
	v_add_u32_e32 v18, v46, v54
	v_lshl_add_u64 v[26:27], v[26:27], 0, v[14:15]
	v_mov_b32_e32 v29, v15
	s_waitcnt lgkmcnt(0)
	v_mfma_f32_16x16x32_bf16 v[10:13], v[2:5], v[20:23], v[10:13]
	ds_read_b128 v[20:23], v18 offset:4640
	v_lshl_add_u64 v[50:51], v[26:27], 0, v[28:29]
	global_store_dwordx2 v[50:51], v[24:25], off
	s_waitcnt lgkmcnt(0)
	v_mfma_f32_16x16x32_bf16 v[20:23], v[6:9], v[20:23], 0
	s_nop 2
	v_cvt_pk_bf16_f32 v10, v10, v11
	v_add_u32_e32 v11, 48, v14
	v_and_b32_e32 v11, 56, v11
	v_lshl_add_u32 v38, v11, 1, v46
	ds_read_b128 v[24:27], v38 offset:4608
	ds_read_b128 v[28:31], v18 offset:9216
	s_waitcnt lgkmcnt(1)
	v_mfma_f32_16x16x32_bf16 v[20:23], v[2:5], v[24:27], v[20:23]
	v_or_b32_e32 v24, 48, v19
	v_mad_u32_u24 v32, v24, s48, 0
	v_cvt_pk_bf16_f32 v11, v12, v13
	v_add_u32_e32 v24, v32, v54
	global_store_dwordx2 v[50:51], v[10:11], off offset:2048
	ds_read_b128 v[10:13], v18 offset:13856
	ds_read_b128 v[24:27], v24 offset:61488
	v_add_u32_e32 v14, 56, v14
	v_and_b32_e32 v14, 56, v14
	v_lshlrev_b32_e32 v14, 1, v14
	v_add_u32_e32 v32, v32, v14
	ds_read_b128 v[32:35], v32 offset:61440
	ds_read_b128 v[38:41], v38 offset:13824
	ds_read_b128 v[42:45], v18 offset:9280
	s_waitcnt lgkmcnt(3)
	v_mfma_f32_16x16x32_bf16 v[24:27], v[6:9], v[24:27], 0
	v_add_u32_e32 v46, v46, v47
	v_cvt_pk_bf16_f32 v52, v20, v21
	v_cvt_pk_bf16_f32 v53, v22, v23
	s_waitcnt lgkmcnt(2)
	v_mfma_f32_16x16x32_bf16 v[24:27], v[2:5], v[32:35], v[24:27]
	ds_read_b128 v[20:23], v18 offset:11536
	ds_read_b128 v[46:49], v46 offset:11520
	v_or_b32_e32 v18, 0x70, v19
	s_waitcnt lgkmcnt(2)
	v_mfma_f32_16x16x32_bf16 v[32:35], v[6:9], v[42:45], 0
	v_add_co_u32_e32 v42, vcc, s28, v50
	s_nop 1
	v_cvt_pk_bf16_f32 v24, v24, v25
	v_mfma_f32_16x16x32_bf16 v[28:31], v[2:5], v[28:31], v[32:35]
	v_addc_co_u32_e32 v43, vcc, 0, v51, vcc
	v_add_co_u32_e32 v44, vcc, s30, v50
	s_waitcnt lgkmcnt(0)
	v_mfma_f32_16x16x32_bf16 v[32:35], v[6:9], v[46:49], 0
	v_cvt_pk_bf16_f32 v25, v26, v27
	v_addc_co_u32_e32 v45, vcc, 0, v51, vcc
	global_store_dwordx2 v[42:43], v[24:25], off offset:2048
	s_nop 0
	v_cvt_pk_bf16_f32 v24, v28, v29
	v_cvt_pk_bf16_f32 v25, v30, v31
	global_store_dwordx2 v[44:45], v[24:25], off
	v_mfma_f32_16x16x32_bf16 v[24:27], v[6:9], v[38:41], 0
	global_store_dwordx2 v[44:45], v[52:53], off offset:-4096
	v_mfma_f32_16x16x32_bf16 v[20:23], v[2:5], v[20:23], v[32:35]
	v_mfma_f32_16x16x32_bf16 v[10:13], v[2:5], v[10:13], v[24:27]
	s_nop 4
	v_mad_u32_u24 v24, v18, s48, 0
	s_nop 0
	v_cvt_pk_bf16_f32 v20, v20, v21
	v_cvt_pk_bf16_f32 v21, v22, v23
	v_add_u32_e32 v14, v24, v14
	global_store_dwordx2 v[44:45], v[20:21], off offset:2048
	ds_read_b128 v[18:21], v14 offset:61440
	v_cvt_pk_bf16_f32 v22, v10, v11
	v_add_u32_e32 v10, v24, v54
	v_cvt_pk_bf16_f32 v23, v12, v13
	ds_read_b128 v[10:13], v10 offset:61488
	s_waitcnt lgkmcnt(1)
	v_mfma_f32_16x16x32_bf16 v[6:9], v[6:9], v[18:21], 0
	v_add_co_u32_e32 v18, vcc, s31, v50
	s_waitcnt lgkmcnt(0)
	v_mfma_f32_16x16x32_bf16 v[2:5], v[2:5], v[10:13], v[6:9]
	v_addc_co_u32_e32 v19, vcc, 0, v51, vcc
	global_store_dwordx2 v[18:19], v[22:23], off
	s_nop 5
	v_cvt_pk_bf16_f32 v2, v2, v3
	v_cvt_pk_bf16_f32 v3, v4, v5
	global_store_dwordx2 v[18:19], v[2:3], off offset:2048
	s_and_saveexec_b64 s[4:5], s[36:37]
	s_cbranch_execz .LBB0_750
	v_mov_b32_e32 v2, s50
	s_waitcnt vmcnt(0)
	ds_write_b32 v2, v255
	s_branch .LBB0_750

.LBB0_801:
	v_mov_b32_e32 v1, 0
	s_and_saveexec_b64 s[6:7], s[36:37]
	s_cbranch_execz .LBB0_805
	s_mov_b64 s[10:11], exec
	v_mbcnt_lo_u32_b32 v1, s10, 0
	v_mbcnt_hi_u32_b32 v1, s11, v1
	v_cmp_eq_u32_e32 vcc, 0, v1
	s_and_saveexec_b64 s[8:9], vcc
	s_cbranch_execz .LBB0_804
	s_bcnt1_i32_b64 s10, s[10:11]
	v_mov_b32_e32 v2, s10
	global_atomic_add v255, v131, v2, s[4:5] sc0

.LBB0_805:
	s_or_b64 exec, exec, s[6:7]
	v_mov_b32 v132, v0
	s_lshl_b32 s6, s38, 6
	v_readfirstlane_b32 s11, v132
	s_ashr_i32 s9, s11, 6
	s_ashr_i32 s10, s38, 8
	s_and_b32 s46, s6, 0x3c00
	s_cmp_eq_u32 s10, 1
	s_cselect_b32 s6, s17, 0xd8
	s_cmpk_lt_u32 s38, 0x100
	s_cselect_b32 s7, 16, 0x90
	s_cselect_b32 s8, 0xc8, s6
	s_add_u32 s6, s13, s7
	s_addc_u32 s7, s14, 0
	s_lshr_b32 s39, s46, 8
	v_mov_b32_e32 v2, s39
	global_load_dword v4, v2, s[6:7] sc1
	s_add_u32 s6, s0, s8
	s_addc_u32 s7, s1, 0
	s_load_dwordx2 s[6:7], s[6:7], 0x0
	s_lshl_b32 s8, s38, 7
	s_mul_i32 s38, s9, 0x4400
	s_and_b32 s8, s8, 0x780
	s_add_i32 s47, s38, 0
	s_lshl_b32 s38, s46, 13
	v_bfe_u32 v133, v132, 3, 3
	s_waitcnt lgkmcnt(0)
	s_add_u32 s6, s6, s38
	v_or_b32_e32 v2, s8, v133
	s_addc_u32 s7, s7, 0
	v_lshlrev_b32_e32 v130, 12, v2
	v_lshlrev_b32_e32 v5, 4, v132
	s_waitcnt vmcnt(1)
	v_lshl_add_u64 v[2:3], s[6:7], 0, v[130:131]
	v_and_b32_e32 v130, 0x70, v5
	s_lshl_b32 s6, s9, 5
	v_lshl_add_u64 v[2:3], v[2:3], 0, v[130:131]
	s_ashr_i32 s7, s6, 31
	v_lshl_add_u64 v[142:143], s[6:7], 2, v[2:3]
	v_add_co_u32_e32 v140, vcc, s19, v142
	global_load_dwordx4 v[66:69], v[142:143], off nt
	s_nop 0
	v_addc_co_u32_e32 v141, vcc, 0, v143, vcc
	v_add_co_u32_e32 v144, vcc, s20, v142
	global_load_dwordx4 v[70:73], v[140:141], off nt
	s_nop 0
	v_addc_co_u32_e32 v145, vcc, 0, v143, vcc
	v_add_co_u32_e32 v146, vcc, s21, v142
	global_load_dwordx4 v[74:77], v[144:145], off nt
	s_nop 0
	v_addc_co_u32_e32 v147, vcc, 0, v143, vcc
	v_add_co_u32_e32 v148, vcc, s22, v142
	global_load_dwordx4 v[78:81], v[146:147], off nt
	s_nop 0
	v_addc_co_u32_e32 v149, vcc, 0, v143, vcc
	v_add_co_u32_e32 v150, vcc, s23, v142
	global_load_dwordx4 v[82:85], v[148:149], off nt
	s_nop 0
	v_addc_co_u32_e32 v151, vcc, 0, v143, vcc
	v_add_co_u32_e32 v152, vcc, s24, v142
	global_load_dwordx4 v[86:89], v[150:151], off nt
	s_nop 0
	v_addc_co_u32_e32 v153, vcc, 0, v143, vcc
	v_add_co_u32_e32 v154, vcc, s25, v142
	global_load_dwordx4 v[90:93], v[152:153], off nt
	s_nop 0
	v_addc_co_u32_e32 v155, vcc, 0, v143, vcc
	v_add_co_u32_e32 v156, vcc, s26, v142
	global_load_dwordx4 v[94:97], v[154:155], off nt
	s_nop 0
	v_addc_co_u32_e32 v157, vcc, 0, v143, vcc
	v_add_co_u32_e32 v158, vcc, s27, v142
	global_load_dwordx4 v[98:101], v[156:157], off nt
	s_nop 0
	v_addc_co_u32_e32 v159, vcc, 0, v143, vcc
	v_add_co_u32_e32 v160, vcc, s28, v142
	global_load_dwordx4 v[102:105], v[158:159], off nt
	s_nop 0
	v_addc_co_u32_e32 v161, vcc, 0, v143, vcc
	v_add_co_u32_e32 v162, vcc, s29, v142
	global_load_dwordx4 v[106:109], v[160:161], off nt
	s_nop 0
	v_addc_co_u32_e32 v163, vcc, 0, v143, vcc
	v_add_co_u32_e32 v164, vcc, s30, v142
	global_load_dwordx4 v[110:113], v[162:163], off nt
	s_nop 0
	v_addc_co_u32_e32 v165, vcc, 0, v143, vcc
	v_add_co_u32_e32 v166, vcc, s31, v142
	global_load_dwordx4 v[114:117], v[164:165], off nt
	s_nop 0
	v_addc_co_u32_e32 v167, vcc, 0, v143, vcc
	v_add_co_u32_e32 v168, vcc, s33, v142
	global_load_dwordx4 v[118:121], v[166:167], off nt
	s_nop 0
	v_addc_co_u32_e32 v169, vcc, 0, v143, vcc
	v_add_co_u32_e32 v170, vcc, s34, v142
	global_load_dwordx4 v[122:125], v[168:169], off nt
	s_nop 0
	v_addc_co_u32_e32 v171, vcc, 0, v143, vcc
	global_load_dwordx4 v[126:129], v[170:171], off nt
	s_waitcnt vmcnt(16)
	v_div_scale_f32 v2, s[38:39], v4, v4, s18
	v_rcp_f32_e32 v3, v2
	v_and_b32_e32 v130, 7, v132
	v_mul_u32_u24_e32 v132, 0x840, v130
	v_lshlrev_b32_e32 v134, 2, v133
	v_fma_f32 v5, -v2, v3, 1.0
	v_fmac_f32_e32 v3, v5, v3
	v_div_scale_f32 v5, vcc, s18, v4, s18
	v_mul_f32_e32 v6, v5, v3
	v_fma_f32 v7, -v2, v6, v5
	v_fmac_f32_e32 v6, v7, v3
	v_fma_f32 v2, -v2, v6, v5
	v_div_fmas_f32 v2, v2, v3, v6
	v_add3_u32 v174, s47, v132, v134
	v_div_fixup_f32 v2, v2, v4, s18
	v_cmp_lt_f32_e32 vcc, 0, v4
	v_add_u32_e32 v175, 0x400, v174
	v_add_u32_e32 v176, 0x600, v174
	v_cndmask_b32_e32 v172, 0, v2, vcc
	global_load_dwordx4 v[50:53], v[142:143], off offset:1024 nt
	global_load_dwordx4 v[54:57], v[140:141], off offset:1024 nt
	global_load_dwordx4 v[58:61], v[144:145], off offset:1024 nt
	global_load_dwordx4 v[62:65], v[146:147], off offset:1024 nt
	global_load_dwordx4 v[34:37], v[148:149], off offset:1024 nt
	global_load_dwordx4 v[38:41], v[150:151], off offset:1024 nt
	global_load_dwordx4 v[42:45], v[152:153], off offset:1024 nt
	global_load_dwordx4 v[46:49], v[154:155], off offset:1024 nt
	global_load_dwordx4 v[18:21], v[156:157], off offset:1024 nt
	global_load_dwordx4 v[22:25], v[158:159], off offset:1024 nt
	global_load_dwordx4 v[26:29], v[160:161], off offset:1024 nt
	global_load_dwordx4 v[30:33], v[162:163], off offset:1024 nt
	global_load_dwordx4 v[2:5], v[164:165], off offset:1024 nt
	global_load_dwordx4 v[6:9], v[166:167], off offset:1024 nt
	global_load_dwordx4 v[10:13], v[168:169], off offset:1024 nt
	global_load_dwordx4 v[14:17], v[170:171], off offset:1024 nt
	s_waitcnt vmcnt(29)
	ds_write2_b32 v174, v66, v74 offset1:8
	s_waitcnt vmcnt(28)
	ds_write2_b32 v174, v70, v78 offset0:64 offset1:72
	ds_write2_b32 v174, v67, v75 offset0:132 offset1:140
	ds_write2_b32 v174, v71, v79 offset0:196 offset1:204
	ds_write2_b32 v175, v68, v76 offset0:8 offset1:16
	ds_write2_b32 v175, v72, v80 offset0:72 offset1:80
	ds_write2_b32 v175, v69, v77 offset0:140 offset1:148
	ds_write2_b32 v175, v73, v81 offset0:204 offset1:212
	s_waitcnt vmcnt(25)
	ds_write2_b32 v174, v82, v90 offset0:16 offset1:24
	s_waitcnt vmcnt(24)
	ds_write2_b32 v174, v86, v94 offset0:80 offset1:88
	ds_write2_b32 v174, v83, v91 offset0:148 offset1:156
	ds_write2_b32 v174, v87, v95 offset0:212 offset1:220
	ds_write2_b32 v175, v84, v92 offset0:24 offset1:32
	ds_write2_b32 v175, v88, v96 offset0:88 offset1:96
	ds_write2_b32 v175, v85, v93 offset0:156 offset1:164
	ds_write2_b32 v175, v89, v97 offset0:220 offset1:228
	s_waitcnt vmcnt(21)
	ds_write2_b32 v174, v98, v106 offset0:32 offset1:40
	s_waitcnt vmcnt(20)
	ds_write2_b32 v174, v102, v110 offset0:96 offset1:104
	ds_write2_b32 v174, v99, v107 offset0:164 offset1:172
	ds_write2_b32 v174, v103, v111 offset0:228 offset1:236
	ds_write2_b32 v175, v100, v108 offset0:40 offset1:48
	ds_write2_b32 v175, v104, v112 offset0:104 offset1:112
	ds_write2_b32 v175, v101, v109 offset0:172 offset1:180
	ds_write2_b32 v175, v105, v113 offset0:236 offset1:244
	s_waitcnt vmcnt(17)
	ds_write2_b32 v174, v114, v122 offset0:48 offset1:56
	s_waitcnt vmcnt(16)
	ds_write2_b32 v174, v118, v126 offset0:112 offset1:120
	ds_write2_b32 v174, v115, v123 offset0:180 offset1:188
	ds_write2_b32 v174, v119, v127 offset0:244 offset1:252
	ds_write2_b32 v175, v116, v124 offset0:56 offset1:64
	ds_write2_b32 v175, v120, v128 offset0:120 offset1:128
	ds_write2_b32 v175, v117, v125 offset0:188 offset1:196
	v_lshlrev_b32_e32 v66, 6, v130
	v_mul_u32_u24_e32 v67, 0x210, v133
	v_add3_u32 v173, s47, v66, v67
	s_lshl_b32 s7, s46, 12
	s_add_u32 s9, s15, s7
	s_addc_u32 s7, s16, 0
	s_and_b32 s38, s11, 0xffffff00
	s_lshl_b32 s10, s10, 7
	s_add_i32 s38, s38, s10
	s_and_b32 s6, s6, 0x60
	s_or_b32 s38, s6, s38
	s_ashr_i32 s39, s38, 31
	s_lshl_b64 s[38:39], s[38:39], 11
	s_add_u32 s38, s9, s38
	s_addc_u32 s39, s7, s39
	s_add_u32 s38, s38, s8
	v_lshlrev_b32_e32 v130, 4, v130
	s_addc_u32 s39, s39, 0
	v_lshlrev_b32_e32 v134, 11, v133
	v_mov_b32_e32 v135, v131
	ds_write2_b32 v176, v121, v129 offset0:124 offset1:132
	s_waitcnt lgkmcnt(0)
	ds_read_b128 v[66:69], v173
	ds_read_b128 v[70:73], v173 offset:16
	ds_read_b128 v[74:77], v173 offset:32
	ds_read_b128 v[78:81], v173 offset:48
	v_or_b32_e32 v136, 0x4000, v134
	v_mov_b32_e32 v137, v131
	s_waitcnt lgkmcnt(2)
	v_mul_f32_e32 v70, v172, v70
	v_mul_f32_e32 v82, v172, v66
	v_mul_f32_e32 v67, v172, v67
	v_mov_b32_e32 v66, 0
	v_cvt_pk_fp8_f32 v66, v82, v67
	v_mul_f32_e32 v71, v172, v71
	v_mov_b32_e32 v67, 0
	v_cvt_pk_fp8_f32 v67, v70, v71
	v_mul_f32_e32 v68, v172, v68
	v_mul_f32_e32 v69, v172, v69
	v_cvt_pk_fp8_f32 v66, v68, v69 op_sel:[0,0,1]
	v_mul_f32_e32 v68, v172, v72
	v_mul_f32_e32 v69, v172, v73
	v_cvt_pk_fp8_f32 v67, v68, v69 op_sel:[0,0,1]
	s_waitcnt lgkmcnt(1)
	v_mul_f32_e32 v69, v172, v74
	v_mul_f32_e32 v70, v172, v75
	v_mov_b32_e32 v68, 0
	v_cvt_pk_fp8_f32 v68, v69, v70
	s_waitcnt lgkmcnt(0)
	v_mul_f32_e32 v72, v172, v78
	v_mul_f32_e32 v73, v172, v79
	v_mov_b32_e32 v69, 0
	v_cvt_pk_fp8_f32 v69, v72, v73
	v_mul_f32_e32 v70, v172, v76
	v_mul_f32_e32 v71, v172, v77
	v_cvt_pk_fp8_f32 v68, v70, v71 op_sel:[0,0,1]
	v_mul_f32_e32 v70, v172, v80
	v_mul_f32_e32 v71, v172, v81
	v_cvt_pk_fp8_f32 v69, v70, v71 op_sel:[0,0,1]
	ds_read_b128 v[70:73], v173 offset:4224
	ds_read_b128 v[74:77], v173 offset:4240
	v_lshl_add_u64 v[78:79], s[38:39], 0, v[130:131]
	v_lshl_add_u64 v[80:81], v[78:79], 0, v[134:135]
	global_store_dwordx4 v[80:81], v[66:69], off nt
	s_waitcnt lgkmcnt(1)
	v_mul_f32_e32 v82, v172, v70
	v_mul_f32_e32 v71, v172, v71
	v_mov_b32_e32 v70, 0
	v_cvt_pk_fp8_f32 v70, v82, v71
	v_mul_f32_e32 v66, v172, v72
	v_mul_f32_e32 v67, v172, v73
	v_mov_b32_e32 v71, 0
	v_cvt_pk_fp8_f32 v70, v66, v67 op_sel:[0,0,1]
	s_waitcnt lgkmcnt(0)
	v_mul_f32_e32 v66, v172, v74
	v_mul_f32_e32 v67, v172, v75
	v_cvt_pk_fp8_f32 v71, v66, v67
	ds_read_b128 v[66:69], v173 offset:4256
	v_mul_f32_e32 v72, v172, v76
	v_mul_f32_e32 v73, v172, v77
	ds_read_b128 v[74:77], v173 offset:4272
	v_cvt_pk_fp8_f32 v71, v72, v73 op_sel:[0,0,1]
	s_waitcnt lgkmcnt(1)
	v_mul_f32_e32 v66, v172, v66
	v_mul_f32_e32 v67, v172, v67
	v_mov_b32_e32 v72, 0
	v_cvt_pk_fp8_f32 v72, v66, v67
	v_mul_f32_e32 v66, v172, v68
	v_mul_f32_e32 v67, v172, v69
	s_waitcnt lgkmcnt(0)
	v_mul_f32_e32 v68, v172, v74
	v_mul_f32_e32 v69, v172, v75
	v_mov_b32_e32 v73, 0
	v_cvt_pk_fp8_f32 v73, v68, v69
	v_cvt_pk_fp8_f32 v72, v66, v67 op_sel:[0,0,1]
	v_mul_f32_e32 v66, v172, v76
	v_mul_f32_e32 v67, v172, v77
	v_cvt_pk_fp8_f32 v73, v66, v67 op_sel:[0,0,1]
	ds_read_b128 v[66:69], v173 offset:8448
	ds_read_b128 v[74:77], v173 offset:8464
	v_lshl_add_u64 v[80:81], v[78:79], 0, v[136:137]
	global_store_dwordx4 v[80:81], v[70:73], off nt
	v_or_b32_e32 v132, 0x8000, v134
	s_waitcnt lgkmcnt(1)
	v_mul_f32_e32 v82, v172, v66
	v_mul_f32_e32 v67, v172, v67
	v_mov_b32_e32 v66, 0
	v_cvt_pk_fp8_f32 v66, v82, v67
	v_mul_f32_e32 v67, v172, v68
	v_mul_f32_e32 v68, v172, v69
	s_waitcnt lgkmcnt(0)
	v_mul_f32_e32 v69, v172, v75
	v_cvt_pk_fp8_f32 v66, v67, v68 op_sel:[0,0,1]
	v_mul_f32_e32 v68, v172, v74
	v_mov_b32_e32 v67, 0
	v_cvt_pk_fp8_f32 v67, v68, v69
	ds_read_b128 v[68:71], v173 offset:8480
	v_mul_f32_e32 v72, v172, v76
	v_mul_f32_e32 v73, v172, v77
	v_cvt_pk_fp8_f32 v67, v72, v73 op_sel:[0,0,1]
	ds_read_b128 v[72:75], v173 offset:8496
	s_waitcnt lgkmcnt(1)
	v_mul_f32_e32 v76, v172, v68
	v_mul_f32_e32 v69, v172, v69
	v_mov_b32_e32 v68, 0
	v_cvt_pk_fp8_f32 v68, v76, v69
	s_waitcnt lgkmcnt(0)
	v_mul_f32_e32 v72, v172, v72
	v_mul_f32_e32 v73, v172, v73
	v_mov_b32_e32 v69, 0
	v_cvt_pk_fp8_f32 v69, v72, v73
	v_mul_f32_e32 v70, v172, v70
	v_mul_f32_e32 v71, v172, v71
	v_cvt_pk_fp8_f32 v68, v70, v71 op_sel:[0,0,1]
	v_mul_f32_e32 v70, v172, v74
	v_mul_f32_e32 v71, v172, v75
	v_cvt_pk_fp8_f32 v69, v70, v71 op_sel:[0,0,1]
	ds_read_b128 v[70:73], v173 offset:12672
	ds_read_b128 v[74:77], v173 offset:12688
	v_mov_b32_e32 v133, v131
	v_lshl_add_u64 v[80:81], v[78:79], 0, v[132:133]
	global_store_dwordx4 v[80:81], v[66:69], off nt
	s_waitcnt lgkmcnt(1)
	v_mul_f32_e32 v82, v172, v70
	v_mul_f32_e32 v71, v172, v71
	v_mov_b32_e32 v70, 0
	v_cvt_pk_fp8_f32 v70, v82, v71
	v_mul_f32_e32 v66, v172, v72
	v_mul_f32_e32 v67, v172, v73
	v_mov_b32_e32 v71, 0
	v_cvt_pk_fp8_f32 v70, v66, v67 op_sel:[0,0,1]
	s_waitcnt lgkmcnt(0)
	v_mul_f32_e32 v66, v172, v74
	v_mul_f32_e32 v67, v172, v75
	v_cvt_pk_fp8_f32 v71, v66, v67
	ds_read_b128 v[66:69], v173 offset:12704
	v_mul_f32_e32 v72, v172, v76
	v_mul_f32_e32 v73, v172, v77
	ds_read_b128 v[74:77], v173 offset:12720
	v_cvt_pk_fp8_f32 v71, v72, v73 op_sel:[0,0,1]
	s_waitcnt lgkmcnt(1)
	v_mul_f32_e32 v66, v172, v66
	v_mul_f32_e32 v67, v172, v67
	v_mov_b32_e32 v72, 0
	v_cvt_pk_fp8_f32 v72, v66, v67
	v_mul_f32_e32 v66, v172, v68
	v_mul_f32_e32 v67, v172, v69
	s_waitcnt lgkmcnt(0)
	v_mul_f32_e32 v68, v172, v74
	v_mul_f32_e32 v69, v172, v75
	v_mov_b32_e32 v73, 0
	v_cvt_pk_fp8_f32 v73, v68, v69
	v_cvt_pk_fp8_f32 v72, v66, v67 op_sel:[0,0,1]
	v_mul_f32_e32 v66, v172, v76
	v_mul_f32_e32 v67, v172, v77
	v_cvt_pk_fp8_f32 v73, v66, v67 op_sel:[0,0,1]
	v_or_b32_e32 v138, 0xc000, v134
	v_mov_b32_e32 v139, v131
	v_lshl_add_u64 v[66:67], v[78:79], 0, v[138:139]
	global_store_dwordx4 v[66:67], v[70:73], off nt
	s_waitcnt lgkmcnt(0)
	global_load_dwordx4 v[114:117], v[142:143], off offset:2048 nt
	global_load_dwordx4 v[118:121], v[140:141], off offset:2048 nt
	global_load_dwordx4 v[122:125], v[144:145], off offset:2048 nt
	global_load_dwordx4 v[126:129], v[146:147], off offset:2048 nt
	global_load_dwordx4 v[98:101], v[148:149], off offset:2048 nt
	global_load_dwordx4 v[102:105], v[150:151], off offset:2048 nt
	global_load_dwordx4 v[106:109], v[152:153], off offset:2048 nt
	global_load_dwordx4 v[110:113], v[154:155], off offset:2048 nt
	global_load_dwordx4 v[82:85], v[156:157], off offset:2048 nt
	global_load_dwordx4 v[86:89], v[158:159], off offset:2048 nt
	global_load_dwordx4 v[90:93], v[160:161], off offset:2048 nt
	global_load_dwordx4 v[94:97], v[162:163], off offset:2048 nt
	global_load_dwordx4 v[66:69], v[164:165], off offset:2048 nt
	global_load_dwordx4 v[70:73], v[166:167], off offset:2048 nt
	global_load_dwordx4 v[74:77], v[168:169], off offset:2048 nt
	global_load_dwordx4 v[78:81], v[170:171], off offset:2048 nt
	s_waitcnt vmcnt(33)
	ds_write2_b32 v174, v50, v58 offset1:8
	s_waitcnt vmcnt(32)
	ds_write2_b32 v174, v54, v62 offset0:64 offset1:72
	ds_write2_b32 v174, v51, v59 offset0:132 offset1:140
	ds_write2_b32 v174, v55, v63 offset0:196 offset1:204
	ds_write2_b32 v175, v52, v60 offset0:8 offset1:16
	ds_write2_b32 v175, v56, v64 offset0:72 offset1:80
	ds_write2_b32 v175, v53, v61 offset0:140 offset1:148
	ds_write2_b32 v175, v57, v65 offset0:204 offset1:212
	s_waitcnt vmcnt(29)
	ds_write2_b32 v174, v34, v42 offset0:16 offset1:24
	s_waitcnt vmcnt(28)
	ds_write2_b32 v174, v38, v46 offset0:80 offset1:88
	ds_write2_b32 v174, v35, v43 offset0:148 offset1:156
	ds_write2_b32 v174, v39, v47 offset0:212 offset1:220
	ds_write2_b32 v175, v36, v44 offset0:24 offset1:32
	ds_write2_b32 v175, v40, v48 offset0:88 offset1:96
	ds_write2_b32 v175, v37, v45 offset0:156 offset1:164
	ds_write2_b32 v175, v41, v49 offset0:220 offset1:228
	s_waitcnt vmcnt(25)
	ds_write2_b32 v174, v18, v26 offset0:32 offset1:40
	s_waitcnt vmcnt(24)
	ds_write2_b32 v174, v22, v30 offset0:96 offset1:104
	ds_write2_b32 v174, v19, v27 offset0:164 offset1:172
	ds_write2_b32 v174, v23, v31 offset0:228 offset1:236
	ds_write2_b32 v175, v20, v28 offset0:40 offset1:48
	ds_write2_b32 v175, v24, v32 offset0:104 offset1:112
	ds_write2_b32 v175, v21, v29 offset0:172 offset1:180
	ds_write2_b32 v175, v25, v33 offset0:236 offset1:244
	s_waitcnt vmcnt(21)
	ds_write2_b32 v174, v2, v10 offset0:48 offset1:56
	s_waitcnt vmcnt(20)
	ds_write2_b32 v174, v6, v14 offset0:112 offset1:120
	ds_write2_b32 v174, v3, v11 offset0:180 offset1:188
	ds_write2_b32 v174, v7, v15 offset0:244 offset1:252
	ds_write2_b32 v175, v4, v12 offset0:56 offset1:64
	ds_write2_b32 v175, v8, v16 offset0:120 offset1:128
	ds_write2_b32 v175, v5, v13 offset0:188 offset1:196
	ds_write2_b32 v176, v9, v17 offset0:124 offset1:132
	s_waitcnt lgkmcnt(0)
	ds_read_b128 v[2:5], v173
	ds_read_b128 v[6:9], v173 offset:16
	ds_read_b128 v[10:13], v173 offset:32
	ds_read_b128 v[14:17], v173 offset:48
	s_andn2_b32 s11, s11, 63
	s_add_i32 s38, s11, 0x200
	s_waitcnt lgkmcnt(2)
	v_mul_f32_e32 v6, v172, v6
	v_mul_f32_e32 v18, v172, v2
	v_mul_f32_e32 v3, v172, v3
	v_mov_b32_e32 v2, 0
	v_cvt_pk_fp8_f32 v2, v18, v3
	v_mul_f32_e32 v7, v172, v7
	v_mov_b32_e32 v3, 0
	v_cvt_pk_fp8_f32 v3, v6, v7
	v_mul_f32_e32 v4, v172, v4
	v_mul_f32_e32 v5, v172, v5
	v_cvt_pk_fp8_f32 v2, v4, v5 op_sel:[0,0,1]
	v_mul_f32_e32 v4, v172, v8
	v_mul_f32_e32 v5, v172, v9
	v_cvt_pk_fp8_f32 v3, v4, v5 op_sel:[0,0,1]
	s_waitcnt lgkmcnt(1)
	v_mul_f32_e32 v5, v172, v10
	v_mul_f32_e32 v6, v172, v11
	v_mov_b32_e32 v4, 0
	v_cvt_pk_fp8_f32 v4, v5, v6
	s_waitcnt lgkmcnt(0)
	v_mul_f32_e32 v8, v172, v14
	v_mul_f32_e32 v9, v172, v15
	v_mov_b32_e32 v5, 0
	v_cvt_pk_fp8_f32 v5, v8, v9
	s_and_b32 s38, s38, 0xffffff00
	v_mul_f32_e32 v6, v172, v12
	v_mul_f32_e32 v7, v172, v13
	s_add_i32 s38, s38, s10
	v_cvt_pk_fp8_f32 v4, v6, v7 op_sel:[0,0,1]
	v_mul_f32_e32 v6, v172, v16
	v_mul_f32_e32 v7, v172, v17
	s_or_b32 s38, s38, s6
	v_cvt_pk_fp8_f32 v5, v6, v7 op_sel:[0,0,1]
	ds_read_b128 v[6:9], v173 offset:4224
	ds_read_b128 v[10:13], v173 offset:4240
	s_ashr_i32 s39, s38, 31
	s_lshl_b64 s[38:39], s[38:39], 11
	s_add_u32 s38, s9, s38
	s_addc_u32 s39, s7, s39
	s_add_u32 s38, s38, s8
	s_waitcnt lgkmcnt(1)
	v_mul_f32_e32 v18, v172, v6
	v_mul_f32_e32 v7, v172, v7
	v_mov_b32_e32 v6, 0
	s_addc_u32 s39, s39, 0
	v_cvt_pk_fp8_f32 v6, v18, v7
	v_lshl_add_u64 v[16:17], s[38:39], 0, v[130:131]
	v_lshl_add_u64 v[14:15], v[16:17], 0, v[134:135]
	global_store_dwordx4 v[14:15], v[2:5], off nt
	v_mov_b32_e32 v7, 0
	s_waitcnt lgkmcnt(0)
	v_mul_f32_e32 v14, v172, v13
	v_mul_f32_e32 v2, v172, v8
	v_mul_f32_e32 v3, v172, v9
	v_cvt_pk_fp8_f32 v6, v2, v3 op_sel:[0,0,1]
	ds_read_b128 v[2:5], v173 offset:4256
	v_mul_f32_e32 v8, v172, v10
	v_mul_f32_e32 v9, v172, v11
	v_cvt_pk_fp8_f32 v7, v8, v9
	v_mul_f32_e32 v9, v172, v12
	ds_read_b128 v[10:13], v173 offset:4272
	s_waitcnt lgkmcnt(1)
	v_mul_f32_e32 v2, v172, v2
	v_mul_f32_e32 v3, v172, v3
	v_mov_b32_e32 v8, 0
	v_cvt_pk_fp8_f32 v8, v2, v3
	v_mul_f32_e32 v2, v172, v4
	v_mul_f32_e32 v3, v172, v5
	v_cvt_pk_fp8_f32 v7, v9, v14 op_sel:[0,0,1]
	v_cvt_pk_fp8_f32 v8, v2, v3 op_sel:[0,0,1]
	s_waitcnt lgkmcnt(0)
	v_mul_f32_e32 v2, v172, v10
	v_mul_f32_e32 v3, v172, v11
	v_mov_b32_e32 v9, 0
	v_cvt_pk_fp8_f32 v9, v2, v3
	ds_read_b128 v[2:5], v173 offset:8448
	v_mul_f32_e32 v10, v172, v12
	v_mul_f32_e32 v11, v172, v13
	v_cvt_pk_fp8_f32 v9, v10, v11 op_sel:[0,0,1]
	ds_read_b128 v[10:13], v173 offset:8464
	s_waitcnt lgkmcnt(1)
	v_mul_f32_e32 v18, v172, v2
	v_mul_f32_e32 v3, v172, v3
	v_mov_b32_e32 v2, 0
	v_cvt_pk_fp8_f32 v2, v18, v3
	v_lshl_add_u64 v[14:15], v[16:17], 0, v[136:137]
	v_mul_f32_e32 v3, v172, v4
	v_mul_f32_e32 v4, v172, v5
	global_store_dwordx4 v[14:15], v[6:9], off nt
	v_cvt_pk_fp8_f32 v2, v3, v4 op_sel:[0,0,1]
	ds_read_b128 v[4:7], v173 offset:8480
	s_waitcnt lgkmcnt(1)
	v_mul_f32_e32 v8, v172, v10
	v_mul_f32_e32 v9, v172, v11
	v_mov_b32_e32 v3, 0
	v_cvt_pk_fp8_f32 v3, v8, v9
	ds_read_b128 v[8:11], v173 offset:8496
	s_waitcnt lgkmcnt(1)
	v_mul_f32_e32 v14, v172, v4
	v_mul_f32_e32 v5, v172, v5
	v_mov_b32_e32 v4, 0
	v_cvt_pk_fp8_f32 v4, v14, v5
	v_mul_f32_e32 v12, v172, v12
	v_mul_f32_e32 v13, v172, v13
	v_mul_f32_e32 v5, v172, v6
	v_mul_f32_e32 v6, v172, v7
	v_cvt_pk_fp8_f32 v3, v12, v13 op_sel:[0,0,1]
	v_cvt_pk_fp8_f32 v4, v5, v6 op_sel:[0,0,1]
	s_waitcnt lgkmcnt(0)
	v_mul_f32_e32 v12, v172, v8
	v_mul_f32_e32 v13, v172, v9
	ds_read_b128 v[6:9], v173 offset:12672
	v_mov_b32_e32 v5, 0
	v_cvt_pk_fp8_f32 v5, v12, v13
	v_mul_f32_e32 v14, v172, v10
	v_mul_f32_e32 v15, v172, v11
	ds_read_b128 v[10:13], v173 offset:12688
	s_waitcnt lgkmcnt(1)
	v_mul_f32_e32 v18, v172, v6
	v_mul_f32_e32 v7, v172, v7
	v_mov_b32_e32 v6, 0
	v_cvt_pk_fp8_f32 v6, v18, v7
	v_mul_f32_e32 v7, v172, v8
	v_mul_f32_e32 v8, v172, v9
	s_waitcnt lgkmcnt(0)
	v_mul_f32_e32 v9, v172, v11
	v_cvt_pk_fp8_f32 v6, v7, v8 op_sel:[0,0,1]
	v_mul_f32_e32 v8, v172, v10
	v_mov_b32_e32 v7, 0
	v_cvt_pk_fp8_f32 v7, v8, v9
	ds_read_b128 v[8:11], v173 offset:12704
	v_mul_f32_e32 v12, v172, v12
	v_mul_f32_e32 v13, v172, v13
	v_cvt_pk_fp8_f32 v5, v14, v15 op_sel:[0,0,1]
	v_cvt_pk_fp8_f32 v7, v12, v13 op_sel:[0,0,1]
	ds_read_b128 v[12:15], v173 offset:12720
	s_waitcnt lgkmcnt(1)
	v_mul_f32_e32 v18, v172, v8
	v_mul_f32_e32 v9, v172, v9
	v_mov_b32_e32 v8, 0
	v_cvt_pk_fp8_f32 v8, v18, v9
	s_waitcnt lgkmcnt(0)
	v_mul_f32_e32 v12, v172, v12
	v_mul_f32_e32 v13, v172, v13
	v_mov_b32_e32 v9, 0
	v_cvt_pk_fp8_f32 v9, v12, v13
	v_mul_f32_e32 v10, v172, v10
	v_mul_f32_e32 v11, v172, v11
	v_cvt_pk_fp8_f32 v8, v10, v11 op_sel:[0,0,1]
	v_mul_f32_e32 v10, v172, v14
	v_mul_f32_e32 v11, v172, v15
	v_cvt_pk_fp8_f32 v9, v10, v11 op_sel:[0,0,1]
	v_lshl_add_u64 v[10:11], v[16:17], 0, v[132:133]
	global_store_dwordx4 v[10:11], v[2:5], off nt
	s_add_i32 s38, s11, 0x400
	s_and_b32 s38, s38, 0xffffff00
	v_lshl_add_u64 v[2:3], v[16:17], 0, v[138:139]
	global_store_dwordx4 v[2:3], v[6:9], off nt
	s_waitcnt lgkmcnt(0)
	global_load_dwordx4 v[42:45], v[142:143], off offset:3072 nt
	global_load_dwordx4 v[46:49], v[140:141], off offset:3072 nt
	global_load_dwordx4 v[58:61], v[144:145], off offset:3072 nt
	global_load_dwordx4 v[62:65], v[146:147], off offset:3072 nt
	global_load_dwordx4 v[34:37], v[148:149], off offset:3072 nt
	global_load_dwordx4 v[38:41], v[150:151], off offset:3072 nt
	global_load_dwordx4 v[50:53], v[152:153], off offset:3072 nt
	global_load_dwordx4 v[54:57], v[154:155], off offset:3072 nt
	global_load_dwordx4 v[18:21], v[156:157], off offset:3072 nt
	global_load_dwordx4 v[22:25], v[158:159], off offset:3072 nt
	global_load_dwordx4 v[26:29], v[160:161], off offset:3072 nt
	global_load_dwordx4 v[30:33], v[162:163], off offset:3072 nt
	global_load_dwordx4 v[2:5], v[164:165], off offset:3072 nt
	global_load_dwordx4 v[6:9], v[166:167], off offset:3072 nt
	global_load_dwordx4 v[10:13], v[168:169], off offset:3072 nt
	global_load_dwordx4 v[14:17], v[170:171], off offset:3072 nt
	s_waitcnt vmcnt(33)
	ds_write2_b32 v174, v114, v122 offset1:8
	s_waitcnt vmcnt(32)
	ds_write2_b32 v174, v118, v126 offset0:64 offset1:72
	ds_write2_b32 v174, v115, v123 offset0:132 offset1:140
	ds_write2_b32 v174, v119, v127 offset0:196 offset1:204
	ds_write2_b32 v175, v116, v124 offset0:8 offset1:16
	ds_write2_b32 v175, v120, v128 offset0:72 offset1:80
	ds_write2_b32 v175, v117, v125 offset0:140 offset1:148
	ds_write2_b32 v175, v121, v129 offset0:204 offset1:212
	s_waitcnt vmcnt(29)
	ds_write2_b32 v174, v98, v106 offset0:16 offset1:24
	s_waitcnt vmcnt(28)
	ds_write2_b32 v174, v102, v110 offset0:80 offset1:88
	ds_write2_b32 v174, v99, v107 offset0:148 offset1:156
	ds_write2_b32 v174, v103, v111 offset0:212 offset1:220
	ds_write2_b32 v175, v100, v108 offset0:24 offset1:32
	ds_write2_b32 v175, v104, v112 offset0:88 offset1:96
	ds_write2_b32 v175, v101, v109 offset0:156 offset1:164
	ds_write2_b32 v175, v105, v113 offset0:220 offset1:228
	s_waitcnt vmcnt(25)
	ds_write2_b32 v174, v82, v90 offset0:32 offset1:40
	s_waitcnt vmcnt(24)
	ds_write2_b32 v174, v86, v94 offset0:96 offset1:104
	ds_write2_b32 v174, v83, v91 offset0:164 offset1:172
	ds_write2_b32 v174, v87, v95 offset0:228 offset1:236
	ds_write2_b32 v175, v84, v92 offset0:40 offset1:48
	ds_write2_b32 v175, v88, v96 offset0:104 offset1:112
	ds_write2_b32 v175, v85, v93 offset0:172 offset1:180
	ds_write2_b32 v175, v89, v97 offset0:236 offset1:244
	s_waitcnt vmcnt(21)
	ds_write2_b32 v174, v66, v74 offset0:48 offset1:56
	s_waitcnt vmcnt(20)
	ds_write2_b32 v174, v70, v78 offset0:112 offset1:120
	ds_write2_b32 v174, v67, v75 offset0:180 offset1:188
	ds_write2_b32 v174, v71, v79 offset0:244 offset1:252
	ds_write2_b32 v175, v68, v76 offset0:56 offset1:64
	ds_write2_b32 v175, v72, v80 offset0:120 offset1:128
	ds_write2_b32 v175, v69, v77 offset0:188 offset1:196
	ds_write2_b32 v176, v73, v81 offset0:124 offset1:132
	s_waitcnt lgkmcnt(0)
	ds_read_b128 v[66:69], v173
	ds_read_b128 v[70:73], v173 offset:16
	ds_read_b128 v[74:77], v173 offset:32
	ds_read_b128 v[78:81], v173 offset:48
	s_add_i32 s38, s38, s10
	s_or_b32 s38, s38, s6
	s_waitcnt lgkmcnt(2)
	v_mul_f32_e32 v70, v172, v70
	v_mul_f32_e32 v82, v172, v66
	v_mul_f32_e32 v67, v172, v67
	v_mov_b32_e32 v66, 0
	v_cvt_pk_fp8_f32 v66, v82, v67
	v_mul_f32_e32 v71, v172, v71
	v_mov_b32_e32 v67, 0
	v_cvt_pk_fp8_f32 v67, v70, v71
	v_mul_f32_e32 v68, v172, v68
	v_mul_f32_e32 v69, v172, v69
	v_cvt_pk_fp8_f32 v66, v68, v69 op_sel:[0,0,1]
	v_mul_f32_e32 v68, v172, v72
	v_mul_f32_e32 v69, v172, v73
	v_cvt_pk_fp8_f32 v67, v68, v69 op_sel:[0,0,1]
	s_waitcnt lgkmcnt(1)
	v_mul_f32_e32 v69, v172, v74
	v_mul_f32_e32 v70, v172, v75
	v_mov_b32_e32 v68, 0
	v_cvt_pk_fp8_f32 v68, v69, v70
	s_waitcnt lgkmcnt(0)
	v_mul_f32_e32 v72, v172, v78
	v_mul_f32_e32 v73, v172, v79
	v_mov_b32_e32 v69, 0
	v_cvt_pk_fp8_f32 v69, v72, v73
	v_mul_f32_e32 v70, v172, v76
	v_mul_f32_e32 v71, v172, v77
	v_cvt_pk_fp8_f32 v68, v70, v71 op_sel:[0,0,1]
	v_mul_f32_e32 v70, v172, v80
	v_mul_f32_e32 v71, v172, v81
	v_cvt_pk_fp8_f32 v69, v70, v71 op_sel:[0,0,1]
	ds_read_b128 v[70:73], v173 offset:4224
	ds_read_b128 v[74:77], v173 offset:4240
	s_ashr_i32 s39, s38, 31
	s_lshl_b64 s[38:39], s[38:39], 11
	s_add_u32 s38, s9, s38
	s_addc_u32 s39, s7, s39
	s_add_u32 s38, s38, s8
	s_waitcnt lgkmcnt(1)
	v_mul_f32_e32 v82, v172, v70
	v_mul_f32_e32 v71, v172, v71
	v_mov_b32_e32 v70, 0
	s_addc_u32 s39, s39, 0
	v_cvt_pk_fp8_f32 v70, v82, v71
	v_lshl_add_u64 v[80:81], s[38:39], 0, v[130:131]
	v_lshl_add_u64 v[78:79], v[80:81], 0, v[134:135]
	global_store_dwordx4 v[78:79], v[66:69], off nt
	v_mov_b32_e32 v71, 0
	s_waitcnt lgkmcnt(0)
	v_mul_f32_e32 v78, v172, v77
	v_mul_f32_e32 v66, v172, v72
	v_mul_f32_e32 v67, v172, v73
	v_cvt_pk_fp8_f32 v70, v66, v67 op_sel:[0,0,1]
	ds_read_b128 v[66:69], v173 offset:4256
	v_mul_f32_e32 v72, v172, v74
	v_mul_f32_e32 v73, v172, v75
	v_cvt_pk_fp8_f32 v71, v72, v73
	v_mul_f32_e32 v73, v172, v76
	ds_read_b128 v[74:77], v173 offset:4272
	s_waitcnt lgkmcnt(1)
	v_mul_f32_e32 v66, v172, v66
	v_mul_f32_e32 v67, v172, v67
	v_mov_b32_e32 v72, 0
	v_cvt_pk_fp8_f32 v72, v66, v67
	v_mul_f32_e32 v66, v172, v68
	v_mul_f32_e32 v67, v172, v69
	v_cvt_pk_fp8_f32 v71, v73, v78 op_sel:[0,0,1]
	v_cvt_pk_fp8_f32 v72, v66, v67 op_sel:[0,0,1]
	s_waitcnt lgkmcnt(0)
	v_mul_f32_e32 v66, v172, v74
	v_mul_f32_e32 v67, v172, v75
	v_mov_b32_e32 v73, 0
	v_cvt_pk_fp8_f32 v73, v66, v67
	ds_read_b128 v[66:69], v173 offset:8448
	v_mul_f32_e32 v74, v172, v76
	v_mul_f32_e32 v75, v172, v77
	v_cvt_pk_fp8_f32 v73, v74, v75 op_sel:[0,0,1]
	ds_read_b128 v[74:77], v173 offset:8464
	s_waitcnt lgkmcnt(1)
	v_mul_f32_e32 v82, v172, v66
	v_mul_f32_e32 v67, v172, v67
	v_mov_b32_e32 v66, 0
	v_cvt_pk_fp8_f32 v66, v82, v67
	v_lshl_add_u64 v[78:79], v[80:81], 0, v[136:137]
	v_mul_f32_e32 v67, v172, v68
	v_mul_f32_e32 v68, v172, v69
	global_store_dwordx4 v[78:79], v[70:73], off nt
	v_cvt_pk_fp8_f32 v66, v67, v68 op_sel:[0,0,1]
	ds_read_b128 v[68:71], v173 offset:8480
	s_waitcnt lgkmcnt(1)
	v_mul_f32_e32 v72, v172, v74
	v_mul_f32_e32 v73, v172, v75
	v_mov_b32_e32 v67, 0
	v_cvt_pk_fp8_f32 v67, v72, v73
	ds_read_b128 v[72:75], v173 offset:8496
	s_waitcnt lgkmcnt(1)
	v_mul_f32_e32 v78, v172, v68
	v_mul_f32_e32 v69, v172, v69
	v_mov_b32_e32 v68, 0
	v_cvt_pk_fp8_f32 v68, v78, v69
	v_mul_f32_e32 v76, v172, v76
	v_mul_f32_e32 v77, v172, v77
	v_mul_f32_e32 v69, v172, v70
	v_mul_f32_e32 v70, v172, v71
	v_cvt_pk_fp8_f32 v67, v76, v77 op_sel:[0,0,1]
	v_cvt_pk_fp8_f32 v68, v69, v70 op_sel:[0,0,1]
	s_waitcnt lgkmcnt(0)
	v_mul_f32_e32 v76, v172, v72
	v_mul_f32_e32 v77, v172, v73
	ds_read_b128 v[70:73], v173 offset:12672
	v_mov_b32_e32 v69, 0
	v_cvt_pk_fp8_f32 v69, v76, v77
	v_mul_f32_e32 v78, v172, v74
	v_mul_f32_e32 v79, v172, v75
	ds_read_b128 v[74:77], v173 offset:12688
	s_waitcnt lgkmcnt(1)
	v_mul_f32_e32 v82, v172, v70
	v_mul_f32_e32 v71, v172, v71
	v_mov_b32_e32 v70, 0
	v_cvt_pk_fp8_f32 v70, v82, v71
	v_mul_f32_e32 v71, v172, v72
	v_mul_f32_e32 v72, v172, v73
	s_waitcnt lgkmcnt(0)
	v_mul_f32_e32 v73, v172, v75
	v_cvt_pk_fp8_f32 v70, v71, v72 op_sel:[0,0,1]
	v_mul_f32_e32 v72, v172, v74
	v_mov_b32_e32 v71, 0
	v_cvt_pk_fp8_f32 v71, v72, v73
	ds_read_b128 v[72:75], v173 offset:12704
	v_mul_f32_e32 v76, v172, v76
	v_mul_f32_e32 v77, v172, v77
	v_cvt_pk_fp8_f32 v69, v78, v79 op_sel:[0,0,1]
	v_cvt_pk_fp8_f32 v71, v76, v77 op_sel:[0,0,1]
	ds_read_b128 v[76:79], v173 offset:12720
	s_waitcnt lgkmcnt(1)
	v_mul_f32_e32 v82, v172, v72
	v_mul_f32_e32 v73, v172, v73
	v_mov_b32_e32 v72, 0
	v_cvt_pk_fp8_f32 v72, v82, v73
	s_waitcnt lgkmcnt(0)
	v_mul_f32_e32 v76, v172, v76
	v_mul_f32_e32 v77, v172, v77
	v_mov_b32_e32 v73, 0
	v_cvt_pk_fp8_f32 v73, v76, v77
	v_mul_f32_e32 v74, v172, v74
	v_mul_f32_e32 v75, v172, v75
	v_cvt_pk_fp8_f32 v72, v74, v75 op_sel:[0,0,1]
	v_mul_f32_e32 v74, v172, v78
	v_mul_f32_e32 v75, v172, v79
	v_cvt_pk_fp8_f32 v73, v74, v75 op_sel:[0,0,1]
	v_lshl_add_u64 v[74:75], v[80:81], 0, v[132:133]
	global_store_dwordx4 v[74:75], v[66:69], off nt
	s_addk_i32 s11, 0x600
	s_and_b32 s11, s11, 0xffffff00
	v_lshl_add_u64 v[66:67], v[80:81], 0, v[138:139]
	global_store_dwordx4 v[66:67], v[70:73], off nt
	s_waitcnt lgkmcnt(0)
	s_waitcnt vmcnt(17)
	ds_write2_b32 v174, v42, v58 offset1:8
	s_waitcnt vmcnt(16)
	ds_write2_b32 v174, v46, v62 offset0:64 offset1:72
	ds_write2_b32 v174, v43, v59 offset0:132 offset1:140
	ds_write2_b32 v174, v47, v63 offset0:196 offset1:204
	ds_write2_b32 v175, v44, v60 offset0:8 offset1:16
	ds_write2_b32 v175, v48, v64 offset0:72 offset1:80
	ds_write2_b32 v175, v45, v61 offset0:140 offset1:148
	ds_write2_b32 v175, v49, v65 offset0:204 offset1:212
	s_waitcnt vmcnt(13)
	ds_write2_b32 v174, v34, v50 offset0:16 offset1:24
	s_waitcnt vmcnt(12)
	ds_write2_b32 v174, v38, v54 offset0:80 offset1:88
	ds_write2_b32 v174, v35, v51 offset0:148 offset1:156
	ds_write2_b32 v174, v39, v55 offset0:212 offset1:220
	ds_write2_b32 v175, v36, v52 offset0:24 offset1:32
	ds_write2_b32 v175, v40, v56 offset0:88 offset1:96
	ds_write2_b32 v175, v37, v53 offset0:156 offset1:164
	ds_write2_b32 v175, v41, v57 offset0:220 offset1:228
	s_waitcnt vmcnt(9)
	ds_write2_b32 v174, v18, v26 offset0:32 offset1:40
	s_waitcnt vmcnt(8)
	ds_write2_b32 v174, v22, v30 offset0:96 offset1:104
	ds_write2_b32 v174, v19, v27 offset0:164 offset1:172
	ds_write2_b32 v174, v23, v31 offset0:228 offset1:236
	ds_write2_b32 v175, v20, v28 offset0:40 offset1:48
	ds_write2_b32 v175, v24, v32 offset0:104 offset1:112
	ds_write2_b32 v175, v21, v29 offset0:172 offset1:180
	ds_write2_b32 v175, v25, v33 offset0:236 offset1:244
	s_waitcnt vmcnt(5)
	ds_write2_b32 v174, v2, v10 offset0:48 offset1:56
	s_waitcnt vmcnt(4)
	ds_write2_b32 v174, v6, v14 offset0:112 offset1:120
	ds_write2_b32 v174, v3, v11 offset0:180 offset1:188
	ds_write2_b32 v174, v7, v15 offset0:244 offset1:252
	ds_write2_b32 v175, v4, v12 offset0:56 offset1:64
	ds_write2_b32 v175, v8, v16 offset0:120 offset1:128
	ds_write2_b32 v175, v5, v13 offset0:188 offset1:196
	ds_write2_b32 v176, v9, v17 offset0:124 offset1:132
	s_waitcnt lgkmcnt(0)
	ds_read_b128 v[2:5], v173
	ds_read_b128 v[6:9], v173 offset:16
	ds_read_b128 v[10:13], v173 offset:32
	ds_read_b128 v[14:17], v173 offset:48
	s_add_i32 s11, s11, s10
	s_or_b32 s10, s11, s6
	s_waitcnt lgkmcnt(2)
	v_mul_f32_e32 v6, v172, v6
	v_mul_f32_e32 v18, v172, v2
	v_mul_f32_e32 v3, v172, v3
	v_mov_b32_e32 v2, 0
	v_cvt_pk_fp8_f32 v2, v18, v3
	v_mul_f32_e32 v7, v172, v7
	v_mov_b32_e32 v3, 0
	v_cvt_pk_fp8_f32 v3, v6, v7
	v_mul_f32_e32 v4, v172, v4
	v_mul_f32_e32 v5, v172, v5
	v_cvt_pk_fp8_f32 v2, v4, v5 op_sel:[0,0,1]
	v_mul_f32_e32 v4, v172, v8
	v_mul_f32_e32 v5, v172, v9
	v_cvt_pk_fp8_f32 v3, v4, v5 op_sel:[0,0,1]
	s_waitcnt lgkmcnt(1)
	v_mul_f32_e32 v5, v172, v10
	v_mul_f32_e32 v6, v172, v11
	v_mov_b32_e32 v4, 0
	v_cvt_pk_fp8_f32 v4, v5, v6
	s_waitcnt lgkmcnt(0)
	v_mul_f32_e32 v8, v172, v14
	v_mul_f32_e32 v9, v172, v15
	v_mov_b32_e32 v5, 0
	v_cvt_pk_fp8_f32 v5, v8, v9
	v_mul_f32_e32 v6, v172, v12
	v_mul_f32_e32 v7, v172, v13
	v_cvt_pk_fp8_f32 v4, v6, v7 op_sel:[0,0,1]
	v_mul_f32_e32 v6, v172, v16
	v_mul_f32_e32 v7, v172, v17
	v_cvt_pk_fp8_f32 v5, v6, v7 op_sel:[0,0,1]
	ds_read_b128 v[6:9], v173 offset:4224
	ds_read_b128 v[10:13], v173 offset:4240
	s_ashr_i32 s11, s10, 31
	s_lshl_b64 s[10:11], s[10:11], 11
	s_add_u32 s6, s9, s10
	s_addc_u32 s7, s7, s11
	s_add_u32 s6, s6, s8
	s_waitcnt lgkmcnt(1)
	v_mul_f32_e32 v18, v172, v6
	v_mul_f32_e32 v7, v172, v7
	v_mov_b32_e32 v6, 0
	s_addc_u32 s7, s7, 0
	v_cvt_pk_fp8_f32 v6, v18, v7
	v_lshl_add_u64 v[16:17], s[6:7], 0, v[130:131]
	v_lshl_add_u64 v[14:15], v[16:17], 0, v[134:135]
	global_store_dwordx4 v[14:15], v[2:5], off nt
	v_mov_b32_e32 v7, 0
	s_waitcnt lgkmcnt(0)
	v_mul_f32_e32 v14, v172, v13
	v_mul_f32_e32 v2, v172, v8
	v_mul_f32_e32 v3, v172, v9
	v_cvt_pk_fp8_f32 v6, v2, v3 op_sel:[0,0,1]
	ds_read_b128 v[2:5], v173 offset:4256
	v_mul_f32_e32 v8, v172, v10
	v_mul_f32_e32 v9, v172, v11
	v_cvt_pk_fp8_f32 v7, v8, v9
	v_mul_f32_e32 v9, v172, v12
	ds_read_b128 v[10:13], v173 offset:4272
	s_waitcnt lgkmcnt(1)
	v_mul_f32_e32 v2, v172, v2
	v_mul_f32_e32 v3, v172, v3
	v_mov_b32_e32 v8, 0
	v_cvt_pk_fp8_f32 v8, v2, v3
	v_mul_f32_e32 v2, v172, v4
	v_mul_f32_e32 v3, v172, v5
	v_cvt_pk_fp8_f32 v7, v9, v14 op_sel:[0,0,1]
	v_cvt_pk_fp8_f32 v8, v2, v3 op_sel:[0,0,1]
	s_waitcnt lgkmcnt(0)
	v_mul_f32_e32 v2, v172, v10
	v_mul_f32_e32 v3, v172, v11
	v_mov_b32_e32 v9, 0
	v_cvt_pk_fp8_f32 v9, v2, v3
	ds_read_b128 v[2:5], v173 offset:8448
	v_mul_f32_e32 v10, v172, v12
	v_mul_f32_e32 v11, v172, v13
	v_cvt_pk_fp8_f32 v9, v10, v11 op_sel:[0,0,1]
	ds_read_b128 v[10:13], v173 offset:8464
	s_waitcnt lgkmcnt(1)
	v_mul_f32_e32 v18, v172, v2
	v_mul_f32_e32 v3, v172, v3
	v_mov_b32_e32 v2, 0
	v_cvt_pk_fp8_f32 v2, v18, v3
	v_lshl_add_u64 v[14:15], v[16:17], 0, v[136:137]
	v_mul_f32_e32 v3, v172, v4
	v_mul_f32_e32 v4, v172, v5
	global_store_dwordx4 v[14:15], v[6:9], off nt
	v_cvt_pk_fp8_f32 v2, v3, v4 op_sel:[0,0,1]
	ds_read_b128 v[4:7], v173 offset:8480
	s_waitcnt lgkmcnt(1)
	v_mul_f32_e32 v8, v172, v10
	v_mul_f32_e32 v9, v172, v11
	v_mov_b32_e32 v3, 0
	v_cvt_pk_fp8_f32 v3, v8, v9
	ds_read_b128 v[8:11], v173 offset:8496
	s_waitcnt lgkmcnt(1)
	v_mul_f32_e32 v14, v172, v4
	v_mul_f32_e32 v5, v172, v5
	v_mov_b32_e32 v4, 0
	v_cvt_pk_fp8_f32 v4, v14, v5
	v_mul_f32_e32 v12, v172, v12
	v_mul_f32_e32 v13, v172, v13
	v_mul_f32_e32 v5, v172, v6
	v_mul_f32_e32 v6, v172, v7
	v_cvt_pk_fp8_f32 v3, v12, v13 op_sel:[0,0,1]
	v_cvt_pk_fp8_f32 v4, v5, v6 op_sel:[0,0,1]
	s_waitcnt lgkmcnt(0)
	v_mul_f32_e32 v12, v172, v8
	v_mul_f32_e32 v13, v172, v9
	ds_read_b128 v[6:9], v173 offset:12672
	v_mov_b32_e32 v5, 0
	v_cvt_pk_fp8_f32 v5, v12, v13
	v_mul_f32_e32 v14, v172, v10
	v_mul_f32_e32 v15, v172, v11
	ds_read_b128 v[10:13], v173 offset:12688
	s_waitcnt lgkmcnt(1)
	v_mul_f32_e32 v18, v172, v6
	v_mul_f32_e32 v7, v172, v7
	v_mov_b32_e32 v6, 0
	v_cvt_pk_fp8_f32 v6, v18, v7
	v_mul_f32_e32 v7, v172, v8
	v_mul_f32_e32 v8, v172, v9
	s_waitcnt lgkmcnt(0)
	v_mul_f32_e32 v9, v172, v11
	v_cvt_pk_fp8_f32 v6, v7, v8 op_sel:[0,0,1]
	v_mul_f32_e32 v8, v172, v10
	v_mov_b32_e32 v7, 0
	v_cvt_pk_fp8_f32 v7, v8, v9
	ds_read_b128 v[8:11], v173 offset:12704
	v_mul_f32_e32 v12, v172, v12
	v_mul_f32_e32 v13, v172, v13
	v_cvt_pk_fp8_f32 v5, v14, v15 op_sel:[0,0,1]
	v_cvt_pk_fp8_f32 v7, v12, v13 op_sel:[0,0,1]
	ds_read_b128 v[12:15], v173 offset:12720
	s_waitcnt lgkmcnt(1)
	v_mul_f32_e32 v18, v172, v8
	v_mul_f32_e32 v9, v172, v9
	v_mov_b32_e32 v8, 0
	v_cvt_pk_fp8_f32 v8, v18, v9
	s_waitcnt lgkmcnt(0)
	v_mul_f32_e32 v12, v172, v12
	v_mul_f32_e32 v13, v172, v13
	v_mov_b32_e32 v9, 0
	v_cvt_pk_fp8_f32 v9, v12, v13
	v_mul_f32_e32 v10, v172, v10
	v_mul_f32_e32 v11, v172, v11
	v_cvt_pk_fp8_f32 v8, v10, v11 op_sel:[0,0,1]
	v_mul_f32_e32 v10, v172, v14
	v_mul_f32_e32 v11, v172, v15
	v_cvt_pk_fp8_f32 v9, v10, v11 op_sel:[0,0,1]
	v_lshl_add_u64 v[10:11], v[16:17], 0, v[132:133]
	global_store_dwordx4 v[10:11], v[2:5], off nt
	s_nop 1
	v_lshl_add_u64 v[2:3], v[16:17], 0, v[138:139]
	global_store_dwordx4 v[2:3], v[6:9], off nt
	s_waitcnt lgkmcnt(0)
	s_barrier
	s_and_saveexec_b64 s[6:7], s[36:37]
	s_cbranch_execz .LBB0_800
	v_mov_b32_e32 v2, s12
	s_waitcnt vmcnt(0)
	ds_write_b32 v2, v255
	s_branch .LBB0_800

.LBB0_931:
	v_mov_b32_e32 v1, 0
	s_and_saveexec_b64 s[8:9], s[36:37]
	s_cbranch_execz .LBB0_935
	s_mov_b64 s[12:13], exec
	v_mbcnt_lo_u32_b32 v1, s12, 0
	v_mbcnt_hi_u32_b32 v1, s13, v1
	v_cmp_eq_u32_e32 vcc, 0, v1
	s_and_saveexec_b64 s[10:11], vcc
	s_cbranch_execz .LBB0_934
	s_bcnt1_i32_b64 s12, s[12:13]
	v_mov_b32_e32 v2, s12
	global_atomic_add v255, v131, v2, s[4:5] sc0
.LBB0_934:
	s_or_b64 exec, exec, s[10:11]
.LBB0_935:
	s_or_b64 exec, exec, s[8:9]
	s_add_i32 s28, s26, 0x180
	s_ashr_i32 s15, s28, 8
	s_bfe_u32 s12, s28, 0x40004
	s_cmp_eq_u32 s15, 2
	s_cselect_b64 s[8:9], -1, 0
	s_cmp_lg_u32 s15, 2
	s_cselect_b64 s[10:11], -1, 0
	v_mov_b32 v66, v0
	s_and_b64 vcc, exec, s[10:11]
	v_readfirstlane_b32 s29, v66
	v_mov_b32_e32 v172, 0
	s_cbranch_vccnz .LBB0_937
	s_lshl_b32 s13, s12, 2
	v_mov_b32_e32 v2, s13
	global_load_dword v2, v2, s[6:7] sc1
	s_waitcnt vmcnt(0)
	v_div_scale_f32 v3, s[30:31], v2, v2, s24
	v_rcp_f32_e32 v4, v3
	v_div_scale_f32 v5, vcc, s24, v2, s24
	v_fma_f32 v6, -v3, v4, 1.0
	v_fmac_f32_e32 v4, v6, v4
	v_mul_f32_e32 v6, v5, v4
	v_fma_f32 v7, -v3, v6, v5
	v_fmac_f32_e32 v6, v7, v4
	v_fma_f32 v3, -v3, v6, v5
	v_div_fmas_f32 v3, v3, v4, v6
	v_div_fixup_f32 v3, v3, v2, s24
	v_cmp_lt_f32_e32 vcc, 0, v2
	s_nop 1
	v_cndmask_b32_e32 v172, 0, v3, vcc

.LBB0_940:
	s_ashr_i32 s13, s29, 6
	s_cmp_eq_u32 s15, 1
	s_cselect_b32 s10, s25, 0xd8
	s_cmpk_gt_u32 s28, 0xff
	s_cselect_b32 s10, s10, 0xc8
	s_add_u32 s10, s0, s10
	s_addc_u32 s11, s1, 0
	s_lshl_b32 s28, s26, 5
	s_and_b32 s30, s28, 32
	s_and_b64 s[28:29], s[8:9], exec
	s_load_dwordx2 s[10:11], s[10:11], 0x0
	s_cselect_b32 s28, s30, 0
	s_and_b32 s30, s26, 14
	s_lshl_b32 s26, s26, 1
	s_add_i32 s31, s13, s28
	s_and_b32 s26, s26, 30
	s_and_b64 s[28:29], s[8:9], exec
	s_mulk_i32 s13, 0x4400
	s_cselect_b32 s26, s30, s26
	s_add_i32 s38, s13, 0
	s_lshl_b32 s30, s27, 11
	s_lshl_b32 s13, s27, 13
	s_waitcnt lgkmcnt(0)
	s_add_u32 s10, s10, s13
	s_addc_u32 s11, s11, 0
	s_lshl_b32 s26, s26, 6
	v_bfe_u32 v128, v66, 3, 3
	v_or_b32_e32 v130, s26, v128
	s_waitcnt vmcnt(0)
	v_lshlrev_b64 v[2:3], s12, v[130:131]
	v_lshlrev_b32_e32 v4, 4, v66
	v_lshl_add_u64 v[2:3], v[2:3], 2, s[10:11]
	v_and_b32_e32 v130, 0x70, v4
	s_lshl_b32 s10, s31, 5
	v_lshl_add_u64 v[2:3], v[2:3], 0, v[130:131]
	s_ashr_i32 s11, s10, 31
	v_lshl_add_u64 v[142:143], s[10:11], 2, v[2:3]
	s_lshl_b64 s[28:29], 64, s12
	v_lshl_add_u64 v[140:141], s[28:29], 2, v[142:143]
	s_lshl_b64 s[28:29], 8, s12
	v_lshl_add_u64 v[144:145], s[28:29], 2, v[142:143]
	s_lshl_b64 s[28:29], 0x48, s12
	v_lshl_add_u64 v[146:147], s[28:29], 2, v[142:143]
	s_lshl_b64 s[28:29], 16, s12
	v_lshl_add_u64 v[148:149], s[28:29], 2, v[142:143]
	s_lshl_b64 s[28:29], 0x50, s12
	v_lshl_add_u64 v[150:151], s[28:29], 2, v[142:143]
	s_lshl_b64 s[28:29], 24, s12
	v_lshl_add_u64 v[152:153], s[28:29], 2, v[142:143]
	s_lshl_b64 s[28:29], 0x58, s12
	v_lshl_add_u64 v[154:155], s[28:29], 2, v[142:143]
	s_lshl_b64 s[28:29], 32, s12
	v_lshl_add_u64 v[156:157], s[28:29], 2, v[142:143]
	s_lshl_b64 s[28:29], 0x60, s12
	v_lshl_add_u64 v[158:159], s[28:29], 2, v[142:143]
	s_lshl_b64 s[28:29], 40, s12
	v_lshl_add_u64 v[160:161], s[28:29], 2, v[142:143]
	s_lshl_b64 s[28:29], 0x68, s12
	v_lshl_add_u64 v[162:163], s[28:29], 2, v[142:143]
	s_lshl_b64 s[28:29], 48, s12
	v_lshl_add_u64 v[164:165], s[28:29], 2, v[142:143]
	s_lshl_b64 s[28:29], 0x70, s12
	v_lshl_add_u64 v[166:167], s[28:29], 2, v[142:143]
	s_lshl_b64 s[28:29], 56, s12
	s_lshl_b64 s[12:13], 0x78, s12
	v_lshl_add_u64 v[168:169], s[28:29], 2, v[142:143]
	v_lshl_add_u64 v[170:171], s[12:13], 2, v[142:143]
	global_load_dwordx4 v[68:71], v[142:143], off nt
	global_load_dwordx4 v[72:75], v[140:141], off nt
	global_load_dwordx4 v[76:79], v[144:145], off nt
	global_load_dwordx4 v[80:83], v[146:147], off nt
	global_load_dwordx4 v[116:119], v[164:165], off nt
	global_load_dwordx4 v[120:123], v[166:167], off nt
	global_load_dwordx4 v[124:127], v[168:169], off nt
	global_load_dwordx4 v[132:135], v[170:171], off nt
	global_load_dwordx4 v[84:87], v[148:149], off nt
	global_load_dwordx4 v[88:91], v[150:151], off nt
	global_load_dwordx4 v[92:95], v[152:153], off nt
	global_load_dwordx4 v[96:99], v[154:155], off nt
	global_load_dwordx4 v[100:103], v[156:157], off nt
	global_load_dwordx4 v[104:107], v[158:159], off nt
	global_load_dwordx4 v[108:111], v[160:161], off nt
	global_load_dwordx4 v[112:115], v[162:163], off nt
	v_and_b32_e32 v129, 7, v66
	v_mul_u32_u24_e32 v66, 0x840, v129
	v_lshlrev_b32_e32 v67, 2, v128
	v_add3_u32 v174, s38, v66, v67
	v_add_u32_e32 v175, 0x400, v174
	v_add_u32_e32 v176, 0x600, v174
	global_load_dwordx4 v[50:53], v[142:143], off offset:1024 nt
	global_load_dwordx4 v[54:57], v[140:141], off offset:1024 nt
	global_load_dwordx4 v[58:61], v[144:145], off offset:1024 nt
	global_load_dwordx4 v[62:65], v[146:147], off offset:1024 nt
	global_load_dwordx4 v[34:37], v[148:149], off offset:1024 nt
	global_load_dwordx4 v[38:41], v[150:151], off offset:1024 nt
	global_load_dwordx4 v[42:45], v[152:153], off offset:1024 nt
	global_load_dwordx4 v[46:49], v[154:155], off offset:1024 nt
	global_load_dwordx4 v[18:21], v[156:157], off offset:1024 nt
	global_load_dwordx4 v[22:25], v[158:159], off offset:1024 nt
	global_load_dwordx4 v[26:29], v[160:161], off offset:1024 nt
	global_load_dwordx4 v[30:33], v[162:163], off offset:1024 nt
	global_load_dwordx4 v[2:5], v[164:165], off offset:1024 nt
	global_load_dwordx4 v[6:9], v[166:167], off offset:1024 nt
	global_load_dwordx4 v[10:13], v[168:169], off offset:1024 nt
	global_load_dwordx4 v[14:17], v[170:171], off offset:1024 nt
	v_lshlrev_b32_e32 v66, 6, v129
	v_mul_u32_u24_e32 v67, 0x210, v128
	v_add3_u32 v173, s38, v66, v67
	s_add_i32 s12, s10, 0x100
	s_ashr_i32 s13, s12, 31
	s_add_u32 s29, s19, s30
	s_addc_u32 s30, s20, 0
	s_lshl_b64 s[34:35], s[10:11], 10
	s_add_u32 s11, s29, s34
	s_addc_u32 s39, s30, s35
	s_lshl_b32 s27, s27, 12
	s_add_u32 s28, s21, s27
	s_addc_u32 s27, s22, 0
	s_waitcnt vmcnt(29)
	ds_write2_b32 v174, v68, v76 offset1:8
	s_waitcnt vmcnt(28)
	ds_write2_b32 v174, v72, v80 offset0:64 offset1:72
	ds_write2_b32 v174, v69, v77 offset0:132 offset1:140
	ds_write2_b32 v174, v73, v81 offset0:196 offset1:204
	ds_write2_b32 v175, v70, v78 offset0:8 offset1:16
	ds_write2_b32 v175, v74, v82 offset0:72 offset1:80
	ds_write2_b32 v175, v71, v79 offset0:140 offset1:148
	ds_write2_b32 v175, v75, v83 offset0:204 offset1:212
	s_waitcnt vmcnt(21)
	ds_write2_b32 v174, v84, v92 offset0:16 offset1:24
	s_waitcnt vmcnt(20)
	ds_write2_b32 v174, v88, v96 offset0:80 offset1:88
	ds_write2_b32 v174, v85, v93 offset0:148 offset1:156
	ds_write2_b32 v174, v89, v97 offset0:212 offset1:220
	ds_write2_b32 v175, v86, v94 offset0:24 offset1:32
	ds_write2_b32 v175, v90, v98 offset0:88 offset1:96
	ds_write2_b32 v175, v87, v95 offset0:156 offset1:164
	ds_write2_b32 v175, v91, v99 offset0:220 offset1:228
	s_waitcnt vmcnt(17)
	ds_write2_b32 v174, v100, v108 offset0:32 offset1:40
	s_waitcnt vmcnt(16)
	ds_write2_b32 v174, v104, v112 offset0:96 offset1:104
	ds_write2_b32 v174, v101, v109 offset0:164 offset1:172
	ds_write2_b32 v174, v105, v113 offset0:228 offset1:236
	ds_write2_b32 v175, v102, v110 offset0:40 offset1:48
	ds_write2_b32 v175, v106, v114 offset0:104 offset1:112
	ds_write2_b32 v175, v103, v111 offset0:172 offset1:180
	ds_write2_b32 v175, v107, v115 offset0:236 offset1:244
	ds_write2_b32 v174, v116, v124 offset0:48 offset1:56
	ds_write2_b32 v174, v120, v132 offset0:112 offset1:120
	ds_write2_b32 v174, v117, v125 offset0:180 offset1:188
	ds_write2_b32 v174, v121, v133 offset0:244 offset1:252
	ds_write2_b32 v175, v118, v126 offset0:56 offset1:64
	ds_write2_b32 v175, v122, v134 offset0:120 offset1:128
	ds_write2_b32 v175, v119, v127 offset0:188 offset1:196
	ds_write2_b32 v176, v123, v135 offset0:124 offset1:132
	s_waitcnt lgkmcnt(0)
	ds_read_b128 v[66:69], v173
	ds_read_b128 v[70:73], v173 offset:16
	ds_read_b128 v[74:77], v173 offset:32
	ds_read_b128 v[78:81], v173 offset:48
	s_lshl_b32 s31, s31, 6
	s_and_b32 s33, s31, 0xffffff00
	s_waitcnt lgkmcnt(2)
	v_mul_f32_e32 v70, v172, v70
	v_mul_f32_e32 v82, v172, v66
	v_mul_f32_e32 v67, v172, v67
	v_mov_b32_e32 v66, 0
	v_cvt_pk_fp8_f32 v66, v82, v67
	v_mul_f32_e32 v71, v172, v71
	v_mov_b32_e32 v67, 0
	v_cvt_pk_fp8_f32 v67, v70, v71
	v_mul_f32_e32 v68, v172, v68
	v_mul_f32_e32 v69, v172, v69
	v_cvt_pk_fp8_f32 v66, v68, v69 op_sel:[0,0,1]
	v_mul_f32_e32 v68, v172, v72
	v_mul_f32_e32 v69, v172, v73
	v_cvt_pk_fp8_f32 v67, v68, v69 op_sel:[0,0,1]
	s_waitcnt lgkmcnt(1)
	v_mul_f32_e32 v69, v172, v74
	v_mul_f32_e32 v70, v172, v75
	v_mov_b32_e32 v68, 0
	v_cvt_pk_fp8_f32 v68, v69, v70
	s_waitcnt lgkmcnt(0)
	v_mul_f32_e32 v72, v172, v78
	v_mul_f32_e32 v73, v172, v79
	v_mov_b32_e32 v69, 0
	s_lshl_b32 s31, s15, 7
	v_cvt_pk_fp8_f32 v69, v72, v73
	s_add_i32 s15, s33, s31
	s_and_b32 s33, s10, 0x60
	s_or_b32 s34, s15, s33
	v_mul_f32_e32 v70, v172, v76
	v_mul_f32_e32 v71, v172, v77
	s_ashr_i32 s35, s34, 31
	v_cvt_pk_fp8_f32 v68, v70, v71 op_sel:[0,0,1]
	v_mul_f32_e32 v70, v172, v80
	v_mul_f32_e32 v71, v172, v81
	s_lshl_b64 s[34:35], s[34:35], 11
	v_cvt_pk_fp8_f32 v69, v70, v71 op_sel:[0,0,1]
	ds_read_b128 v[70:73], v173 offset:4224
	ds_read_b128 v[74:77], v173 offset:4240
	s_add_u32 s15, s28, s34
	s_addc_u32 s48, s27, s35
	s_and_b64 s[34:35], s[8:9], exec
	s_cselect_b32 s11, s11, s15
	s_cselect_b32 s35, s39, s48
	s_add_u32 s34, s11, s26
	s_waitcnt lgkmcnt(1)
	v_mul_f32_e32 v83, v172, v70
	v_mul_f32_e32 v71, v172, v71
	v_mov_b32_e32 v70, 0
	v_lshlrev_b32_e32 v130, 4, v129
	s_addc_u32 s35, s35, 0
	v_cvt_pk_fp8_f32 v70, v83, v71
	v_lshl_add_u64 v[78:79], s[34:35], 0, v[130:131]
	v_lshlrev_b32_e32 v136, s14, v128
	v_mov_b32_e32 v137, v131
	v_lshl_add_u64 v[80:81], v[78:79], 0, v[136:137]
	global_store_dwordx4 v[80:81], v[66:69], off nt
	v_mov_b32_e32 v71, 0
	v_or_b32_e32 v82, 8, v128
	v_mul_f32_e32 v66, v172, v72
	v_mul_f32_e32 v67, v172, v73
	v_cvt_pk_fp8_f32 v70, v66, v67 op_sel:[0,0,1]
	s_waitcnt lgkmcnt(0)
	v_mul_f32_e32 v66, v172, v74
	v_mul_f32_e32 v67, v172, v75
	v_cvt_pk_fp8_f32 v71, v66, v67
	ds_read_b128 v[66:69], v173 offset:4256
	v_mul_f32_e32 v72, v172, v76
	v_mul_f32_e32 v73, v172, v77
	ds_read_b128 v[74:77], v173 offset:4272
	v_cvt_pk_fp8_f32 v71, v72, v73 op_sel:[0,0,1]
	s_waitcnt lgkmcnt(1)
	v_mul_f32_e32 v66, v172, v66
	v_mul_f32_e32 v67, v172, v67
	v_mov_b32_e32 v72, 0
	v_cvt_pk_fp8_f32 v72, v66, v67
	v_mul_f32_e32 v66, v172, v68
	v_mul_f32_e32 v67, v172, v69
	s_waitcnt lgkmcnt(0)
	v_mul_f32_e32 v68, v172, v74
	v_mul_f32_e32 v69, v172, v75
	v_mov_b32_e32 v73, 0
	v_cvt_pk_fp8_f32 v73, v68, v69
	v_cvt_pk_fp8_f32 v72, v66, v67 op_sel:[0,0,1]
	v_mul_f32_e32 v66, v172, v76
	v_mul_f32_e32 v67, v172, v77
	v_cvt_pk_fp8_f32 v73, v66, v67 op_sel:[0,0,1]
	ds_read_b128 v[66:69], v173 offset:8448
	v_lshlrev_b32_e32 v134, s14, v82
	v_mov_b32_e32 v135, v131
	v_lshl_add_u64 v[74:75], v[78:79], 0, v[134:135]
	global_store_dwordx4 v[74:75], v[70:73], off nt
	ds_read_b128 v[70:73], v173 offset:8464
	s_waitcnt lgkmcnt(1)
	v_mul_f32_e32 v74, v172, v66
	v_mul_f32_e32 v67, v172, v67
	v_mov_b32_e32 v66, 0
	v_cvt_pk_fp8_f32 v66, v74, v67
	v_mul_f32_e32 v67, v172, v68
	v_mul_f32_e32 v68, v172, v69
	s_waitcnt lgkmcnt(0)
	v_mul_f32_e32 v69, v172, v71
	v_cvt_pk_fp8_f32 v66, v67, v68 op_sel:[0,0,1]
	v_mul_f32_e32 v68, v172, v70
	v_mov_b32_e32 v67, 0
	v_cvt_pk_fp8_f32 v67, v68, v69
	ds_read_b128 v[68:71], v173 offset:8480
	v_mul_f32_e32 v72, v172, v72
	v_mul_f32_e32 v73, v172, v73
	v_cvt_pk_fp8_f32 v67, v72, v73 op_sel:[0,0,1]
	ds_read_b128 v[72:75], v173 offset:8496
	s_waitcnt lgkmcnt(1)
	v_mul_f32_e32 v77, v172, v68
	v_mul_f32_e32 v69, v172, v69
	v_mov_b32_e32 v68, 0
	v_cvt_pk_fp8_f32 v68, v77, v69
	s_waitcnt lgkmcnt(0)
	v_mul_f32_e32 v72, v172, v72
	v_mul_f32_e32 v73, v172, v73
	v_mov_b32_e32 v69, 0
	v_cvt_pk_fp8_f32 v69, v72, v73
	v_mul_f32_e32 v70, v172, v70
	v_mul_f32_e32 v71, v172, v71
	v_cvt_pk_fp8_f32 v68, v70, v71 op_sel:[0,0,1]
	v_mul_f32_e32 v70, v172, v74
	v_mul_f32_e32 v71, v172, v75
	v_cvt_pk_fp8_f32 v69, v70, v71 op_sel:[0,0,1]
	ds_read_b128 v[70:73], v173 offset:12672
	v_or_b32_e32 v76, 16, v128
	v_lshlrev_b32_e32 v132, s14, v76
	v_mov_b32_e32 v133, v131
	v_lshl_add_u64 v[74:75], v[78:79], 0, v[132:133]
	global_store_dwordx4 v[74:75], v[66:69], off nt
	ds_read_b128 v[66:69], v173 offset:12688
	s_waitcnt lgkmcnt(1)
	v_mul_f32_e32 v74, v172, v70
	v_mul_f32_e32 v71, v172, v71
	v_mov_b32_e32 v70, 0
	v_cvt_pk_fp8_f32 v70, v74, v71
	v_mul_f32_e32 v71, v172, v72
	v_mul_f32_e32 v72, v172, v73
	s_waitcnt lgkmcnt(0)
	v_mul_f32_e32 v66, v172, v66
	v_cvt_pk_fp8_f32 v70, v71, v72 op_sel:[0,0,1]
	v_mul_f32_e32 v67, v172, v67
	v_mov_b32_e32 v71, 0
	v_cvt_pk_fp8_f32 v71, v66, v67
	ds_read_b128 v[72:75], v173 offset:12704
	v_mul_f32_e32 v66, v172, v68
	v_mul_f32_e32 v67, v172, v69
	v_cvt_pk_fp8_f32 v71, v66, v67 op_sel:[0,0,1]
	ds_read_b128 v[66:69], v173 offset:12720
	s_waitcnt lgkmcnt(1)
	v_mul_f32_e32 v77, v172, v72
	v_mul_f32_e32 v73, v172, v73
	v_mov_b32_e32 v72, 0
	v_cvt_pk_fp8_f32 v72, v77, v73
	s_waitcnt lgkmcnt(0)
	v_mul_f32_e32 v66, v172, v66
	v_mul_f32_e32 v67, v172, v67
	v_mov_b32_e32 v73, 0
	v_cvt_pk_fp8_f32 v73, v66, v67
	v_mul_f32_e32 v74, v172, v74
	v_mul_f32_e32 v75, v172, v75
	v_mul_f32_e32 v66, v172, v68
	v_mul_f32_e32 v67, v172, v69
	v_cvt_pk_fp8_f32 v72, v74, v75 op_sel:[0,0,1]
	v_cvt_pk_fp8_f32 v73, v66, v67 op_sel:[0,0,1]
	v_or_b32_e32 v76, 24, v128
	v_lshlrev_b32_e32 v138, s14, v76
	v_mov_b32_e32 v139, v131
	v_lshl_add_u64 v[66:67], v[78:79], 0, v[138:139]
	global_store_dwordx4 v[66:67], v[70:73], off nt
	s_waitcnt lgkmcnt(0)
	global_load_dwordx4 v[114:117], v[142:143], off offset:2048 nt
	global_load_dwordx4 v[118:121], v[140:141], off offset:2048 nt
	global_load_dwordx4 v[122:125], v[144:145], off offset:2048 nt
	global_load_dwordx4 v[126:129], v[146:147], off offset:2048 nt
	global_load_dwordx4 v[98:101], v[148:149], off offset:2048 nt
	global_load_dwordx4 v[102:105], v[150:151], off offset:2048 nt
	global_load_dwordx4 v[106:109], v[152:153], off offset:2048 nt
	global_load_dwordx4 v[110:113], v[154:155], off offset:2048 nt
	global_load_dwordx4 v[82:85], v[156:157], off offset:2048 nt
	global_load_dwordx4 v[86:89], v[158:159], off offset:2048 nt
	global_load_dwordx4 v[90:93], v[160:161], off offset:2048 nt
	global_load_dwordx4 v[94:97], v[162:163], off offset:2048 nt
	global_load_dwordx4 v[66:69], v[164:165], off offset:2048 nt
	global_load_dwordx4 v[70:73], v[166:167], off offset:2048 nt
	global_load_dwordx4 v[74:77], v[168:169], off offset:2048 nt
	global_load_dwordx4 v[78:81], v[170:171], off offset:2048 nt
	s_waitcnt vmcnt(33)
	ds_write2_b32 v174, v50, v58 offset1:8
	s_waitcnt vmcnt(32)
	ds_write2_b32 v174, v54, v62 offset0:64 offset1:72
	ds_write2_b32 v174, v51, v59 offset0:132 offset1:140
	ds_write2_b32 v174, v55, v63 offset0:196 offset1:204
	ds_write2_b32 v175, v52, v60 offset0:8 offset1:16
	ds_write2_b32 v175, v56, v64 offset0:72 offset1:80
	ds_write2_b32 v175, v53, v61 offset0:140 offset1:148
	ds_write2_b32 v175, v57, v65 offset0:204 offset1:212
	s_waitcnt vmcnt(29)
	ds_write2_b32 v174, v34, v42 offset0:16 offset1:24
	s_waitcnt vmcnt(28)
	ds_write2_b32 v174, v38, v46 offset0:80 offset1:88
	ds_write2_b32 v174, v35, v43 offset0:148 offset1:156
	ds_write2_b32 v174, v39, v47 offset0:212 offset1:220
	ds_write2_b32 v175, v36, v44 offset0:24 offset1:32
	ds_write2_b32 v175, v40, v48 offset0:88 offset1:96
	ds_write2_b32 v175, v37, v45 offset0:156 offset1:164
	ds_write2_b32 v175, v41, v49 offset0:220 offset1:228
	s_waitcnt vmcnt(25)
	ds_write2_b32 v174, v18, v26 offset0:32 offset1:40
	s_waitcnt vmcnt(24)
	ds_write2_b32 v174, v22, v30 offset0:96 offset1:104
	ds_write2_b32 v174, v19, v27 offset0:164 offset1:172
	ds_write2_b32 v174, v23, v31 offset0:228 offset1:236
	ds_write2_b32 v175, v20, v28 offset0:40 offset1:48
	ds_write2_b32 v175, v24, v32 offset0:104 offset1:112
	ds_write2_b32 v175, v21, v29 offset0:172 offset1:180
	ds_write2_b32 v175, v25, v33 offset0:236 offset1:244
	s_waitcnt vmcnt(21)
	ds_write2_b32 v174, v2, v10 offset0:48 offset1:56
	s_waitcnt vmcnt(20)
	ds_write2_b32 v174, v6, v14 offset0:112 offset1:120
	ds_write2_b32 v174, v3, v11 offset0:180 offset1:188
	ds_write2_b32 v174, v7, v15 offset0:244 offset1:252
	ds_write2_b32 v175, v4, v12 offset0:56 offset1:64
	ds_write2_b32 v175, v8, v16 offset0:120 offset1:128
	ds_write2_b32 v175, v5, v13 offset0:188 offset1:196
	ds_write2_b32 v176, v9, v17 offset0:124 offset1:132
	s_waitcnt lgkmcnt(0)
	ds_read_b128 v[2:5], v173
	ds_read_b128 v[6:9], v173 offset:16
	ds_read_b128 v[10:13], v173 offset:32
	ds_read_b128 v[14:17], v173 offset:48
	s_add_i32 s14, s10, 0x200
	s_ashr_i32 s15, s14, 31
	s_waitcnt lgkmcnt(2)
	v_mul_f32_e32 v6, v172, v6
	v_mul_f32_e32 v18, v172, v2
	v_mul_f32_e32 v3, v172, v3
	v_mov_b32_e32 v2, 0
	v_cvt_pk_fp8_f32 v2, v18, v3
	v_mul_f32_e32 v7, v172, v7
	v_mov_b32_e32 v3, 0
	v_cvt_pk_fp8_f32 v3, v6, v7
	v_mul_f32_e32 v4, v172, v4
	v_mul_f32_e32 v5, v172, v5
	s_lshl_b64 s[34:35], s[12:13], 10
	v_cvt_pk_fp8_f32 v2, v4, v5 op_sel:[0,0,1]
	v_mul_f32_e32 v4, v172, v8
	v_mul_f32_e32 v5, v172, v9
	s_add_u32 s11, s29, s34
	v_cvt_pk_fp8_f32 v3, v4, v5 op_sel:[0,0,1]
	s_waitcnt lgkmcnt(1)
	v_mul_f32_e32 v5, v172, v10
	v_mul_f32_e32 v6, v172, v11
	v_mov_b32_e32 v4, 0
	s_addc_u32 s34, s30, s35
	s_lshl_b32 s12, s12, 1
	v_cvt_pk_fp8_f32 v4, v5, v6
	s_waitcnt lgkmcnt(0)
	v_mul_f32_e32 v8, v172, v14
	v_mul_f32_e32 v9, v172, v15
	v_mov_b32_e32 v5, 0
	s_and_b32 s12, s12, 0xffffff00
	v_cvt_pk_fp8_f32 v5, v8, v9
	s_add_i32 s12, s12, s31
	s_or_b32 s12, s12, s33
	v_mul_f32_e32 v6, v172, v12
	v_mul_f32_e32 v7, v172, v13
	s_ashr_i32 s13, s12, 31
	v_cvt_pk_fp8_f32 v4, v6, v7 op_sel:[0,0,1]
	v_mul_f32_e32 v6, v172, v16
	v_mul_f32_e32 v7, v172, v17
	s_lshl_b64 s[12:13], s[12:13], 11
	v_cvt_pk_fp8_f32 v5, v6, v7 op_sel:[0,0,1]
	ds_read_b128 v[6:9], v173 offset:4224
	ds_read_b128 v[10:13], v173 offset:4240
	s_add_u32 s35, s28, s12
	s_addc_u32 s38, s27, s13
	s_and_b64 s[12:13], s[8:9], exec
	s_cselect_b32 s11, s11, s35
	s_cselect_b32 s13, s34, s38
	s_add_u32 s12, s11, s26
	s_waitcnt lgkmcnt(1)
	v_mul_f32_e32 v18, v172, v6
	v_mul_f32_e32 v7, v172, v7
	v_mov_b32_e32 v6, 0
	s_addc_u32 s13, s13, 0
	v_cvt_pk_fp8_f32 v6, v18, v7
	v_lshl_add_u64 v[16:17], s[12:13], 0, v[130:131]
	v_lshl_add_u64 v[14:15], v[16:17], 0, v[136:137]
	global_store_dwordx4 v[14:15], v[2:5], off nt
	v_mov_b32_e32 v7, 0
	s_waitcnt lgkmcnt(0)
	v_mul_f32_e32 v14, v172, v13
	v_mul_f32_e32 v2, v172, v8
	v_mul_f32_e32 v3, v172, v9
	v_cvt_pk_fp8_f32 v6, v2, v3 op_sel:[0,0,1]
	ds_read_b128 v[2:5], v173 offset:4256
	v_mul_f32_e32 v8, v172, v10
	v_mul_f32_e32 v9, v172, v11
	v_cvt_pk_fp8_f32 v7, v8, v9
	v_mul_f32_e32 v9, v172, v12
	ds_read_b128 v[10:13], v173 offset:4272
	s_waitcnt lgkmcnt(1)
	v_mul_f32_e32 v2, v172, v2
	v_mul_f32_e32 v3, v172, v3
	v_mov_b32_e32 v8, 0
	v_cvt_pk_fp8_f32 v8, v2, v3
	v_mul_f32_e32 v2, v172, v4
	v_mul_f32_e32 v3, v172, v5
	v_cvt_pk_fp8_f32 v7, v9, v14 op_sel:[0,0,1]
	v_cvt_pk_fp8_f32 v8, v2, v3 op_sel:[0,0,1]
	s_waitcnt lgkmcnt(0)
	v_mul_f32_e32 v2, v172, v10
	v_mul_f32_e32 v3, v172, v11
	v_mov_b32_e32 v9, 0
	v_cvt_pk_fp8_f32 v9, v2, v3
	ds_read_b128 v[2:5], v173 offset:8448
	v_mul_f32_e32 v10, v172, v12
	v_mul_f32_e32 v11, v172, v13
	v_cvt_pk_fp8_f32 v9, v10, v11 op_sel:[0,0,1]
	ds_read_b128 v[10:13], v173 offset:8464
	s_waitcnt lgkmcnt(1)
	v_mul_f32_e32 v18, v172, v2
	v_mul_f32_e32 v3, v172, v3
	v_mov_b32_e32 v2, 0
	v_cvt_pk_fp8_f32 v2, v18, v3
	v_lshl_add_u64 v[14:15], v[16:17], 0, v[134:135]
	v_mul_f32_e32 v3, v172, v4
	v_mul_f32_e32 v4, v172, v5
	global_store_dwordx4 v[14:15], v[6:9], off nt
	v_cvt_pk_fp8_f32 v2, v3, v4 op_sel:[0,0,1]
	ds_read_b128 v[4:7], v173 offset:8480
	s_waitcnt lgkmcnt(1)
	v_mul_f32_e32 v8, v172, v10
	v_mul_f32_e32 v9, v172, v11
	v_mov_b32_e32 v3, 0
	v_cvt_pk_fp8_f32 v3, v8, v9
	ds_read_b128 v[8:11], v173 offset:8496
	s_waitcnt lgkmcnt(1)
	v_mul_f32_e32 v14, v172, v4
	v_mul_f32_e32 v5, v172, v5
	v_mov_b32_e32 v4, 0
	v_cvt_pk_fp8_f32 v4, v14, v5
	v_mul_f32_e32 v12, v172, v12
	v_mul_f32_e32 v13, v172, v13
	v_mul_f32_e32 v5, v172, v6
	v_mul_f32_e32 v6, v172, v7
	v_cvt_pk_fp8_f32 v3, v12, v13 op_sel:[0,0,1]
	v_cvt_pk_fp8_f32 v4, v5, v6 op_sel:[0,0,1]
	s_waitcnt lgkmcnt(0)
	v_mul_f32_e32 v12, v172, v8
	v_mul_f32_e32 v13, v172, v9
	ds_read_b128 v[6:9], v173 offset:12672
	v_mov_b32_e32 v5, 0
	v_cvt_pk_fp8_f32 v5, v12, v13
	v_mul_f32_e32 v14, v172, v10
	v_mul_f32_e32 v15, v172, v11
	ds_read_b128 v[10:13], v173 offset:12688
	s_waitcnt lgkmcnt(1)
	v_mul_f32_e32 v18, v172, v6
	v_mul_f32_e32 v7, v172, v7
	v_mov_b32_e32 v6, 0
	v_cvt_pk_fp8_f32 v6, v18, v7
	v_mul_f32_e32 v7, v172, v8
	v_mul_f32_e32 v8, v172, v9
	s_waitcnt lgkmcnt(0)
	v_mul_f32_e32 v9, v172, v11
	v_cvt_pk_fp8_f32 v6, v7, v8 op_sel:[0,0,1]
	v_mul_f32_e32 v8, v172, v10
	v_mov_b32_e32 v7, 0
	v_cvt_pk_fp8_f32 v7, v8, v9
	ds_read_b128 v[8:11], v173 offset:12704
	v_mul_f32_e32 v12, v172, v12
	v_mul_f32_e32 v13, v172, v13
	v_cvt_pk_fp8_f32 v5, v14, v15 op_sel:[0,0,1]
	v_cvt_pk_fp8_f32 v7, v12, v13 op_sel:[0,0,1]
	ds_read_b128 v[12:15], v173 offset:12720
	s_waitcnt lgkmcnt(1)
	v_mul_f32_e32 v18, v172, v8
	v_mul_f32_e32 v9, v172, v9
	v_mov_b32_e32 v8, 0
	v_cvt_pk_fp8_f32 v8, v18, v9
	s_waitcnt lgkmcnt(0)
	v_mul_f32_e32 v12, v172, v12
	v_mul_f32_e32 v13, v172, v13
	v_mov_b32_e32 v9, 0
	v_cvt_pk_fp8_f32 v9, v12, v13
	v_mul_f32_e32 v10, v172, v10
	v_mul_f32_e32 v11, v172, v11
	v_cvt_pk_fp8_f32 v8, v10, v11 op_sel:[0,0,1]
	v_mul_f32_e32 v10, v172, v14
	v_mul_f32_e32 v11, v172, v15
	v_cvt_pk_fp8_f32 v9, v10, v11 op_sel:[0,0,1]
	v_lshl_add_u64 v[10:11], v[16:17], 0, v[132:133]
	global_store_dwordx4 v[10:11], v[2:5], off nt
	s_addk_i32 s10, 0x300
	s_ashr_i32 s11, s10, 31
	v_lshl_add_u64 v[2:3], v[16:17], 0, v[138:139]
	global_store_dwordx4 v[2:3], v[6:9], off nt
	s_waitcnt lgkmcnt(0)
	global_load_dwordx4 v[42:45], v[142:143], off offset:3072 nt
	global_load_dwordx4 v[46:49], v[140:141], off offset:3072 nt
	global_load_dwordx4 v[58:61], v[144:145], off offset:3072 nt
	global_load_dwordx4 v[62:65], v[146:147], off offset:3072 nt
	global_load_dwordx4 v[34:37], v[148:149], off offset:3072 nt
	global_load_dwordx4 v[38:41], v[150:151], off offset:3072 nt
	global_load_dwordx4 v[50:53], v[152:153], off offset:3072 nt
	global_load_dwordx4 v[54:57], v[154:155], off offset:3072 nt
	global_load_dwordx4 v[18:21], v[156:157], off offset:3072 nt
	global_load_dwordx4 v[22:25], v[158:159], off offset:3072 nt
	global_load_dwordx4 v[26:29], v[160:161], off offset:3072 nt
	global_load_dwordx4 v[30:33], v[162:163], off offset:3072 nt
	global_load_dwordx4 v[2:5], v[164:165], off offset:3072 nt
	global_load_dwordx4 v[6:9], v[166:167], off offset:3072 nt
	global_load_dwordx4 v[10:13], v[168:169], off offset:3072 nt
	global_load_dwordx4 v[14:17], v[170:171], off offset:3072 nt
	s_waitcnt vmcnt(33)
	ds_write2_b32 v174, v114, v122 offset1:8
	s_waitcnt vmcnt(32)
	ds_write2_b32 v174, v118, v126 offset0:64 offset1:72
	ds_write2_b32 v174, v115, v123 offset0:132 offset1:140
	ds_write2_b32 v174, v119, v127 offset0:196 offset1:204
	ds_write2_b32 v175, v116, v124 offset0:8 offset1:16
	ds_write2_b32 v175, v120, v128 offset0:72 offset1:80
	ds_write2_b32 v175, v117, v125 offset0:140 offset1:148
	ds_write2_b32 v175, v121, v129 offset0:204 offset1:212
	s_waitcnt vmcnt(29)
	ds_write2_b32 v174, v98, v106 offset0:16 offset1:24
	s_waitcnt vmcnt(28)
	ds_write2_b32 v174, v102, v110 offset0:80 offset1:88
	ds_write2_b32 v174, v99, v107 offset0:148 offset1:156
	ds_write2_b32 v174, v103, v111 offset0:212 offset1:220
	ds_write2_b32 v175, v100, v108 offset0:24 offset1:32
	ds_write2_b32 v175, v104, v112 offset0:88 offset1:96
	ds_write2_b32 v175, v101, v109 offset0:156 offset1:164
	ds_write2_b32 v175, v105, v113 offset0:220 offset1:228
	s_waitcnt vmcnt(25)
	ds_write2_b32 v174, v82, v90 offset0:32 offset1:40
	s_waitcnt vmcnt(24)
	ds_write2_b32 v174, v86, v94 offset0:96 offset1:104
	ds_write2_b32 v174, v83, v91 offset0:164 offset1:172
	ds_write2_b32 v174, v87, v95 offset0:228 offset1:236
	ds_write2_b32 v175, v84, v92 offset0:40 offset1:48
	ds_write2_b32 v175, v88, v96 offset0:104 offset1:112
	ds_write2_b32 v175, v85, v93 offset0:172 offset1:180
	ds_write2_b32 v175, v89, v97 offset0:236 offset1:244
	s_waitcnt vmcnt(21)
	ds_write2_b32 v174, v66, v74 offset0:48 offset1:56
	s_waitcnt vmcnt(20)
	ds_write2_b32 v174, v70, v78 offset0:112 offset1:120
	ds_write2_b32 v174, v67, v75 offset0:180 offset1:188
	ds_write2_b32 v174, v71, v79 offset0:244 offset1:252
	ds_write2_b32 v175, v68, v76 offset0:56 offset1:64
	ds_write2_b32 v175, v72, v80 offset0:120 offset1:128
	ds_write2_b32 v175, v69, v77 offset0:188 offset1:196
	ds_write2_b32 v176, v73, v81 offset0:124 offset1:132
	s_waitcnt lgkmcnt(0)
	ds_read_b128 v[66:69], v173
	ds_read_b128 v[70:73], v173 offset:16
	ds_read_b128 v[74:77], v173 offset:32
	ds_read_b128 v[78:81], v173 offset:48
	s_lshl_b64 s[12:13], s[14:15], 10
	s_add_u32 s15, s29, s12
	s_waitcnt lgkmcnt(2)
	v_mul_f32_e32 v70, v172, v70
	v_mul_f32_e32 v82, v172, v66
	v_mul_f32_e32 v67, v172, v67
	v_mov_b32_e32 v66, 0
	v_cvt_pk_fp8_f32 v66, v82, v67
	v_mul_f32_e32 v71, v172, v71
	v_mov_b32_e32 v67, 0
	v_cvt_pk_fp8_f32 v67, v70, v71
	v_mul_f32_e32 v68, v172, v68
	v_mul_f32_e32 v69, v172, v69
	v_cvt_pk_fp8_f32 v66, v68, v69 op_sel:[0,0,1]
	v_mul_f32_e32 v68, v172, v72
	v_mul_f32_e32 v69, v172, v73
	v_cvt_pk_fp8_f32 v67, v68, v69 op_sel:[0,0,1]
	s_waitcnt lgkmcnt(1)
	v_mul_f32_e32 v69, v172, v74
	v_mul_f32_e32 v70, v172, v75
	v_mov_b32_e32 v68, 0
	s_addc_u32 s34, s30, s13
	s_lshl_b32 s12, s14, 1
	v_cvt_pk_fp8_f32 v68, v69, v70
	s_waitcnt lgkmcnt(0)
	v_mul_f32_e32 v72, v172, v78
	v_mul_f32_e32 v73, v172, v79
	v_mov_b32_e32 v69, 0
	s_and_b32 s12, s12, 0xffffff00
	v_cvt_pk_fp8_f32 v69, v72, v73
	s_add_i32 s12, s12, s31
	s_or_b32 s12, s12, s33
	v_mul_f32_e32 v70, v172, v76
	v_mul_f32_e32 v71, v172, v77
	s_ashr_i32 s13, s12, 31
	v_cvt_pk_fp8_f32 v68, v70, v71 op_sel:[0,0,1]
	v_mul_f32_e32 v70, v172, v80
	v_mul_f32_e32 v71, v172, v81
	s_lshl_b64 s[12:13], s[12:13], 11
	v_cvt_pk_fp8_f32 v69, v70, v71 op_sel:[0,0,1]
	ds_read_b128 v[70:73], v173 offset:4224
	ds_read_b128 v[74:77], v173 offset:4240
	s_add_u32 s14, s28, s12
	s_addc_u32 s35, s27, s13
	s_and_b64 s[12:13], s[8:9], exec
	s_cselect_b32 s12, s15, s14
	s_cselect_b32 s13, s34, s35
	s_add_u32 s12, s12, s26
	s_waitcnt lgkmcnt(1)
	v_mul_f32_e32 v82, v172, v70
	v_mul_f32_e32 v71, v172, v71
	v_mov_b32_e32 v70, 0
	s_addc_u32 s13, s13, 0
	v_cvt_pk_fp8_f32 v70, v82, v71
	v_lshl_add_u64 v[80:81], s[12:13], 0, v[130:131]
	v_lshl_add_u64 v[78:79], v[80:81], 0, v[136:137]
	global_store_dwordx4 v[78:79], v[66:69], off nt
	v_mov_b32_e32 v71, 0
	s_waitcnt lgkmcnt(0)
	v_mul_f32_e32 v78, v172, v77
	v_mul_f32_e32 v66, v172, v72
	v_mul_f32_e32 v67, v172, v73
	v_cvt_pk_fp8_f32 v70, v66, v67 op_sel:[0,0,1]
	ds_read_b128 v[66:69], v173 offset:4256
	v_mul_f32_e32 v72, v172, v74
	v_mul_f32_e32 v73, v172, v75
	v_cvt_pk_fp8_f32 v71, v72, v73
	v_mul_f32_e32 v73, v172, v76
	ds_read_b128 v[74:77], v173 offset:4272
	s_waitcnt lgkmcnt(1)
	v_mul_f32_e32 v66, v172, v66
	v_mul_f32_e32 v67, v172, v67
	v_mov_b32_e32 v72, 0
	v_cvt_pk_fp8_f32 v72, v66, v67
	v_mul_f32_e32 v66, v172, v68
	v_mul_f32_e32 v67, v172, v69
	v_cvt_pk_fp8_f32 v71, v73, v78 op_sel:[0,0,1]
	v_cvt_pk_fp8_f32 v72, v66, v67 op_sel:[0,0,1]
	s_waitcnt lgkmcnt(0)
	v_mul_f32_e32 v66, v172, v74
	v_mul_f32_e32 v67, v172, v75
	v_mov_b32_e32 v73, 0
	v_cvt_pk_fp8_f32 v73, v66, v67
	ds_read_b128 v[66:69], v173 offset:8448
	v_mul_f32_e32 v74, v172, v76
	v_mul_f32_e32 v75, v172, v77
	v_cvt_pk_fp8_f32 v73, v74, v75 op_sel:[0,0,1]
	ds_read_b128 v[74:77], v173 offset:8464
	s_waitcnt lgkmcnt(1)
	v_mul_f32_e32 v82, v172, v66
	v_mul_f32_e32 v67, v172, v67
	v_mov_b32_e32 v66, 0
	v_cvt_pk_fp8_f32 v66, v82, v67
	v_lshl_add_u64 v[78:79], v[80:81], 0, v[134:135]
	v_mul_f32_e32 v67, v172, v68
	v_mul_f32_e32 v68, v172, v69
	global_store_dwordx4 v[78:79], v[70:73], off nt
	v_cvt_pk_fp8_f32 v66, v67, v68 op_sel:[0,0,1]
	ds_read_b128 v[68:71], v173 offset:8480
	s_waitcnt lgkmcnt(1)
	v_mul_f32_e32 v72, v172, v74
	v_mul_f32_e32 v73, v172, v75
	v_mov_b32_e32 v67, 0
	v_cvt_pk_fp8_f32 v67, v72, v73
	ds_read_b128 v[72:75], v173 offset:8496
	s_waitcnt lgkmcnt(1)
	v_mul_f32_e32 v78, v172, v68
	v_mul_f32_e32 v69, v172, v69
	v_mov_b32_e32 v68, 0
	v_cvt_pk_fp8_f32 v68, v78, v69
	v_mul_f32_e32 v76, v172, v76
	v_mul_f32_e32 v77, v172, v77
	v_mul_f32_e32 v69, v172, v70
	v_mul_f32_e32 v70, v172, v71
	v_cvt_pk_fp8_f32 v67, v76, v77 op_sel:[0,0,1]
	v_cvt_pk_fp8_f32 v68, v69, v70 op_sel:[0,0,1]
	s_waitcnt lgkmcnt(0)
	v_mul_f32_e32 v76, v172, v72
	v_mul_f32_e32 v77, v172, v73
	ds_read_b128 v[70:73], v173 offset:12672
	v_mov_b32_e32 v69, 0
	v_cvt_pk_fp8_f32 v69, v76, v77
	v_mul_f32_e32 v78, v172, v74
	v_mul_f32_e32 v79, v172, v75
	ds_read_b128 v[74:77], v173 offset:12688
	s_waitcnt lgkmcnt(1)
	v_mul_f32_e32 v82, v172, v70
	v_mul_f32_e32 v71, v172, v71
	v_mov_b32_e32 v70, 0
	v_cvt_pk_fp8_f32 v70, v82, v71
	v_mul_f32_e32 v71, v172, v72
	v_mul_f32_e32 v72, v172, v73
	s_waitcnt lgkmcnt(0)
	v_mul_f32_e32 v73, v172, v75
	v_cvt_pk_fp8_f32 v70, v71, v72 op_sel:[0,0,1]
	v_mul_f32_e32 v72, v172, v74
	v_mov_b32_e32 v71, 0
	v_cvt_pk_fp8_f32 v71, v72, v73
	ds_read_b128 v[72:75], v173 offset:12704
	v_mul_f32_e32 v76, v172, v76
	v_mul_f32_e32 v77, v172, v77
	v_cvt_pk_fp8_f32 v69, v78, v79 op_sel:[0,0,1]
	v_cvt_pk_fp8_f32 v71, v76, v77 op_sel:[0,0,1]
	ds_read_b128 v[76:79], v173 offset:12720
	s_waitcnt lgkmcnt(1)
	v_mul_f32_e32 v82, v172, v72
	v_mul_f32_e32 v73, v172, v73
	v_mov_b32_e32 v72, 0
	v_cvt_pk_fp8_f32 v72, v82, v73
	s_waitcnt lgkmcnt(0)
	v_mul_f32_e32 v76, v172, v76
	v_mul_f32_e32 v77, v172, v77
	v_mov_b32_e32 v73, 0
	v_cvt_pk_fp8_f32 v73, v76, v77
	v_mul_f32_e32 v74, v172, v74
	v_mul_f32_e32 v75, v172, v75
	v_cvt_pk_fp8_f32 v72, v74, v75 op_sel:[0,0,1]
	v_mul_f32_e32 v74, v172, v78
	v_mul_f32_e32 v75, v172, v79
	v_cvt_pk_fp8_f32 v73, v74, v75 op_sel:[0,0,1]
	v_lshl_add_u64 v[74:75], v[80:81], 0, v[132:133]
	global_store_dwordx4 v[74:75], v[66:69], off nt
	s_lshl_b64 s[12:13], s[10:11], 10
	s_add_u32 s12, s29, s12
	v_lshl_add_u64 v[66:67], v[80:81], 0, v[138:139]
	global_store_dwordx4 v[66:67], v[70:73], off nt
	s_waitcnt lgkmcnt(0)
	s_waitcnt vmcnt(17)
	ds_write2_b32 v174, v42, v58 offset1:8
	s_waitcnt vmcnt(16)
	ds_write2_b32 v174, v46, v62 offset0:64 offset1:72
	ds_write2_b32 v174, v43, v59 offset0:132 offset1:140
	ds_write2_b32 v174, v47, v63 offset0:196 offset1:204
	ds_write2_b32 v175, v44, v60 offset0:8 offset1:16
	ds_write2_b32 v175, v48, v64 offset0:72 offset1:80
	ds_write2_b32 v175, v45, v61 offset0:140 offset1:148
	ds_write2_b32 v175, v49, v65 offset0:204 offset1:212
	s_waitcnt vmcnt(13)
	ds_write2_b32 v174, v34, v50 offset0:16 offset1:24
	s_waitcnt vmcnt(12)
	ds_write2_b32 v174, v38, v54 offset0:80 offset1:88
	ds_write2_b32 v174, v35, v51 offset0:148 offset1:156
	ds_write2_b32 v174, v39, v55 offset0:212 offset1:220
	ds_write2_b32 v175, v36, v52 offset0:24 offset1:32
	ds_write2_b32 v175, v40, v56 offset0:88 offset1:96
	ds_write2_b32 v175, v37, v53 offset0:156 offset1:164
	ds_write2_b32 v175, v41, v57 offset0:220 offset1:228
	s_waitcnt vmcnt(9)
	ds_write2_b32 v174, v18, v26 offset0:32 offset1:40
	s_waitcnt vmcnt(8)
	ds_write2_b32 v174, v22, v30 offset0:96 offset1:104
	ds_write2_b32 v174, v19, v27 offset0:164 offset1:172
	ds_write2_b32 v174, v23, v31 offset0:228 offset1:236
	ds_write2_b32 v175, v20, v28 offset0:40 offset1:48
	ds_write2_b32 v175, v24, v32 offset0:104 offset1:112
	ds_write2_b32 v175, v21, v29 offset0:172 offset1:180
	ds_write2_b32 v175, v25, v33 offset0:236 offset1:244
	s_waitcnt vmcnt(5)
	ds_write2_b32 v174, v2, v10 offset0:48 offset1:56
	s_waitcnt vmcnt(4)
	ds_write2_b32 v174, v6, v14 offset0:112 offset1:120
	ds_write2_b32 v174, v3, v11 offset0:180 offset1:188
	ds_write2_b32 v174, v7, v15 offset0:244 offset1:252
	ds_write2_b32 v175, v4, v12 offset0:56 offset1:64
	ds_write2_b32 v175, v8, v16 offset0:120 offset1:128
	ds_write2_b32 v175, v5, v13 offset0:188 offset1:196
	ds_write2_b32 v176, v9, v17 offset0:124 offset1:132
	s_waitcnt lgkmcnt(0)
	ds_read_b128 v[2:5], v173
	ds_read_b128 v[6:9], v173 offset:16
	ds_read_b128 v[10:13], v173 offset:32
	ds_read_b128 v[14:17], v173 offset:48
	s_addc_u32 s13, s30, s13
	s_lshl_b32 s10, s10, 1
	s_waitcnt lgkmcnt(2)
	v_mul_f32_e32 v6, v172, v6
	v_mul_f32_e32 v18, v172, v2
	v_mul_f32_e32 v3, v172, v3
	v_mov_b32_e32 v2, 0
	v_cvt_pk_fp8_f32 v2, v18, v3
	v_mul_f32_e32 v7, v172, v7
	v_mov_b32_e32 v3, 0
	v_cvt_pk_fp8_f32 v3, v6, v7
	v_mul_f32_e32 v4, v172, v4
	v_mul_f32_e32 v5, v172, v5
	v_cvt_pk_fp8_f32 v2, v4, v5 op_sel:[0,0,1]
	v_mul_f32_e32 v4, v172, v8
	v_mul_f32_e32 v5, v172, v9
	v_cvt_pk_fp8_f32 v3, v4, v5 op_sel:[0,0,1]
	s_waitcnt lgkmcnt(1)
	v_mul_f32_e32 v5, v172, v10
	v_mul_f32_e32 v6, v172, v11
	v_mov_b32_e32 v4, 0
	v_cvt_pk_fp8_f32 v4, v5, v6
	s_waitcnt lgkmcnt(0)
	v_mul_f32_e32 v8, v172, v14
	v_mul_f32_e32 v9, v172, v15
	v_mov_b32_e32 v5, 0
	s_and_b32 s10, s10, 0xffffff00
	v_cvt_pk_fp8_f32 v5, v8, v9
	s_add_i32 s10, s10, s31
	s_or_b32 s10, s10, s33
	v_mul_f32_e32 v6, v172, v12
	v_mul_f32_e32 v7, v172, v13
	s_ashr_i32 s11, s10, 31
	v_cvt_pk_fp8_f32 v4, v6, v7 op_sel:[0,0,1]
	v_mul_f32_e32 v6, v172, v16
	v_mul_f32_e32 v7, v172, v17
	s_lshl_b64 s[10:11], s[10:11], 11
	v_cvt_pk_fp8_f32 v5, v6, v7 op_sel:[0,0,1]
	ds_read_b128 v[6:9], v173 offset:4224
	ds_read_b128 v[10:13], v173 offset:4240
	s_add_u32 s10, s28, s10
	s_addc_u32 s11, s27, s11
	s_and_b64 s[8:9], s[8:9], exec
	s_cselect_b32 s8, s12, s10
	s_cselect_b32 s9, s13, s11
	s_add_u32 s8, s8, s26
	s_waitcnt lgkmcnt(1)
	v_mul_f32_e32 v18, v172, v6
	v_mul_f32_e32 v7, v172, v7
	v_mov_b32_e32 v6, 0
	s_addc_u32 s9, s9, 0
	v_cvt_pk_fp8_f32 v6, v18, v7
	v_lshl_add_u64 v[16:17], s[8:9], 0, v[130:131]
	v_lshl_add_u64 v[14:15], v[16:17], 0, v[136:137]
	global_store_dwordx4 v[14:15], v[2:5], off nt
	v_mov_b32_e32 v7, 0
	s_waitcnt lgkmcnt(0)
	v_mul_f32_e32 v14, v172, v13
	v_mul_f32_e32 v2, v172, v8
	v_mul_f32_e32 v3, v172, v9
	v_cvt_pk_fp8_f32 v6, v2, v3 op_sel:[0,0,1]
	ds_read_b128 v[2:5], v173 offset:4256
	v_mul_f32_e32 v8, v172, v10
	v_mul_f32_e32 v9, v172, v11
	v_cvt_pk_fp8_f32 v7, v8, v9
	v_mul_f32_e32 v9, v172, v12
	ds_read_b128 v[10:13], v173 offset:4272
	s_waitcnt lgkmcnt(1)
	v_mul_f32_e32 v2, v172, v2
	v_mul_f32_e32 v3, v172, v3
	v_mov_b32_e32 v8, 0
	v_cvt_pk_fp8_f32 v8, v2, v3
	v_mul_f32_e32 v2, v172, v4
	v_mul_f32_e32 v3, v172, v5
	v_cvt_pk_fp8_f32 v7, v9, v14 op_sel:[0,0,1]
	v_cvt_pk_fp8_f32 v8, v2, v3 op_sel:[0,0,1]
	s_waitcnt lgkmcnt(0)
	v_mul_f32_e32 v2, v172, v10
	v_mul_f32_e32 v3, v172, v11
	v_mov_b32_e32 v9, 0
	v_cvt_pk_fp8_f32 v9, v2, v3
	ds_read_b128 v[2:5], v173 offset:8448
	v_mul_f32_e32 v10, v172, v12
	v_mul_f32_e32 v11, v172, v13
	v_cvt_pk_fp8_f32 v9, v10, v11 op_sel:[0,0,1]
	ds_read_b128 v[10:13], v173 offset:8464
	s_waitcnt lgkmcnt(1)
	v_mul_f32_e32 v18, v172, v2
	v_mul_f32_e32 v3, v172, v3
	v_mov_b32_e32 v2, 0
	v_cvt_pk_fp8_f32 v2, v18, v3
	v_lshl_add_u64 v[14:15], v[16:17], 0, v[134:135]
	v_mul_f32_e32 v3, v172, v4
	v_mul_f32_e32 v4, v172, v5
	global_store_dwordx4 v[14:15], v[6:9], off nt
	v_cvt_pk_fp8_f32 v2, v3, v4 op_sel:[0,0,1]
	ds_read_b128 v[4:7], v173 offset:8480
	s_waitcnt lgkmcnt(1)
	v_mul_f32_e32 v8, v172, v10
	v_mul_f32_e32 v9, v172, v11
	v_mov_b32_e32 v3, 0
	v_cvt_pk_fp8_f32 v3, v8, v9
	ds_read_b128 v[8:11], v173 offset:8496
	s_waitcnt lgkmcnt(1)
	v_mul_f32_e32 v14, v172, v4
	v_mul_f32_e32 v5, v172, v5
	v_mov_b32_e32 v4, 0
	v_cvt_pk_fp8_f32 v4, v14, v5
	v_mul_f32_e32 v12, v172, v12
	v_mul_f32_e32 v13, v172, v13
	v_mul_f32_e32 v5, v172, v6
	v_mul_f32_e32 v6, v172, v7
	v_cvt_pk_fp8_f32 v3, v12, v13 op_sel:[0,0,1]
	v_cvt_pk_fp8_f32 v4, v5, v6 op_sel:[0,0,1]
	s_waitcnt lgkmcnt(0)
	v_mul_f32_e32 v12, v172, v8
	v_mul_f32_e32 v13, v172, v9
	ds_read_b128 v[6:9], v173 offset:12672
	v_mov_b32_e32 v5, 0
	v_cvt_pk_fp8_f32 v5, v12, v13
	v_mul_f32_e32 v14, v172, v10
	v_mul_f32_e32 v15, v172, v11
	ds_read_b128 v[10:13], v173 offset:12688
	s_waitcnt lgkmcnt(1)
	v_mul_f32_e32 v18, v172, v6
	v_mul_f32_e32 v7, v172, v7
	v_mov_b32_e32 v6, 0
	v_cvt_pk_fp8_f32 v6, v18, v7
	v_mul_f32_e32 v7, v172, v8
	v_mul_f32_e32 v8, v172, v9
	s_waitcnt lgkmcnt(0)
	v_mul_f32_e32 v9, v172, v11
	v_cvt_pk_fp8_f32 v6, v7, v8 op_sel:[0,0,1]
	v_mul_f32_e32 v8, v172, v10
	v_mov_b32_e32 v7, 0
	v_cvt_pk_fp8_f32 v7, v8, v9
	ds_read_b128 v[8:11], v173 offset:12704
	v_mul_f32_e32 v12, v172, v12
	v_mul_f32_e32 v13, v172, v13
	v_cvt_pk_fp8_f32 v5, v14, v15 op_sel:[0,0,1]
	v_cvt_pk_fp8_f32 v7, v12, v13 op_sel:[0,0,1]
	ds_read_b128 v[12:15], v173 offset:12720
	s_waitcnt lgkmcnt(1)
	v_mul_f32_e32 v18, v172, v8
	v_mul_f32_e32 v9, v172, v9
	v_mov_b32_e32 v8, 0
	v_cvt_pk_fp8_f32 v8, v18, v9
	s_waitcnt lgkmcnt(0)
	v_mul_f32_e32 v12, v172, v12
	v_mul_f32_e32 v13, v172, v13
	v_mov_b32_e32 v9, 0
	v_cvt_pk_fp8_f32 v9, v12, v13
	v_mul_f32_e32 v10, v172, v10
	v_mul_f32_e32 v11, v172, v11
	v_cvt_pk_fp8_f32 v8, v10, v11 op_sel:[0,0,1]
	v_mul_f32_e32 v10, v172, v14
	v_mul_f32_e32 v11, v172, v15
	v_cvt_pk_fp8_f32 v9, v10, v11 op_sel:[0,0,1]
	v_lshl_add_u64 v[10:11], v[16:17], 0, v[132:133]
	global_store_dwordx4 v[10:11], v[2:5], off nt
	s_nop 1
	v_lshl_add_u64 v[2:3], v[16:17], 0, v[138:139]
	global_store_dwordx4 v[2:3], v[6:9], off nt
	s_waitcnt lgkmcnt(0)
	s_barrier
	s_and_saveexec_b64 s[8:9], s[36:37]
	s_cbranch_execz .LBB0_930
	v_mov_b32_e32 v2, s16
	s_waitcnt vmcnt(0)
	ds_write_b32 v2, v255
	s_branch .LBB0_930

.LBB0_950:
	v_mov_b32_e32 v181, v3
	s_and_saveexec_b64 s[4:5], s[36:37]
	s_cbranch_execz .LBB0_954
	s_mov_b64 s[8:9], exec
	v_mbcnt_lo_u32_b32 v2, s8, 0
	v_mbcnt_hi_u32_b32 v2, s9, v2
	v_cmp_eq_u32_e32 vcc, 0, v2
	s_and_saveexec_b64 s[6:7], vcc
	s_cbranch_execz .LBB0_953
	s_bcnt1_i32_b64 s8, s[8:9]
	v_mov_b32_e32 v4, s8
	global_atomic_add v255, v3, v4, s[48:49] sc0
.LBB0_953:
	s_or_b64 exec, exec, s[6:7]
.LBB0_954:
	s_or_b64 exec, exec, s[4:5]
	s_cmp_lt_i32 s85, 0
	s_cselect_b64 s[4:5], -1, 0
	s_cmp_gt_i32 s85, -1
	s_cselect_b64 s[30:31], -1, 0
	v_mov_b32 v74, v0
	s_mov_b64 s[8:9], -1
	v_readfirstlane_b32 s38, v74
	s_and_b64 vcc, exec, s[30:31]
	s_cbranch_vccz .LBB0_956
	s_lshr_b32 s6, s85, 2
	s_mov_b64 s[8:9], 0

.LBB0_1157:
	v_mov_b32_e32 v2, s23
	s_waitcnt vmcnt(0)
	ds_write_b32 v2, v255
	s_branch .LBB0_949

.LBB0_1161:
	v_mov_b32_e32 v102, 0
	s_and_saveexec_b64 s[4:5], s[36:37]
	s_cbranch_execz .LBB0_1165
	s_mov_b64 s[18:19], exec
	v_mbcnt_lo_u32_b32 v2, s18, 0
	v_mbcnt_hi_u32_b32 v2, s19, v2
	v_cmp_eq_u32_e32 vcc, 0, v2
	s_and_saveexec_b64 s[6:7], vcc
	s_cbranch_execz .LBB0_1164
	s_bcnt1_i32_b64 s16, s[18:19]
	s_waitcnt vmcnt(0)
	v_mov_b32_e32 v3, s16
	global_atomic_add v255, v79, v3, s[48:49] sc0
.LBB0_1164:
	s_or_b64 exec, exec, s[6:7]
.LBB0_1165:
	s_or_b64 exec, exec, s[4:5]
	v_mov_b32 v85, v0
	s_add_i32 s16, s85, -8
	v_readfirstlane_b32 s22, v85
	s_ashr_i32 s20, s16, 1
	s_ashr_i32 s16, s22, 2
	s_ashr_i32 s21, s20, 31
	s_and_b32 s22, s16, -16
	s_lshl_b64 s[20:21], s[20:21], 7
	s_ashr_i32 s23, s22, 31
	s_add_u32 s16, s20, s22
	s_addc_u32 s59, s21, s23
	s_mulk_i32 s59, 0x2100
	s_mul_hi_u32 s60, s16, 0x2100
	s_add_i32 s59, s60, s59
	s_mulk_i32 s16, 0x2100
	v_and_b32_e32 v103, 63, v85
	s_add_u32 s60, s8, s16
	s_addc_u32 s61, s9, s59
	v_lshlrev_b32_e32 v78, 4, v103
	s_and_b32 s16, s85, 1
	v_lshlrev_b32_e32 v4, 4, v85
	v_ashrrev_i32_e32 v83, 4, v85
	s_load_dwordx4 s[4:7], s[0:1], 0x68
	s_load_dwordx2 s[18:19], s[0:1], 0x80
	s_waitcnt lgkmcnt(0)
	s_barrier
	s_waitcnt vmcnt(3)
	v_lshl_add_u64 v[18:19], s[60:61], 0, v[78:79]
	global_load_dwordx4 v[6:9], v78, s[60:61] offset:3584
	s_lshl_b32 s59, s16, 8
	v_and_b32_e32 v78, 0xf0, v4
	v_and_b32_e32 v4, 0xffffff80, v83
	v_bfe_u32 v82, v85, 4, 7
	v_add_u32_e32 v4, s59, v4
	v_add_co_u32_e32 v14, vcc, s26, v18
	v_or_b32_e32 v4, v4, v82
	s_nop 0
	v_addc_co_u32_e32 v15, vcc, 0, v19, vcc
	v_ashrrev_i32_e32 v5, 31, v4
	v_add_co_u32_e32 v2, vcc, s53, v18
	v_lshl_add_u64 v[20:21], s[12:13], 0, v[78:79]
	v_lshlrev_b64 v[4:5], 8, v[4:5]
	s_waitcnt vmcnt(1)
	v_addc_co_u32_e32 v3, vcc, 0, v19, vcc
	v_lshl_add_u64 v[10:11], v[20:21], 0, v[4:5]
	global_load_dwordx4 v[2:5], v[2:3], off offset:3328
	s_nop 0
	global_load_dwordx4 v[10:13], v[10:11], off
	v_add_u32_e32 v84, 0x200, v85
	v_add_co_u32_e32 v16, vcc, s27, v18
	v_ashrrev_i32_e32 v86, 4, v84
	s_nop 0
	v_addc_co_u32_e32 v17, vcc, 0, v19, vcc
	global_load_dwordx4 v[74:77], v[14:15], off offset:3840
	global_load_dwordx4 v[70:73], v[16:17], off
	v_and_b32_e32 v15, 0xffffff80, v86
	v_bfe_u32 v14, v84, 4, 7
	v_add_u32_e32 v15, s59, v15
	v_or_b32_e32 v14, v15, v14
	v_ashrrev_i32_e32 v15, 31, v14
	v_lshlrev_b64 v[14:15], 8, v[14:15]
	v_lshl_add_u64 v[14:15], v[20:21], 0, v[14:15]
	global_load_dwordx4 v[14:17], v[14:15], off
	v_add_co_u32_e32 v22, vcc, s28, v18
	v_lshrrev_b32_e32 v111, 4, v85
	s_nop 0
	v_addc_co_u32_e32 v23, vcc, 0, v19, vcc
	v_add_co_u32_e32 v24, vcc, s29, v18
	v_add_u32_e32 v90, s54, v78
	s_nop 0
	v_addc_co_u32_e32 v25, vcc, 0, v19, vcc
	global_load_dwordx4 v[66:69], v[22:23], off offset:256
	global_load_dwordx4 v[62:65], v[24:25], off offset:512
	v_add_co_u32_e32 v22, vcc, s30, v18
	v_add_u32_e32 v137, 0xa00, v85
	s_nop 0
	v_addc_co_u32_e32 v23, vcc, 0, v19, vcc
	v_add_co_u32_e32 v24, vcc, s31, v18
	v_ashrrev_i32_e32 v138, 4, v137
	s_nop 0
	v_addc_co_u32_e32 v25, vcc, 0, v19, vcc
	global_load_dwordx4 v[58:61], v[22:23], off offset:768
	global_load_dwordx4 v[54:57], v[24:25], off offset:1024
	v_add_co_u32_e32 v22, vcc, s33, v18
	v_add_u32_e32 v139, 0xc00, v85
	s_nop 0
	v_addc_co_u32_e32 v23, vcc, 0, v19, vcc
	v_add_co_u32_e32 v24, vcc, s34, v18
	v_ashrrev_i32_e32 v140, 4, v139
	s_nop 0
	v_addc_co_u32_e32 v25, vcc, 0, v19, vcc
	global_load_dwordx4 v[50:53], v[22:23], off offset:1280
	global_load_dwordx4 v[46:49], v[24:25], off offset:1536
	v_add_co_u32_e32 v22, vcc, s35, v18
	v_add_u32_e32 v141, 0xe00, v85
	s_nop 0
	v_addc_co_u32_e32 v23, vcc, 0, v19, vcc
	v_add_co_u32_e32 v24, vcc, s38, v18
	v_ashrrev_i32_e32 v142, 4, v141
	s_nop 0
	v_addc_co_u32_e32 v25, vcc, 0, v19, vcc
	global_load_dwordx4 v[42:45], v[22:23], off offset:1792
	global_load_dwordx4 v[38:41], v[24:25], off offset:2048
	v_add_co_u32_e32 v22, vcc, s39, v18
	s_waitcnt vmcnt(13)
	v_lshlrev_b32_e32 v110, 16, v6
	v_addc_co_u32_e32 v23, vcc, 0, v19, vcc
	v_add_co_u32_e32 v24, vcc, s50, v18
	v_and_b32_e32 v109, 0xffff0000, v6
	s_nop 0
	v_addc_co_u32_e32 v25, vcc, 0, v19, vcc
	global_load_dwordx4 v[34:37], v[22:23], off offset:2304
	global_load_dwordx4 v[30:33], v[24:25], off offset:2560
	v_add_co_u32_e32 v22, vcc, s51, v18
	v_add_f32_e32 v6, 0, v110
	s_nop 0
	v_addc_co_u32_e32 v23, vcc, 0, v19, vcc
	v_add_co_u32_e32 v18, vcc, s52, v18
	v_lshlrev_b32_e32 v108, 16, v7
	s_nop 0
	v_addc_co_u32_e32 v19, vcc, 0, v19, vcc
	global_load_dwordx4 v[26:29], v[22:23], off offset:2816
	s_nop 0
	global_load_dwordx4 v[22:25], v[18:19], off offset:3072
	v_bfi_b32 v18, s55, v83, v111
	v_mad_u64_u32 v[18:19], s[60:61], v18, s56, v[90:91]
	s_waitcnt vmcnt(15)
	ds_write_b128 v18, v[10:13]
	v_lshrrev_b32_e32 v10, 4, v84
	v_bfi_b32 v10, s55, v86, v10
	v_mad_u64_u32 v[10:11], s[60:61], v10, s56, v[90:91]
	v_add_u32_e32 v11, 0x400, v85
	v_ashrrev_i32_e32 v18, 4, v11
	v_and_b32_e32 v13, 0xffffff80, v18
	v_bfe_u32 v12, v11, 4, 7
	v_add_u32_e32 v13, s59, v13
	v_or_b32_e32 v12, v13, v12
	v_ashrrev_i32_e32 v13, 31, v12
	v_lshlrev_b64 v[12:13], 8, v[12:13]
	v_lshl_add_u64 v[12:13], v[20:21], 0, v[12:13]
	global_load_dwordx4 v[86:89], v[12:13], off
	s_waitcnt vmcnt(13)
	ds_write_b128 v10, v[14:17]
	v_lshrrev_b32_e32 v10, 4, v11
	v_bfi_b32 v10, s55, v18, v10
	v_mad_u64_u32 v[132:133], s[60:61], v10, s56, v[90:91]
	v_add_u32_e32 v133, 0x600, v85
	v_ashrrev_i32_e32 v135, 4, v133
	v_add_u32_e32 v12, 0x800, v85
	v_and_b32_e32 v11, 0xffffff80, v135
	v_ashrrev_i32_e32 v136, 4, v12
	v_bfe_u32 v10, v133, 4, 7
	v_add_u32_e32 v11, s59, v11
	v_and_b32_e32 v12, 0xffffff80, v136
	v_or_b32_e32 v10, v11, v10
	v_add_u32_e32 v12, s59, v12
	v_ashrrev_i32_e32 v11, 31, v10
	v_or_b32_e32 v12, v12, v82
	v_lshlrev_b64 v[10:11], 8, v[10:11]
	v_ashrrev_i32_e32 v13, 31, v12
	v_lshl_add_u64 v[10:11], v[20:21], 0, v[10:11]
	v_lshlrev_b64 v[12:13], 8, v[12:13]
	v_lshl_add_u64 v[12:13], v[20:21], 0, v[12:13]
	global_load_dwordx4 v[112:115], v[10:11], off
	global_load_dwordx4 v[116:119], v[12:13], off
	v_and_b32_e32 v11, 0xffffff80, v138
	v_bfe_u32 v10, v137, 4, 7
	v_add_u32_e32 v11, s59, v11
	v_and_b32_e32 v13, 0xffffff80, v140
	v_or_b32_e32 v10, v11, v10
	v_bfe_u32 v12, v139, 4, 7
	v_add_u32_e32 v13, s59, v13
	v_ashrrev_i32_e32 v11, 31, v10
	v_or_b32_e32 v12, v13, v12
	v_lshlrev_b64 v[10:11], 8, v[10:11]
	v_ashrrev_i32_e32 v13, 31, v12
	v_lshl_add_u64 v[10:11], v[20:21], 0, v[10:11]
	v_lshlrev_b64 v[12:13], 8, v[12:13]
	v_lshl_add_u64 v[12:13], v[20:21], 0, v[12:13]
	global_load_dwordx4 v[120:123], v[10:11], off
	global_load_dwordx4 v[124:127], v[12:13], off
	v_and_b32_e32 v11, 0xffffff80, v142
	v_bfe_u32 v10, v141, 4, 7
	v_add_u32_e32 v11, s59, v11
	v_add_f32_e32 v6, v6, v109
	v_or_b32_e32 v10, v11, v10
	v_and_b32_e32 v107, 0xffff0000, v7
	v_add_f32_e32 v6, v6, v108
	v_ashrrev_i32_e32 v11, 31, v10
	v_lshlrev_b32_e32 v106, 16, v8
	v_add_f32_e32 v6, v6, v107
	v_lshlrev_b64 v[10:11], 8, v[10:11]
	v_and_b32_e32 v105, 0xffff0000, v8
	v_add_f32_e32 v6, v6, v106
	v_lshl_add_u64 v[10:11], v[20:21], 0, v[10:11]
	v_cmp_lt_i32_e32 vcc, v93, v92
	v_lshlrev_b32_e32 v104, 16, v9
	v_add_f32_e32 v6, v6, v105
	global_load_dwordx4 v[128:131], v[10:11], off
	v_cndmask_b32_e32 v11, v1, v93, vcc
	v_and_b32_e32 v91, 0xffff0000, v9
	v_add_f32_e32 v6, v6, v104
	v_lshlrev_b32_e32 v78, 2, v11
	v_add_f32_e32 v6, v6, v91
	ds_bpermute_b32 v7, v78, v6
	v_cmp_lt_i32_e32 vcc, v94, v92
	v_lshlrev_b32_e32 v10, 5, v103
	global_load_dwordx4 v[14:17], v10, s[4:5]
	global_load_dwordx4 v[18:21], v10, s[6:7]
	v_cndmask_b32_e32 v8, v1, v94, vcc
	v_lshlrev_b32_e32 v82, 2, v8
	s_waitcnt lgkmcnt(0)
	v_add_f32_e32 v84, v6, v7
	global_load_dwordx4 v[6:9], v10, s[4:5] offset:16
	s_nop 0
	global_load_dwordx4 v[10:13], v10, s[6:7] offset:16
	ds_bpermute_b32 v143, v82, v84
	v_cmp_lt_i32_e32 vcc, v95, v92
	v_lshlrev_b32_e32 v134, 3, v103
	s_waitcnt lgkmcnt(0)
	v_add_f32_e32 v143, v84, v143
	v_cndmask_b32_e32 v83, v1, v95, vcc
	v_lshlrev_b32_e32 v83, 2, v83
	ds_bpermute_b32 v144, v83, v143
	v_cmp_lt_i32_e32 vcc, v96, v92
	s_waitcnt vmcnt(9)
	ds_write_b128 v132, v[86:89]
	v_lshrrev_b32_e32 v89, 4, v133
	v_cndmask_b32_e32 v84, v1, v96, vcc
	v_lshlrev_b32_e32 v84, 2, v84
	s_waitcnt lgkmcnt(1)
	v_add_f32_e32 v87, v143, v144
	ds_bpermute_b32 v88, v84, v87
	v_cmp_lt_i32_e32 vcc, v97, v92
	v_bfi_b32 v89, s55, v135, v89
	s_waitcnt lgkmcnt(0)
	v_add_f32_e32 v88, v87, v88
	v_cndmask_b32_e32 v86, v1, v97, vcc
	v_lshlrev_b32_e32 v86, 2, v86
	ds_bpermute_b32 v132, v86, v88
	v_cmp_lt_i32_e32 vcc, v98, v92
	s_waitcnt lgkmcnt(0)
	v_add_f32_e32 v132, v88, v132
	v_cndmask_b32_e32 v87, v1, v98, vcc
	v_lshlrev_b32_e32 v87, 2, v87
	ds_bpermute_b32 v133, v87, v132
	v_mad_u64_u32 v[88:89], s[4:5], v89, s56, v[90:91]
	s_waitcnt vmcnt(8)
	ds_write_b128 v88, v[112:115]
	v_bfi_b32 v88, s55, v136, v111
	s_waitcnt lgkmcnt(1)
	v_add_f32_e32 v89, v132, v133
	v_fmac_f32_e32 v109, 0xbb000000, v89
	v_fmac_f32_e32 v110, 0xbb000000, v89
	v_mul_f32_e32 v111, v109, v109
	v_fmac_f32_e32 v111, v110, v110
	v_fmac_f32_e32 v108, 0xbb000000, v89
	v_fmac_f32_e32 v111, v108, v108
	v_fmac_f32_e32 v107, 0xbb000000, v89
	v_fmac_f32_e32 v111, v107, v107
	v_fmac_f32_e32 v106, 0xbb000000, v89
	v_fmac_f32_e32 v111, v106, v106
	v_fmac_f32_e32 v105, 0xbb000000, v89
	v_fmac_f32_e32 v111, v105, v105
	v_fmac_f32_e32 v104, 0xbb000000, v89
	v_fmac_f32_e32 v111, v104, v104
	v_fmac_f32_e32 v91, 0xbb000000, v89
	v_fmac_f32_e32 v111, v91, v91
	ds_bpermute_b32 v112, v78, v111
	v_mad_u64_u32 v[88:89], s[4:5], v88, s56, v[90:91]
	s_waitcnt vmcnt(7)
	ds_write_b128 v88, v[116:119]
	v_lshrrev_b32_e32 v88, 4, v137
	s_waitcnt lgkmcnt(1)
	v_add_f32_e32 v111, v111, v112
	ds_bpermute_b32 v112, v82, v111
	v_bfi_b32 v88, s55, v138, v88
	v_mad_u64_u32 v[88:89], s[4:5], v88, s56, v[90:91]
	s_waitcnt vmcnt(6)
	ds_write_b128 v88, v[120:123]
	s_waitcnt lgkmcnt(1)
	v_add_f32_e32 v111, v111, v112
	ds_bpermute_b32 v112, v83, v111
	v_lshrrev_b32_e32 v88, 4, v139
	v_bfi_b32 v88, s55, v140, v88
	v_mad_u64_u32 v[88:89], s[4:5], v88, s56, v[90:91]
	s_waitcnt lgkmcnt(0)
	v_add_f32_e32 v111, v111, v112
	ds_bpermute_b32 v112, v84, v111
	s_waitcnt vmcnt(5)
	ds_write_b128 v88, v[124:127]
	v_lshrrev_b32_e32 v88, 4, v141
	v_bfi_b32 v88, s55, v142, v88
	v_mad_u64_u32 v[88:89], s[4:5], v88, s56, v[90:91]
	s_waitcnt lgkmcnt(1)
	v_add_f32_e32 v89, v111, v112
	ds_bpermute_b32 v90, v86, v89
	s_waitcnt vmcnt(4)
	ds_write_b128 v88, v[128:131]
	v_bfe_u32 v88, v85, 5, 1
	v_cmp_eq_u32_e32 vcc, s16, v88
	v_subrev_u32_e32 v88, s59, v134
	s_waitcnt lgkmcnt(1)
	v_add_f32_e32 v111, v89, v90
	ds_bpermute_b32 v112, v87, v111
	v_add_u32_e32 v89, s22, v134
	v_and_b32_e32 v90, 0x78, v89
	v_mul_i32_i24_e32 v88, 0x110, v88
	v_lshlrev_b32_e32 v90, 1, v90
	s_and_saveexec_b64 s[6:7], vcc
	s_cbranch_execz .LBB0_1167
	s_waitcnt lgkmcnt(0)
	v_add_f32_e32 v111, v111, v112
	v_fmamk_f32 v111, v111, 0x3b000000, v99
	v_mul_f32_e32 v112, 0x4b800000, v111
	v_cmp_gt_f32_e64 s[4:5], s57, v111
	s_nop 1
	v_cndmask_b32_e64 v111, v111, v112, s[4:5]
	v_rsq_f32_e32 v111, v111
	v_add3_u32 v112, 0, v90, v88
	v_mul_f32_e32 v113, 0x45800000, v111
	v_cndmask_b32_e64 v111, v111, v113, s[4:5]
	v_mul_f32_e32 v110, v110, v111
	v_mul_f32_e32 v109, v109, v111
	v_mul_f32_e32 v108, v108, v111
	v_mul_f32_e32 v107, v107, v111
	v_mul_f32_e32 v106, v106, v111
	v_mul_f32_e32 v105, v105, v111
	v_mul_f32_e32 v104, v104, v111
	v_mul_f32_e32 v91, v91, v111
	s_waitcnt vmcnt(2)
	v_fma_f32 v110, v14, v110, v18
	v_fma_f32 v109, v15, v109, v19
	v_fma_f32 v108, v16, v108, v20
	v_fma_f32 v107, v17, v107, v21
	s_waitcnt vmcnt(0)
	v_fma_f32 v106, v6, v106, v10
	v_fma_f32 v105, v7, v105, v11
	v_fma_f32 v104, v8, v104, v12
	v_fma_f32 v91, v9, v91, v13
	v_cvt_pk_bf16_f32 v110, v110, s0
	v_cvt_pk_bf16_f32 v109, v109, s0
	v_cvt_pk_bf16_f32 v108, v108, s0
	v_cvt_pk_bf16_f32 v107, v107, s0
	v_cvt_pk_bf16_f32 v106, v106, s0
	v_cvt_pk_bf16_f32 v105, v105, s0
	v_cvt_pk_bf16_f32 v104, v104, s0
	v_cvt_pk_bf16_f32 v91, v91, s0
	ds_write_b16 v112, v110
	ds_write_b16 v112, v109 offset:272
	ds_write_b16 v112, v108 offset:544
	ds_write_b16 v112, v107 offset:816
	ds_write_b16 v112, v106 offset:1088
	ds_write_b16 v112, v105 offset:1360
	ds_write_b16 v112, v104 offset:1632
	ds_write_b16 v112, v91 offset:1904

.LBB0_1262:
	v_mov_b32_e32 v2, s58
	s_waitcnt vmcnt(0)
	ds_write_b32 v2, v255
	s_branch .LBB0_1160

.LBB0_1266:
	v_mov_b32_e32 v107, 0
	s_and_saveexec_b64 s[4:5], s[36:37]
	s_cbranch_execz .LBB0_1270
	s_mov_b64 s[8:9], exec
	v_mbcnt_lo_u32_b32 v2, s8, 0
	v_mbcnt_hi_u32_b32 v2, s9, v2
	v_cmp_eq_u32_e32 vcc, 0, v2
	s_and_saveexec_b64 s[6:7], vcc
	s_cbranch_execz .LBB0_1269
	s_bcnt1_i32_b64 s8, s[8:9]
	s_waitcnt vmcnt(0)
	v_mov_b32_e32 v3, s8
	global_atomic_add v255, v67, v3, s[48:49] sc0
.LBB0_1269:
	s_or_b64 exec, exec, s[6:7]
.LBB0_1270:
	s_or_b64 exec, exec, s[4:5]
	v_mov_b32 v111, v0
	s_lshl_b32 s86, s85, 5
	v_readfirstlane_b32 s4, v111
	s_ashr_i32 s4, s4, 6
	s_and_b32 s87, s4, 3
	s_lshl_b32 s4, s4, 2
	s_and_b32 s4, s4, -16
	s_add_i32 s86, s86, s4
	v_and_b32_e32 v108, 15, v111
	s_add_i32 s85, s86, 0xffffde00
	s_barrier
	s_load_dwordx2 s[62:63], s[0:1], 0x60
	v_or_b32_e32 v68, s85, v108
	v_cmp_gt_i32_e32 vcc, s66, v68
	v_and_b32_e32 v112, 3, v111
	s_cmp_lt_i32 s87, 2
	v_cndmask_b32_e32 v2, v105, v106, vcc
	v_bitop3_b32 v109, v2, s85, v108 bitop3:0xe0
	v_lshrrev_b32_e32 v2, 1, v111
	v_cndmask_b32_e32 v110, v1, v104, vcc
	v_and_b32_e32 v66, 24, v2
	s_mov_b64 s[4:5], -1
	s_cbranch_scc1 .LBB0_1311
	v_add_u32_e32 v113, 3, v109
	s_mov_b64 s[6:7], -1
	s_cmp_gt_i32 s87, 2
	v_add_u32_e32 v114, 4, v109
	v_cmp_lt_u32_e64 s[4:5], v113, v110
	s_cbranch_scc0 .LBB0_1291
	v_subrev_co_u32_e32 v2, vcc, 8, v109
	v_add_u32_e32 v6, 8, v109
	v_max_i32_e32 v5, 0, v2
	v_min_u32_e32 v6, v6, v110
	v_sub_u32_e32 v5, v6, v5
	v_cvt_f32_i32_e32 v5, v5
	s_waitcnt vmcnt(0)
	v_add_u32_e32 v3, -1, v110
	v_min_i32_e32 v4, v2, v3
	v_cndmask_b32_e64 v4, v4, 0, vcc
	v_div_scale_f32 v6, s[6:7], v5, v5, 1.0
	v_rcp_f32_e32 v7, v6
	v_add_u32_e32 v20, 6, v109
	v_add_u32_e32 v22, 7, v109
	v_min_u32_e32 v21, v20, v3
	v_fma_f32 v8, -v6, v7, 1.0
	v_fmac_f32_e32 v7, v8, v7
	v_div_scale_f32 v8, vcc, 1.0, v5, 1.0
	v_mul_f32_e32 v9, v8, v7
	v_fma_f32 v10, -v6, v9, v8
	v_fmac_f32_e32 v9, v10, v7
	v_fma_f32 v6, -v6, v9, v8
	v_div_fmas_f32 v6, v6, v7, v9
	v_div_fixup_f32 v69, v6, v5, 1.0
	v_subrev_co_u32_e32 v5, vcc, 7, v109
	v_min_i32_e32 v6, v5, v3
	s_nop 0
	v_cndmask_b32_e64 v6, v6, 0, vcc
	v_subrev_co_u32_e32 v7, vcc, 6, v109
	v_min_i32_e32 v8, v7, v3
	s_nop 0
	v_cndmask_b32_e64 v8, v8, 0, vcc
	v_subrev_co_u32_e32 v9, vcc, 5, v109
	v_min_i32_e32 v10, v9, v3
	s_nop 0
	v_cndmask_b32_e64 v10, v10, 0, vcc
	v_subrev_co_u32_e32 v11, vcc, 4, v109
	v_min_i32_e32 v12, v11, v3
	s_nop 0
	v_cndmask_b32_e64 v12, v12, 0, vcc
	v_subrev_co_u32_e32 v13, vcc, 3, v109
	v_min_i32_e32 v14, v13, v3
	s_nop 0
	v_cndmask_b32_e64 v14, v14, 0, vcc
	v_subrev_co_u32_e32 v15, vcc, 2, v109
	v_min_i32_e32 v16, v15, v3
	s_nop 0
	v_cndmask_b32_e64 v16, v16, 0, vcc
	v_subrev_co_u32_e32 v17, vcc, 1, v109
	v_min_i32_e32 v18, v17, v3
	s_nop 0
	v_cndmask_b32_e64 v18, v18, 0, vcc
	v_cmp_lt_u32_e32 vcc, v2, v110
	v_cmp_lt_u32_e64 s[10:11], v9, v110
	v_cmp_lt_u32_e64 s[18:19], v17, v110
	v_add_u32_e32 v2, 1, v109
	v_add_u32_e32 v9, 2, v109
	v_add_u32_e32 v17, 5, v109
	v_cmp_lt_u32_e64 s[6:7], v5, v110
	v_cmp_lt_u32_e64 s[8:9], v7, v110
	v_cmp_lt_u32_e64 s[12:13], v11, v110
	v_cmp_lt_u32_e64 s[14:15], v13, v110
	v_cmp_lt_u32_e64 s[16:17], v15, v110
	v_min_u32_e32 v5, v109, v3
	v_min_u32_e32 v7, v2, v3
	v_min_u32_e32 v11, v9, v3
	v_min_u32_e32 v13, v113, v3
	v_min_u32_e32 v15, v114, v3
	v_min_u32_e32 v19, v17, v3
	v_min_u32_e32 v23, v22, v3
	v_lshlrev_b32_e32 v3, 9, v111
	v_cmp_lt_u32_e64 s[22:23], v2, v110
	v_cmp_lt_u32_e64 s[24:25], v9, v110
	v_and_b32_e32 v9, 48, v111
	v_lshlrev_b32_e32 v2, 8, v112
	v_and_b32_e32 v3, 0x1800, v3
	v_or3_b32 v2, v3, v2, v9
	v_mov_b32_e32 v3, v67
	v_lshl_add_u64 v[70:71], s[40:41], 0, v[2:3]
	v_add3_u32 v2, v4, s86, v108
	v_sub_u32_e32 v2, v2, v109
	v_add_u32_e32 v2, 0xffffde00, v2
	v_mad_i64_i32 v[2:3], s[38:39], v2, s67, 0
	v_or_b32_e32 v2, v2, v9
	v_lshl_add_u64 v[72:73], s[54:55], 0, v[2:3]
	v_add3_u32 v2, v6, s86, v108
	v_sub_u32_e32 v2, v2, v109
	v_add_u32_e32 v2, 0xffffde00, v2
	v_mad_i64_i32 v[2:3], s[38:39], v2, s67, 0
	v_or_b32_e32 v2, v2, v9
	v_lshl_add_u64 v[74:75], s[54:55], 0, v[2:3]
	v_add3_u32 v2, v8, s86, v108
	v_sub_u32_e32 v2, v2, v109
	v_add_u32_e32 v2, 0xffffde00, v2
	v_mad_i64_i32 v[2:3], s[38:39], v2, s67, 0
	v_or_b32_e32 v2, v2, v9
	v_lshl_add_u64 v[76:77], s[54:55], 0, v[2:3]
	v_add3_u32 v2, v10, s86, v108
	v_sub_u32_e32 v2, v2, v109
	v_add_u32_e32 v2, 0xffffde00, v2
	v_mad_i64_i32 v[2:3], s[38:39], v2, s67, 0
	v_or_b32_e32 v2, v2, v9
	v_lshl_add_u64 v[78:79], s[54:55], 0, v[2:3]
	v_add3_u32 v2, v12, s86, v108
	v_sub_u32_e32 v2, v2, v109
	v_add_u32_e32 v2, 0xffffde00, v2
	v_mad_i64_i32 v[2:3], s[38:39], v2, s67, 0
	v_or_b32_e32 v2, v2, v9
	v_lshl_add_u64 v[80:81], s[54:55], 0, v[2:3]
	v_add3_u32 v2, v14, s86, v108
	v_sub_u32_e32 v2, v2, v109
	v_add_u32_e32 v2, 0xffffde00, v2
	v_mad_i64_i32 v[2:3], s[38:39], v2, s67, 0
	v_or_b32_e32 v2, v2, v9
	v_lshl_add_u64 v[82:83], s[54:55], 0, v[2:3]
	v_add3_u32 v2, v16, s86, v108
	v_sub_u32_e32 v2, v2, v109
	v_add_u32_e32 v2, 0xffffde00, v2
	v_mad_i64_i32 v[2:3], s[38:39], v2, s67, 0
	v_or_b32_e32 v2, v2, v9
	v_lshl_add_u64 v[84:85], s[54:55], 0, v[2:3]
	v_add3_u32 v2, v18, s86, v108
	v_sub_u32_e32 v2, v2, v109
	v_add_u32_e32 v2, 0xffffde00, v2
	v_mad_i64_i32 v[2:3], s[38:39], v2, s67, 0
	v_or_b32_e32 v2, v2, v9
	v_lshl_add_u64 v[86:87], s[54:55], 0, v[2:3]
	v_add3_u32 v2, v5, s86, v108
	v_sub_u32_e32 v2, v2, v109
	v_add_u32_e32 v2, 0xffffde00, v2
	v_mad_i64_i32 v[2:3], s[38:39], v2, s67, 0
	v_or_b32_e32 v2, v2, v9
	v_lshl_add_u64 v[88:89], s[54:55], 0, v[2:3]
	v_add3_u32 v2, v7, s86, v108
	v_sub_u32_e32 v2, v2, v109
	v_add_u32_e32 v2, 0xffffde00, v2
	v_mad_i64_i32 v[2:3], s[38:39], v2, s67, 0
	v_or_b32_e32 v2, v2, v9
	v_lshl_add_u64 v[90:91], s[54:55], 0, v[2:3]
	v_add3_u32 v2, v11, s86, v108
	v_sub_u32_e32 v2, v2, v109
	v_add_u32_e32 v2, 0xffffde00, v2
	v_mad_i64_i32 v[2:3], s[38:39], v2, s67, 0
	v_or_b32_e32 v2, v2, v9
	v_lshl_add_u64 v[92:93], s[54:55], 0, v[2:3]
	v_add3_u32 v2, v13, s86, v108
	v_sub_u32_e32 v2, v2, v109
	v_add_u32_e32 v2, 0xffffde00, v2
	v_mad_i64_i32 v[2:3], s[38:39], v2, s67, 0
	v_or_b32_e32 v2, v2, v9
	v_lshl_add_u64 v[94:95], s[54:55], 0, v[2:3]
	v_add3_u32 v2, v15, s86, v108
	v_sub_u32_e32 v2, v2, v109
	v_add_u32_e32 v2, 0xffffde00, v2
	v_mad_i64_i32 v[2:3], s[38:39], v2, s67, 0
	v_or_b32_e32 v2, v2, v9
	v_lshl_add_u64 v[96:97], s[54:55], 0, v[2:3]
	v_add3_u32 v2, v19, s86, v108
	v_sub_u32_e32 v2, v2, v109
	v_add_u32_e32 v2, 0xffffde00, v2
	v_mad_i64_i32 v[2:3], s[38:39], v2, s67, 0
	v_or_b32_e32 v2, v2, v9
	v_lshl_add_u64 v[98:99], s[54:55], 0, v[2:3]
	v_add3_u32 v2, v21, s86, v108
	v_sub_u32_e32 v2, v2, v109
	v_add_u32_e32 v2, 0xffffde00, v2
	v_mad_i64_i32 v[2:3], s[38:39], v2, s67, 0
	v_or_b32_e32 v2, v2, v9
	v_lshl_add_u64 v[100:101], s[54:55], 0, v[2:3]
	v_add3_u32 v2, v23, s86, v108
	v_sub_u32_e32 v2, v2, v109
	v_add_u32_e32 v2, 0xffffde00, v2
	v_mad_i64_i32 v[2:3], s[38:39], v2, s67, 0
	v_or_b32_e32 v2, v2, v9
	v_mov_b32_e32 v26, 0
	v_cmp_lt_u32_e64 s[20:21], v109, v110
	v_cmp_lt_u32_e64 s[26:27], v114, v110
	v_cmp_lt_u32_e64 s[28:29], v17, v110
	v_cmp_lt_u32_e64 s[30:31], v20, v110
	v_cmp_lt_u32_e64 s[34:35], v22, v110
	v_lshl_add_u64 v[102:103], s[54:55], 0, v[2:3]
	s_mov_b64 s[64:65], 0
	v_mov_b32_e32 v27, v26
	v_mov_b32_e32 v28, v26
	v_mov_b32_e32 v29, v26
	v_mov_b32_e32 v30, v26
	v_mov_b32_e32 v31, v26
	v_mov_b32_e32 v32, v26
	v_mov_b32_e32 v33, v26
	v_mov_b32_e32 v18, v26
	v_mov_b32_e32 v19, v26
	v_mov_b32_e32 v20, v26
	v_mov_b32_e32 v21, v26
	v_mov_b32_e32 v22, v26
	v_mov_b32_e32 v23, v26
	v_mov_b32_e32 v24, v26
	v_mov_b32_e32 v25, v26
	v_mov_b32_e32 v10, v26
	v_mov_b32_e32 v11, v26
	v_mov_b32_e32 v12, v26
	v_mov_b32_e32 v13, v26
	v_mov_b32_e32 v14, v26
	v_mov_b32_e32 v15, v26
	v_mov_b32_e32 v16, v26
	v_mov_b32_e32 v17, v26
	v_mov_b32_e32 v2, v26
	v_mov_b32_e32 v3, v26
	v_mov_b32_e32 v4, v26
	v_mov_b32_e32 v5, v26
	v_mov_b32_e32 v6, v26
	v_mov_b32_e32 v7, v26
	v_mov_b32_e32 v8, v26
	v_mov_b32_e32 v9, v26

.LBB0_1351:
	s_and_saveexec_b64 s[4:5], s[36:37]
	s_cbranch_execz .LBB0_1265
	v_mov_b32_e32 v2, s84
	s_waitcnt vmcnt(0)
	ds_write_b32 v2, v255
	s_branch .LBB0_1265

.LBB0_1356:
	v_mov_b32_e32 v85, 0
	s_and_saveexec_b64 s[4:5], s[36:37]
	s_cbranch_execz .LBB0_1360
	s_mov_b64 s[24:25], exec
	v_mbcnt_lo_u32_b32 v2, s24, 0
	v_mbcnt_hi_u32_b32 v2, s25, v2
	v_cmp_eq_u32_e32 vcc, 0, v2
	s_and_saveexec_b64 s[6:7], vcc
	s_cbranch_execz .LBB0_1359
	s_bcnt1_i32_b64 s14, s[24:25]
	s_waitcnt vmcnt(0)
	v_mov_b32_e32 v3, s14
	global_atomic_add v255, v75, v3, s[48:49] sc0
.LBB0_1359:
	s_or_b64 exec, exec, s[6:7]
.LBB0_1360:
	s_or_b64 exec, exec, s[4:5]
	s_add_i32 s4, s85, 0xfffffce0
	s_mul_hi_i32 s5, s4, 0x3e0f83e1
	s_lshr_b32 s6, s5, 31
	s_ashr_i32 s67, s5, 5
	s_add_i32 s67, s67, s6
	s_mul_i32 s5, s67, 0x84
	s_sub_i32 s68, s4, s5
	s_ashr_i32 s4, s67, 2
	s_and_b32 s34, s67, 3
	s_cmp_lt_i32 s68, 4
	s_cselect_b64 s[6:7], -1, 0
	s_cmp_gt_i32 s68, 3
	s_cselect_b64 s[28:29], -1, 0
	s_ashr_i32 s5, s4, 31
	s_lshl_b32 s26, s4, 8
	s_lshl_b32 s14, s68, 6
	s_lshl_b64 s[24:25], s[4:5], 13
	s_ashr_i32 s27, s26, 31
	s_and_b64 s[4:5], s[6:7], exec
	s_cselect_b32 s4, s38, 0xffffff00
	s_cselect_b32 s5, s27, s25
	s_cselect_b32 s6, s26, s24
	s_add_i32 s4, s4, s14
	v_mov_b32 v87, v0
	s_add_u32 s26, s6, s4
	s_waitcnt vmcnt(3)
	v_ashrrev_i32_e32 v18, 3, v87
	s_addc_u32 s27, s5, 0
	v_ashrrev_i32_e32 v19, 31, v18
	s_waitcnt vmcnt(0)
	v_lshl_add_u64 v[2:3], s[26:27], 0, v[18:19]
	v_mad_u64_u32 v[4:5], s[4:5], v2, s39, v[76:77]
	v_and_b32_e32 v36, 7, v87
	v_mad_i32_i24 v5, v3, s39, v5
	s_lshl_b32 s14, s34, 7
	v_lshlrev_b32_e32 v74, 4, v36
	v_lshl_add_u64 v[2:3], v[4:5], 0, s[14:15]
	v_lshl_add_u64 v[2:3], v[2:3], 0, v[74:75]
	v_add_co_u32_e32 v2, vcc, s50, v2
	s_lshl_b32 s4, s34, 8
	s_nop 0
	v_addc_co_u32_e32 v3, vcc, 0, v3, vcc
	s_mov_b32 s5, s15
	global_load_dwordx4 v[14:17], v[2:3], off offset:512
	global_load_dwordx4 v[10:13], v[2:3], off offset:1024
	v_lshl_add_u64 v[2:3], v[4:5], 0, s[4:5]
	v_lshlrev_b32_e32 v74, 5, v36
	v_lshl_add_u64 v[2:3], v[2:3], 0, v[74:75]
	v_lshl_add_u64 v[4:5], v[2:3], 0, s[16:17]
	v_add_co_u32_e32 v2, vcc, 0x1000, v2
	v_readfirstlane_b32 s69, v87
	s_nop 0
	v_addc_co_u32_e32 v3, vcc, 0, v3, vcc
	global_load_dwordx4 v[6:9], v[2:3], off offset:1536
	s_nop 0
	global_load_dwordx4 v[2:5], v[4:5], off offset:16
	s_load_dwordx4 s[4:7], s[0:1], 0x88
	s_load_dwordx2 s[24:25], s[0:1], 0x98
	v_cmp_gt_i32_e32 vcc, s51, v87
	s_waitcnt lgkmcnt(0)
	s_barrier
	s_and_saveexec_b64 s[30:31], vcc
	s_cbranch_execz .LBB0_1362
	v_ashrrev_i32_e32 v24, 2, v87
	v_ashrrev_i32_e32 v25, 31, v24
	v_lshl_add_u64 v[20:21], s[26:27], 0, v[24:25]
	v_mad_u64_u32 v[22:23], s[70:71], v20, s39, v[76:77]
	v_mov_b32_e32 v20, v23
	v_lshlrev_b32_e32 v19, 3, v87
	v_mad_u64_u32 v[20:21], s[70:71], v21, s39, v[20:21]
	v_and_b32_e32 v19, 24, v19
	v_mov_b32_e32 v23, v20
	v_lshlrev_b32_e32 v74, 1, v19
	v_lshl_add_u64 v[20:21], v[22:23], 0, v[74:75]
	v_add_co_u32_e32 v20, vcc, s50, v20
	v_lshlrev_b32_e32 v24, 7, v24
	s_nop 0
	v_addc_co_u32_e32 v21, vcc, 0, v21, vcc
	global_load_dwordx4 v[20:23], v[20:21], off offset:3584
	v_lshlrev_b32_e32 v19, 2, v19
	v_add3_u32 v19, 0, v24, v19
	s_waitcnt vmcnt(0)
	v_lshlrev_b32_e32 v24, 16, v20
	v_and_b32_e32 v25, 0xffff0000, v20
	v_lshlrev_b32_e32 v26, 16, v21
	v_and_b32_e32 v27, 0xffff0000, v21
	v_lshlrev_b32_e32 v20, 16, v22
	v_and_b32_e32 v21, 0xffff0000, v22
	v_lshlrev_b32_e32 v22, 16, v23
	v_and_b32_e32 v23, 0xffff0000, v23
	ds_write_b128 v19, v[24:27] offset:32768
	ds_write_b128 v19, v[20:23] offset:32784

.LBB0_1428:
	s_and_saveexec_b64 s[4:5], s[36:37]
	s_cbranch_execz .LBB0_1355
	s_nop 0
	v_mov_b32_e32 v2, s65
	s_waitcnt vmcnt(0)
	ds_write_b32 v2, v255
	s_branch .LBB0_1355

.LBB0_1441:
	s_or_b64 exec, exec, s[10:11]
.LBB0_1442:
	s_or_b64 exec, exec, s[8:9]
	s_add_i32 s28, s26, 0x180
	s_ashr_i32 s15, s28, 8
	s_bfe_u32 s12, s28, 0x40004
	s_cmp_eq_u32 s15, 2
	s_cselect_b64 s[8:9], -1, 0
	s_cmp_lg_u32 s15, 2
	s_cselect_b64 s[10:11], -1, 0
	v_mov_b32 v66, v0
	s_and_b64 vcc, exec, s[10:11]
	v_readfirstlane_b32 s29, v66
	v_mov_b32_e32 v172, 0
	s_cbranch_vccnz .LBB0_1444
	s_lshl_b32 s13, s12, 2
	v_mov_b32_e32 v2, s13
	global_load_dword v2, v2, s[6:7] sc1
	s_waitcnt vmcnt(0)
	v_div_scale_f32 v3, s[30:31], v2, v2, s24
	v_rcp_f32_e32 v4, v3
	v_div_scale_f32 v5, vcc, s24, v2, s24
	v_fma_f32 v6, -v3, v4, 1.0
	v_fmac_f32_e32 v4, v6, v4
	v_mul_f32_e32 v6, v5, v4
	v_fma_f32 v7, -v3, v6, v5
	v_fmac_f32_e32 v6, v7, v4
	v_fma_f32 v3, -v3, v6, v5
	v_div_fmas_f32 v3, v3, v4, v6
	v_div_fixup_f32 v3, v3, v2, s24
	v_cmp_lt_f32_e32 vcc, 0, v2
	s_nop 1
	v_cndmask_b32_e32 v172, 0, v3, vcc

.LBB0_1447:
	s_ashr_i32 s13, s29, 6
	s_cmp_eq_u32 s15, 1
	s_cselect_b32 s10, s25, 0xd8
	s_cmpk_gt_u32 s28, 0xff
	s_cselect_b32 s10, s10, 0xc8
	s_add_u32 s10, s0, s10
	s_addc_u32 s11, s1, 0
	s_lshl_b32 s28, s26, 5
	s_and_b32 s30, s28, 32
	s_and_b64 s[28:29], s[8:9], exec
	s_load_dwordx2 s[10:11], s[10:11], 0x0
	s_cselect_b32 s28, s30, 0
	s_and_b32 s30, s26, 14
	s_lshl_b32 s26, s26, 1
	s_add_i32 s31, s13, s28
	s_and_b32 s26, s26, 30
	s_and_b64 s[28:29], s[8:9], exec
	s_mulk_i32 s13, 0x4400
	s_cselect_b32 s26, s30, s26
	s_add_i32 s38, s13, 0
	s_lshl_b32 s30, s27, 11
	s_lshl_b32 s13, s27, 13
	s_waitcnt lgkmcnt(0)
	s_add_u32 s10, s10, s13
	s_addc_u32 s11, s11, 0
	s_lshl_b32 s26, s26, 6
	v_bfe_u32 v128, v66, 3, 3
	v_or_b32_e32 v130, s26, v128
	s_waitcnt vmcnt(0)
	v_lshlrev_b64 v[2:3], s12, v[130:131]
	v_lshlrev_b32_e32 v4, 4, v66
	v_lshl_add_u64 v[2:3], v[2:3], 2, s[10:11]
	v_and_b32_e32 v130, 0x70, v4
	s_lshl_b32 s10, s31, 5
	v_lshl_add_u64 v[2:3], v[2:3], 0, v[130:131]
	s_ashr_i32 s11, s10, 31
	v_lshl_add_u64 v[142:143], s[10:11], 2, v[2:3]
	s_lshl_b64 s[28:29], 64, s12
	v_lshl_add_u64 v[140:141], s[28:29], 2, v[142:143]
	s_lshl_b64 s[28:29], 8, s12
	v_lshl_add_u64 v[144:145], s[28:29], 2, v[142:143]
	s_lshl_b64 s[28:29], 0x48, s12
	v_lshl_add_u64 v[146:147], s[28:29], 2, v[142:143]
	s_lshl_b64 s[28:29], 16, s12
	v_lshl_add_u64 v[148:149], s[28:29], 2, v[142:143]
	s_lshl_b64 s[28:29], 0x50, s12
	v_lshl_add_u64 v[150:151], s[28:29], 2, v[142:143]
	s_lshl_b64 s[28:29], 24, s12
	v_lshl_add_u64 v[152:153], s[28:29], 2, v[142:143]
	s_lshl_b64 s[28:29], 0x58, s12
	v_lshl_add_u64 v[154:155], s[28:29], 2, v[142:143]
	s_lshl_b64 s[28:29], 32, s12
	v_lshl_add_u64 v[156:157], s[28:29], 2, v[142:143]
	s_lshl_b64 s[28:29], 0x60, s12
	v_lshl_add_u64 v[158:159], s[28:29], 2, v[142:143]
	s_lshl_b64 s[28:29], 40, s12
	v_lshl_add_u64 v[160:161], s[28:29], 2, v[142:143]
	s_lshl_b64 s[28:29], 0x68, s12
	v_lshl_add_u64 v[162:163], s[28:29], 2, v[142:143]
	s_lshl_b64 s[28:29], 48, s12
	v_lshl_add_u64 v[164:165], s[28:29], 2, v[142:143]
	s_lshl_b64 s[28:29], 0x70, s12
	v_lshl_add_u64 v[166:167], s[28:29], 2, v[142:143]
	s_lshl_b64 s[28:29], 56, s12
	s_lshl_b64 s[12:13], 0x78, s12
	v_lshl_add_u64 v[168:169], s[28:29], 2, v[142:143]
	v_lshl_add_u64 v[170:171], s[12:13], 2, v[142:143]
	global_load_dwordx4 v[68:71], v[142:143], off nt
	global_load_dwordx4 v[72:75], v[140:141], off nt
	global_load_dwordx4 v[76:79], v[144:145], off nt
	global_load_dwordx4 v[80:83], v[146:147], off nt
	global_load_dwordx4 v[116:119], v[164:165], off nt
	global_load_dwordx4 v[120:123], v[166:167], off nt
	global_load_dwordx4 v[124:127], v[168:169], off nt
	global_load_dwordx4 v[132:135], v[170:171], off nt
	global_load_dwordx4 v[84:87], v[148:149], off nt
	global_load_dwordx4 v[88:91], v[150:151], off nt
	global_load_dwordx4 v[92:95], v[152:153], off nt
	global_load_dwordx4 v[96:99], v[154:155], off nt
	global_load_dwordx4 v[100:103], v[156:157], off nt
	global_load_dwordx4 v[104:107], v[158:159], off nt
	global_load_dwordx4 v[108:111], v[160:161], off nt
	global_load_dwordx4 v[112:115], v[162:163], off nt
	v_and_b32_e32 v129, 7, v66
	v_mul_u32_u24_e32 v66, 0x840, v129
	v_lshlrev_b32_e32 v67, 2, v128
	v_add3_u32 v174, s38, v66, v67
	v_add_u32_e32 v175, 0x400, v174
	v_add_u32_e32 v176, 0x600, v174
	global_load_dwordx4 v[50:53], v[142:143], off offset:1024 nt
	global_load_dwordx4 v[54:57], v[140:141], off offset:1024 nt
	global_load_dwordx4 v[58:61], v[144:145], off offset:1024 nt
	global_load_dwordx4 v[62:65], v[146:147], off offset:1024 nt
	global_load_dwordx4 v[34:37], v[148:149], off offset:1024 nt
	global_load_dwordx4 v[38:41], v[150:151], off offset:1024 nt
	global_load_dwordx4 v[42:45], v[152:153], off offset:1024 nt
	global_load_dwordx4 v[46:49], v[154:155], off offset:1024 nt
	global_load_dwordx4 v[18:21], v[156:157], off offset:1024 nt
	global_load_dwordx4 v[22:25], v[158:159], off offset:1024 nt
	global_load_dwordx4 v[26:29], v[160:161], off offset:1024 nt
	global_load_dwordx4 v[30:33], v[162:163], off offset:1024 nt
	global_load_dwordx4 v[2:5], v[164:165], off offset:1024 nt
	global_load_dwordx4 v[6:9], v[166:167], off offset:1024 nt
	global_load_dwordx4 v[10:13], v[168:169], off offset:1024 nt
	global_load_dwordx4 v[14:17], v[170:171], off offset:1024 nt
	v_lshlrev_b32_e32 v66, 6, v129
	v_mul_u32_u24_e32 v67, 0x210, v128
	v_add3_u32 v173, s38, v66, v67
	s_add_i32 s12, s10, 0x100
	s_ashr_i32 s13, s12, 31
	s_add_u32 s29, s19, s30
	s_addc_u32 s30, s20, 0
	s_lshl_b64 s[34:35], s[10:11], 10
	s_add_u32 s11, s29, s34
	s_addc_u32 s39, s30, s35
	s_lshl_b32 s27, s27, 12
	s_add_u32 s28, s21, s27
	s_addc_u32 s27, s22, 0
	s_waitcnt vmcnt(29)
	ds_write2_b32 v174, v68, v76 offset1:8
	s_waitcnt vmcnt(28)
	ds_write2_b32 v174, v72, v80 offset0:64 offset1:72
	ds_write2_b32 v174, v69, v77 offset0:132 offset1:140
	ds_write2_b32 v174, v73, v81 offset0:196 offset1:204
	ds_write2_b32 v175, v70, v78 offset0:8 offset1:16
	ds_write2_b32 v175, v74, v82 offset0:72 offset1:80
	ds_write2_b32 v175, v71, v79 offset0:140 offset1:148
	ds_write2_b32 v175, v75, v83 offset0:204 offset1:212
	s_waitcnt vmcnt(21)
	ds_write2_b32 v174, v84, v92 offset0:16 offset1:24
	s_waitcnt vmcnt(20)
	ds_write2_b32 v174, v88, v96 offset0:80 offset1:88
	ds_write2_b32 v174, v85, v93 offset0:148 offset1:156
	ds_write2_b32 v174, v89, v97 offset0:212 offset1:220
	ds_write2_b32 v175, v86, v94 offset0:24 offset1:32
	ds_write2_b32 v175, v90, v98 offset0:88 offset1:96
	ds_write2_b32 v175, v87, v95 offset0:156 offset1:164
	ds_write2_b32 v175, v91, v99 offset0:220 offset1:228
	s_waitcnt vmcnt(17)
	ds_write2_b32 v174, v100, v108 offset0:32 offset1:40
	s_waitcnt vmcnt(16)
	ds_write2_b32 v174, v104, v112 offset0:96 offset1:104
	ds_write2_b32 v174, v101, v109 offset0:164 offset1:172
	ds_write2_b32 v174, v105, v113 offset0:228 offset1:236
	ds_write2_b32 v175, v102, v110 offset0:40 offset1:48
	ds_write2_b32 v175, v106, v114 offset0:104 offset1:112
	ds_write2_b32 v175, v103, v111 offset0:172 offset1:180
	ds_write2_b32 v175, v107, v115 offset0:236 offset1:244
	ds_write2_b32 v174, v116, v124 offset0:48 offset1:56
	ds_write2_b32 v174, v120, v132 offset0:112 offset1:120
	ds_write2_b32 v174, v117, v125 offset0:180 offset1:188
	ds_write2_b32 v174, v121, v133 offset0:244 offset1:252
	ds_write2_b32 v175, v118, v126 offset0:56 offset1:64
	ds_write2_b32 v175, v122, v134 offset0:120 offset1:128
	ds_write2_b32 v175, v119, v127 offset0:188 offset1:196
	ds_write2_b32 v176, v123, v135 offset0:124 offset1:132
	s_waitcnt lgkmcnt(0)
	ds_read_b128 v[66:69], v173
	ds_read_b128 v[70:73], v173 offset:16
	ds_read_b128 v[74:77], v173 offset:32
	ds_read_b128 v[78:81], v173 offset:48
	s_lshl_b32 s31, s31, 6
	s_and_b32 s33, s31, 0xffffff00
	s_waitcnt lgkmcnt(2)
	v_mul_f32_e32 v70, v172, v70
	v_mul_f32_e32 v82, v172, v66
	v_mul_f32_e32 v67, v172, v67
	v_mov_b32_e32 v66, 0
	v_cvt_pk_fp8_f32 v66, v82, v67
	v_mul_f32_e32 v71, v172, v71
	v_mov_b32_e32 v67, 0
	v_cvt_pk_fp8_f32 v67, v70, v71
	v_mul_f32_e32 v68, v172, v68
	v_mul_f32_e32 v69, v172, v69
	v_cvt_pk_fp8_f32 v66, v68, v69 op_sel:[0,0,1]
	v_mul_f32_e32 v68, v172, v72
	v_mul_f32_e32 v69, v172, v73
	v_cvt_pk_fp8_f32 v67, v68, v69 op_sel:[0,0,1]
	s_waitcnt lgkmcnt(1)
	v_mul_f32_e32 v69, v172, v74
	v_mul_f32_e32 v70, v172, v75
	v_mov_b32_e32 v68, 0
	v_cvt_pk_fp8_f32 v68, v69, v70
	s_waitcnt lgkmcnt(0)
	v_mul_f32_e32 v72, v172, v78
	v_mul_f32_e32 v73, v172, v79
	v_mov_b32_e32 v69, 0
	s_lshl_b32 s31, s15, 7
	v_cvt_pk_fp8_f32 v69, v72, v73
	s_add_i32 s15, s33, s31
	s_and_b32 s33, s10, 0x60
	s_or_b32 s34, s15, s33
	v_mul_f32_e32 v70, v172, v76
	v_mul_f32_e32 v71, v172, v77
	s_ashr_i32 s35, s34, 31
	v_cvt_pk_fp8_f32 v68, v70, v71 op_sel:[0,0,1]
	v_mul_f32_e32 v70, v172, v80
	v_mul_f32_e32 v71, v172, v81
	s_lshl_b64 s[34:35], s[34:35], 11
	v_cvt_pk_fp8_f32 v69, v70, v71 op_sel:[0,0,1]
	ds_read_b128 v[70:73], v173 offset:4224
	ds_read_b128 v[74:77], v173 offset:4240
	s_add_u32 s15, s28, s34
	s_addc_u32 s46, s27, s35
	s_and_b64 s[34:35], s[8:9], exec
	s_cselect_b32 s11, s11, s15
	s_cselect_b32 s35, s39, s46
	s_add_u32 s34, s11, s26
	s_waitcnt lgkmcnt(1)
	v_mul_f32_e32 v83, v172, v70
	v_mul_f32_e32 v71, v172, v71
	v_mov_b32_e32 v70, 0
	v_lshlrev_b32_e32 v130, 4, v129
	s_addc_u32 s35, s35, 0
	v_cvt_pk_fp8_f32 v70, v83, v71
	v_lshl_add_u64 v[78:79], s[34:35], 0, v[130:131]
	v_lshlrev_b32_e32 v136, s14, v128
	v_mov_b32_e32 v137, v131
	v_lshl_add_u64 v[80:81], v[78:79], 0, v[136:137]
	global_store_dwordx4 v[80:81], v[66:69], off nt
	v_mov_b32_e32 v71, 0
	v_or_b32_e32 v82, 8, v128
	v_mul_f32_e32 v66, v172, v72
	v_mul_f32_e32 v67, v172, v73
	v_cvt_pk_fp8_f32 v70, v66, v67 op_sel:[0,0,1]
	s_waitcnt lgkmcnt(0)
	v_mul_f32_e32 v66, v172, v74
	v_mul_f32_e32 v67, v172, v75
	v_cvt_pk_fp8_f32 v71, v66, v67
	ds_read_b128 v[66:69], v173 offset:4256
	v_mul_f32_e32 v72, v172, v76
	v_mul_f32_e32 v73, v172, v77
	ds_read_b128 v[74:77], v173 offset:4272
	v_cvt_pk_fp8_f32 v71, v72, v73 op_sel:[0,0,1]
	s_waitcnt lgkmcnt(1)
	v_mul_f32_e32 v66, v172, v66
	v_mul_f32_e32 v67, v172, v67
	v_mov_b32_e32 v72, 0
	v_cvt_pk_fp8_f32 v72, v66, v67
	v_mul_f32_e32 v66, v172, v68
	v_mul_f32_e32 v67, v172, v69
	s_waitcnt lgkmcnt(0)
	v_mul_f32_e32 v68, v172, v74
	v_mul_f32_e32 v69, v172, v75
	v_mov_b32_e32 v73, 0
	v_cvt_pk_fp8_f32 v73, v68, v69
	v_cvt_pk_fp8_f32 v72, v66, v67 op_sel:[0,0,1]
	v_mul_f32_e32 v66, v172, v76
	v_mul_f32_e32 v67, v172, v77
	v_cvt_pk_fp8_f32 v73, v66, v67 op_sel:[0,0,1]
	ds_read_b128 v[66:69], v173 offset:8448
	v_lshlrev_b32_e32 v134, s14, v82
	v_mov_b32_e32 v135, v131
	v_lshl_add_u64 v[74:75], v[78:79], 0, v[134:135]
	global_store_dwordx4 v[74:75], v[70:73], off nt
	ds_read_b128 v[70:73], v173 offset:8464
	s_waitcnt lgkmcnt(1)
	v_mul_f32_e32 v74, v172, v66
	v_mul_f32_e32 v67, v172, v67
	v_mov_b32_e32 v66, 0
	v_cvt_pk_fp8_f32 v66, v74, v67
	v_mul_f32_e32 v67, v172, v68
	v_mul_f32_e32 v68, v172, v69
	s_waitcnt lgkmcnt(0)
	v_mul_f32_e32 v69, v172, v71
	v_cvt_pk_fp8_f32 v66, v67, v68 op_sel:[0,0,1]
	v_mul_f32_e32 v68, v172, v70
	v_mov_b32_e32 v67, 0
	v_cvt_pk_fp8_f32 v67, v68, v69
	ds_read_b128 v[68:71], v173 offset:8480
	v_mul_f32_e32 v72, v172, v72
	v_mul_f32_e32 v73, v172, v73
	v_cvt_pk_fp8_f32 v67, v72, v73 op_sel:[0,0,1]
	ds_read_b128 v[72:75], v173 offset:8496
	s_waitcnt lgkmcnt(1)
	v_mul_f32_e32 v77, v172, v68
	v_mul_f32_e32 v69, v172, v69
	v_mov_b32_e32 v68, 0
	v_cvt_pk_fp8_f32 v68, v77, v69
	s_waitcnt lgkmcnt(0)
	v_mul_f32_e32 v72, v172, v72
	v_mul_f32_e32 v73, v172, v73
	v_mov_b32_e32 v69, 0
	v_cvt_pk_fp8_f32 v69, v72, v73
	v_mul_f32_e32 v70, v172, v70
	v_mul_f32_e32 v71, v172, v71
	v_cvt_pk_fp8_f32 v68, v70, v71 op_sel:[0,0,1]
	v_mul_f32_e32 v70, v172, v74
	v_mul_f32_e32 v71, v172, v75
	v_cvt_pk_fp8_f32 v69, v70, v71 op_sel:[0,0,1]
	ds_read_b128 v[70:73], v173 offset:12672
	v_or_b32_e32 v76, 16, v128
	v_lshlrev_b32_e32 v132, s14, v76
	v_mov_b32_e32 v133, v131
	v_lshl_add_u64 v[74:75], v[78:79], 0, v[132:133]
	global_store_dwordx4 v[74:75], v[66:69], off nt
	ds_read_b128 v[66:69], v173 offset:12688
	s_waitcnt lgkmcnt(1)
	v_mul_f32_e32 v74, v172, v70
	v_mul_f32_e32 v71, v172, v71
	v_mov_b32_e32 v70, 0
	v_cvt_pk_fp8_f32 v70, v74, v71
	v_mul_f32_e32 v71, v172, v72
	v_mul_f32_e32 v72, v172, v73
	s_waitcnt lgkmcnt(0)
	v_mul_f32_e32 v66, v172, v66
	v_cvt_pk_fp8_f32 v70, v71, v72 op_sel:[0,0,1]
	v_mul_f32_e32 v67, v172, v67
	v_mov_b32_e32 v71, 0
	v_cvt_pk_fp8_f32 v71, v66, v67
	ds_read_b128 v[72:75], v173 offset:12704
	v_mul_f32_e32 v66, v172, v68
	v_mul_f32_e32 v67, v172, v69
	v_cvt_pk_fp8_f32 v71, v66, v67 op_sel:[0,0,1]
	ds_read_b128 v[66:69], v173 offset:12720
	s_waitcnt lgkmcnt(1)
	v_mul_f32_e32 v77, v172, v72
	v_mul_f32_e32 v73, v172, v73
	v_mov_b32_e32 v72, 0
	v_cvt_pk_fp8_f32 v72, v77, v73
	s_waitcnt lgkmcnt(0)
	v_mul_f32_e32 v66, v172, v66
	v_mul_f32_e32 v67, v172, v67
	v_mov_b32_e32 v73, 0
	v_cvt_pk_fp8_f32 v73, v66, v67
	v_mul_f32_e32 v74, v172, v74
	v_mul_f32_e32 v75, v172, v75
	v_mul_f32_e32 v66, v172, v68
	v_mul_f32_e32 v67, v172, v69
	v_cvt_pk_fp8_f32 v72, v74, v75 op_sel:[0,0,1]
	v_cvt_pk_fp8_f32 v73, v66, v67 op_sel:[0,0,1]
	v_or_b32_e32 v76, 24, v128
	v_lshlrev_b32_e32 v138, s14, v76
	v_mov_b32_e32 v139, v131
	v_lshl_add_u64 v[66:67], v[78:79], 0, v[138:139]
	global_store_dwordx4 v[66:67], v[70:73], off nt
	s_waitcnt lgkmcnt(0)
	global_load_dwordx4 v[114:117], v[142:143], off offset:2048 nt
	global_load_dwordx4 v[118:121], v[140:141], off offset:2048 nt
	global_load_dwordx4 v[122:125], v[144:145], off offset:2048 nt
	global_load_dwordx4 v[126:129], v[146:147], off offset:2048 nt
	global_load_dwordx4 v[98:101], v[148:149], off offset:2048 nt
	global_load_dwordx4 v[102:105], v[150:151], off offset:2048 nt
	global_load_dwordx4 v[106:109], v[152:153], off offset:2048 nt
	global_load_dwordx4 v[110:113], v[154:155], off offset:2048 nt
	global_load_dwordx4 v[82:85], v[156:157], off offset:2048 nt
	global_load_dwordx4 v[86:89], v[158:159], off offset:2048 nt
	global_load_dwordx4 v[90:93], v[160:161], off offset:2048 nt
	global_load_dwordx4 v[94:97], v[162:163], off offset:2048 nt
	global_load_dwordx4 v[66:69], v[164:165], off offset:2048 nt
	global_load_dwordx4 v[70:73], v[166:167], off offset:2048 nt
	global_load_dwordx4 v[74:77], v[168:169], off offset:2048 nt
	global_load_dwordx4 v[78:81], v[170:171], off offset:2048 nt
	s_waitcnt vmcnt(33)
	ds_write2_b32 v174, v50, v58 offset1:8
	s_waitcnt vmcnt(32)
	ds_write2_b32 v174, v54, v62 offset0:64 offset1:72
	ds_write2_b32 v174, v51, v59 offset0:132 offset1:140
	ds_write2_b32 v174, v55, v63 offset0:196 offset1:204
	ds_write2_b32 v175, v52, v60 offset0:8 offset1:16
	ds_write2_b32 v175, v56, v64 offset0:72 offset1:80
	ds_write2_b32 v175, v53, v61 offset0:140 offset1:148
	ds_write2_b32 v175, v57, v65 offset0:204 offset1:212
	s_waitcnt vmcnt(29)
	ds_write2_b32 v174, v34, v42 offset0:16 offset1:24
	s_waitcnt vmcnt(28)
	ds_write2_b32 v174, v38, v46 offset0:80 offset1:88
	ds_write2_b32 v174, v35, v43 offset0:148 offset1:156
	ds_write2_b32 v174, v39, v47 offset0:212 offset1:220
	ds_write2_b32 v175, v36, v44 offset0:24 offset1:32
	ds_write2_b32 v175, v40, v48 offset0:88 offset1:96
	ds_write2_b32 v175, v37, v45 offset0:156 offset1:164
	ds_write2_b32 v175, v41, v49 offset0:220 offset1:228
	s_waitcnt vmcnt(25)
	ds_write2_b32 v174, v18, v26 offset0:32 offset1:40
	s_waitcnt vmcnt(24)
	ds_write2_b32 v174, v22, v30 offset0:96 offset1:104
	ds_write2_b32 v174, v19, v27 offset0:164 offset1:172
	ds_write2_b32 v174, v23, v31 offset0:228 offset1:236
	ds_write2_b32 v175, v20, v28 offset0:40 offset1:48
	ds_write2_b32 v175, v24, v32 offset0:104 offset1:112
	ds_write2_b32 v175, v21, v29 offset0:172 offset1:180
	ds_write2_b32 v175, v25, v33 offset0:236 offset1:244
	s_waitcnt vmcnt(21)
	ds_write2_b32 v174, v2, v10 offset0:48 offset1:56
	s_waitcnt vmcnt(20)
	ds_write2_b32 v174, v6, v14 offset0:112 offset1:120
	ds_write2_b32 v174, v3, v11 offset0:180 offset1:188
	ds_write2_b32 v174, v7, v15 offset0:244 offset1:252
	ds_write2_b32 v175, v4, v12 offset0:56 offset1:64
	ds_write2_b32 v175, v8, v16 offset0:120 offset1:128
	ds_write2_b32 v175, v5, v13 offset0:188 offset1:196
	ds_write2_b32 v176, v9, v17 offset0:124 offset1:132
	s_waitcnt lgkmcnt(0)
	ds_read_b128 v[2:5], v173
	ds_read_b128 v[6:9], v173 offset:16
	ds_read_b128 v[10:13], v173 offset:32
	ds_read_b128 v[14:17], v173 offset:48
	s_add_i32 s14, s10, 0x200
	s_ashr_i32 s15, s14, 31
	s_waitcnt lgkmcnt(2)
	v_mul_f32_e32 v6, v172, v6
	v_mul_f32_e32 v18, v172, v2
	v_mul_f32_e32 v3, v172, v3
	v_mov_b32_e32 v2, 0
	v_cvt_pk_fp8_f32 v2, v18, v3
	v_mul_f32_e32 v7, v172, v7
	v_mov_b32_e32 v3, 0
	v_cvt_pk_fp8_f32 v3, v6, v7
	v_mul_f32_e32 v4, v172, v4
	v_mul_f32_e32 v5, v172, v5
	s_lshl_b64 s[34:35], s[12:13], 10
	v_cvt_pk_fp8_f32 v2, v4, v5 op_sel:[0,0,1]
	v_mul_f32_e32 v4, v172, v8
	v_mul_f32_e32 v5, v172, v9
	s_add_u32 s11, s29, s34
	v_cvt_pk_fp8_f32 v3, v4, v5 op_sel:[0,0,1]
	s_waitcnt lgkmcnt(1)
	v_mul_f32_e32 v5, v172, v10
	v_mul_f32_e32 v6, v172, v11
	v_mov_b32_e32 v4, 0
	s_addc_u32 s34, s30, s35
	s_lshl_b32 s12, s12, 1
	v_cvt_pk_fp8_f32 v4, v5, v6
	s_waitcnt lgkmcnt(0)
	v_mul_f32_e32 v8, v172, v14
	v_mul_f32_e32 v9, v172, v15
	v_mov_b32_e32 v5, 0
	s_and_b32 s12, s12, 0xffffff00
	v_cvt_pk_fp8_f32 v5, v8, v9
	s_add_i32 s12, s12, s31
	s_or_b32 s12, s12, s33
	v_mul_f32_e32 v6, v172, v12
	v_mul_f32_e32 v7, v172, v13
	s_ashr_i32 s13, s12, 31
	v_cvt_pk_fp8_f32 v4, v6, v7 op_sel:[0,0,1]
	v_mul_f32_e32 v6, v172, v16
	v_mul_f32_e32 v7, v172, v17
	s_lshl_b64 s[12:13], s[12:13], 11
	v_cvt_pk_fp8_f32 v5, v6, v7 op_sel:[0,0,1]
	ds_read_b128 v[6:9], v173 offset:4224
	ds_read_b128 v[10:13], v173 offset:4240
	s_add_u32 s35, s28, s12
	s_addc_u32 s38, s27, s13
	s_and_b64 s[12:13], s[8:9], exec
	s_cselect_b32 s11, s11, s35
	s_cselect_b32 s13, s34, s38
	s_add_u32 s12, s11, s26
	s_waitcnt lgkmcnt(1)
	v_mul_f32_e32 v18, v172, v6
	v_mul_f32_e32 v7, v172, v7
	v_mov_b32_e32 v6, 0
	s_addc_u32 s13, s13, 0
	v_cvt_pk_fp8_f32 v6, v18, v7
	v_lshl_add_u64 v[16:17], s[12:13], 0, v[130:131]
	v_lshl_add_u64 v[14:15], v[16:17], 0, v[136:137]
	global_store_dwordx4 v[14:15], v[2:5], off nt
	v_mov_b32_e32 v7, 0
	s_waitcnt lgkmcnt(0)
	v_mul_f32_e32 v14, v172, v13
	v_mul_f32_e32 v2, v172, v8
	v_mul_f32_e32 v3, v172, v9
	v_cvt_pk_fp8_f32 v6, v2, v3 op_sel:[0,0,1]
	ds_read_b128 v[2:5], v173 offset:4256
	v_mul_f32_e32 v8, v172, v10
	v_mul_f32_e32 v9, v172, v11
	v_cvt_pk_fp8_f32 v7, v8, v9
	v_mul_f32_e32 v9, v172, v12
	ds_read_b128 v[10:13], v173 offset:4272
	s_waitcnt lgkmcnt(1)
	v_mul_f32_e32 v2, v172, v2
	v_mul_f32_e32 v3, v172, v3
	v_mov_b32_e32 v8, 0
	v_cvt_pk_fp8_f32 v8, v2, v3
	v_mul_f32_e32 v2, v172, v4
	v_mul_f32_e32 v3, v172, v5
	v_cvt_pk_fp8_f32 v7, v9, v14 op_sel:[0,0,1]
	v_cvt_pk_fp8_f32 v8, v2, v3 op_sel:[0,0,1]
	s_waitcnt lgkmcnt(0)
	v_mul_f32_e32 v2, v172, v10
	v_mul_f32_e32 v3, v172, v11
	v_mov_b32_e32 v9, 0
	v_cvt_pk_fp8_f32 v9, v2, v3
	ds_read_b128 v[2:5], v173 offset:8448
	v_mul_f32_e32 v10, v172, v12
	v_mul_f32_e32 v11, v172, v13
	v_cvt_pk_fp8_f32 v9, v10, v11 op_sel:[0,0,1]
	ds_read_b128 v[10:13], v173 offset:8464
	s_waitcnt lgkmcnt(1)
	v_mul_f32_e32 v18, v172, v2
	v_mul_f32_e32 v3, v172, v3
	v_mov_b32_e32 v2, 0
	v_cvt_pk_fp8_f32 v2, v18, v3
	v_lshl_add_u64 v[14:15], v[16:17], 0, v[134:135]
	v_mul_f32_e32 v3, v172, v4
	v_mul_f32_e32 v4, v172, v5
	global_store_dwordx4 v[14:15], v[6:9], off nt
	v_cvt_pk_fp8_f32 v2, v3, v4 op_sel:[0,0,1]
	ds_read_b128 v[4:7], v173 offset:8480
	s_waitcnt lgkmcnt(1)
	v_mul_f32_e32 v8, v172, v10
	v_mul_f32_e32 v9, v172, v11
	v_mov_b32_e32 v3, 0
	v_cvt_pk_fp8_f32 v3, v8, v9
	ds_read_b128 v[8:11], v173 offset:8496
	s_waitcnt lgkmcnt(1)
	v_mul_f32_e32 v14, v172, v4
	v_mul_f32_e32 v5, v172, v5
	v_mov_b32_e32 v4, 0
	v_cvt_pk_fp8_f32 v4, v14, v5
	v_mul_f32_e32 v12, v172, v12
	v_mul_f32_e32 v13, v172, v13
	v_mul_f32_e32 v5, v172, v6
	v_mul_f32_e32 v6, v172, v7
	v_cvt_pk_fp8_f32 v3, v12, v13 op_sel:[0,0,1]
	v_cvt_pk_fp8_f32 v4, v5, v6 op_sel:[0,0,1]
	s_waitcnt lgkmcnt(0)
	v_mul_f32_e32 v12, v172, v8
	v_mul_f32_e32 v13, v172, v9
	ds_read_b128 v[6:9], v173 offset:12672
	v_mov_b32_e32 v5, 0
	v_cvt_pk_fp8_f32 v5, v12, v13
	v_mul_f32_e32 v14, v172, v10
	v_mul_f32_e32 v15, v172, v11
	ds_read_b128 v[10:13], v173 offset:12688
	s_waitcnt lgkmcnt(1)
	v_mul_f32_e32 v18, v172, v6
	v_mul_f32_e32 v7, v172, v7
	v_mov_b32_e32 v6, 0
	v_cvt_pk_fp8_f32 v6, v18, v7
	v_mul_f32_e32 v7, v172, v8
	v_mul_f32_e32 v8, v172, v9
	s_waitcnt lgkmcnt(0)
	v_mul_f32_e32 v9, v172, v11
	v_cvt_pk_fp8_f32 v6, v7, v8 op_sel:[0,0,1]
	v_mul_f32_e32 v8, v172, v10
	v_mov_b32_e32 v7, 0
	v_cvt_pk_fp8_f32 v7, v8, v9
	ds_read_b128 v[8:11], v173 offset:12704
	v_mul_f32_e32 v12, v172, v12
	v_mul_f32_e32 v13, v172, v13
	v_cvt_pk_fp8_f32 v5, v14, v15 op_sel:[0,0,1]
	v_cvt_pk_fp8_f32 v7, v12, v13 op_sel:[0,0,1]
	ds_read_b128 v[12:15], v173 offset:12720
	s_waitcnt lgkmcnt(1)
	v_mul_f32_e32 v18, v172, v8
	v_mul_f32_e32 v9, v172, v9
	v_mov_b32_e32 v8, 0
	v_cvt_pk_fp8_f32 v8, v18, v9
	s_waitcnt lgkmcnt(0)
	v_mul_f32_e32 v12, v172, v12
	v_mul_f32_e32 v13, v172, v13
	v_mov_b32_e32 v9, 0
	v_cvt_pk_fp8_f32 v9, v12, v13
	v_mul_f32_e32 v10, v172, v10
	v_mul_f32_e32 v11, v172, v11
	v_cvt_pk_fp8_f32 v8, v10, v11 op_sel:[0,0,1]
	v_mul_f32_e32 v10, v172, v14
	v_mul_f32_e32 v11, v172, v15
	v_cvt_pk_fp8_f32 v9, v10, v11 op_sel:[0,0,1]
	v_lshl_add_u64 v[10:11], v[16:17], 0, v[132:133]
	global_store_dwordx4 v[10:11], v[2:5], off nt
	s_addk_i32 s10, 0x300
	s_ashr_i32 s11, s10, 31
	v_lshl_add_u64 v[2:3], v[16:17], 0, v[138:139]
	global_store_dwordx4 v[2:3], v[6:9], off nt
	s_waitcnt lgkmcnt(0)
	global_load_dwordx4 v[42:45], v[142:143], off offset:3072 nt
	global_load_dwordx4 v[46:49], v[140:141], off offset:3072 nt
	global_load_dwordx4 v[58:61], v[144:145], off offset:3072 nt
	global_load_dwordx4 v[62:65], v[146:147], off offset:3072 nt
	global_load_dwordx4 v[34:37], v[148:149], off offset:3072 nt
	global_load_dwordx4 v[38:41], v[150:151], off offset:3072 nt
	global_load_dwordx4 v[50:53], v[152:153], off offset:3072 nt
	global_load_dwordx4 v[54:57], v[154:155], off offset:3072 nt
	global_load_dwordx4 v[18:21], v[156:157], off offset:3072 nt
	global_load_dwordx4 v[22:25], v[158:159], off offset:3072 nt
	global_load_dwordx4 v[26:29], v[160:161], off offset:3072 nt
	global_load_dwordx4 v[30:33], v[162:163], off offset:3072 nt
	global_load_dwordx4 v[2:5], v[164:165], off offset:3072 nt
	global_load_dwordx4 v[6:9], v[166:167], off offset:3072 nt
	global_load_dwordx4 v[10:13], v[168:169], off offset:3072 nt
	global_load_dwordx4 v[14:17], v[170:171], off offset:3072 nt
	s_waitcnt vmcnt(33)
	ds_write2_b32 v174, v114, v122 offset1:8
	s_waitcnt vmcnt(32)
	ds_write2_b32 v174, v118, v126 offset0:64 offset1:72
	ds_write2_b32 v174, v115, v123 offset0:132 offset1:140
	ds_write2_b32 v174, v119, v127 offset0:196 offset1:204
	ds_write2_b32 v175, v116, v124 offset0:8 offset1:16
	ds_write2_b32 v175, v120, v128 offset0:72 offset1:80
	ds_write2_b32 v175, v117, v125 offset0:140 offset1:148
	ds_write2_b32 v175, v121, v129 offset0:204 offset1:212
	s_waitcnt vmcnt(29)
	ds_write2_b32 v174, v98, v106 offset0:16 offset1:24
	s_waitcnt vmcnt(28)
	ds_write2_b32 v174, v102, v110 offset0:80 offset1:88
	ds_write2_b32 v174, v99, v107 offset0:148 offset1:156
	ds_write2_b32 v174, v103, v111 offset0:212 offset1:220
	ds_write2_b32 v175, v100, v108 offset0:24 offset1:32
	ds_write2_b32 v175, v104, v112 offset0:88 offset1:96
	ds_write2_b32 v175, v101, v109 offset0:156 offset1:164
	ds_write2_b32 v175, v105, v113 offset0:220 offset1:228
	s_waitcnt vmcnt(25)
	ds_write2_b32 v174, v82, v90 offset0:32 offset1:40
	s_waitcnt vmcnt(24)
	ds_write2_b32 v174, v86, v94 offset0:96 offset1:104
	ds_write2_b32 v174, v83, v91 offset0:164 offset1:172
	ds_write2_b32 v174, v87, v95 offset0:228 offset1:236
	ds_write2_b32 v175, v84, v92 offset0:40 offset1:48
	ds_write2_b32 v175, v88, v96 offset0:104 offset1:112
	ds_write2_b32 v175, v85, v93 offset0:172 offset1:180
	ds_write2_b32 v175, v89, v97 offset0:236 offset1:244
	s_waitcnt vmcnt(21)
	ds_write2_b32 v174, v66, v74 offset0:48 offset1:56
	s_waitcnt vmcnt(20)
	ds_write2_b32 v174, v70, v78 offset0:112 offset1:120
	ds_write2_b32 v174, v67, v75 offset0:180 offset1:188
	ds_write2_b32 v174, v71, v79 offset0:244 offset1:252
	ds_write2_b32 v175, v68, v76 offset0:56 offset1:64
	ds_write2_b32 v175, v72, v80 offset0:120 offset1:128
	ds_write2_b32 v175, v69, v77 offset0:188 offset1:196
	ds_write2_b32 v176, v73, v81 offset0:124 offset1:132
	s_waitcnt lgkmcnt(0)
	ds_read_b128 v[66:69], v173
	ds_read_b128 v[70:73], v173 offset:16
	ds_read_b128 v[74:77], v173 offset:32
	ds_read_b128 v[78:81], v173 offset:48
	s_lshl_b64 s[12:13], s[14:15], 10
	s_add_u32 s15, s29, s12
	s_waitcnt lgkmcnt(2)
	v_mul_f32_e32 v70, v172, v70
	v_mul_f32_e32 v82, v172, v66
	v_mul_f32_e32 v67, v172, v67
	v_mov_b32_e32 v66, 0
	v_cvt_pk_fp8_f32 v66, v82, v67
	v_mul_f32_e32 v71, v172, v71
	v_mov_b32_e32 v67, 0
	v_cvt_pk_fp8_f32 v67, v70, v71
	v_mul_f32_e32 v68, v172, v68
	v_mul_f32_e32 v69, v172, v69
	v_cvt_pk_fp8_f32 v66, v68, v69 op_sel:[0,0,1]
	v_mul_f32_e32 v68, v172, v72
	v_mul_f32_e32 v69, v172, v73
	v_cvt_pk_fp8_f32 v67, v68, v69 op_sel:[0,0,1]
	s_waitcnt lgkmcnt(1)
	v_mul_f32_e32 v69, v172, v74
	v_mul_f32_e32 v70, v172, v75
	v_mov_b32_e32 v68, 0
	s_addc_u32 s34, s30, s13
	s_lshl_b32 s12, s14, 1
	v_cvt_pk_fp8_f32 v68, v69, v70
	s_waitcnt lgkmcnt(0)
	v_mul_f32_e32 v72, v172, v78
	v_mul_f32_e32 v73, v172, v79
	v_mov_b32_e32 v69, 0
	s_and_b32 s12, s12, 0xffffff00
	v_cvt_pk_fp8_f32 v69, v72, v73
	s_add_i32 s12, s12, s31
	s_or_b32 s12, s12, s33
	v_mul_f32_e32 v70, v172, v76
	v_mul_f32_e32 v71, v172, v77
	s_ashr_i32 s13, s12, 31
	v_cvt_pk_fp8_f32 v68, v70, v71 op_sel:[0,0,1]
	v_mul_f32_e32 v70, v172, v80
	v_mul_f32_e32 v71, v172, v81
	s_lshl_b64 s[12:13], s[12:13], 11
	v_cvt_pk_fp8_f32 v69, v70, v71 op_sel:[0,0,1]
	ds_read_b128 v[70:73], v173 offset:4224
	ds_read_b128 v[74:77], v173 offset:4240
	s_add_u32 s14, s28, s12
	s_addc_u32 s35, s27, s13
	s_and_b64 s[12:13], s[8:9], exec
	s_cselect_b32 s12, s15, s14
	s_cselect_b32 s13, s34, s35
	s_add_u32 s12, s12, s26
	s_waitcnt lgkmcnt(1)
	v_mul_f32_e32 v82, v172, v70
	v_mul_f32_e32 v71, v172, v71
	v_mov_b32_e32 v70, 0
	s_addc_u32 s13, s13, 0
	v_cvt_pk_fp8_f32 v70, v82, v71
	v_lshl_add_u64 v[80:81], s[12:13], 0, v[130:131]
	v_lshl_add_u64 v[78:79], v[80:81], 0, v[136:137]
	global_store_dwordx4 v[78:79], v[66:69], off nt
	v_mov_b32_e32 v71, 0
	s_waitcnt lgkmcnt(0)
	v_mul_f32_e32 v78, v172, v77
	v_mul_f32_e32 v66, v172, v72
	v_mul_f32_e32 v67, v172, v73
	v_cvt_pk_fp8_f32 v70, v66, v67 op_sel:[0,0,1]
	ds_read_b128 v[66:69], v173 offset:4256
	v_mul_f32_e32 v72, v172, v74
	v_mul_f32_e32 v73, v172, v75
	v_cvt_pk_fp8_f32 v71, v72, v73
	v_mul_f32_e32 v73, v172, v76
	ds_read_b128 v[74:77], v173 offset:4272
	s_waitcnt lgkmcnt(1)
	v_mul_f32_e32 v66, v172, v66
	v_mul_f32_e32 v67, v172, v67
	v_mov_b32_e32 v72, 0
	v_cvt_pk_fp8_f32 v72, v66, v67
	v_mul_f32_e32 v66, v172, v68
	v_mul_f32_e32 v67, v172, v69
	v_cvt_pk_fp8_f32 v71, v73, v78 op_sel:[0,0,1]
	v_cvt_pk_fp8_f32 v72, v66, v67 op_sel:[0,0,1]
	s_waitcnt lgkmcnt(0)
	v_mul_f32_e32 v66, v172, v74
	v_mul_f32_e32 v67, v172, v75
	v_mov_b32_e32 v73, 0
	v_cvt_pk_fp8_f32 v73, v66, v67
	ds_read_b128 v[66:69], v173 offset:8448
	v_mul_f32_e32 v74, v172, v76
	v_mul_f32_e32 v75, v172, v77
	v_cvt_pk_fp8_f32 v73, v74, v75 op_sel:[0,0,1]
	ds_read_b128 v[74:77], v173 offset:8464
	s_waitcnt lgkmcnt(1)
	v_mul_f32_e32 v82, v172, v66
	v_mul_f32_e32 v67, v172, v67
	v_mov_b32_e32 v66, 0
	v_cvt_pk_fp8_f32 v66, v82, v67
	v_lshl_add_u64 v[78:79], v[80:81], 0, v[134:135]
	v_mul_f32_e32 v67, v172, v68
	v_mul_f32_e32 v68, v172, v69
	global_store_dwordx4 v[78:79], v[70:73], off nt
	v_cvt_pk_fp8_f32 v66, v67, v68 op_sel:[0,0,1]
	ds_read_b128 v[68:71], v173 offset:8480
	s_waitcnt lgkmcnt(1)
	v_mul_f32_e32 v72, v172, v74
	v_mul_f32_e32 v73, v172, v75
	v_mov_b32_e32 v67, 0
	v_cvt_pk_fp8_f32 v67, v72, v73
	ds_read_b128 v[72:75], v173 offset:8496
	s_waitcnt lgkmcnt(1)
	v_mul_f32_e32 v78, v172, v68
	v_mul_f32_e32 v69, v172, v69
	v_mov_b32_e32 v68, 0
	v_cvt_pk_fp8_f32 v68, v78, v69
	v_mul_f32_e32 v76, v172, v76
	v_mul_f32_e32 v77, v172, v77
	v_mul_f32_e32 v69, v172, v70
	v_mul_f32_e32 v70, v172, v71
	v_cvt_pk_fp8_f32 v67, v76, v77 op_sel:[0,0,1]
	v_cvt_pk_fp8_f32 v68, v69, v70 op_sel:[0,0,1]
	s_waitcnt lgkmcnt(0)
	v_mul_f32_e32 v76, v172, v72
	v_mul_f32_e32 v77, v172, v73
	ds_read_b128 v[70:73], v173 offset:12672
	v_mov_b32_e32 v69, 0
	v_cvt_pk_fp8_f32 v69, v76, v77
	v_mul_f32_e32 v78, v172, v74
	v_mul_f32_e32 v79, v172, v75
	ds_read_b128 v[74:77], v173 offset:12688
	s_waitcnt lgkmcnt(1)
	v_mul_f32_e32 v82, v172, v70
	v_mul_f32_e32 v71, v172, v71
	v_mov_b32_e32 v70, 0
	v_cvt_pk_fp8_f32 v70, v82, v71
	v_mul_f32_e32 v71, v172, v72
	v_mul_f32_e32 v72, v172, v73
	s_waitcnt lgkmcnt(0)
	v_mul_f32_e32 v73, v172, v75
	v_cvt_pk_fp8_f32 v70, v71, v72 op_sel:[0,0,1]
	v_mul_f32_e32 v72, v172, v74
	v_mov_b32_e32 v71, 0
	v_cvt_pk_fp8_f32 v71, v72, v73
	ds_read_b128 v[72:75], v173 offset:12704
	v_mul_f32_e32 v76, v172, v76
	v_mul_f32_e32 v77, v172, v77
	v_cvt_pk_fp8_f32 v69, v78, v79 op_sel:[0,0,1]
	v_cvt_pk_fp8_f32 v71, v76, v77 op_sel:[0,0,1]
	ds_read_b128 v[76:79], v173 offset:12720
	s_waitcnt lgkmcnt(1)
	v_mul_f32_e32 v82, v172, v72
	v_mul_f32_e32 v73, v172, v73
	v_mov_b32_e32 v72, 0
	v_cvt_pk_fp8_f32 v72, v82, v73
	s_waitcnt lgkmcnt(0)
	v_mul_f32_e32 v76, v172, v76
	v_mul_f32_e32 v77, v172, v77
	v_mov_b32_e32 v73, 0
	v_cvt_pk_fp8_f32 v73, v76, v77
	v_mul_f32_e32 v74, v172, v74
	v_mul_f32_e32 v75, v172, v75
	v_cvt_pk_fp8_f32 v72, v74, v75 op_sel:[0,0,1]
	v_mul_f32_e32 v74, v172, v78
	v_mul_f32_e32 v75, v172, v79
	v_cvt_pk_fp8_f32 v73, v74, v75 op_sel:[0,0,1]
	v_lshl_add_u64 v[74:75], v[80:81], 0, v[132:133]
	global_store_dwordx4 v[74:75], v[66:69], off nt
	s_lshl_b64 s[12:13], s[10:11], 10
	s_add_u32 s12, s29, s12
	v_lshl_add_u64 v[66:67], v[80:81], 0, v[138:139]
	global_store_dwordx4 v[66:67], v[70:73], off nt
	s_waitcnt lgkmcnt(0)
	s_waitcnt vmcnt(17)
	ds_write2_b32 v174, v42, v58 offset1:8
	s_waitcnt vmcnt(16)
	ds_write2_b32 v174, v46, v62 offset0:64 offset1:72
	ds_write2_b32 v174, v43, v59 offset0:132 offset1:140
	ds_write2_b32 v174, v47, v63 offset0:196 offset1:204
	ds_write2_b32 v175, v44, v60 offset0:8 offset1:16
	ds_write2_b32 v175, v48, v64 offset0:72 offset1:80
	ds_write2_b32 v175, v45, v61 offset0:140 offset1:148
	ds_write2_b32 v175, v49, v65 offset0:204 offset1:212
	s_waitcnt vmcnt(13)
	ds_write2_b32 v174, v34, v50 offset0:16 offset1:24
	s_waitcnt vmcnt(12)
	ds_write2_b32 v174, v38, v54 offset0:80 offset1:88
	ds_write2_b32 v174, v35, v51 offset0:148 offset1:156
	ds_write2_b32 v174, v39, v55 offset0:212 offset1:220
	ds_write2_b32 v175, v36, v52 offset0:24 offset1:32
	ds_write2_b32 v175, v40, v56 offset0:88 offset1:96
	ds_write2_b32 v175, v37, v53 offset0:156 offset1:164
	ds_write2_b32 v175, v41, v57 offset0:220 offset1:228
	s_waitcnt vmcnt(9)
	ds_write2_b32 v174, v18, v26 offset0:32 offset1:40
	s_waitcnt vmcnt(8)
	ds_write2_b32 v174, v22, v30 offset0:96 offset1:104
	ds_write2_b32 v174, v19, v27 offset0:164 offset1:172
	ds_write2_b32 v174, v23, v31 offset0:228 offset1:236
	ds_write2_b32 v175, v20, v28 offset0:40 offset1:48
	ds_write2_b32 v175, v24, v32 offset0:104 offset1:112
	ds_write2_b32 v175, v21, v29 offset0:172 offset1:180
	ds_write2_b32 v175, v25, v33 offset0:236 offset1:244
	s_waitcnt vmcnt(5)
	ds_write2_b32 v174, v2, v10 offset0:48 offset1:56
	s_waitcnt vmcnt(4)
	ds_write2_b32 v174, v6, v14 offset0:112 offset1:120
	ds_write2_b32 v174, v3, v11 offset0:180 offset1:188
	ds_write2_b32 v174, v7, v15 offset0:244 offset1:252
	ds_write2_b32 v175, v4, v12 offset0:56 offset1:64
	ds_write2_b32 v175, v8, v16 offset0:120 offset1:128
	ds_write2_b32 v175, v5, v13 offset0:188 offset1:196
	ds_write2_b32 v176, v9, v17 offset0:124 offset1:132
	s_waitcnt lgkmcnt(0)
	ds_read_b128 v[2:5], v173
	ds_read_b128 v[6:9], v173 offset:16
	ds_read_b128 v[10:13], v173 offset:32
	ds_read_b128 v[14:17], v173 offset:48
	s_addc_u32 s13, s30, s13
	s_lshl_b32 s10, s10, 1
	s_waitcnt lgkmcnt(2)
	v_mul_f32_e32 v6, v172, v6
	v_mul_f32_e32 v18, v172, v2
	v_mul_f32_e32 v3, v172, v3
	v_mov_b32_e32 v2, 0
	v_cvt_pk_fp8_f32 v2, v18, v3
	v_mul_f32_e32 v7, v172, v7
	v_mov_b32_e32 v3, 0
	v_cvt_pk_fp8_f32 v3, v6, v7
	v_mul_f32_e32 v4, v172, v4
	v_mul_f32_e32 v5, v172, v5
	v_cvt_pk_fp8_f32 v2, v4, v5 op_sel:[0,0,1]
	v_mul_f32_e32 v4, v172, v8
	v_mul_f32_e32 v5, v172, v9
	v_cvt_pk_fp8_f32 v3, v4, v5 op_sel:[0,0,1]
	s_waitcnt lgkmcnt(1)
	v_mul_f32_e32 v5, v172, v10
	v_mul_f32_e32 v6, v172, v11
	v_mov_b32_e32 v4, 0
	v_cvt_pk_fp8_f32 v4, v5, v6
	s_waitcnt lgkmcnt(0)
	v_mul_f32_e32 v8, v172, v14
	v_mul_f32_e32 v9, v172, v15
	v_mov_b32_e32 v5, 0
	s_and_b32 s10, s10, 0xffffff00
	v_cvt_pk_fp8_f32 v5, v8, v9
	s_add_i32 s10, s10, s31
	s_or_b32 s10, s10, s33
	v_mul_f32_e32 v6, v172, v12
	v_mul_f32_e32 v7, v172, v13
	s_ashr_i32 s11, s10, 31
	v_cvt_pk_fp8_f32 v4, v6, v7 op_sel:[0,0,1]
	v_mul_f32_e32 v6, v172, v16
	v_mul_f32_e32 v7, v172, v17
	s_lshl_b64 s[10:11], s[10:11], 11
	v_cvt_pk_fp8_f32 v5, v6, v7 op_sel:[0,0,1]
	ds_read_b128 v[6:9], v173 offset:4224
	ds_read_b128 v[10:13], v173 offset:4240
	s_add_u32 s10, s28, s10
	s_addc_u32 s11, s27, s11
	s_and_b64 s[8:9], s[8:9], exec
	s_cselect_b32 s8, s12, s10
	s_cselect_b32 s9, s13, s11
	s_add_u32 s8, s8, s26
	s_waitcnt lgkmcnt(1)
	v_mul_f32_e32 v18, v172, v6
	v_mul_f32_e32 v7, v172, v7
	v_mov_b32_e32 v6, 0
	s_addc_u32 s9, s9, 0
	v_cvt_pk_fp8_f32 v6, v18, v7
	v_lshl_add_u64 v[16:17], s[8:9], 0, v[130:131]
	v_lshl_add_u64 v[14:15], v[16:17], 0, v[136:137]
	global_store_dwordx4 v[14:15], v[2:5], off nt
	v_mov_b32_e32 v7, 0
	s_waitcnt lgkmcnt(0)
	v_mul_f32_e32 v14, v172, v13
	v_mul_f32_e32 v2, v172, v8
	v_mul_f32_e32 v3, v172, v9
	v_cvt_pk_fp8_f32 v6, v2, v3 op_sel:[0,0,1]
	ds_read_b128 v[2:5], v173 offset:4256
	v_mul_f32_e32 v8, v172, v10
	v_mul_f32_e32 v9, v172, v11
	v_cvt_pk_fp8_f32 v7, v8, v9
	v_mul_f32_e32 v9, v172, v12
	ds_read_b128 v[10:13], v173 offset:4272
	s_waitcnt lgkmcnt(1)
	v_mul_f32_e32 v2, v172, v2
	v_mul_f32_e32 v3, v172, v3
	v_mov_b32_e32 v8, 0
	v_cvt_pk_fp8_f32 v8, v2, v3
	v_mul_f32_e32 v2, v172, v4
	v_mul_f32_e32 v3, v172, v5
	v_cvt_pk_fp8_f32 v7, v9, v14 op_sel:[0,0,1]
	v_cvt_pk_fp8_f32 v8, v2, v3 op_sel:[0,0,1]
	s_waitcnt lgkmcnt(0)
	v_mul_f32_e32 v2, v172, v10
	v_mul_f32_e32 v3, v172, v11
	v_mov_b32_e32 v9, 0
	v_cvt_pk_fp8_f32 v9, v2, v3
	ds_read_b128 v[2:5], v173 offset:8448
	v_mul_f32_e32 v10, v172, v12
	v_mul_f32_e32 v11, v172, v13
	v_cvt_pk_fp8_f32 v9, v10, v11 op_sel:[0,0,1]
	ds_read_b128 v[10:13], v173 offset:8464
	s_waitcnt lgkmcnt(1)
	v_mul_f32_e32 v18, v172, v2
	v_mul_f32_e32 v3, v172, v3
	v_mov_b32_e32 v2, 0
	v_cvt_pk_fp8_f32 v2, v18, v3
	v_lshl_add_u64 v[14:15], v[16:17], 0, v[134:135]
	v_mul_f32_e32 v3, v172, v4
	v_mul_f32_e32 v4, v172, v5
	global_store_dwordx4 v[14:15], v[6:9], off nt
	v_cvt_pk_fp8_f32 v2, v3, v4 op_sel:[0,0,1]
	ds_read_b128 v[4:7], v173 offset:8480
	s_waitcnt lgkmcnt(1)
	v_mul_f32_e32 v8, v172, v10
	v_mul_f32_e32 v9, v172, v11
	v_mov_b32_e32 v3, 0
	v_cvt_pk_fp8_f32 v3, v8, v9
	ds_read_b128 v[8:11], v173 offset:8496
	s_waitcnt lgkmcnt(1)
	v_mul_f32_e32 v14, v172, v4
	v_mul_f32_e32 v5, v172, v5
	v_mov_b32_e32 v4, 0
	v_cvt_pk_fp8_f32 v4, v14, v5
	v_mul_f32_e32 v12, v172, v12
	v_mul_f32_e32 v13, v172, v13
	v_mul_f32_e32 v5, v172, v6
	v_mul_f32_e32 v6, v172, v7
	v_cvt_pk_fp8_f32 v3, v12, v13 op_sel:[0,0,1]
	v_cvt_pk_fp8_f32 v4, v5, v6 op_sel:[0,0,1]
	s_waitcnt lgkmcnt(0)
	v_mul_f32_e32 v12, v172, v8
	v_mul_f32_e32 v13, v172, v9
	ds_read_b128 v[6:9], v173 offset:12672
	v_mov_b32_e32 v5, 0
	v_cvt_pk_fp8_f32 v5, v12, v13
	v_mul_f32_e32 v14, v172, v10
	v_mul_f32_e32 v15, v172, v11
	ds_read_b128 v[10:13], v173 offset:12688
	s_waitcnt lgkmcnt(1)
	v_mul_f32_e32 v18, v172, v6
	v_mul_f32_e32 v7, v172, v7
	v_mov_b32_e32 v6, 0
	v_cvt_pk_fp8_f32 v6, v18, v7
	v_mul_f32_e32 v7, v172, v8
	v_mul_f32_e32 v8, v172, v9
	s_waitcnt lgkmcnt(0)
	v_mul_f32_e32 v9, v172, v11
	v_cvt_pk_fp8_f32 v6, v7, v8 op_sel:[0,0,1]
	v_mul_f32_e32 v8, v172, v10
	v_mov_b32_e32 v7, 0
	v_cvt_pk_fp8_f32 v7, v8, v9
	ds_read_b128 v[8:11], v173 offset:12704
	v_mul_f32_e32 v12, v172, v12
	v_mul_f32_e32 v13, v172, v13
	v_cvt_pk_fp8_f32 v5, v14, v15 op_sel:[0,0,1]
	v_cvt_pk_fp8_f32 v7, v12, v13 op_sel:[0,0,1]
	ds_read_b128 v[12:15], v173 offset:12720
	s_waitcnt lgkmcnt(1)
	v_mul_f32_e32 v18, v172, v8
	v_mul_f32_e32 v9, v172, v9
	v_mov_b32_e32 v8, 0
	v_cvt_pk_fp8_f32 v8, v18, v9
	s_waitcnt lgkmcnt(0)
	v_mul_f32_e32 v12, v172, v12
	v_mul_f32_e32 v13, v172, v13
	v_mov_b32_e32 v9, 0
	v_cvt_pk_fp8_f32 v9, v12, v13
	v_mul_f32_e32 v10, v172, v10
	v_mul_f32_e32 v11, v172, v11
	v_cvt_pk_fp8_f32 v8, v10, v11 op_sel:[0,0,1]
	v_mul_f32_e32 v10, v172, v14
	v_mul_f32_e32 v11, v172, v15
	v_cvt_pk_fp8_f32 v9, v10, v11 op_sel:[0,0,1]
	v_lshl_add_u64 v[10:11], v[16:17], 0, v[132:133]
	global_store_dwordx4 v[10:11], v[2:5], off nt
	s_nop 1
	v_lshl_add_u64 v[2:3], v[16:17], 0, v[138:139]
	global_store_dwordx4 v[2:3], v[6:9], off nt
	s_waitcnt lgkmcnt(0)
	s_barrier
	s_and_saveexec_b64 s[8:9], s[36:37]
	s_cbranch_execz .LBB0_1437
	v_mov_b32_e32 v2, s16
	s_waitcnt vmcnt(0)
	ds_write_b32 v2, v255
	s_branch .LBB0_1437

.LBB0_2292:
	s_or_b64 exec, exec, s[6:7]
	s_lshl_b32 s6, s46, 6
	v_mov_b32 v132, v0
	s_and_b32 s6, s6, 0x3c00
	v_readfirstlane_b32 s13, v132
	s_ashr_i32 s11, s13, 6
	s_ashr_i32 s12, s46, 8
	s_or_b32 s48, s6, 0x4000
	s_cmp_eq_u32 s12, 1
	s_cselect_b32 s6, s19, 0xd8
	s_cmpk_lt_u32 s46, 0x100
	s_cselect_b32 s7, 16, 0x90
	s_cselect_b32 s10, 0xc8, s6
	s_add_u32 s6, s15, s7
	s_addc_u32 s7, s16, 0
	s_lshr_b32 s47, s48, 8
	v_mov_b32_e32 v2, s47
	global_load_dword v4, v2, s[6:7] sc1
	s_add_u32 s6, s0, s10
	s_addc_u32 s7, s1, 0
	s_load_dwordx2 s[6:7], s[6:7], 0x0
	s_lshl_b32 s10, s46, 7
	s_mul_i32 s46, s11, 0x4400
	s_and_b32 s10, s10, 0x780
	s_add_i32 s49, s46, 0
	s_lshl_b32 s46, s48, 13
	v_bfe_u32 v133, v132, 3, 3
	s_waitcnt lgkmcnt(0)
	s_add_u32 s6, s6, s46
	v_or_b32_e32 v2, s10, v133
	s_addc_u32 s7, s7, 0
	v_lshlrev_b32_e32 v130, 12, v2
	v_lshlrev_b32_e32 v5, 4, v132
	v_lshl_add_u64 v[2:3], s[6:7], 0, v[130:131]
	v_and_b32_e32 v130, 0x70, v5
	s_lshl_b32 s6, s11, 5
	v_lshl_add_u64 v[2:3], v[2:3], 0, v[130:131]
	s_ashr_i32 s7, s6, 31
	v_lshl_add_u64 v[142:143], s[6:7], 2, v[2:3]
	v_add_co_u32_e32 v140, vcc, s21, v142
	global_load_dwordx4 v[66:69], v[142:143], off nt
	s_nop 0
	v_addc_co_u32_e32 v141, vcc, 0, v143, vcc
	v_add_co_u32_e32 v144, vcc, s22, v142
	global_load_dwordx4 v[70:73], v[140:141], off nt
	s_nop 0
	v_addc_co_u32_e32 v145, vcc, 0, v143, vcc
	v_add_co_u32_e32 v146, vcc, s23, v142
	global_load_dwordx4 v[74:77], v[144:145], off nt
	s_nop 0
	v_addc_co_u32_e32 v147, vcc, 0, v143, vcc
	v_add_co_u32_e32 v148, vcc, s24, v142
	global_load_dwordx4 v[78:81], v[146:147], off nt
	s_nop 0
	v_addc_co_u32_e32 v149, vcc, 0, v143, vcc
	v_add_co_u32_e32 v150, vcc, s25, v142
	global_load_dwordx4 v[82:85], v[148:149], off nt
	s_nop 0
	v_addc_co_u32_e32 v151, vcc, 0, v143, vcc
	v_add_co_u32_e32 v152, vcc, s26, v142
	global_load_dwordx4 v[86:89], v[150:151], off nt
	s_nop 0
	v_addc_co_u32_e32 v153, vcc, 0, v143, vcc
	v_add_co_u32_e32 v154, vcc, s27, v142
	global_load_dwordx4 v[90:93], v[152:153], off nt
	s_nop 0
	v_addc_co_u32_e32 v155, vcc, 0, v143, vcc
	v_add_co_u32_e32 v156, vcc, s28, v142
	global_load_dwordx4 v[94:97], v[154:155], off nt
	s_nop 0
	v_addc_co_u32_e32 v157, vcc, 0, v143, vcc
	v_add_co_u32_e32 v158, vcc, s29, v142
	global_load_dwordx4 v[98:101], v[156:157], off nt
	s_nop 0
	v_addc_co_u32_e32 v159, vcc, 0, v143, vcc
	v_add_co_u32_e32 v160, vcc, s30, v142
	global_load_dwordx4 v[102:105], v[158:159], off nt
	s_nop 0
	v_addc_co_u32_e32 v161, vcc, 0, v143, vcc
	v_add_co_u32_e32 v162, vcc, s31, v142
	global_load_dwordx4 v[106:109], v[160:161], off nt
	s_nop 0
	v_addc_co_u32_e32 v163, vcc, 0, v143, vcc
	v_add_co_u32_e32 v164, vcc, s33, v142
	global_load_dwordx4 v[110:113], v[162:163], off nt
	s_nop 0
	v_addc_co_u32_e32 v165, vcc, 0, v143, vcc
	v_add_co_u32_e32 v166, vcc, s34, v142
	global_load_dwordx4 v[114:117], v[164:165], off nt
	s_nop 0
	v_addc_co_u32_e32 v167, vcc, 0, v143, vcc
	v_add_co_u32_e32 v168, vcc, s35, v142
	global_load_dwordx4 v[118:121], v[166:167], off nt
	s_nop 0
	v_addc_co_u32_e32 v169, vcc, 0, v143, vcc
	v_add_co_u32_e32 v170, vcc, s38, v142
	global_load_dwordx4 v[122:125], v[168:169], off nt
	s_nop 0
	v_addc_co_u32_e32 v171, vcc, 0, v143, vcc
	global_load_dwordx4 v[126:129], v[170:171], off nt
	s_waitcnt vmcnt(16)
	v_div_scale_f32 v2, s[46:47], v4, v4, s20
	v_rcp_f32_e32 v3, v2
	v_and_b32_e32 v130, 7, v132
	v_mul_u32_u24_e32 v132, 0x840, v130
	v_lshlrev_b32_e32 v134, 2, v133
	v_fma_f32 v5, -v2, v3, 1.0
	v_fmac_f32_e32 v3, v5, v3
	v_div_scale_f32 v5, vcc, s20, v4, s20
	v_mul_f32_e32 v6, v5, v3
	v_fma_f32 v7, -v2, v6, v5
	v_fmac_f32_e32 v6, v7, v3
	v_fma_f32 v2, -v2, v6, v5
	v_div_fmas_f32 v2, v2, v3, v6
	v_add3_u32 v174, s49, v132, v134
	v_div_fixup_f32 v2, v2, v4, s20
	v_cmp_lt_f32_e32 vcc, 0, v4
	v_add_u32_e32 v175, 0x400, v174
	v_add_u32_e32 v176, 0x600, v174
	v_cndmask_b32_e32 v172, 0, v2, vcc
	global_load_dwordx4 v[50:53], v[142:143], off offset:1024 nt
	global_load_dwordx4 v[54:57], v[140:141], off offset:1024 nt
	global_load_dwordx4 v[58:61], v[144:145], off offset:1024 nt
	global_load_dwordx4 v[62:65], v[146:147], off offset:1024 nt
	global_load_dwordx4 v[34:37], v[148:149], off offset:1024 nt
	global_load_dwordx4 v[38:41], v[150:151], off offset:1024 nt
	global_load_dwordx4 v[42:45], v[152:153], off offset:1024 nt
	global_load_dwordx4 v[46:49], v[154:155], off offset:1024 nt
	global_load_dwordx4 v[18:21], v[156:157], off offset:1024 nt
	global_load_dwordx4 v[22:25], v[158:159], off offset:1024 nt
	global_load_dwordx4 v[26:29], v[160:161], off offset:1024 nt
	global_load_dwordx4 v[30:33], v[162:163], off offset:1024 nt
	global_load_dwordx4 v[2:5], v[164:165], off offset:1024 nt
	global_load_dwordx4 v[6:9], v[166:167], off offset:1024 nt
	global_load_dwordx4 v[10:13], v[168:169], off offset:1024 nt
	global_load_dwordx4 v[14:17], v[170:171], off offset:1024 nt
	s_waitcnt vmcnt(29)
	ds_write2_b32 v174, v66, v74 offset1:8
	s_waitcnt vmcnt(28)
	ds_write2_b32 v174, v70, v78 offset0:64 offset1:72
	ds_write2_b32 v174, v67, v75 offset0:132 offset1:140
	ds_write2_b32 v174, v71, v79 offset0:196 offset1:204
	ds_write2_b32 v175, v68, v76 offset0:8 offset1:16
	ds_write2_b32 v175, v72, v80 offset0:72 offset1:80
	ds_write2_b32 v175, v69, v77 offset0:140 offset1:148
	ds_write2_b32 v175, v73, v81 offset0:204 offset1:212
	s_waitcnt vmcnt(25)
	ds_write2_b32 v174, v82, v90 offset0:16 offset1:24
	s_waitcnt vmcnt(24)
	ds_write2_b32 v174, v86, v94 offset0:80 offset1:88
	ds_write2_b32 v174, v83, v91 offset0:148 offset1:156
	ds_write2_b32 v174, v87, v95 offset0:212 offset1:220
	ds_write2_b32 v175, v84, v92 offset0:24 offset1:32
	ds_write2_b32 v175, v88, v96 offset0:88 offset1:96
	ds_write2_b32 v175, v85, v93 offset0:156 offset1:164
	ds_write2_b32 v175, v89, v97 offset0:220 offset1:228
	s_waitcnt vmcnt(21)
	ds_write2_b32 v174, v98, v106 offset0:32 offset1:40
	s_waitcnt vmcnt(20)
	ds_write2_b32 v174, v102, v110 offset0:96 offset1:104
	ds_write2_b32 v174, v99, v107 offset0:164 offset1:172
	ds_write2_b32 v174, v103, v111 offset0:228 offset1:236
	ds_write2_b32 v175, v100, v108 offset0:40 offset1:48
	ds_write2_b32 v175, v104, v112 offset0:104 offset1:112
	ds_write2_b32 v175, v101, v109 offset0:172 offset1:180
	ds_write2_b32 v175, v105, v113 offset0:236 offset1:244
	s_waitcnt vmcnt(17)
	ds_write2_b32 v174, v114, v122 offset0:48 offset1:56
	s_waitcnt vmcnt(16)
	ds_write2_b32 v174, v118, v126 offset0:112 offset1:120
	ds_write2_b32 v174, v115, v123 offset0:180 offset1:188
	ds_write2_b32 v174, v119, v127 offset0:244 offset1:252
	ds_write2_b32 v175, v116, v124 offset0:56 offset1:64
	ds_write2_b32 v175, v120, v128 offset0:120 offset1:128
	ds_write2_b32 v175, v117, v125 offset0:188 offset1:196
	v_lshlrev_b32_e32 v66, 6, v130
	v_mul_u32_u24_e32 v67, 0x210, v133
	v_add3_u32 v173, s49, v66, v67
	s_lshl_b32 s7, s48, 12
	s_add_u32 s11, s17, s7
	s_addc_u32 s7, s18, 0
	s_and_b32 s46, s13, 0xffffff00
	s_lshl_b32 s12, s12, 7
	s_add_i32 s46, s46, s12
	s_and_b32 s6, s6, 0x60
	s_or_b32 s46, s6, s46
	s_ashr_i32 s47, s46, 31
	s_lshl_b64 s[46:47], s[46:47], 11
	s_add_u32 s46, s11, s46
	s_addc_u32 s47, s7, s47
	s_add_u32 s46, s46, s10
	v_lshlrev_b32_e32 v130, 4, v130
	s_addc_u32 s47, s47, 0
	v_lshlrev_b32_e32 v134, 11, v133
	v_mov_b32_e32 v135, v131
	ds_write2_b32 v176, v121, v129 offset0:124 offset1:132
	s_waitcnt lgkmcnt(0)
	ds_read_b128 v[66:69], v173
	ds_read_b128 v[70:73], v173 offset:16
	ds_read_b128 v[74:77], v173 offset:32
	ds_read_b128 v[78:81], v173 offset:48
	v_or_b32_e32 v136, 0x4000, v134
	v_mov_b32_e32 v137, v131
	s_waitcnt lgkmcnt(2)
	v_mul_f32_e32 v70, v172, v70
	v_mul_f32_e32 v82, v172, v66
	v_mul_f32_e32 v67, v172, v67
	v_mov_b32_e32 v66, 0
	v_cvt_pk_fp8_f32 v66, v82, v67
	v_mul_f32_e32 v71, v172, v71
	v_mov_b32_e32 v67, 0
	v_cvt_pk_fp8_f32 v67, v70, v71
	v_mul_f32_e32 v68, v172, v68
	v_mul_f32_e32 v69, v172, v69
	v_cvt_pk_fp8_f32 v66, v68, v69 op_sel:[0,0,1]
	v_mul_f32_e32 v68, v172, v72
	v_mul_f32_e32 v69, v172, v73
	v_cvt_pk_fp8_f32 v67, v68, v69 op_sel:[0,0,1]
	s_waitcnt lgkmcnt(1)
	v_mul_f32_e32 v69, v172, v74
	v_mul_f32_e32 v70, v172, v75
	v_mov_b32_e32 v68, 0
	v_cvt_pk_fp8_f32 v68, v69, v70
	s_waitcnt lgkmcnt(0)
	v_mul_f32_e32 v72, v172, v78
	v_mul_f32_e32 v73, v172, v79
	v_mov_b32_e32 v69, 0
	v_cvt_pk_fp8_f32 v69, v72, v73
	v_mul_f32_e32 v70, v172, v76
	v_mul_f32_e32 v71, v172, v77
	v_cvt_pk_fp8_f32 v68, v70, v71 op_sel:[0,0,1]
	v_mul_f32_e32 v70, v172, v80
	v_mul_f32_e32 v71, v172, v81
	v_cvt_pk_fp8_f32 v69, v70, v71 op_sel:[0,0,1]
	ds_read_b128 v[70:73], v173 offset:4224
	ds_read_b128 v[74:77], v173 offset:4240
	v_lshl_add_u64 v[78:79], s[46:47], 0, v[130:131]
	v_lshl_add_u64 v[80:81], v[78:79], 0, v[134:135]
	global_store_dwordx4 v[80:81], v[66:69], off nt
	s_waitcnt lgkmcnt(1)
	v_mul_f32_e32 v82, v172, v70
	v_mul_f32_e32 v71, v172, v71
	v_mov_b32_e32 v70, 0
	v_cvt_pk_fp8_f32 v70, v82, v71
	v_mul_f32_e32 v66, v172, v72
	v_mul_f32_e32 v67, v172, v73
	v_mov_b32_e32 v71, 0
	v_cvt_pk_fp8_f32 v70, v66, v67 op_sel:[0,0,1]
	s_waitcnt lgkmcnt(0)
	v_mul_f32_e32 v66, v172, v74
	v_mul_f32_e32 v67, v172, v75
	v_cvt_pk_fp8_f32 v71, v66, v67
	ds_read_b128 v[66:69], v173 offset:4256
	v_mul_f32_e32 v72, v172, v76
	v_mul_f32_e32 v73, v172, v77
	ds_read_b128 v[74:77], v173 offset:4272
	v_cvt_pk_fp8_f32 v71, v72, v73 op_sel:[0,0,1]
	s_waitcnt lgkmcnt(1)
	v_mul_f32_e32 v66, v172, v66
	v_mul_f32_e32 v67, v172, v67
	v_mov_b32_e32 v72, 0
	v_cvt_pk_fp8_f32 v72, v66, v67
	v_mul_f32_e32 v66, v172, v68
	v_mul_f32_e32 v67, v172, v69
	s_waitcnt lgkmcnt(0)
	v_mul_f32_e32 v68, v172, v74
	v_mul_f32_e32 v69, v172, v75
	v_mov_b32_e32 v73, 0
	v_cvt_pk_fp8_f32 v73, v68, v69
	v_cvt_pk_fp8_f32 v72, v66, v67 op_sel:[0,0,1]
	v_mul_f32_e32 v66, v172, v76
	v_mul_f32_e32 v67, v172, v77
	v_cvt_pk_fp8_f32 v73, v66, v67 op_sel:[0,0,1]
	ds_read_b128 v[66:69], v173 offset:8448
	ds_read_b128 v[74:77], v173 offset:8464
	v_lshl_add_u64 v[80:81], v[78:79], 0, v[136:137]
	global_store_dwordx4 v[80:81], v[70:73], off nt
	v_or_b32_e32 v132, 0x8000, v134
	s_waitcnt lgkmcnt(1)
	v_mul_f32_e32 v82, v172, v66
	v_mul_f32_e32 v67, v172, v67
	v_mov_b32_e32 v66, 0
	v_cvt_pk_fp8_f32 v66, v82, v67
	v_mul_f32_e32 v67, v172, v68
	v_mul_f32_e32 v68, v172, v69
	s_waitcnt lgkmcnt(0)
	v_mul_f32_e32 v69, v172, v75
	v_cvt_pk_fp8_f32 v66, v67, v68 op_sel:[0,0,1]
	v_mul_f32_e32 v68, v172, v74
	v_mov_b32_e32 v67, 0
	v_cvt_pk_fp8_f32 v67, v68, v69
	ds_read_b128 v[68:71], v173 offset:8480
	v_mul_f32_e32 v72, v172, v76
	v_mul_f32_e32 v73, v172, v77
	v_cvt_pk_fp8_f32 v67, v72, v73 op_sel:[0,0,1]
	ds_read_b128 v[72:75], v173 offset:8496
	s_waitcnt lgkmcnt(1)
	v_mul_f32_e32 v76, v172, v68
	v_mul_f32_e32 v69, v172, v69
	v_mov_b32_e32 v68, 0
	v_cvt_pk_fp8_f32 v68, v76, v69
	s_waitcnt lgkmcnt(0)
	v_mul_f32_e32 v72, v172, v72
	v_mul_f32_e32 v73, v172, v73
	v_mov_b32_e32 v69, 0
	v_cvt_pk_fp8_f32 v69, v72, v73
	v_mul_f32_e32 v70, v172, v70
	v_mul_f32_e32 v71, v172, v71
	v_cvt_pk_fp8_f32 v68, v70, v71 op_sel:[0,0,1]
	v_mul_f32_e32 v70, v172, v74
	v_mul_f32_e32 v71, v172, v75
	v_cvt_pk_fp8_f32 v69, v70, v71 op_sel:[0,0,1]
	ds_read_b128 v[70:73], v173 offset:12672
	ds_read_b128 v[74:77], v173 offset:12688
	v_mov_b32_e32 v133, v131
	v_lshl_add_u64 v[80:81], v[78:79], 0, v[132:133]
	global_store_dwordx4 v[80:81], v[66:69], off nt
	s_waitcnt lgkmcnt(1)
	v_mul_f32_e32 v82, v172, v70
	v_mul_f32_e32 v71, v172, v71
	v_mov_b32_e32 v70, 0
	v_cvt_pk_fp8_f32 v70, v82, v71
	v_mul_f32_e32 v66, v172, v72
	v_mul_f32_e32 v67, v172, v73
	v_mov_b32_e32 v71, 0
	v_cvt_pk_fp8_f32 v70, v66, v67 op_sel:[0,0,1]
	s_waitcnt lgkmcnt(0)
	v_mul_f32_e32 v66, v172, v74
	v_mul_f32_e32 v67, v172, v75
	v_cvt_pk_fp8_f32 v71, v66, v67
	ds_read_b128 v[66:69], v173 offset:12704
	v_mul_f32_e32 v72, v172, v76
	v_mul_f32_e32 v73, v172, v77
	ds_read_b128 v[74:77], v173 offset:12720
	v_cvt_pk_fp8_f32 v71, v72, v73 op_sel:[0,0,1]
	s_waitcnt lgkmcnt(1)
	v_mul_f32_e32 v66, v172, v66
	v_mul_f32_e32 v67, v172, v67
	v_mov_b32_e32 v72, 0
	v_cvt_pk_fp8_f32 v72, v66, v67
	v_mul_f32_e32 v66, v172, v68
	v_mul_f32_e32 v67, v172, v69
	s_waitcnt lgkmcnt(0)
	v_mul_f32_e32 v68, v172, v74
	v_mul_f32_e32 v69, v172, v75
	v_mov_b32_e32 v73, 0
	v_cvt_pk_fp8_f32 v73, v68, v69
	v_cvt_pk_fp8_f32 v72, v66, v67 op_sel:[0,0,1]
	v_mul_f32_e32 v66, v172, v76
	v_mul_f32_e32 v67, v172, v77
	v_cvt_pk_fp8_f32 v73, v66, v67 op_sel:[0,0,1]
	v_or_b32_e32 v138, 0xc000, v134
	v_mov_b32_e32 v139, v131
	v_lshl_add_u64 v[66:67], v[78:79], 0, v[138:139]
	global_store_dwordx4 v[66:67], v[70:73], off nt
	s_waitcnt lgkmcnt(0)
	global_load_dwordx4 v[114:117], v[142:143], off offset:2048 nt
	global_load_dwordx4 v[118:121], v[140:141], off offset:2048 nt
	global_load_dwordx4 v[122:125], v[144:145], off offset:2048 nt
	global_load_dwordx4 v[126:129], v[146:147], off offset:2048 nt
	global_load_dwordx4 v[98:101], v[148:149], off offset:2048 nt
	global_load_dwordx4 v[102:105], v[150:151], off offset:2048 nt
	global_load_dwordx4 v[106:109], v[152:153], off offset:2048 nt
	global_load_dwordx4 v[110:113], v[154:155], off offset:2048 nt
	global_load_dwordx4 v[82:85], v[156:157], off offset:2048 nt
	global_load_dwordx4 v[86:89], v[158:159], off offset:2048 nt
	global_load_dwordx4 v[90:93], v[160:161], off offset:2048 nt
	global_load_dwordx4 v[94:97], v[162:163], off offset:2048 nt
	global_load_dwordx4 v[66:69], v[164:165], off offset:2048 nt
	global_load_dwordx4 v[70:73], v[166:167], off offset:2048 nt
	global_load_dwordx4 v[74:77], v[168:169], off offset:2048 nt
	global_load_dwordx4 v[78:81], v[170:171], off offset:2048 nt
	s_waitcnt vmcnt(33)
	ds_write2_b32 v174, v50, v58 offset1:8
	s_waitcnt vmcnt(32)
	ds_write2_b32 v174, v54, v62 offset0:64 offset1:72
	ds_write2_b32 v174, v51, v59 offset0:132 offset1:140
	ds_write2_b32 v174, v55, v63 offset0:196 offset1:204
	ds_write2_b32 v175, v52, v60 offset0:8 offset1:16
	ds_write2_b32 v175, v56, v64 offset0:72 offset1:80
	ds_write2_b32 v175, v53, v61 offset0:140 offset1:148
	ds_write2_b32 v175, v57, v65 offset0:204 offset1:212
	s_waitcnt vmcnt(29)
	ds_write2_b32 v174, v34, v42 offset0:16 offset1:24
	s_waitcnt vmcnt(28)
	ds_write2_b32 v174, v38, v46 offset0:80 offset1:88
	ds_write2_b32 v174, v35, v43 offset0:148 offset1:156
	ds_write2_b32 v174, v39, v47 offset0:212 offset1:220
	ds_write2_b32 v175, v36, v44 offset0:24 offset1:32
	ds_write2_b32 v175, v40, v48 offset0:88 offset1:96
	ds_write2_b32 v175, v37, v45 offset0:156 offset1:164
	ds_write2_b32 v175, v41, v49 offset0:220 offset1:228
	s_waitcnt vmcnt(25)
	ds_write2_b32 v174, v18, v26 offset0:32 offset1:40
	s_waitcnt vmcnt(24)
	ds_write2_b32 v174, v22, v30 offset0:96 offset1:104
	ds_write2_b32 v174, v19, v27 offset0:164 offset1:172
	ds_write2_b32 v174, v23, v31 offset0:228 offset1:236
	ds_write2_b32 v175, v20, v28 offset0:40 offset1:48
	ds_write2_b32 v175, v24, v32 offset0:104 offset1:112
	ds_write2_b32 v175, v21, v29 offset0:172 offset1:180
	ds_write2_b32 v175, v25, v33 offset0:236 offset1:244
	s_waitcnt vmcnt(21)
	ds_write2_b32 v174, v2, v10 offset0:48 offset1:56
	s_waitcnt vmcnt(20)
	ds_write2_b32 v174, v6, v14 offset0:112 offset1:120
	ds_write2_b32 v174, v3, v11 offset0:180 offset1:188
	ds_write2_b32 v174, v7, v15 offset0:244 offset1:252
	ds_write2_b32 v175, v4, v12 offset0:56 offset1:64
	ds_write2_b32 v175, v8, v16 offset0:120 offset1:128
	ds_write2_b32 v175, v5, v13 offset0:188 offset1:196
	ds_write2_b32 v176, v9, v17 offset0:124 offset1:132
	s_waitcnt lgkmcnt(0)
	ds_read_b128 v[2:5], v173
	ds_read_b128 v[6:9], v173 offset:16
	ds_read_b128 v[10:13], v173 offset:32
	ds_read_b128 v[14:17], v173 offset:48
	s_andn2_b32 s13, s13, 63
	s_add_i32 s46, s13, 0x200
	s_waitcnt lgkmcnt(2)
	v_mul_f32_e32 v6, v172, v6
	v_mul_f32_e32 v18, v172, v2
	v_mul_f32_e32 v3, v172, v3
	v_mov_b32_e32 v2, 0
	v_cvt_pk_fp8_f32 v2, v18, v3
	v_mul_f32_e32 v7, v172, v7
	v_mov_b32_e32 v3, 0
	v_cvt_pk_fp8_f32 v3, v6, v7
	v_mul_f32_e32 v4, v172, v4
	v_mul_f32_e32 v5, v172, v5
	v_cvt_pk_fp8_f32 v2, v4, v5 op_sel:[0,0,1]
	v_mul_f32_e32 v4, v172, v8
	v_mul_f32_e32 v5, v172, v9
	v_cvt_pk_fp8_f32 v3, v4, v5 op_sel:[0,0,1]
	s_waitcnt lgkmcnt(1)
	v_mul_f32_e32 v5, v172, v10
	v_mul_f32_e32 v6, v172, v11
	v_mov_b32_e32 v4, 0
	v_cvt_pk_fp8_f32 v4, v5, v6
	s_waitcnt lgkmcnt(0)
	v_mul_f32_e32 v8, v172, v14
	v_mul_f32_e32 v9, v172, v15
	v_mov_b32_e32 v5, 0
	v_cvt_pk_fp8_f32 v5, v8, v9
	s_and_b32 s46, s46, 0xffffff00
	v_mul_f32_e32 v6, v172, v12
	v_mul_f32_e32 v7, v172, v13
	s_add_i32 s46, s46, s12
	v_cvt_pk_fp8_f32 v4, v6, v7 op_sel:[0,0,1]
	v_mul_f32_e32 v6, v172, v16
	v_mul_f32_e32 v7, v172, v17
	s_or_b32 s46, s46, s6
	v_cvt_pk_fp8_f32 v5, v6, v7 op_sel:[0,0,1]
	ds_read_b128 v[6:9], v173 offset:4224
	ds_read_b128 v[10:13], v173 offset:4240
	s_ashr_i32 s47, s46, 31
	s_lshl_b64 s[46:47], s[46:47], 11
	s_add_u32 s46, s11, s46
	s_addc_u32 s47, s7, s47
	s_add_u32 s46, s46, s10
	s_waitcnt lgkmcnt(1)
	v_mul_f32_e32 v18, v172, v6
	v_mul_f32_e32 v7, v172, v7
	v_mov_b32_e32 v6, 0
	s_addc_u32 s47, s47, 0
	v_cvt_pk_fp8_f32 v6, v18, v7
	v_lshl_add_u64 v[16:17], s[46:47], 0, v[130:131]
	v_lshl_add_u64 v[14:15], v[16:17], 0, v[134:135]
	global_store_dwordx4 v[14:15], v[2:5], off nt
	v_mov_b32_e32 v7, 0
	s_waitcnt lgkmcnt(0)
	v_mul_f32_e32 v14, v172, v13
	v_mul_f32_e32 v2, v172, v8
	v_mul_f32_e32 v3, v172, v9
	v_cvt_pk_fp8_f32 v6, v2, v3 op_sel:[0,0,1]
	ds_read_b128 v[2:5], v173 offset:4256
	v_mul_f32_e32 v8, v172, v10
	v_mul_f32_e32 v9, v172, v11
	v_cvt_pk_fp8_f32 v7, v8, v9
	v_mul_f32_e32 v9, v172, v12
	ds_read_b128 v[10:13], v173 offset:4272
	s_waitcnt lgkmcnt(1)
	v_mul_f32_e32 v2, v172, v2
	v_mul_f32_e32 v3, v172, v3
	v_mov_b32_e32 v8, 0
	v_cvt_pk_fp8_f32 v8, v2, v3
	v_mul_f32_e32 v2, v172, v4
	v_mul_f32_e32 v3, v172, v5
	v_cvt_pk_fp8_f32 v7, v9, v14 op_sel:[0,0,1]
	v_cvt_pk_fp8_f32 v8, v2, v3 op_sel:[0,0,1]
	s_waitcnt lgkmcnt(0)
	v_mul_f32_e32 v2, v172, v10
	v_mul_f32_e32 v3, v172, v11
	v_mov_b32_e32 v9, 0
	v_cvt_pk_fp8_f32 v9, v2, v3
	ds_read_b128 v[2:5], v173 offset:8448
	v_mul_f32_e32 v10, v172, v12
	v_mul_f32_e32 v11, v172, v13
	v_cvt_pk_fp8_f32 v9, v10, v11 op_sel:[0,0,1]
	ds_read_b128 v[10:13], v173 offset:8464
	s_waitcnt lgkmcnt(1)
	v_mul_f32_e32 v18, v172, v2
	v_mul_f32_e32 v3, v172, v3
	v_mov_b32_e32 v2, 0
	v_cvt_pk_fp8_f32 v2, v18, v3
	v_lshl_add_u64 v[14:15], v[16:17], 0, v[136:137]
	v_mul_f32_e32 v3, v172, v4
	v_mul_f32_e32 v4, v172, v5
	global_store_dwordx4 v[14:15], v[6:9], off nt
	v_cvt_pk_fp8_f32 v2, v3, v4 op_sel:[0,0,1]
	ds_read_b128 v[4:7], v173 offset:8480
	s_waitcnt lgkmcnt(1)
	v_mul_f32_e32 v8, v172, v10
	v_mul_f32_e32 v9, v172, v11
	v_mov_b32_e32 v3, 0
	v_cvt_pk_fp8_f32 v3, v8, v9
	ds_read_b128 v[8:11], v173 offset:8496
	s_waitcnt lgkmcnt(1)
	v_mul_f32_e32 v14, v172, v4
	v_mul_f32_e32 v5, v172, v5
	v_mov_b32_e32 v4, 0
	v_cvt_pk_fp8_f32 v4, v14, v5
	v_mul_f32_e32 v12, v172, v12
	v_mul_f32_e32 v13, v172, v13
	v_mul_f32_e32 v5, v172, v6
	v_mul_f32_e32 v6, v172, v7
	v_cvt_pk_fp8_f32 v3, v12, v13 op_sel:[0,0,1]
	v_cvt_pk_fp8_f32 v4, v5, v6 op_sel:[0,0,1]
	s_waitcnt lgkmcnt(0)
	v_mul_f32_e32 v12, v172, v8
	v_mul_f32_e32 v13, v172, v9
	ds_read_b128 v[6:9], v173 offset:12672
	v_mov_b32_e32 v5, 0
	v_cvt_pk_fp8_f32 v5, v12, v13
	v_mul_f32_e32 v14, v172, v10
	v_mul_f32_e32 v15, v172, v11
	ds_read_b128 v[10:13], v173 offset:12688
	s_waitcnt lgkmcnt(1)
	v_mul_f32_e32 v18, v172, v6
	v_mul_f32_e32 v7, v172, v7
	v_mov_b32_e32 v6, 0
	v_cvt_pk_fp8_f32 v6, v18, v7
	v_mul_f32_e32 v7, v172, v8
	v_mul_f32_e32 v8, v172, v9
	s_waitcnt lgkmcnt(0)
	v_mul_f32_e32 v9, v172, v11
	v_cvt_pk_fp8_f32 v6, v7, v8 op_sel:[0,0,1]
	v_mul_f32_e32 v8, v172, v10
	v_mov_b32_e32 v7, 0
	v_cvt_pk_fp8_f32 v7, v8, v9
	ds_read_b128 v[8:11], v173 offset:12704
	v_mul_f32_e32 v12, v172, v12
	v_mul_f32_e32 v13, v172, v13
	v_cvt_pk_fp8_f32 v5, v14, v15 op_sel:[0,0,1]
	v_cvt_pk_fp8_f32 v7, v12, v13 op_sel:[0,0,1]
	ds_read_b128 v[12:15], v173 offset:12720
	s_waitcnt lgkmcnt(1)
	v_mul_f32_e32 v18, v172, v8
	v_mul_f32_e32 v9, v172, v9
	v_mov_b32_e32 v8, 0
	v_cvt_pk_fp8_f32 v8, v18, v9
	s_waitcnt lgkmcnt(0)
	v_mul_f32_e32 v12, v172, v12
	v_mul_f32_e32 v13, v172, v13
	v_mov_b32_e32 v9, 0
	v_cvt_pk_fp8_f32 v9, v12, v13
	v_mul_f32_e32 v10, v172, v10
	v_mul_f32_e32 v11, v172, v11
	v_cvt_pk_fp8_f32 v8, v10, v11 op_sel:[0,0,1]
	v_mul_f32_e32 v10, v172, v14
	v_mul_f32_e32 v11, v172, v15
	v_cvt_pk_fp8_f32 v9, v10, v11 op_sel:[0,0,1]
	v_lshl_add_u64 v[10:11], v[16:17], 0, v[132:133]
	global_store_dwordx4 v[10:11], v[2:5], off nt
	s_add_i32 s46, s13, 0x400
	s_and_b32 s46, s46, 0xffffff00
	v_lshl_add_u64 v[2:3], v[16:17], 0, v[138:139]
	global_store_dwordx4 v[2:3], v[6:9], off nt
	s_waitcnt lgkmcnt(0)
	global_load_dwordx4 v[42:45], v[142:143], off offset:3072 nt
	global_load_dwordx4 v[46:49], v[140:141], off offset:3072 nt
	global_load_dwordx4 v[58:61], v[144:145], off offset:3072 nt
	global_load_dwordx4 v[62:65], v[146:147], off offset:3072 nt
	global_load_dwordx4 v[34:37], v[148:149], off offset:3072 nt
	global_load_dwordx4 v[38:41], v[150:151], off offset:3072 nt
	global_load_dwordx4 v[50:53], v[152:153], off offset:3072 nt
	global_load_dwordx4 v[54:57], v[154:155], off offset:3072 nt
	global_load_dwordx4 v[18:21], v[156:157], off offset:3072 nt
	global_load_dwordx4 v[22:25], v[158:159], off offset:3072 nt
	global_load_dwordx4 v[26:29], v[160:161], off offset:3072 nt
	global_load_dwordx4 v[30:33], v[162:163], off offset:3072 nt
	global_load_dwordx4 v[2:5], v[164:165], off offset:3072 nt
	global_load_dwordx4 v[6:9], v[166:167], off offset:3072 nt
	global_load_dwordx4 v[10:13], v[168:169], off offset:3072 nt
	global_load_dwordx4 v[14:17], v[170:171], off offset:3072 nt
	s_waitcnt vmcnt(33)
	ds_write2_b32 v174, v114, v122 offset1:8
	s_waitcnt vmcnt(32)
	ds_write2_b32 v174, v118, v126 offset0:64 offset1:72
	ds_write2_b32 v174, v115, v123 offset0:132 offset1:140
	ds_write2_b32 v174, v119, v127 offset0:196 offset1:204
	ds_write2_b32 v175, v116, v124 offset0:8 offset1:16
	ds_write2_b32 v175, v120, v128 offset0:72 offset1:80
	ds_write2_b32 v175, v117, v125 offset0:140 offset1:148
	ds_write2_b32 v175, v121, v129 offset0:204 offset1:212
	s_waitcnt vmcnt(29)
	ds_write2_b32 v174, v98, v106 offset0:16 offset1:24
	s_waitcnt vmcnt(28)
	ds_write2_b32 v174, v102, v110 offset0:80 offset1:88
	ds_write2_b32 v174, v99, v107 offset0:148 offset1:156
	ds_write2_b32 v174, v103, v111 offset0:212 offset1:220
	ds_write2_b32 v175, v100, v108 offset0:24 offset1:32
	ds_write2_b32 v175, v104, v112 offset0:88 offset1:96
	ds_write2_b32 v175, v101, v109 offset0:156 offset1:164
	ds_write2_b32 v175, v105, v113 offset0:220 offset1:228
	s_waitcnt vmcnt(25)
	ds_write2_b32 v174, v82, v90 offset0:32 offset1:40
	s_waitcnt vmcnt(24)
	ds_write2_b32 v174, v86, v94 offset0:96 offset1:104
	ds_write2_b32 v174, v83, v91 offset0:164 offset1:172
	ds_write2_b32 v174, v87, v95 offset0:228 offset1:236
	ds_write2_b32 v175, v84, v92 offset0:40 offset1:48
	ds_write2_b32 v175, v88, v96 offset0:104 offset1:112
	ds_write2_b32 v175, v85, v93 offset0:172 offset1:180
	ds_write2_b32 v175, v89, v97 offset0:236 offset1:244
	s_waitcnt vmcnt(21)
	ds_write2_b32 v174, v66, v74 offset0:48 offset1:56
	s_waitcnt vmcnt(20)
	ds_write2_b32 v174, v70, v78 offset0:112 offset1:120
	ds_write2_b32 v174, v67, v75 offset0:180 offset1:188
	ds_write2_b32 v174, v71, v79 offset0:244 offset1:252
	ds_write2_b32 v175, v68, v76 offset0:56 offset1:64
	ds_write2_b32 v175, v72, v80 offset0:120 offset1:128
	ds_write2_b32 v175, v69, v77 offset0:188 offset1:196
	ds_write2_b32 v176, v73, v81 offset0:124 offset1:132
	s_waitcnt lgkmcnt(0)
	ds_read_b128 v[66:69], v173
	ds_read_b128 v[70:73], v173 offset:16
	ds_read_b128 v[74:77], v173 offset:32
	ds_read_b128 v[78:81], v173 offset:48
	s_add_i32 s46, s46, s12
	s_or_b32 s46, s46, s6
	s_waitcnt lgkmcnt(2)
	v_mul_f32_e32 v70, v172, v70
	v_mul_f32_e32 v82, v172, v66
	v_mul_f32_e32 v67, v172, v67
	v_mov_b32_e32 v66, 0
	v_cvt_pk_fp8_f32 v66, v82, v67
	v_mul_f32_e32 v71, v172, v71
	v_mov_b32_e32 v67, 0
	v_cvt_pk_fp8_f32 v67, v70, v71
	v_mul_f32_e32 v68, v172, v68
	v_mul_f32_e32 v69, v172, v69
	v_cvt_pk_fp8_f32 v66, v68, v69 op_sel:[0,0,1]
	v_mul_f32_e32 v68, v172, v72
	v_mul_f32_e32 v69, v172, v73
	v_cvt_pk_fp8_f32 v67, v68, v69 op_sel:[0,0,1]
	s_waitcnt lgkmcnt(1)
	v_mul_f32_e32 v69, v172, v74
	v_mul_f32_e32 v70, v172, v75
	v_mov_b32_e32 v68, 0
	v_cvt_pk_fp8_f32 v68, v69, v70
	s_waitcnt lgkmcnt(0)
	v_mul_f32_e32 v72, v172, v78
	v_mul_f32_e32 v73, v172, v79
	v_mov_b32_e32 v69, 0
	v_cvt_pk_fp8_f32 v69, v72, v73
	v_mul_f32_e32 v70, v172, v76
	v_mul_f32_e32 v71, v172, v77
	v_cvt_pk_fp8_f32 v68, v70, v71 op_sel:[0,0,1]
	v_mul_f32_e32 v70, v172, v80
	v_mul_f32_e32 v71, v172, v81
	v_cvt_pk_fp8_f32 v69, v70, v71 op_sel:[0,0,1]
	ds_read_b128 v[70:73], v173 offset:4224
	ds_read_b128 v[74:77], v173 offset:4240
	s_ashr_i32 s47, s46, 31
	s_lshl_b64 s[46:47], s[46:47], 11
	s_add_u32 s46, s11, s46
	s_addc_u32 s47, s7, s47
	s_add_u32 s46, s46, s10
	s_waitcnt lgkmcnt(1)
	v_mul_f32_e32 v82, v172, v70
	v_mul_f32_e32 v71, v172, v71
	v_mov_b32_e32 v70, 0
	s_addc_u32 s47, s47, 0
	v_cvt_pk_fp8_f32 v70, v82, v71
	v_lshl_add_u64 v[80:81], s[46:47], 0, v[130:131]
	v_lshl_add_u64 v[78:79], v[80:81], 0, v[134:135]
	global_store_dwordx4 v[78:79], v[66:69], off nt
	v_mov_b32_e32 v71, 0
	s_waitcnt lgkmcnt(0)
	v_mul_f32_e32 v78, v172, v77
	v_mul_f32_e32 v66, v172, v72
	v_mul_f32_e32 v67, v172, v73
	v_cvt_pk_fp8_f32 v70, v66, v67 op_sel:[0,0,1]
	ds_read_b128 v[66:69], v173 offset:4256
	v_mul_f32_e32 v72, v172, v74
	v_mul_f32_e32 v73, v172, v75
	v_cvt_pk_fp8_f32 v71, v72, v73
	v_mul_f32_e32 v73, v172, v76
	ds_read_b128 v[74:77], v173 offset:4272
	s_waitcnt lgkmcnt(1)
	v_mul_f32_e32 v66, v172, v66
	v_mul_f32_e32 v67, v172, v67
	v_mov_b32_e32 v72, 0
	v_cvt_pk_fp8_f32 v72, v66, v67
	v_mul_f32_e32 v66, v172, v68
	v_mul_f32_e32 v67, v172, v69
	v_cvt_pk_fp8_f32 v71, v73, v78 op_sel:[0,0,1]
	v_cvt_pk_fp8_f32 v72, v66, v67 op_sel:[0,0,1]
	s_waitcnt lgkmcnt(0)
	v_mul_f32_e32 v66, v172, v74
	v_mul_f32_e32 v67, v172, v75
	v_mov_b32_e32 v73, 0
	v_cvt_pk_fp8_f32 v73, v66, v67
	ds_read_b128 v[66:69], v173 offset:8448
	v_mul_f32_e32 v74, v172, v76
	v_mul_f32_e32 v75, v172, v77
	v_cvt_pk_fp8_f32 v73, v74, v75 op_sel:[0,0,1]
	ds_read_b128 v[74:77], v173 offset:8464
	s_waitcnt lgkmcnt(1)
	v_mul_f32_e32 v82, v172, v66
	v_mul_f32_e32 v67, v172, v67
	v_mov_b32_e32 v66, 0
	v_cvt_pk_fp8_f32 v66, v82, v67
	v_lshl_add_u64 v[78:79], v[80:81], 0, v[136:137]
	v_mul_f32_e32 v67, v172, v68
	v_mul_f32_e32 v68, v172, v69
	global_store_dwordx4 v[78:79], v[70:73], off nt
	v_cvt_pk_fp8_f32 v66, v67, v68 op_sel:[0,0,1]
	ds_read_b128 v[68:71], v173 offset:8480
	s_waitcnt lgkmcnt(1)
	v_mul_f32_e32 v72, v172, v74
	v_mul_f32_e32 v73, v172, v75
	v_mov_b32_e32 v67, 0
	v_cvt_pk_fp8_f32 v67, v72, v73
	ds_read_b128 v[72:75], v173 offset:8496
	s_waitcnt lgkmcnt(1)
	v_mul_f32_e32 v78, v172, v68
	v_mul_f32_e32 v69, v172, v69
	v_mov_b32_e32 v68, 0
	v_cvt_pk_fp8_f32 v68, v78, v69
	v_mul_f32_e32 v76, v172, v76
	v_mul_f32_e32 v77, v172, v77
	v_mul_f32_e32 v69, v172, v70
	v_mul_f32_e32 v70, v172, v71
	v_cvt_pk_fp8_f32 v67, v76, v77 op_sel:[0,0,1]
	v_cvt_pk_fp8_f32 v68, v69, v70 op_sel:[0,0,1]
	s_waitcnt lgkmcnt(0)
	v_mul_f32_e32 v76, v172, v72
	v_mul_f32_e32 v77, v172, v73
	ds_read_b128 v[70:73], v173 offset:12672
	v_mov_b32_e32 v69, 0
	v_cvt_pk_fp8_f32 v69, v76, v77
	v_mul_f32_e32 v78, v172, v74
	v_mul_f32_e32 v79, v172, v75
	ds_read_b128 v[74:77], v173 offset:12688
	s_waitcnt lgkmcnt(1)
	v_mul_f32_e32 v82, v172, v70
	v_mul_f32_e32 v71, v172, v71
	v_mov_b32_e32 v70, 0
	v_cvt_pk_fp8_f32 v70, v82, v71
	v_mul_f32_e32 v71, v172, v72
	v_mul_f32_e32 v72, v172, v73
	s_waitcnt lgkmcnt(0)
	v_mul_f32_e32 v73, v172, v75
	v_cvt_pk_fp8_f32 v70, v71, v72 op_sel:[0,0,1]
	v_mul_f32_e32 v72, v172, v74
	v_mov_b32_e32 v71, 0
	v_cvt_pk_fp8_f32 v71, v72, v73
	ds_read_b128 v[72:75], v173 offset:12704
	v_mul_f32_e32 v76, v172, v76
	v_mul_f32_e32 v77, v172, v77
	v_cvt_pk_fp8_f32 v69, v78, v79 op_sel:[0,0,1]
	v_cvt_pk_fp8_f32 v71, v76, v77 op_sel:[0,0,1]
	ds_read_b128 v[76:79], v173 offset:12720
	s_waitcnt lgkmcnt(1)
	v_mul_f32_e32 v82, v172, v72
	v_mul_f32_e32 v73, v172, v73
	v_mov_b32_e32 v72, 0
	v_cvt_pk_fp8_f32 v72, v82, v73
	s_waitcnt lgkmcnt(0)
	v_mul_f32_e32 v76, v172, v76
	v_mul_f32_e32 v77, v172, v77
	v_mov_b32_e32 v73, 0
	v_cvt_pk_fp8_f32 v73, v76, v77
	v_mul_f32_e32 v74, v172, v74
	v_mul_f32_e32 v75, v172, v75
	v_cvt_pk_fp8_f32 v72, v74, v75 op_sel:[0,0,1]
	v_mul_f32_e32 v74, v172, v78
	v_mul_f32_e32 v75, v172, v79
	v_cvt_pk_fp8_f32 v73, v74, v75 op_sel:[0,0,1]
	v_lshl_add_u64 v[74:75], v[80:81], 0, v[132:133]
	global_store_dwordx4 v[74:75], v[66:69], off nt
	s_addk_i32 s13, 0x600
	s_and_b32 s13, s13, 0xffffff00
	v_lshl_add_u64 v[66:67], v[80:81], 0, v[138:139]
	global_store_dwordx4 v[66:67], v[70:73], off nt
	s_waitcnt lgkmcnt(0)
	s_waitcnt vmcnt(17)
	ds_write2_b32 v174, v42, v58 offset1:8
	s_waitcnt vmcnt(16)
	ds_write2_b32 v174, v46, v62 offset0:64 offset1:72
	ds_write2_b32 v174, v43, v59 offset0:132 offset1:140
	ds_write2_b32 v174, v47, v63 offset0:196 offset1:204
	ds_write2_b32 v175, v44, v60 offset0:8 offset1:16
	ds_write2_b32 v175, v48, v64 offset0:72 offset1:80
	ds_write2_b32 v175, v45, v61 offset0:140 offset1:148
	ds_write2_b32 v175, v49, v65 offset0:204 offset1:212
	s_waitcnt vmcnt(13)
	ds_write2_b32 v174, v34, v50 offset0:16 offset1:24
	s_waitcnt vmcnt(12)
	ds_write2_b32 v174, v38, v54 offset0:80 offset1:88
	ds_write2_b32 v174, v35, v51 offset0:148 offset1:156
	ds_write2_b32 v174, v39, v55 offset0:212 offset1:220
	ds_write2_b32 v175, v36, v52 offset0:24 offset1:32
	ds_write2_b32 v175, v40, v56 offset0:88 offset1:96
	ds_write2_b32 v175, v37, v53 offset0:156 offset1:164
	ds_write2_b32 v175, v41, v57 offset0:220 offset1:228
	s_waitcnt vmcnt(9)
	ds_write2_b32 v174, v18, v26 offset0:32 offset1:40
	s_waitcnt vmcnt(8)
	ds_write2_b32 v174, v22, v30 offset0:96 offset1:104
	ds_write2_b32 v174, v19, v27 offset0:164 offset1:172
	ds_write2_b32 v174, v23, v31 offset0:228 offset1:236
	ds_write2_b32 v175, v20, v28 offset0:40 offset1:48
	ds_write2_b32 v175, v24, v32 offset0:104 offset1:112
	ds_write2_b32 v175, v21, v29 offset0:172 offset1:180
	ds_write2_b32 v175, v25, v33 offset0:236 offset1:244
	s_waitcnt vmcnt(5)
	ds_write2_b32 v174, v2, v10 offset0:48 offset1:56
	s_waitcnt vmcnt(4)
	ds_write2_b32 v174, v6, v14 offset0:112 offset1:120
	ds_write2_b32 v174, v3, v11 offset0:180 offset1:188
	ds_write2_b32 v174, v7, v15 offset0:244 offset1:252
	ds_write2_b32 v175, v4, v12 offset0:56 offset1:64
	ds_write2_b32 v175, v8, v16 offset0:120 offset1:128
	ds_write2_b32 v175, v5, v13 offset0:188 offset1:196
	ds_write2_b32 v176, v9, v17 offset0:124 offset1:132
	s_waitcnt lgkmcnt(0)
	ds_read_b128 v[2:5], v173
	ds_read_b128 v[6:9], v173 offset:16
	ds_read_b128 v[10:13], v173 offset:32
	ds_read_b128 v[14:17], v173 offset:48
	s_add_i32 s13, s13, s12
	s_or_b32 s12, s13, s6
	s_waitcnt lgkmcnt(2)
	v_mul_f32_e32 v6, v172, v6
	v_mul_f32_e32 v18, v172, v2
	v_mul_f32_e32 v3, v172, v3
	v_mov_b32_e32 v2, 0
	v_cvt_pk_fp8_f32 v2, v18, v3
	v_mul_f32_e32 v7, v172, v7
	v_mov_b32_e32 v3, 0
	v_cvt_pk_fp8_f32 v3, v6, v7
	v_mul_f32_e32 v4, v172, v4
	v_mul_f32_e32 v5, v172, v5
	v_cvt_pk_fp8_f32 v2, v4, v5 op_sel:[0,0,1]
	v_mul_f32_e32 v4, v172, v8
	v_mul_f32_e32 v5, v172, v9
	v_cvt_pk_fp8_f32 v3, v4, v5 op_sel:[0,0,1]
	s_waitcnt lgkmcnt(1)
	v_mul_f32_e32 v5, v172, v10
	v_mul_f32_e32 v6, v172, v11
	v_mov_b32_e32 v4, 0
	v_cvt_pk_fp8_f32 v4, v5, v6
	s_waitcnt lgkmcnt(0)
	v_mul_f32_e32 v8, v172, v14
	v_mul_f32_e32 v9, v172, v15
	v_mov_b32_e32 v5, 0
	v_cvt_pk_fp8_f32 v5, v8, v9
	v_mul_f32_e32 v6, v172, v12
	v_mul_f32_e32 v7, v172, v13
	v_cvt_pk_fp8_f32 v4, v6, v7 op_sel:[0,0,1]
	v_mul_f32_e32 v6, v172, v16
	v_mul_f32_e32 v7, v172, v17
	v_cvt_pk_fp8_f32 v5, v6, v7 op_sel:[0,0,1]
	ds_read_b128 v[6:9], v173 offset:4224
	ds_read_b128 v[10:13], v173 offset:4240
	s_ashr_i32 s13, s12, 31
	s_lshl_b64 s[12:13], s[12:13], 11
	s_add_u32 s6, s11, s12
	s_addc_u32 s7, s7, s13
	s_add_u32 s6, s6, s10
	s_waitcnt lgkmcnt(1)
	v_mul_f32_e32 v18, v172, v6
	v_mul_f32_e32 v7, v172, v7
	v_mov_b32_e32 v6, 0
	s_addc_u32 s7, s7, 0
	v_cvt_pk_fp8_f32 v6, v18, v7
	v_lshl_add_u64 v[16:17], s[6:7], 0, v[130:131]
	v_lshl_add_u64 v[14:15], v[16:17], 0, v[134:135]
	global_store_dwordx4 v[14:15], v[2:5], off nt
	v_mov_b32_e32 v7, 0
	s_waitcnt lgkmcnt(0)
	v_mul_f32_e32 v14, v172, v13
	v_mul_f32_e32 v2, v172, v8
	v_mul_f32_e32 v3, v172, v9
	v_cvt_pk_fp8_f32 v6, v2, v3 op_sel:[0,0,1]
	ds_read_b128 v[2:5], v173 offset:4256
	v_mul_f32_e32 v8, v172, v10
	v_mul_f32_e32 v9, v172, v11
	v_cvt_pk_fp8_f32 v7, v8, v9
	v_mul_f32_e32 v9, v172, v12
	ds_read_b128 v[10:13], v173 offset:4272
	s_waitcnt lgkmcnt(1)
	v_mul_f32_e32 v2, v172, v2
	v_mul_f32_e32 v3, v172, v3
	v_mov_b32_e32 v8, 0
	v_cvt_pk_fp8_f32 v8, v2, v3
	v_mul_f32_e32 v2, v172, v4
	v_mul_f32_e32 v3, v172, v5
	v_cvt_pk_fp8_f32 v7, v9, v14 op_sel:[0,0,1]
	v_cvt_pk_fp8_f32 v8, v2, v3 op_sel:[0,0,1]
	s_waitcnt lgkmcnt(0)
	v_mul_f32_e32 v2, v172, v10
	v_mul_f32_e32 v3, v172, v11
	v_mov_b32_e32 v9, 0
	v_cvt_pk_fp8_f32 v9, v2, v3
	ds_read_b128 v[2:5], v173 offset:8448
	v_mul_f32_e32 v10, v172, v12
	v_mul_f32_e32 v11, v172, v13
	v_cvt_pk_fp8_f32 v9, v10, v11 op_sel:[0,0,1]
	ds_read_b128 v[10:13], v173 offset:8464
	s_waitcnt lgkmcnt(1)
	v_mul_f32_e32 v18, v172, v2
	v_mul_f32_e32 v3, v172, v3
	v_mov_b32_e32 v2, 0
	v_cvt_pk_fp8_f32 v2, v18, v3
	v_lshl_add_u64 v[14:15], v[16:17], 0, v[136:137]
	v_mul_f32_e32 v3, v172, v4
	v_mul_f32_e32 v4, v172, v5
	global_store_dwordx4 v[14:15], v[6:9], off nt
	v_cvt_pk_fp8_f32 v2, v3, v4 op_sel:[0,0,1]
	ds_read_b128 v[4:7], v173 offset:8480
	s_waitcnt lgkmcnt(1)
	v_mul_f32_e32 v8, v172, v10
	v_mul_f32_e32 v9, v172, v11
	v_mov_b32_e32 v3, 0
	v_cvt_pk_fp8_f32 v3, v8, v9
	ds_read_b128 v[8:11], v173 offset:8496
	s_waitcnt lgkmcnt(1)
	v_mul_f32_e32 v14, v172, v4
	v_mul_f32_e32 v5, v172, v5
	v_mov_b32_e32 v4, 0
	v_cvt_pk_fp8_f32 v4, v14, v5
	v_mul_f32_e32 v12, v172, v12
	v_mul_f32_e32 v13, v172, v13
	v_mul_f32_e32 v5, v172, v6
	v_mul_f32_e32 v6, v172, v7
	v_cvt_pk_fp8_f32 v3, v12, v13 op_sel:[0,0,1]
	v_cvt_pk_fp8_f32 v4, v5, v6 op_sel:[0,0,1]
	s_waitcnt lgkmcnt(0)
	v_mul_f32_e32 v12, v172, v8
	v_mul_f32_e32 v13, v172, v9
	ds_read_b128 v[6:9], v173 offset:12672
	v_mov_b32_e32 v5, 0
	v_cvt_pk_fp8_f32 v5, v12, v13
	v_mul_f32_e32 v14, v172, v10
	v_mul_f32_e32 v15, v172, v11
	ds_read_b128 v[10:13], v173 offset:12688
	s_waitcnt lgkmcnt(1)
	v_mul_f32_e32 v18, v172, v6
	v_mul_f32_e32 v7, v172, v7
	v_mov_b32_e32 v6, 0
	v_cvt_pk_fp8_f32 v6, v18, v7
	v_mul_f32_e32 v7, v172, v8
	v_mul_f32_e32 v8, v172, v9
	s_waitcnt lgkmcnt(0)
	v_mul_f32_e32 v9, v172, v11
	v_cvt_pk_fp8_f32 v6, v7, v8 op_sel:[0,0,1]
	v_mul_f32_e32 v8, v172, v10
	v_mov_b32_e32 v7, 0
	v_cvt_pk_fp8_f32 v7, v8, v9
	ds_read_b128 v[8:11], v173 offset:12704
	v_mul_f32_e32 v12, v172, v12
	v_mul_f32_e32 v13, v172, v13
	v_cvt_pk_fp8_f32 v5, v14, v15 op_sel:[0,0,1]
	v_cvt_pk_fp8_f32 v7, v12, v13 op_sel:[0,0,1]
	ds_read_b128 v[12:15], v173 offset:12720
	s_waitcnt lgkmcnt(1)
	v_mul_f32_e32 v18, v172, v8
	v_mul_f32_e32 v9, v172, v9
	v_mov_b32_e32 v8, 0
	v_cvt_pk_fp8_f32 v8, v18, v9
	s_waitcnt lgkmcnt(0)
	v_mul_f32_e32 v12, v172, v12
	v_mul_f32_e32 v13, v172, v13
	v_mov_b32_e32 v9, 0
	v_cvt_pk_fp8_f32 v9, v12, v13
	v_mul_f32_e32 v10, v172, v10
	v_mul_f32_e32 v11, v172, v11
	v_cvt_pk_fp8_f32 v8, v10, v11 op_sel:[0,0,1]
	v_mul_f32_e32 v10, v172, v14
	v_mul_f32_e32 v11, v172, v15
	v_cvt_pk_fp8_f32 v9, v10, v11 op_sel:[0,0,1]
	v_lshl_add_u64 v[10:11], v[16:17], 0, v[132:133]
	global_store_dwordx4 v[10:11], v[2:5], off nt
	s_nop 1
	v_lshl_add_u64 v[2:3], v[16:17], 0, v[138:139]
	global_store_dwordx4 v[2:3], v[6:9], off nt
	s_waitcnt lgkmcnt(0)
	s_barrier
	s_and_saveexec_b64 s[6:7], s[36:37]
	s_cbranch_execz .LBB0_2287
	v_mov_b32_e32 v2, s14
	s_waitcnt vmcnt(0)
	ds_write_b32 v2, v255
	s_branch .LBB0_2287

.LBB0_2305:
	s_or_b64 exec, exec, s[6:7]
.LBB0_2306:
	s_or_b64 exec, exec, s[4:5]
	v_mov_b32 v68, v0
	s_ashr_i32 s6, s66, 7
	v_lshlrev_b32_e32 v2, 3, v68
	v_and_b32_e32 v10, 8, v2
	s_and_b32 s46, s66, 63
	s_bfe_u32 s39, s66, 0x10006
	s_ashr_i32 s7, s6, 31
	v_bfe_u32 v6, v68, 1, 1
	v_lshlrev_b32_e32 v2, 2, v10
	s_add_i32 s66, s46, -1
	s_lshl_b64 s[28:29], s[6:7], 13
	v_ashrrev_i32_e32 v168, 2, v68
	s_lshl_b32 s34, s39, 6
	v_lshlrev_b32_e32 v7, 5, v6
	v_cmp_eq_u32_e64 s[4:5], 0, v6
	v_lshl_add_u64 v[4:5], s[18:19], 0, v[2:3]
	v_lshl_add_u64 v[8:9], s[20:21], 0, v[2:3]
	v_lshlrev_b32_e32 v2, 6, v6
	v_lshlrev_b32_e32 v6, 1, v10
	v_readfirstlane_b32 s38, v68
	v_ashrrev_i32_e32 v169, 31, v168
	v_and_b32_e32 v11, 63, v168
	v_add3_u32 v10, 0, v2, v6
	s_mov_b64 s[30:31], -1
	s_cmp_lt_u32 s66, 64
	v_lshlrev_b32_e32 v2, 1, v7
	v_mul_lo_u32 v13, v168, s57
	s_barrier
	s_cbranch_scc0 .LBB0_2308
	s_lshl_b32 s7, s66, 7
	s_or_b32 s30, s28, s7
	s_mov_b32 s31, s29
	v_lshl_add_u64 v[14:15], s[30:31], 0, v[168:169]
	v_mov_b64_e32 v[16:17], s[14:15]
	v_mad_u64_u32 v[16:17], s[30:31], v14, s56, v[16:17]
	v_mad_i32_i24 v17, v15, s56, v17
	s_lshl_b32 s12, s34, 1
	v_lshl_add_u64 v[14:15], v[16:17], 0, s[12:13]
	v_lshl_add_u64 v[14:15], v[14:15], 0, v[2:3]
	v_mov_b32_e32 v7, v3
	v_lshl_add_u64 v[18:19], v[14:15], 0, v[6:7]
	v_add_u32_e32 v7, s7, v168
	v_ashrrev_i32_e32 v7, 6, v7
	v_cndmask_b32_e64 v7, v11, v7, s[4:5]
	v_lshlrev_b32_e32 v22, 4, v7
	v_ashrrev_i32_e32 v23, 31, v22
	v_lshlrev_b64 v[30:31], 2, v[22:23]
	global_load_dwordx4 v[14:17], v[18:19], off offset:1024
	s_nop 0
	global_load_dwordx4 v[18:21], v[18:19], off offset:1056
	v_lshl_add_u64 v[26:27], v[8:9], 0, v[30:31]
	global_load_dwordx4 v[22:25], v[26:27], off
	s_nop 0
	global_load_dwordx4 v[26:29], v[26:27], off offset:16
	v_lshl_add_u64 v[34:35], v[4:5], 0, v[30:31]
	global_load_dwordx4 v[30:33], v[34:35], off
	s_nop 0
	global_load_dwordx4 v[34:37], v[34:35], off offset:16
	v_mul_lo_u32 v12, v168, s57
	v_add_u32_e32 v7, v10, v12
	s_mov_b64 s[30:31], 0
	s_waitcnt vmcnt(5)
	v_lshlrev_b32_e32 v38, 16, v14
	v_and_b32_e32 v39, 0xffff0000, v14
	s_waitcnt vmcnt(4)
	v_lshlrev_b32_e32 v40, 16, v18
	v_and_b32_e32 v41, 0xffff0000, v18
	v_lshlrev_b32_e32 v14, 16, v15
	v_and_b32_e32 v15, 0xffff0000, v15
	v_lshlrev_b32_e32 v18, 16, v19
	v_and_b32_e32 v19, 0xffff0000, v19
	v_lshlrev_b32_e32 v42, 16, v16
	v_and_b32_e32 v43, 0xffff0000, v16
	v_lshlrev_b32_e32 v44, 16, v20
	v_and_b32_e32 v45, 0xffff0000, v20
	v_lshlrev_b32_e32 v16, 16, v17
	v_and_b32_e32 v17, 0xffff0000, v17
	v_lshlrev_b32_e32 v20, 16, v21
	v_and_b32_e32 v21, 0xffff0000, v21
	s_waitcnt vmcnt(3)
	v_pk_mul_f32 v[46:47], v[22:23], v[38:39]
	v_pk_mul_f32 v[22:23], v[22:23], v[40:41]
	v_pk_mul_f32 v[48:49], v[24:25], v[14:15]
	v_pk_mul_f32 v[24:25], v[24:25], v[18:19]
	s_waitcnt vmcnt(2)
	v_pk_mul_f32 v[50:51], v[26:27], v[42:43]
	v_pk_mul_f32 v[26:27], v[26:27], v[44:45]
	v_pk_mul_f32 v[52:53], v[28:29], v[16:17]
	v_pk_mul_f32 v[28:29], v[28:29], v[20:21]
	s_waitcnt vmcnt(1)
	v_pk_fma_f32 v[40:41], v[30:31], v[40:41], v[46:47]
	v_pk_fma_f32 v[22:23], v[30:31], v[38:39], v[22:23] neg_lo:[0,0,1] neg_hi:[0,0,1]
	v_pk_fma_f32 v[30:31], v[32:33], v[18:19], v[48:49]
	v_pk_fma_f32 v[18:19], v[32:33], v[14:15], v[24:25] neg_lo:[0,0,1] neg_hi:[0,0,1]
	s_waitcnt vmcnt(0)
	v_pk_fma_f32 v[26:27], v[34:35], v[42:43], v[26:27] neg_lo:[0,0,1] neg_hi:[0,0,1]
	v_pk_fma_f32 v[32:33], v[36:37], v[20:21], v[52:53]
	v_pk_fma_f32 v[20:21], v[36:37], v[16:17], v[28:29] neg_lo:[0,0,1] neg_hi:[0,0,1]
	v_pk_fma_f32 v[24:25], v[34:35], v[44:45], v[50:51]
	v_cvt_pk_bf16_f32 v14, v22, v23
	v_cvt_pk_bf16_f32 v15, v18, v19
	v_cvt_pk_bf16_f32 v16, v26, v27
	v_cvt_pk_bf16_f32 v17, v20, v21
	v_cvt_pk_bf16_f32 v18, v40, v41
	v_cvt_pk_bf16_f32 v19, v30, v31
	v_cvt_pk_bf16_f32 v20, v24, v25
	v_cvt_pk_bf16_f32 v21, v32, v33
	ds_write_b128 v7, v[14:17]
	ds_write_b128 v7, v[18:21] offset:32

.LBB0_2477:
	v_mov_b32_e32 v37, 0
	s_and_saveexec_b64 s[4:5], s[36:37]
	s_cbranch_execz .LBB0_2481
	s_mov_b64 s[22:23], exec
	v_mbcnt_lo_u32_b32 v2, s22, 0
	v_mbcnt_hi_u32_b32 v2, s23, v2
	v_cmp_eq_u32_e32 vcc, 0, v2
	s_and_saveexec_b64 s[6:7], vcc
	s_cbranch_execz .LBB0_2480
	s_bcnt1_i32_b64 s16, s[22:23]
	v_mov_b32_e32 v3, s16
	global_atomic_add v255, v15, v3, s[10:11] sc0
.LBB0_2480:
	s_or_b64 exec, exec, s[6:7]
.LBB0_2481:
	s_or_b64 exec, exec, s[4:5]
	s_add_i32 s4, s66, 0xffffff00
	s_mul_hi_i32 s5, s4, 0x3e0f83e1
	s_lshr_b32 s6, s5, 31
	s_ashr_i32 s59, s5, 5
	s_add_i32 s59, s59, s6
	s_mul_i32 s5, s59, 0x84
	s_sub_i32 s57, s4, s5
	s_ashr_i32 s4, s59, 2
	s_cmp_gt_i32 s57, 3
	s_cselect_b64 s[22:23], -1, 0
	v_mov_b32 v39, v0
	s_mov_b64 s[6:7], -1
	v_readfirstlane_b32 s58, v39
	s_and_b64 vcc, exec, s[22:23]
	s_cbranch_vccz .LBB0_2483
	s_ashr_i32 s5, s4, 31
	s_lshl_b64 s[6:7], s[4:5], 13
	s_lshl_b32 s5, s57, 6
	s_addk_i32 s5, 0xff00
	s_add_u32 s24, s6, s5
	s_addc_u32 s25, s7, 0
	s_mov_b64 s[6:7], 0

.LBB0_2515:
	s_ashr_i32 s4, s57, 31
	v_mad_u32_u24 v18, v20, s51, 0
	v_lshlrev_b32_e32 v54, 1, v14
	v_add_u32_e32 v12, s7, v21
	v_mov_b32_e32 v10, s57
	v_mov_b32_e32 v11, s4
	v_add_u32_e32 v21, v18, v54
	v_mad_i64_i32 v[22:23], s[4:5], v12, s28, v[10:11]
	ds_read_b128 v[10:13], v21 offset:61440
	v_lshlrev_b64 v[22:23], 14, v[22:23]
	v_lshl_add_u64 v[26:27], s[14:15], 0, v[22:23]
	ds_read_b128 v[22:25], v21 offset:61504
	s_waitcnt lgkmcnt(1)
	v_mfma_f32_16x16x32_bf16 v[10:13], v[6:9], v[10:13], 0
	v_lshlrev_b32_e32 v28, 7, v20
	v_add_u32_e32 v20, 40, v14
	v_and_b32_e32 v20, 56, v20
	s_waitcnt lgkmcnt(0)
	v_mfma_f32_16x16x32_bf16 v[10:13], v[2:5], v[22:25], v[10:13]
	v_lshlrev_b32_e32 v47, 1, v20
	v_add_u32_e32 v46, 0xf000, v18
	v_add_u32_e32 v18, v18, v47
	s_lshl_b32 s16, s6, 1
	v_lshl_add_u64 v[26:27], v[26:27], 0, s[16:17]
	s_nop 2
	v_cvt_pk_bf16_f32 v24, v10, v11
	v_cvt_pk_bf16_f32 v25, v12, v13
	ds_read_b128 v[10:13], v21 offset:63760
	ds_read_b128 v[20:23], v18 offset:63744
	s_waitcnt lgkmcnt(1)
	v_mfma_f32_16x16x32_bf16 v[10:13], v[6:9], v[10:13], 0
	v_add_u32_e32 v18, v46, v54
	v_lshl_add_u64 v[26:27], v[26:27], 0, v[14:15]
	v_mov_b32_e32 v29, v15
	s_waitcnt lgkmcnt(0)
	v_mfma_f32_16x16x32_bf16 v[10:13], v[2:5], v[20:23], v[10:13]
	ds_read_b128 v[20:23], v18 offset:4640
	v_lshl_add_u64 v[50:51], v[26:27], 0, v[28:29]
	global_store_dwordx2 v[50:51], v[24:25], off
	s_waitcnt lgkmcnt(0)
	v_mfma_f32_16x16x32_bf16 v[20:23], v[6:9], v[20:23], 0
	s_nop 2
	v_cvt_pk_bf16_f32 v10, v10, v11
	v_add_u32_e32 v11, 48, v14
	v_and_b32_e32 v11, 56, v11
	v_lshl_add_u32 v38, v11, 1, v46
	ds_read_b128 v[24:27], v38 offset:4608
	ds_read_b128 v[28:31], v18 offset:9216
	s_waitcnt lgkmcnt(1)
	v_mfma_f32_16x16x32_bf16 v[20:23], v[2:5], v[24:27], v[20:23]
	v_or_b32_e32 v24, 48, v19
	v_mad_u32_u24 v32, v24, s51, 0
	v_cvt_pk_bf16_f32 v11, v12, v13
	v_add_u32_e32 v24, v32, v54
	global_store_dwordx2 v[50:51], v[10:11], off offset:2048
	ds_read_b128 v[10:13], v18 offset:13856
	ds_read_b128 v[24:27], v24 offset:61488
	v_add_u32_e32 v14, 56, v14
	v_and_b32_e32 v14, 56, v14
	v_lshlrev_b32_e32 v14, 1, v14
	v_add_u32_e32 v32, v32, v14
	ds_read_b128 v[32:35], v32 offset:61440
	ds_read_b128 v[38:41], v38 offset:13824
	ds_read_b128 v[42:45], v18 offset:9280
	s_waitcnt lgkmcnt(3)
	v_mfma_f32_16x16x32_bf16 v[24:27], v[6:9], v[24:27], 0
	v_add_u32_e32 v46, v46, v47
	v_cvt_pk_bf16_f32 v52, v20, v21
	v_cvt_pk_bf16_f32 v53, v22, v23
	s_waitcnt lgkmcnt(2)
	v_mfma_f32_16x16x32_bf16 v[24:27], v[2:5], v[32:35], v[24:27]
	ds_read_b128 v[20:23], v18 offset:11536
	ds_read_b128 v[46:49], v46 offset:11520
	v_or_b32_e32 v18, 0x70, v19
	s_waitcnt lgkmcnt(2)
	v_mfma_f32_16x16x32_bf16 v[32:35], v[6:9], v[42:45], 0
	v_add_co_u32_e32 v42, vcc, s30, v50
	s_nop 1
	v_cvt_pk_bf16_f32 v24, v24, v25
	v_mfma_f32_16x16x32_bf16 v[28:31], v[2:5], v[28:31], v[32:35]
	v_addc_co_u32_e32 v43, vcc, 0, v51, vcc
	v_add_co_u32_e32 v44, vcc, s53, v50
	s_waitcnt lgkmcnt(0)
	v_mfma_f32_16x16x32_bf16 v[32:35], v[6:9], v[46:49], 0
	v_cvt_pk_bf16_f32 v25, v26, v27
	v_addc_co_u32_e32 v45, vcc, 0, v51, vcc
	global_store_dwordx2 v[42:43], v[24:25], off offset:2048
	s_nop 0
	v_cvt_pk_bf16_f32 v24, v28, v29
	v_cvt_pk_bf16_f32 v25, v30, v31
	global_store_dwordx2 v[44:45], v[24:25], off
	v_mfma_f32_16x16x32_bf16 v[24:27], v[6:9], v[38:41], 0
	global_store_dwordx2 v[44:45], v[52:53], off offset:-4096
	v_mfma_f32_16x16x32_bf16 v[20:23], v[2:5], v[20:23], v[32:35]
	v_mfma_f32_16x16x32_bf16 v[10:13], v[2:5], v[10:13], v[24:27]
	s_nop 4
	v_mad_u32_u24 v24, v18, s51, 0
	s_nop 0
	v_cvt_pk_bf16_f32 v20, v20, v21
	v_cvt_pk_bf16_f32 v21, v22, v23
	v_add_u32_e32 v14, v24, v14
	global_store_dwordx2 v[44:45], v[20:21], off offset:2048
	ds_read_b128 v[18:21], v14 offset:61440
	v_cvt_pk_bf16_f32 v22, v10, v11
	v_add_u32_e32 v10, v24, v54
	v_cvt_pk_bf16_f32 v23, v12, v13
	ds_read_b128 v[10:13], v10 offset:61488
	s_waitcnt lgkmcnt(1)
	v_mfma_f32_16x16x32_bf16 v[6:9], v[6:9], v[18:21], 0
	v_add_co_u32_e32 v18, vcc, s54, v50
	s_waitcnt lgkmcnt(0)
	v_mfma_f32_16x16x32_bf16 v[2:5], v[2:5], v[10:13], v[6:9]
	v_addc_co_u32_e32 v19, vcc, 0, v51, vcc
	global_store_dwordx2 v[18:19], v[22:23], off
	s_nop 5
	v_cvt_pk_bf16_f32 v2, v2, v3
	v_cvt_pk_bf16_f32 v3, v4, v5
	global_store_dwordx2 v[18:19], v[2:3], off offset:2048
	s_and_saveexec_b64 s[4:5], s[36:37]
	s_cbranch_execz .LBB0_2476
	v_mov_b32_e32 v2, s55
	s_waitcnt vmcnt(0)
	ds_write_b32 v2, v255
	s_branch .LBB0_2476

.LBB0_2531:
	s_or_b64 exec, exec, s[6:7]
	s_lshl_b32 s6, s38, 6
	v_mov_b32 v132, v0
	s_and_b32 s6, s6, 0x3c00
	v_readfirstlane_b32 s11, v132
	s_ashr_i32 s9, s11, 6
	s_ashr_i32 s10, s38, 8
	s_or_b32 s46, s6, 0x4000
	s_cmp_eq_u32 s10, 1
	s_cselect_b32 s6, s17, 0xd8
	s_cmpk_lt_u32 s38, 0x100
	s_cselect_b32 s7, 16, 0x90
	s_cselect_b32 s8, 0xc8, s6
	s_add_u32 s6, s13, s7
	s_addc_u32 s7, s14, 0
	s_lshr_b32 s39, s46, 8
	v_mov_b32_e32 v2, s39
	global_load_dword v4, v2, s[6:7] sc1
	s_add_u32 s6, s0, s8
	s_addc_u32 s7, s1, 0
	s_load_dwordx2 s[6:7], s[6:7], 0x0
	s_lshl_b32 s8, s38, 7
	s_mul_i32 s38, s9, 0x4400
	s_and_b32 s8, s8, 0x780
	s_add_i32 s47, s38, 0
	s_lshl_b32 s38, s46, 13
	v_bfe_u32 v133, v132, 3, 3
	s_waitcnt lgkmcnt(0)
	s_add_u32 s6, s6, s38
	v_or_b32_e32 v2, s8, v133
	s_addc_u32 s7, s7, 0
	v_lshlrev_b32_e32 v130, 12, v2
	v_lshlrev_b32_e32 v5, 4, v132
	v_lshl_add_u64 v[2:3], s[6:7], 0, v[130:131]
	v_and_b32_e32 v130, 0x70, v5
	s_lshl_b32 s6, s9, 5
	v_lshl_add_u64 v[2:3], v[2:3], 0, v[130:131]
	s_ashr_i32 s7, s6, 31
	v_lshl_add_u64 v[142:143], s[6:7], 2, v[2:3]
	v_add_co_u32_e32 v140, vcc, s19, v142
	global_load_dwordx4 v[66:69], v[142:143], off nt
	s_nop 0
	v_addc_co_u32_e32 v141, vcc, 0, v143, vcc
	v_add_co_u32_e32 v144, vcc, s20, v142
	global_load_dwordx4 v[70:73], v[140:141], off nt
	s_nop 0
	v_addc_co_u32_e32 v145, vcc, 0, v143, vcc
	v_add_co_u32_e32 v146, vcc, s21, v142
	global_load_dwordx4 v[74:77], v[144:145], off nt
	s_nop 0
	v_addc_co_u32_e32 v147, vcc, 0, v143, vcc
	v_add_co_u32_e32 v148, vcc, s22, v142
	global_load_dwordx4 v[78:81], v[146:147], off nt
	s_nop 0
	v_addc_co_u32_e32 v149, vcc, 0, v143, vcc
	v_add_co_u32_e32 v150, vcc, s23, v142
	global_load_dwordx4 v[82:85], v[148:149], off nt
	s_nop 0
	v_addc_co_u32_e32 v151, vcc, 0, v143, vcc
	v_add_co_u32_e32 v152, vcc, s24, v142
	global_load_dwordx4 v[86:89], v[150:151], off nt
	s_nop 0
	v_addc_co_u32_e32 v153, vcc, 0, v143, vcc
	v_add_co_u32_e32 v154, vcc, s25, v142
	global_load_dwordx4 v[90:93], v[152:153], off nt
	s_nop 0
	v_addc_co_u32_e32 v155, vcc, 0, v143, vcc
	v_add_co_u32_e32 v156, vcc, s26, v142
	global_load_dwordx4 v[94:97], v[154:155], off nt
	s_nop 0
	v_addc_co_u32_e32 v157, vcc, 0, v143, vcc
	v_add_co_u32_e32 v158, vcc, s27, v142
	global_load_dwordx4 v[98:101], v[156:157], off nt
	s_nop 0
	v_addc_co_u32_e32 v159, vcc, 0, v143, vcc
	v_add_co_u32_e32 v160, vcc, s28, v142
	global_load_dwordx4 v[102:105], v[158:159], off nt
	s_nop 0
	v_addc_co_u32_e32 v161, vcc, 0, v143, vcc
	v_add_co_u32_e32 v162, vcc, s29, v142
	global_load_dwordx4 v[106:109], v[160:161], off nt
	s_nop 0
	v_addc_co_u32_e32 v163, vcc, 0, v143, vcc
	v_add_co_u32_e32 v164, vcc, s30, v142
	global_load_dwordx4 v[110:113], v[162:163], off nt
	s_nop 0
	v_addc_co_u32_e32 v165, vcc, 0, v143, vcc
	v_add_co_u32_e32 v166, vcc, s31, v142
	global_load_dwordx4 v[114:117], v[164:165], off nt
	s_nop 0
	v_addc_co_u32_e32 v167, vcc, 0, v143, vcc
	v_add_co_u32_e32 v168, vcc, s33, v142
	global_load_dwordx4 v[118:121], v[166:167], off nt
	s_nop 0
	v_addc_co_u32_e32 v169, vcc, 0, v143, vcc
	v_add_co_u32_e32 v170, vcc, s34, v142
	global_load_dwordx4 v[122:125], v[168:169], off nt
	s_nop 0
	v_addc_co_u32_e32 v171, vcc, 0, v143, vcc
	global_load_dwordx4 v[126:129], v[170:171], off nt
	s_waitcnt vmcnt(16)
	v_div_scale_f32 v2, s[38:39], v4, v4, s18
	v_rcp_f32_e32 v3, v2
	v_and_b32_e32 v130, 7, v132
	v_mul_u32_u24_e32 v132, 0x840, v130
	v_lshlrev_b32_e32 v134, 2, v133
	v_fma_f32 v5, -v2, v3, 1.0
	v_fmac_f32_e32 v3, v5, v3
	v_div_scale_f32 v5, vcc, s18, v4, s18
	v_mul_f32_e32 v6, v5, v3
	v_fma_f32 v7, -v2, v6, v5
	v_fmac_f32_e32 v6, v7, v3
	v_fma_f32 v2, -v2, v6, v5
	v_div_fmas_f32 v2, v2, v3, v6
	v_add3_u32 v174, s47, v132, v134
	v_div_fixup_f32 v2, v2, v4, s18
	v_cmp_lt_f32_e32 vcc, 0, v4
	v_add_u32_e32 v175, 0x400, v174
	v_add_u32_e32 v176, 0x600, v174
	v_cndmask_b32_e32 v172, 0, v2, vcc
	global_load_dwordx4 v[50:53], v[142:143], off offset:1024 nt
	global_load_dwordx4 v[54:57], v[140:141], off offset:1024 nt
	global_load_dwordx4 v[58:61], v[144:145], off offset:1024 nt
	global_load_dwordx4 v[62:65], v[146:147], off offset:1024 nt
	global_load_dwordx4 v[34:37], v[148:149], off offset:1024 nt
	global_load_dwordx4 v[38:41], v[150:151], off offset:1024 nt
	global_load_dwordx4 v[42:45], v[152:153], off offset:1024 nt
	global_load_dwordx4 v[46:49], v[154:155], off offset:1024 nt
	global_load_dwordx4 v[18:21], v[156:157], off offset:1024 nt
	global_load_dwordx4 v[22:25], v[158:159], off offset:1024 nt
	global_load_dwordx4 v[26:29], v[160:161], off offset:1024 nt
	global_load_dwordx4 v[30:33], v[162:163], off offset:1024 nt
	global_load_dwordx4 v[2:5], v[164:165], off offset:1024 nt
	global_load_dwordx4 v[6:9], v[166:167], off offset:1024 nt
	global_load_dwordx4 v[10:13], v[168:169], off offset:1024 nt
	global_load_dwordx4 v[14:17], v[170:171], off offset:1024 nt
	s_waitcnt vmcnt(29)
	ds_write2_b32 v174, v66, v74 offset1:8
	s_waitcnt vmcnt(28)
	ds_write2_b32 v174, v70, v78 offset0:64 offset1:72
	ds_write2_b32 v174, v67, v75 offset0:132 offset1:140
	ds_write2_b32 v174, v71, v79 offset0:196 offset1:204
	ds_write2_b32 v175, v68, v76 offset0:8 offset1:16
	ds_write2_b32 v175, v72, v80 offset0:72 offset1:80
	ds_write2_b32 v175, v69, v77 offset0:140 offset1:148
	ds_write2_b32 v175, v73, v81 offset0:204 offset1:212
	s_waitcnt vmcnt(25)
	ds_write2_b32 v174, v82, v90 offset0:16 offset1:24
	s_waitcnt vmcnt(24)
	ds_write2_b32 v174, v86, v94 offset0:80 offset1:88
	ds_write2_b32 v174, v83, v91 offset0:148 offset1:156
	ds_write2_b32 v174, v87, v95 offset0:212 offset1:220
	ds_write2_b32 v175, v84, v92 offset0:24 offset1:32
	ds_write2_b32 v175, v88, v96 offset0:88 offset1:96
	ds_write2_b32 v175, v85, v93 offset0:156 offset1:164
	ds_write2_b32 v175, v89, v97 offset0:220 offset1:228
	s_waitcnt vmcnt(21)
	ds_write2_b32 v174, v98, v106 offset0:32 offset1:40
	s_waitcnt vmcnt(20)
	ds_write2_b32 v174, v102, v110 offset0:96 offset1:104
	ds_write2_b32 v174, v99, v107 offset0:164 offset1:172
	ds_write2_b32 v174, v103, v111 offset0:228 offset1:236
	ds_write2_b32 v175, v100, v108 offset0:40 offset1:48
	ds_write2_b32 v175, v104, v112 offset0:104 offset1:112
	ds_write2_b32 v175, v101, v109 offset0:172 offset1:180
	ds_write2_b32 v175, v105, v113 offset0:236 offset1:244
	s_waitcnt vmcnt(17)
	ds_write2_b32 v174, v114, v122 offset0:48 offset1:56
	s_waitcnt vmcnt(16)
	ds_write2_b32 v174, v118, v126 offset0:112 offset1:120
	ds_write2_b32 v174, v115, v123 offset0:180 offset1:188
	ds_write2_b32 v174, v119, v127 offset0:244 offset1:252
	ds_write2_b32 v175, v116, v124 offset0:56 offset1:64
	ds_write2_b32 v175, v120, v128 offset0:120 offset1:128
	ds_write2_b32 v175, v117, v125 offset0:188 offset1:196
	v_lshlrev_b32_e32 v66, 6, v130
	v_mul_u32_u24_e32 v67, 0x210, v133
	v_add3_u32 v173, s47, v66, v67
	s_lshl_b32 s7, s46, 12
	s_add_u32 s9, s15, s7
	s_addc_u32 s7, s16, 0
	s_and_b32 s38, s11, 0xffffff00
	s_lshl_b32 s10, s10, 7
	s_add_i32 s38, s38, s10
	s_and_b32 s6, s6, 0x60
	s_or_b32 s38, s6, s38
	s_ashr_i32 s39, s38, 31
	s_lshl_b64 s[38:39], s[38:39], 11
	s_add_u32 s38, s9, s38
	s_addc_u32 s39, s7, s39
	s_add_u32 s38, s38, s8
	v_lshlrev_b32_e32 v130, 4, v130
	s_addc_u32 s39, s39, 0
	v_lshlrev_b32_e32 v134, 11, v133
	v_mov_b32_e32 v135, v131
	ds_write2_b32 v176, v121, v129 offset0:124 offset1:132
	s_waitcnt lgkmcnt(0)
	ds_read_b128 v[66:69], v173
	ds_read_b128 v[70:73], v173 offset:16
	ds_read_b128 v[74:77], v173 offset:32
	ds_read_b128 v[78:81], v173 offset:48
	v_or_b32_e32 v136, 0x4000, v134
	v_mov_b32_e32 v137, v131
	s_waitcnt lgkmcnt(2)
	v_mul_f32_e32 v70, v172, v70
	v_mul_f32_e32 v82, v172, v66
	v_mul_f32_e32 v67, v172, v67
	v_mov_b32_e32 v66, 0
	v_cvt_pk_fp8_f32 v66, v82, v67
	v_mul_f32_e32 v71, v172, v71
	v_mov_b32_e32 v67, 0
	v_cvt_pk_fp8_f32 v67, v70, v71
	v_mul_f32_e32 v68, v172, v68
	v_mul_f32_e32 v69, v172, v69
	v_cvt_pk_fp8_f32 v66, v68, v69 op_sel:[0,0,1]
	v_mul_f32_e32 v68, v172, v72
	v_mul_f32_e32 v69, v172, v73
	v_cvt_pk_fp8_f32 v67, v68, v69 op_sel:[0,0,1]
	s_waitcnt lgkmcnt(1)
	v_mul_f32_e32 v69, v172, v74
	v_mul_f32_e32 v70, v172, v75
	v_mov_b32_e32 v68, 0
	v_cvt_pk_fp8_f32 v68, v69, v70
	s_waitcnt lgkmcnt(0)
	v_mul_f32_e32 v72, v172, v78
	v_mul_f32_e32 v73, v172, v79
	v_mov_b32_e32 v69, 0
	v_cvt_pk_fp8_f32 v69, v72, v73
	v_mul_f32_e32 v70, v172, v76
	v_mul_f32_e32 v71, v172, v77
	v_cvt_pk_fp8_f32 v68, v70, v71 op_sel:[0,0,1]
	v_mul_f32_e32 v70, v172, v80
	v_mul_f32_e32 v71, v172, v81
	v_cvt_pk_fp8_f32 v69, v70, v71 op_sel:[0,0,1]
	ds_read_b128 v[70:73], v173 offset:4224
	ds_read_b128 v[74:77], v173 offset:4240
	v_lshl_add_u64 v[78:79], s[38:39], 0, v[130:131]
	v_lshl_add_u64 v[80:81], v[78:79], 0, v[134:135]
	global_store_dwordx4 v[80:81], v[66:69], off nt
	s_waitcnt lgkmcnt(1)
	v_mul_f32_e32 v82, v172, v70
	v_mul_f32_e32 v71, v172, v71
	v_mov_b32_e32 v70, 0
	v_cvt_pk_fp8_f32 v70, v82, v71
	v_mul_f32_e32 v66, v172, v72
	v_mul_f32_e32 v67, v172, v73
	v_mov_b32_e32 v71, 0
	v_cvt_pk_fp8_f32 v70, v66, v67 op_sel:[0,0,1]
	s_waitcnt lgkmcnt(0)
	v_mul_f32_e32 v66, v172, v74
	v_mul_f32_e32 v67, v172, v75
	v_cvt_pk_fp8_f32 v71, v66, v67
	ds_read_b128 v[66:69], v173 offset:4256
	v_mul_f32_e32 v72, v172, v76
	v_mul_f32_e32 v73, v172, v77
	ds_read_b128 v[74:77], v173 offset:4272
	v_cvt_pk_fp8_f32 v71, v72, v73 op_sel:[0,0,1]
	s_waitcnt lgkmcnt(1)
	v_mul_f32_e32 v66, v172, v66
	v_mul_f32_e32 v67, v172, v67
	v_mov_b32_e32 v72, 0
	v_cvt_pk_fp8_f32 v72, v66, v67
	v_mul_f32_e32 v66, v172, v68
	v_mul_f32_e32 v67, v172, v69
	s_waitcnt lgkmcnt(0)
	v_mul_f32_e32 v68, v172, v74
	v_mul_f32_e32 v69, v172, v75
	v_mov_b32_e32 v73, 0
	v_cvt_pk_fp8_f32 v73, v68, v69
	v_cvt_pk_fp8_f32 v72, v66, v67 op_sel:[0,0,1]
	v_mul_f32_e32 v66, v172, v76
	v_mul_f32_e32 v67, v172, v77
	v_cvt_pk_fp8_f32 v73, v66, v67 op_sel:[0,0,1]
	ds_read_b128 v[66:69], v173 offset:8448
	ds_read_b128 v[74:77], v173 offset:8464
	v_lshl_add_u64 v[80:81], v[78:79], 0, v[136:137]
	global_store_dwordx4 v[80:81], v[70:73], off nt
	v_or_b32_e32 v132, 0x8000, v134
	s_waitcnt lgkmcnt(1)
	v_mul_f32_e32 v82, v172, v66
	v_mul_f32_e32 v67, v172, v67
	v_mov_b32_e32 v66, 0
	v_cvt_pk_fp8_f32 v66, v82, v67
	v_mul_f32_e32 v67, v172, v68
	v_mul_f32_e32 v68, v172, v69
	s_waitcnt lgkmcnt(0)
	v_mul_f32_e32 v69, v172, v75
	v_cvt_pk_fp8_f32 v66, v67, v68 op_sel:[0,0,1]
	v_mul_f32_e32 v68, v172, v74
	v_mov_b32_e32 v67, 0
	v_cvt_pk_fp8_f32 v67, v68, v69
	ds_read_b128 v[68:71], v173 offset:8480
	v_mul_f32_e32 v72, v172, v76
	v_mul_f32_e32 v73, v172, v77
	v_cvt_pk_fp8_f32 v67, v72, v73 op_sel:[0,0,1]
	ds_read_b128 v[72:75], v173 offset:8496
	s_waitcnt lgkmcnt(1)
	v_mul_f32_e32 v76, v172, v68
	v_mul_f32_e32 v69, v172, v69
	v_mov_b32_e32 v68, 0
	v_cvt_pk_fp8_f32 v68, v76, v69
	s_waitcnt lgkmcnt(0)
	v_mul_f32_e32 v72, v172, v72
	v_mul_f32_e32 v73, v172, v73
	v_mov_b32_e32 v69, 0
	v_cvt_pk_fp8_f32 v69, v72, v73
	v_mul_f32_e32 v70, v172, v70
	v_mul_f32_e32 v71, v172, v71
	v_cvt_pk_fp8_f32 v68, v70, v71 op_sel:[0,0,1]
	v_mul_f32_e32 v70, v172, v74
	v_mul_f32_e32 v71, v172, v75
	v_cvt_pk_fp8_f32 v69, v70, v71 op_sel:[0,0,1]
	ds_read_b128 v[70:73], v173 offset:12672
	ds_read_b128 v[74:77], v173 offset:12688
	v_mov_b32_e32 v133, v131
	v_lshl_add_u64 v[80:81], v[78:79], 0, v[132:133]
	global_store_dwordx4 v[80:81], v[66:69], off nt
	s_waitcnt lgkmcnt(1)
	v_mul_f32_e32 v82, v172, v70
	v_mul_f32_e32 v71, v172, v71
	v_mov_b32_e32 v70, 0
	v_cvt_pk_fp8_f32 v70, v82, v71
	v_mul_f32_e32 v66, v172, v72
	v_mul_f32_e32 v67, v172, v73
	v_mov_b32_e32 v71, 0
	v_cvt_pk_fp8_f32 v70, v66, v67 op_sel:[0,0,1]
	s_waitcnt lgkmcnt(0)
	v_mul_f32_e32 v66, v172, v74
	v_mul_f32_e32 v67, v172, v75
	v_cvt_pk_fp8_f32 v71, v66, v67
	ds_read_b128 v[66:69], v173 offset:12704
	v_mul_f32_e32 v72, v172, v76
	v_mul_f32_e32 v73, v172, v77
	ds_read_b128 v[74:77], v173 offset:12720
	v_cvt_pk_fp8_f32 v71, v72, v73 op_sel:[0,0,1]
	s_waitcnt lgkmcnt(1)
	v_mul_f32_e32 v66, v172, v66
	v_mul_f32_e32 v67, v172, v67
	v_mov_b32_e32 v72, 0
	v_cvt_pk_fp8_f32 v72, v66, v67
	v_mul_f32_e32 v66, v172, v68
	v_mul_f32_e32 v67, v172, v69
	s_waitcnt lgkmcnt(0)
	v_mul_f32_e32 v68, v172, v74
	v_mul_f32_e32 v69, v172, v75
	v_mov_b32_e32 v73, 0
	v_cvt_pk_fp8_f32 v73, v68, v69
	v_cvt_pk_fp8_f32 v72, v66, v67 op_sel:[0,0,1]
	v_mul_f32_e32 v66, v172, v76
	v_mul_f32_e32 v67, v172, v77
	v_cvt_pk_fp8_f32 v73, v66, v67 op_sel:[0,0,1]
	v_or_b32_e32 v138, 0xc000, v134
	v_mov_b32_e32 v139, v131
	v_lshl_add_u64 v[66:67], v[78:79], 0, v[138:139]
	global_store_dwordx4 v[66:67], v[70:73], off nt
	s_waitcnt lgkmcnt(0)
	global_load_dwordx4 v[114:117], v[142:143], off offset:2048 nt
	global_load_dwordx4 v[118:121], v[140:141], off offset:2048 nt
	global_load_dwordx4 v[122:125], v[144:145], off offset:2048 nt
	global_load_dwordx4 v[126:129], v[146:147], off offset:2048 nt
	global_load_dwordx4 v[98:101], v[148:149], off offset:2048 nt
	global_load_dwordx4 v[102:105], v[150:151], off offset:2048 nt
	global_load_dwordx4 v[106:109], v[152:153], off offset:2048 nt
	global_load_dwordx4 v[110:113], v[154:155], off offset:2048 nt
	global_load_dwordx4 v[82:85], v[156:157], off offset:2048 nt
	global_load_dwordx4 v[86:89], v[158:159], off offset:2048 nt
	global_load_dwordx4 v[90:93], v[160:161], off offset:2048 nt
	global_load_dwordx4 v[94:97], v[162:163], off offset:2048 nt
	global_load_dwordx4 v[66:69], v[164:165], off offset:2048 nt
	global_load_dwordx4 v[70:73], v[166:167], off offset:2048 nt
	global_load_dwordx4 v[74:77], v[168:169], off offset:2048 nt
	global_load_dwordx4 v[78:81], v[170:171], off offset:2048 nt
	s_waitcnt vmcnt(33)
	ds_write2_b32 v174, v50, v58 offset1:8
	s_waitcnt vmcnt(32)
	ds_write2_b32 v174, v54, v62 offset0:64 offset1:72
	ds_write2_b32 v174, v51, v59 offset0:132 offset1:140
	ds_write2_b32 v174, v55, v63 offset0:196 offset1:204
	ds_write2_b32 v175, v52, v60 offset0:8 offset1:16
	ds_write2_b32 v175, v56, v64 offset0:72 offset1:80
	ds_write2_b32 v175, v53, v61 offset0:140 offset1:148
	ds_write2_b32 v175, v57, v65 offset0:204 offset1:212
	s_waitcnt vmcnt(29)
	ds_write2_b32 v174, v34, v42 offset0:16 offset1:24
	s_waitcnt vmcnt(28)
	ds_write2_b32 v174, v38, v46 offset0:80 offset1:88
	ds_write2_b32 v174, v35, v43 offset0:148 offset1:156
	ds_write2_b32 v174, v39, v47 offset0:212 offset1:220
	ds_write2_b32 v175, v36, v44 offset0:24 offset1:32
	ds_write2_b32 v175, v40, v48 offset0:88 offset1:96
	ds_write2_b32 v175, v37, v45 offset0:156 offset1:164
	ds_write2_b32 v175, v41, v49 offset0:220 offset1:228
	s_waitcnt vmcnt(25)
	ds_write2_b32 v174, v18, v26 offset0:32 offset1:40
	s_waitcnt vmcnt(24)
	ds_write2_b32 v174, v22, v30 offset0:96 offset1:104
	ds_write2_b32 v174, v19, v27 offset0:164 offset1:172
	ds_write2_b32 v174, v23, v31 offset0:228 offset1:236
	ds_write2_b32 v175, v20, v28 offset0:40 offset1:48
	ds_write2_b32 v175, v24, v32 offset0:104 offset1:112
	ds_write2_b32 v175, v21, v29 offset0:172 offset1:180
	ds_write2_b32 v175, v25, v33 offset0:236 offset1:244
	s_waitcnt vmcnt(21)
	ds_write2_b32 v174, v2, v10 offset0:48 offset1:56
	s_waitcnt vmcnt(20)
	ds_write2_b32 v174, v6, v14 offset0:112 offset1:120
	ds_write2_b32 v174, v3, v11 offset0:180 offset1:188
	ds_write2_b32 v174, v7, v15 offset0:244 offset1:252
	ds_write2_b32 v175, v4, v12 offset0:56 offset1:64
	ds_write2_b32 v175, v8, v16 offset0:120 offset1:128
	ds_write2_b32 v175, v5, v13 offset0:188 offset1:196
	ds_write2_b32 v176, v9, v17 offset0:124 offset1:132
	s_waitcnt lgkmcnt(0)
	ds_read_b128 v[2:5], v173
	ds_read_b128 v[6:9], v173 offset:16
	ds_read_b128 v[10:13], v173 offset:32
	ds_read_b128 v[14:17], v173 offset:48
	s_andn2_b32 s11, s11, 63
	s_add_i32 s38, s11, 0x200
	s_waitcnt lgkmcnt(2)
	v_mul_f32_e32 v6, v172, v6
	v_mul_f32_e32 v18, v172, v2
	v_mul_f32_e32 v3, v172, v3
	v_mov_b32_e32 v2, 0
	v_cvt_pk_fp8_f32 v2, v18, v3
	v_mul_f32_e32 v7, v172, v7
	v_mov_b32_e32 v3, 0
	v_cvt_pk_fp8_f32 v3, v6, v7
	v_mul_f32_e32 v4, v172, v4
	v_mul_f32_e32 v5, v172, v5
	v_cvt_pk_fp8_f32 v2, v4, v5 op_sel:[0,0,1]
	v_mul_f32_e32 v4, v172, v8
	v_mul_f32_e32 v5, v172, v9
	v_cvt_pk_fp8_f32 v3, v4, v5 op_sel:[0,0,1]
	s_waitcnt lgkmcnt(1)
	v_mul_f32_e32 v5, v172, v10
	v_mul_f32_e32 v6, v172, v11
	v_mov_b32_e32 v4, 0
	v_cvt_pk_fp8_f32 v4, v5, v6
	s_waitcnt lgkmcnt(0)
	v_mul_f32_e32 v8, v172, v14
	v_mul_f32_e32 v9, v172, v15
	v_mov_b32_e32 v5, 0
	v_cvt_pk_fp8_f32 v5, v8, v9
	s_and_b32 s38, s38, 0xffffff00
	v_mul_f32_e32 v6, v172, v12
	v_mul_f32_e32 v7, v172, v13
	s_add_i32 s38, s38, s10
	v_cvt_pk_fp8_f32 v4, v6, v7 op_sel:[0,0,1]
	v_mul_f32_e32 v6, v172, v16
	v_mul_f32_e32 v7, v172, v17
	s_or_b32 s38, s38, s6
	v_cvt_pk_fp8_f32 v5, v6, v7 op_sel:[0,0,1]
	ds_read_b128 v[6:9], v173 offset:4224
	ds_read_b128 v[10:13], v173 offset:4240
	s_ashr_i32 s39, s38, 31
	s_lshl_b64 s[38:39], s[38:39], 11
	s_add_u32 s38, s9, s38
	s_addc_u32 s39, s7, s39
	s_add_u32 s38, s38, s8
	s_waitcnt lgkmcnt(1)
	v_mul_f32_e32 v18, v172, v6
	v_mul_f32_e32 v7, v172, v7
	v_mov_b32_e32 v6, 0
	s_addc_u32 s39, s39, 0
	v_cvt_pk_fp8_f32 v6, v18, v7
	v_lshl_add_u64 v[16:17], s[38:39], 0, v[130:131]
	v_lshl_add_u64 v[14:15], v[16:17], 0, v[134:135]
	global_store_dwordx4 v[14:15], v[2:5], off nt
	v_mov_b32_e32 v7, 0
	s_waitcnt lgkmcnt(0)
	v_mul_f32_e32 v14, v172, v13
	v_mul_f32_e32 v2, v172, v8
	v_mul_f32_e32 v3, v172, v9
	v_cvt_pk_fp8_f32 v6, v2, v3 op_sel:[0,0,1]
	ds_read_b128 v[2:5], v173 offset:4256
	v_mul_f32_e32 v8, v172, v10
	v_mul_f32_e32 v9, v172, v11
	v_cvt_pk_fp8_f32 v7, v8, v9
	v_mul_f32_e32 v9, v172, v12
	ds_read_b128 v[10:13], v173 offset:4272
	s_waitcnt lgkmcnt(1)
	v_mul_f32_e32 v2, v172, v2
	v_mul_f32_e32 v3, v172, v3
	v_mov_b32_e32 v8, 0
	v_cvt_pk_fp8_f32 v8, v2, v3
	v_mul_f32_e32 v2, v172, v4
	v_mul_f32_e32 v3, v172, v5
	v_cvt_pk_fp8_f32 v7, v9, v14 op_sel:[0,0,1]
	v_cvt_pk_fp8_f32 v8, v2, v3 op_sel:[0,0,1]
	s_waitcnt lgkmcnt(0)
	v_mul_f32_e32 v2, v172, v10
	v_mul_f32_e32 v3, v172, v11
	v_mov_b32_e32 v9, 0
	v_cvt_pk_fp8_f32 v9, v2, v3
	ds_read_b128 v[2:5], v173 offset:8448
	v_mul_f32_e32 v10, v172, v12
	v_mul_f32_e32 v11, v172, v13
	v_cvt_pk_fp8_f32 v9, v10, v11 op_sel:[0,0,1]
	ds_read_b128 v[10:13], v173 offset:8464
	s_waitcnt lgkmcnt(1)
	v_mul_f32_e32 v18, v172, v2
	v_mul_f32_e32 v3, v172, v3
	v_mov_b32_e32 v2, 0
	v_cvt_pk_fp8_f32 v2, v18, v3
	v_lshl_add_u64 v[14:15], v[16:17], 0, v[136:137]
	v_mul_f32_e32 v3, v172, v4
	v_mul_f32_e32 v4, v172, v5
	global_store_dwordx4 v[14:15], v[6:9], off nt
	v_cvt_pk_fp8_f32 v2, v3, v4 op_sel:[0,0,1]
	ds_read_b128 v[4:7], v173 offset:8480
	s_waitcnt lgkmcnt(1)
	v_mul_f32_e32 v8, v172, v10
	v_mul_f32_e32 v9, v172, v11
	v_mov_b32_e32 v3, 0
	v_cvt_pk_fp8_f32 v3, v8, v9
	ds_read_b128 v[8:11], v173 offset:8496
	s_waitcnt lgkmcnt(1)
	v_mul_f32_e32 v14, v172, v4
	v_mul_f32_e32 v5, v172, v5
	v_mov_b32_e32 v4, 0
	v_cvt_pk_fp8_f32 v4, v14, v5
	v_mul_f32_e32 v12, v172, v12
	v_mul_f32_e32 v13, v172, v13
	v_mul_f32_e32 v5, v172, v6
	v_mul_f32_e32 v6, v172, v7
	v_cvt_pk_fp8_f32 v3, v12, v13 op_sel:[0,0,1]
	v_cvt_pk_fp8_f32 v4, v5, v6 op_sel:[0,0,1]
	s_waitcnt lgkmcnt(0)
	v_mul_f32_e32 v12, v172, v8
	v_mul_f32_e32 v13, v172, v9
	ds_read_b128 v[6:9], v173 offset:12672
	v_mov_b32_e32 v5, 0
	v_cvt_pk_fp8_f32 v5, v12, v13
	v_mul_f32_e32 v14, v172, v10
	v_mul_f32_e32 v15, v172, v11
	ds_read_b128 v[10:13], v173 offset:12688
	s_waitcnt lgkmcnt(1)
	v_mul_f32_e32 v18, v172, v6
	v_mul_f32_e32 v7, v172, v7
	v_mov_b32_e32 v6, 0
	v_cvt_pk_fp8_f32 v6, v18, v7
	v_mul_f32_e32 v7, v172, v8
	v_mul_f32_e32 v8, v172, v9
	s_waitcnt lgkmcnt(0)
	v_mul_f32_e32 v9, v172, v11
	v_cvt_pk_fp8_f32 v6, v7, v8 op_sel:[0,0,1]
	v_mul_f32_e32 v8, v172, v10
	v_mov_b32_e32 v7, 0
	v_cvt_pk_fp8_f32 v7, v8, v9
	ds_read_b128 v[8:11], v173 offset:12704
	v_mul_f32_e32 v12, v172, v12
	v_mul_f32_e32 v13, v172, v13
	v_cvt_pk_fp8_f32 v5, v14, v15 op_sel:[0,0,1]
	v_cvt_pk_fp8_f32 v7, v12, v13 op_sel:[0,0,1]
	ds_read_b128 v[12:15], v173 offset:12720
	s_waitcnt lgkmcnt(1)
	v_mul_f32_e32 v18, v172, v8
	v_mul_f32_e32 v9, v172, v9
	v_mov_b32_e32 v8, 0
	v_cvt_pk_fp8_f32 v8, v18, v9
	s_waitcnt lgkmcnt(0)
	v_mul_f32_e32 v12, v172, v12
	v_mul_f32_e32 v13, v172, v13
	v_mov_b32_e32 v9, 0
	v_cvt_pk_fp8_f32 v9, v12, v13
	v_mul_f32_e32 v10, v172, v10
	v_mul_f32_e32 v11, v172, v11
	v_cvt_pk_fp8_f32 v8, v10, v11 op_sel:[0,0,1]
	v_mul_f32_e32 v10, v172, v14
	v_mul_f32_e32 v11, v172, v15
	v_cvt_pk_fp8_f32 v9, v10, v11 op_sel:[0,0,1]
	v_lshl_add_u64 v[10:11], v[16:17], 0, v[132:133]
	global_store_dwordx4 v[10:11], v[2:5], off nt
	s_add_i32 s38, s11, 0x400
	s_and_b32 s38, s38, 0xffffff00
	v_lshl_add_u64 v[2:3], v[16:17], 0, v[138:139]
	global_store_dwordx4 v[2:3], v[6:9], off nt
	s_waitcnt lgkmcnt(0)
	global_load_dwordx4 v[42:45], v[142:143], off offset:3072 nt
	global_load_dwordx4 v[46:49], v[140:141], off offset:3072 nt
	global_load_dwordx4 v[58:61], v[144:145], off offset:3072 nt
	global_load_dwordx4 v[62:65], v[146:147], off offset:3072 nt
	global_load_dwordx4 v[34:37], v[148:149], off offset:3072 nt
	global_load_dwordx4 v[38:41], v[150:151], off offset:3072 nt
	global_load_dwordx4 v[50:53], v[152:153], off offset:3072 nt
	global_load_dwordx4 v[54:57], v[154:155], off offset:3072 nt
	global_load_dwordx4 v[18:21], v[156:157], off offset:3072 nt
	global_load_dwordx4 v[22:25], v[158:159], off offset:3072 nt
	global_load_dwordx4 v[26:29], v[160:161], off offset:3072 nt
	global_load_dwordx4 v[30:33], v[162:163], off offset:3072 nt
	global_load_dwordx4 v[2:5], v[164:165], off offset:3072 nt
	global_load_dwordx4 v[6:9], v[166:167], off offset:3072 nt
	global_load_dwordx4 v[10:13], v[168:169], off offset:3072 nt
	global_load_dwordx4 v[14:17], v[170:171], off offset:3072 nt
	s_waitcnt vmcnt(33)
	ds_write2_b32 v174, v114, v122 offset1:8
	s_waitcnt vmcnt(32)
	ds_write2_b32 v174, v118, v126 offset0:64 offset1:72
	ds_write2_b32 v174, v115, v123 offset0:132 offset1:140
	ds_write2_b32 v174, v119, v127 offset0:196 offset1:204
	ds_write2_b32 v175, v116, v124 offset0:8 offset1:16
	ds_write2_b32 v175, v120, v128 offset0:72 offset1:80
	ds_write2_b32 v175, v117, v125 offset0:140 offset1:148
	ds_write2_b32 v175, v121, v129 offset0:204 offset1:212
	s_waitcnt vmcnt(29)
	ds_write2_b32 v174, v98, v106 offset0:16 offset1:24
	s_waitcnt vmcnt(28)
	ds_write2_b32 v174, v102, v110 offset0:80 offset1:88
	ds_write2_b32 v174, v99, v107 offset0:148 offset1:156
	ds_write2_b32 v174, v103, v111 offset0:212 offset1:220
	ds_write2_b32 v175, v100, v108 offset0:24 offset1:32
	ds_write2_b32 v175, v104, v112 offset0:88 offset1:96
	ds_write2_b32 v175, v101, v109 offset0:156 offset1:164
	ds_write2_b32 v175, v105, v113 offset0:220 offset1:228
	s_waitcnt vmcnt(25)
	ds_write2_b32 v174, v82, v90 offset0:32 offset1:40
	s_waitcnt vmcnt(24)
	ds_write2_b32 v174, v86, v94 offset0:96 offset1:104
	ds_write2_b32 v174, v83, v91 offset0:164 offset1:172
	ds_write2_b32 v174, v87, v95 offset0:228 offset1:236
	ds_write2_b32 v175, v84, v92 offset0:40 offset1:48
	ds_write2_b32 v175, v88, v96 offset0:104 offset1:112
	ds_write2_b32 v175, v85, v93 offset0:172 offset1:180
	ds_write2_b32 v175, v89, v97 offset0:236 offset1:244
	s_waitcnt vmcnt(21)
	ds_write2_b32 v174, v66, v74 offset0:48 offset1:56
	s_waitcnt vmcnt(20)
	ds_write2_b32 v174, v70, v78 offset0:112 offset1:120
	ds_write2_b32 v174, v67, v75 offset0:180 offset1:188
	ds_write2_b32 v174, v71, v79 offset0:244 offset1:252
	ds_write2_b32 v175, v68, v76 offset0:56 offset1:64
	ds_write2_b32 v175, v72, v80 offset0:120 offset1:128
	ds_write2_b32 v175, v69, v77 offset0:188 offset1:196
	ds_write2_b32 v176, v73, v81 offset0:124 offset1:132
	s_waitcnt lgkmcnt(0)
	ds_read_b128 v[66:69], v173
	ds_read_b128 v[70:73], v173 offset:16
	ds_read_b128 v[74:77], v173 offset:32
	ds_read_b128 v[78:81], v173 offset:48
	s_add_i32 s38, s38, s10
	s_or_b32 s38, s38, s6
	s_waitcnt lgkmcnt(2)
	v_mul_f32_e32 v70, v172, v70
	v_mul_f32_e32 v82, v172, v66
	v_mul_f32_e32 v67, v172, v67
	v_mov_b32_e32 v66, 0
	v_cvt_pk_fp8_f32 v66, v82, v67
	v_mul_f32_e32 v71, v172, v71
	v_mov_b32_e32 v67, 0
	v_cvt_pk_fp8_f32 v67, v70, v71
	v_mul_f32_e32 v68, v172, v68
	v_mul_f32_e32 v69, v172, v69
	v_cvt_pk_fp8_f32 v66, v68, v69 op_sel:[0,0,1]
	v_mul_f32_e32 v68, v172, v72
	v_mul_f32_e32 v69, v172, v73
	v_cvt_pk_fp8_f32 v67, v68, v69 op_sel:[0,0,1]
	s_waitcnt lgkmcnt(1)
	v_mul_f32_e32 v69, v172, v74
	v_mul_f32_e32 v70, v172, v75
	v_mov_b32_e32 v68, 0
	v_cvt_pk_fp8_f32 v68, v69, v70
	s_waitcnt lgkmcnt(0)
	v_mul_f32_e32 v72, v172, v78
	v_mul_f32_e32 v73, v172, v79
	v_mov_b32_e32 v69, 0
	v_cvt_pk_fp8_f32 v69, v72, v73
	v_mul_f32_e32 v70, v172, v76
	v_mul_f32_e32 v71, v172, v77
	v_cvt_pk_fp8_f32 v68, v70, v71 op_sel:[0,0,1]
	v_mul_f32_e32 v70, v172, v80
	v_mul_f32_e32 v71, v172, v81
	v_cvt_pk_fp8_f32 v69, v70, v71 op_sel:[0,0,1]
	ds_read_b128 v[70:73], v173 offset:4224
	ds_read_b128 v[74:77], v173 offset:4240
	s_ashr_i32 s39, s38, 31
	s_lshl_b64 s[38:39], s[38:39], 11
	s_add_u32 s38, s9, s38
	s_addc_u32 s39, s7, s39
	s_add_u32 s38, s38, s8
	s_waitcnt lgkmcnt(1)
	v_mul_f32_e32 v82, v172, v70
	v_mul_f32_e32 v71, v172, v71
	v_mov_b32_e32 v70, 0
	s_addc_u32 s39, s39, 0
	v_cvt_pk_fp8_f32 v70, v82, v71
	v_lshl_add_u64 v[80:81], s[38:39], 0, v[130:131]
	v_lshl_add_u64 v[78:79], v[80:81], 0, v[134:135]
	global_store_dwordx4 v[78:79], v[66:69], off nt
	v_mov_b32_e32 v71, 0
	s_waitcnt lgkmcnt(0)
	v_mul_f32_e32 v78, v172, v77
	v_mul_f32_e32 v66, v172, v72
	v_mul_f32_e32 v67, v172, v73
	v_cvt_pk_fp8_f32 v70, v66, v67 op_sel:[0,0,1]
	ds_read_b128 v[66:69], v173 offset:4256
	v_mul_f32_e32 v72, v172, v74
	v_mul_f32_e32 v73, v172, v75
	v_cvt_pk_fp8_f32 v71, v72, v73
	v_mul_f32_e32 v73, v172, v76
	ds_read_b128 v[74:77], v173 offset:4272
	s_waitcnt lgkmcnt(1)
	v_mul_f32_e32 v66, v172, v66
	v_mul_f32_e32 v67, v172, v67
	v_mov_b32_e32 v72, 0
	v_cvt_pk_fp8_f32 v72, v66, v67
	v_mul_f32_e32 v66, v172, v68
	v_mul_f32_e32 v67, v172, v69
	v_cvt_pk_fp8_f32 v71, v73, v78 op_sel:[0,0,1]
	v_cvt_pk_fp8_f32 v72, v66, v67 op_sel:[0,0,1]
	s_waitcnt lgkmcnt(0)
	v_mul_f32_e32 v66, v172, v74
	v_mul_f32_e32 v67, v172, v75
	v_mov_b32_e32 v73, 0
	v_cvt_pk_fp8_f32 v73, v66, v67
	ds_read_b128 v[66:69], v173 offset:8448
	v_mul_f32_e32 v74, v172, v76
	v_mul_f32_e32 v75, v172, v77
	v_cvt_pk_fp8_f32 v73, v74, v75 op_sel:[0,0,1]
	ds_read_b128 v[74:77], v173 offset:8464
	s_waitcnt lgkmcnt(1)
	v_mul_f32_e32 v82, v172, v66
	v_mul_f32_e32 v67, v172, v67
	v_mov_b32_e32 v66, 0
	v_cvt_pk_fp8_f32 v66, v82, v67
	v_lshl_add_u64 v[78:79], v[80:81], 0, v[136:137]
	v_mul_f32_e32 v67, v172, v68
	v_mul_f32_e32 v68, v172, v69
	global_store_dwordx4 v[78:79], v[70:73], off nt
	v_cvt_pk_fp8_f32 v66, v67, v68 op_sel:[0,0,1]
	ds_read_b128 v[68:71], v173 offset:8480
	s_waitcnt lgkmcnt(1)
	v_mul_f32_e32 v72, v172, v74
	v_mul_f32_e32 v73, v172, v75
	v_mov_b32_e32 v67, 0
	v_cvt_pk_fp8_f32 v67, v72, v73
	ds_read_b128 v[72:75], v173 offset:8496
	s_waitcnt lgkmcnt(1)
	v_mul_f32_e32 v78, v172, v68
	v_mul_f32_e32 v69, v172, v69
	v_mov_b32_e32 v68, 0
	v_cvt_pk_fp8_f32 v68, v78, v69
	v_mul_f32_e32 v76, v172, v76
	v_mul_f32_e32 v77, v172, v77
	v_mul_f32_e32 v69, v172, v70
	v_mul_f32_e32 v70, v172, v71
	v_cvt_pk_fp8_f32 v67, v76, v77 op_sel:[0,0,1]
	v_cvt_pk_fp8_f32 v68, v69, v70 op_sel:[0,0,1]
	s_waitcnt lgkmcnt(0)
	v_mul_f32_e32 v76, v172, v72
	v_mul_f32_e32 v77, v172, v73
	ds_read_b128 v[70:73], v173 offset:12672
	v_mov_b32_e32 v69, 0
	v_cvt_pk_fp8_f32 v69, v76, v77
	v_mul_f32_e32 v78, v172, v74
	v_mul_f32_e32 v79, v172, v75
	ds_read_b128 v[74:77], v173 offset:12688
	s_waitcnt lgkmcnt(1)
	v_mul_f32_e32 v82, v172, v70
	v_mul_f32_e32 v71, v172, v71
	v_mov_b32_e32 v70, 0
	v_cvt_pk_fp8_f32 v70, v82, v71
	v_mul_f32_e32 v71, v172, v72
	v_mul_f32_e32 v72, v172, v73
	s_waitcnt lgkmcnt(0)
	v_mul_f32_e32 v73, v172, v75
	v_cvt_pk_fp8_f32 v70, v71, v72 op_sel:[0,0,1]
	v_mul_f32_e32 v72, v172, v74
	v_mov_b32_e32 v71, 0
	v_cvt_pk_fp8_f32 v71, v72, v73
	ds_read_b128 v[72:75], v173 offset:12704
	v_mul_f32_e32 v76, v172, v76
	v_mul_f32_e32 v77, v172, v77
	v_cvt_pk_fp8_f32 v69, v78, v79 op_sel:[0,0,1]
	v_cvt_pk_fp8_f32 v71, v76, v77 op_sel:[0,0,1]
	ds_read_b128 v[76:79], v173 offset:12720
	s_waitcnt lgkmcnt(1)
	v_mul_f32_e32 v82, v172, v72
	v_mul_f32_e32 v73, v172, v73
	v_mov_b32_e32 v72, 0
	v_cvt_pk_fp8_f32 v72, v82, v73
	s_waitcnt lgkmcnt(0)
	v_mul_f32_e32 v76, v172, v76
	v_mul_f32_e32 v77, v172, v77
	v_mov_b32_e32 v73, 0
	v_cvt_pk_fp8_f32 v73, v76, v77
	v_mul_f32_e32 v74, v172, v74
	v_mul_f32_e32 v75, v172, v75
	v_cvt_pk_fp8_f32 v72, v74, v75 op_sel:[0,0,1]
	v_mul_f32_e32 v74, v172, v78
	v_mul_f32_e32 v75, v172, v79
	v_cvt_pk_fp8_f32 v73, v74, v75 op_sel:[0,0,1]
	v_lshl_add_u64 v[74:75], v[80:81], 0, v[132:133]
	global_store_dwordx4 v[74:75], v[66:69], off nt
	s_addk_i32 s11, 0x600
	s_and_b32 s11, s11, 0xffffff00
	v_lshl_add_u64 v[66:67], v[80:81], 0, v[138:139]
	global_store_dwordx4 v[66:67], v[70:73], off nt
	s_waitcnt lgkmcnt(0)
	s_waitcnt vmcnt(17)
	ds_write2_b32 v174, v42, v58 offset1:8
	s_waitcnt vmcnt(16)
	ds_write2_b32 v174, v46, v62 offset0:64 offset1:72
	ds_write2_b32 v174, v43, v59 offset0:132 offset1:140
	ds_write2_b32 v174, v47, v63 offset0:196 offset1:204
	ds_write2_b32 v175, v44, v60 offset0:8 offset1:16
	ds_write2_b32 v175, v48, v64 offset0:72 offset1:80
	ds_write2_b32 v175, v45, v61 offset0:140 offset1:148
	ds_write2_b32 v175, v49, v65 offset0:204 offset1:212
	s_waitcnt vmcnt(13)
	ds_write2_b32 v174, v34, v50 offset0:16 offset1:24
	s_waitcnt vmcnt(12)
	ds_write2_b32 v174, v38, v54 offset0:80 offset1:88
	ds_write2_b32 v174, v35, v51 offset0:148 offset1:156
	ds_write2_b32 v174, v39, v55 offset0:212 offset1:220
	ds_write2_b32 v175, v36, v52 offset0:24 offset1:32
	ds_write2_b32 v175, v40, v56 offset0:88 offset1:96
	ds_write2_b32 v175, v37, v53 offset0:156 offset1:164
	ds_write2_b32 v175, v41, v57 offset0:220 offset1:228
	s_waitcnt vmcnt(9)
	ds_write2_b32 v174, v18, v26 offset0:32 offset1:40
	s_waitcnt vmcnt(8)
	ds_write2_b32 v174, v22, v30 offset0:96 offset1:104
	ds_write2_b32 v174, v19, v27 offset0:164 offset1:172
	ds_write2_b32 v174, v23, v31 offset0:228 offset1:236
	ds_write2_b32 v175, v20, v28 offset0:40 offset1:48
	ds_write2_b32 v175, v24, v32 offset0:104 offset1:112
	ds_write2_b32 v175, v21, v29 offset0:172 offset1:180
	ds_write2_b32 v175, v25, v33 offset0:236 offset1:244
	s_waitcnt vmcnt(5)
	ds_write2_b32 v174, v2, v10 offset0:48 offset1:56
	s_waitcnt vmcnt(4)
	ds_write2_b32 v174, v6, v14 offset0:112 offset1:120
	ds_write2_b32 v174, v3, v11 offset0:180 offset1:188
	ds_write2_b32 v174, v7, v15 offset0:244 offset1:252
	ds_write2_b32 v175, v4, v12 offset0:56 offset1:64
	ds_write2_b32 v175, v8, v16 offset0:120 offset1:128
	ds_write2_b32 v175, v5, v13 offset0:188 offset1:196
	ds_write2_b32 v176, v9, v17 offset0:124 offset1:132
	s_waitcnt lgkmcnt(0)
	ds_read_b128 v[2:5], v173
	ds_read_b128 v[6:9], v173 offset:16
	ds_read_b128 v[10:13], v173 offset:32
	ds_read_b128 v[14:17], v173 offset:48
	s_add_i32 s11, s11, s10
	s_or_b32 s10, s11, s6
	s_waitcnt lgkmcnt(2)
	v_mul_f32_e32 v6, v172, v6
	v_mul_f32_e32 v18, v172, v2
	v_mul_f32_e32 v3, v172, v3
	v_mov_b32_e32 v2, 0
	v_cvt_pk_fp8_f32 v2, v18, v3
	v_mul_f32_e32 v7, v172, v7
	v_mov_b32_e32 v3, 0
	v_cvt_pk_fp8_f32 v3, v6, v7
	v_mul_f32_e32 v4, v172, v4
	v_mul_f32_e32 v5, v172, v5
	v_cvt_pk_fp8_f32 v2, v4, v5 op_sel:[0,0,1]
	v_mul_f32_e32 v4, v172, v8
	v_mul_f32_e32 v5, v172, v9
	v_cvt_pk_fp8_f32 v3, v4, v5 op_sel:[0,0,1]
	s_waitcnt lgkmcnt(1)
	v_mul_f32_e32 v5, v172, v10
	v_mul_f32_e32 v6, v172, v11
	v_mov_b32_e32 v4, 0
	v_cvt_pk_fp8_f32 v4, v5, v6
	s_waitcnt lgkmcnt(0)
	v_mul_f32_e32 v8, v172, v14
	v_mul_f32_e32 v9, v172, v15
	v_mov_b32_e32 v5, 0
	v_cvt_pk_fp8_f32 v5, v8, v9
	v_mul_f32_e32 v6, v172, v12
	v_mul_f32_e32 v7, v172, v13
	v_cvt_pk_fp8_f32 v4, v6, v7 op_sel:[0,0,1]
	v_mul_f32_e32 v6, v172, v16
	v_mul_f32_e32 v7, v172, v17
	v_cvt_pk_fp8_f32 v5, v6, v7 op_sel:[0,0,1]
	ds_read_b128 v[6:9], v173 offset:4224
	ds_read_b128 v[10:13], v173 offset:4240
	s_ashr_i32 s11, s10, 31
	s_lshl_b64 s[10:11], s[10:11], 11
	s_add_u32 s6, s9, s10
	s_addc_u32 s7, s7, s11
	s_add_u32 s6, s6, s8
	s_waitcnt lgkmcnt(1)
	v_mul_f32_e32 v18, v172, v6
	v_mul_f32_e32 v7, v172, v7
	v_mov_b32_e32 v6, 0
	s_addc_u32 s7, s7, 0
	v_cvt_pk_fp8_f32 v6, v18, v7
	v_lshl_add_u64 v[16:17], s[6:7], 0, v[130:131]
	v_lshl_add_u64 v[14:15], v[16:17], 0, v[134:135]
	global_store_dwordx4 v[14:15], v[2:5], off nt
	v_mov_b32_e32 v7, 0
	s_waitcnt lgkmcnt(0)
	v_mul_f32_e32 v14, v172, v13
	v_mul_f32_e32 v2, v172, v8
	v_mul_f32_e32 v3, v172, v9
	v_cvt_pk_fp8_f32 v6, v2, v3 op_sel:[0,0,1]
	ds_read_b128 v[2:5], v173 offset:4256
	v_mul_f32_e32 v8, v172, v10
	v_mul_f32_e32 v9, v172, v11
	v_cvt_pk_fp8_f32 v7, v8, v9
	v_mul_f32_e32 v9, v172, v12
	ds_read_b128 v[10:13], v173 offset:4272
	s_waitcnt lgkmcnt(1)
	v_mul_f32_e32 v2, v172, v2
	v_mul_f32_e32 v3, v172, v3
	v_mov_b32_e32 v8, 0
	v_cvt_pk_fp8_f32 v8, v2, v3
	v_mul_f32_e32 v2, v172, v4
	v_mul_f32_e32 v3, v172, v5
	v_cvt_pk_fp8_f32 v7, v9, v14 op_sel:[0,0,1]
	v_cvt_pk_fp8_f32 v8, v2, v3 op_sel:[0,0,1]
	s_waitcnt lgkmcnt(0)
	v_mul_f32_e32 v2, v172, v10
	v_mul_f32_e32 v3, v172, v11
	v_mov_b32_e32 v9, 0
	v_cvt_pk_fp8_f32 v9, v2, v3
	ds_read_b128 v[2:5], v173 offset:8448
	v_mul_f32_e32 v10, v172, v12
	v_mul_f32_e32 v11, v172, v13
	v_cvt_pk_fp8_f32 v9, v10, v11 op_sel:[0,0,1]
	ds_read_b128 v[10:13], v173 offset:8464
	s_waitcnt lgkmcnt(1)
	v_mul_f32_e32 v18, v172, v2
	v_mul_f32_e32 v3, v172, v3
	v_mov_b32_e32 v2, 0
	v_cvt_pk_fp8_f32 v2, v18, v3
	v_lshl_add_u64 v[14:15], v[16:17], 0, v[136:137]
	v_mul_f32_e32 v3, v172, v4
	v_mul_f32_e32 v4, v172, v5
	global_store_dwordx4 v[14:15], v[6:9], off nt
	v_cvt_pk_fp8_f32 v2, v3, v4 op_sel:[0,0,1]
	ds_read_b128 v[4:7], v173 offset:8480
	s_waitcnt lgkmcnt(1)
	v_mul_f32_e32 v8, v172, v10
	v_mul_f32_e32 v9, v172, v11
	v_mov_b32_e32 v3, 0
	v_cvt_pk_fp8_f32 v3, v8, v9
	ds_read_b128 v[8:11], v173 offset:8496
	s_waitcnt lgkmcnt(1)
	v_mul_f32_e32 v14, v172, v4
	v_mul_f32_e32 v5, v172, v5
	v_mov_b32_e32 v4, 0
	v_cvt_pk_fp8_f32 v4, v14, v5
	v_mul_f32_e32 v12, v172, v12
	v_mul_f32_e32 v13, v172, v13
	v_mul_f32_e32 v5, v172, v6
	v_mul_f32_e32 v6, v172, v7
	v_cvt_pk_fp8_f32 v3, v12, v13 op_sel:[0,0,1]
	v_cvt_pk_fp8_f32 v4, v5, v6 op_sel:[0,0,1]
	s_waitcnt lgkmcnt(0)
	v_mul_f32_e32 v12, v172, v8
	v_mul_f32_e32 v13, v172, v9
	ds_read_b128 v[6:9], v173 offset:12672
	v_mov_b32_e32 v5, 0
	v_cvt_pk_fp8_f32 v5, v12, v13
	v_mul_f32_e32 v14, v172, v10
	v_mul_f32_e32 v15, v172, v11
	ds_read_b128 v[10:13], v173 offset:12688
	s_waitcnt lgkmcnt(1)
	v_mul_f32_e32 v18, v172, v6
	v_mul_f32_e32 v7, v172, v7
	v_mov_b32_e32 v6, 0
	v_cvt_pk_fp8_f32 v6, v18, v7
	v_mul_f32_e32 v7, v172, v8
	v_mul_f32_e32 v8, v172, v9
	s_waitcnt lgkmcnt(0)
	v_mul_f32_e32 v9, v172, v11
	v_cvt_pk_fp8_f32 v6, v7, v8 op_sel:[0,0,1]
	v_mul_f32_e32 v8, v172, v10
	v_mov_b32_e32 v7, 0
	v_cvt_pk_fp8_f32 v7, v8, v9
	ds_read_b128 v[8:11], v173 offset:12704
	v_mul_f32_e32 v12, v172, v12
	v_mul_f32_e32 v13, v172, v13
	v_cvt_pk_fp8_f32 v5, v14, v15 op_sel:[0,0,1]
	v_cvt_pk_fp8_f32 v7, v12, v13 op_sel:[0,0,1]
	ds_read_b128 v[12:15], v173 offset:12720
	s_waitcnt lgkmcnt(1)
	v_mul_f32_e32 v18, v172, v8
	v_mul_f32_e32 v9, v172, v9
	v_mov_b32_e32 v8, 0
	v_cvt_pk_fp8_f32 v8, v18, v9
	s_waitcnt lgkmcnt(0)
	v_mul_f32_e32 v12, v172, v12
	v_mul_f32_e32 v13, v172, v13
	v_mov_b32_e32 v9, 0
	v_cvt_pk_fp8_f32 v9, v12, v13
	v_mul_f32_e32 v10, v172, v10
	v_mul_f32_e32 v11, v172, v11
	v_cvt_pk_fp8_f32 v8, v10, v11 op_sel:[0,0,1]
	v_mul_f32_e32 v10, v172, v14
	v_mul_f32_e32 v11, v172, v15
	v_cvt_pk_fp8_f32 v9, v10, v11 op_sel:[0,0,1]
	v_lshl_add_u64 v[10:11], v[16:17], 0, v[132:133]
	global_store_dwordx4 v[10:11], v[2:5], off nt
	s_nop 1
	v_lshl_add_u64 v[2:3], v[16:17], 0, v[138:139]
	global_store_dwordx4 v[2:3], v[6:9], off nt
	s_waitcnt lgkmcnt(0)
	s_barrier
	s_and_saveexec_b64 s[6:7], s[36:37]
	s_cbranch_execz .LBB0_2526
	v_mov_b32_e32 v2, s12
	s_waitcnt vmcnt(0)
	ds_write_b32 v2, v255
	s_branch .LBB0_2526

.LBB0_2660:
	s_or_b64 exec, exec, s[10:11]
.LBB0_2661:
	s_or_b64 exec, exec, s[8:9]
	s_add_i32 s28, s26, 0x180
	s_lshl_b32 s8, s28, 6
	s_and_b32 s27, s8, 0x3c00
	s_bitset1_b32 s27, 14
	s_ashr_i32 s15, s28, 8
	s_lshr_b32 s12, s27, 10
	s_cmp_eq_u32 s15, 2
	s_cselect_b64 s[8:9], -1, 0
	s_cmp_lg_u32 s15, 2
	s_cselect_b64 s[10:11], -1, 0
	v_mov_b32 v66, v0
	s_and_b64 vcc, exec, s[10:11]
	v_readfirstlane_b32 s29, v66
	v_mov_b32_e32 v172, 0
	s_cbranch_vccnz .LBB0_2663
	s_lshl_b32 s13, s12, 2
	v_mov_b32_e32 v2, s13
	global_load_dword v2, v2, s[6:7] sc1
	s_waitcnt vmcnt(0)
	v_div_scale_f32 v3, s[30:31], v2, v2, s24
	v_rcp_f32_e32 v4, v3
	v_div_scale_f32 v5, vcc, s24, v2, s24
	v_fma_f32 v6, -v3, v4, 1.0
	v_fmac_f32_e32 v4, v6, v4
	v_mul_f32_e32 v6, v5, v4
	v_fma_f32 v7, -v3, v6, v5
	v_fmac_f32_e32 v6, v7, v4
	v_fma_f32 v3, -v3, v6, v5
	v_div_fmas_f32 v3, v3, v4, v6
	v_div_fixup_f32 v3, v3, v2, s24
	v_cmp_lt_f32_e32 vcc, 0, v2
	s_nop 1
	v_cndmask_b32_e32 v172, 0, v3, vcc

.LBB0_2666:
	s_ashr_i32 s13, s29, 6
	s_cmp_eq_u32 s15, 1
	s_cselect_b32 s10, s25, 0xd8
	s_cmpk_gt_u32 s28, 0xff
	s_cselect_b32 s10, s10, 0xc8
	s_add_u32 s10, s0, s10
	s_addc_u32 s11, s1, 0
	s_lshl_b32 s28, s26, 5
	s_and_b32 s30, s28, 32
	s_and_b64 s[28:29], s[8:9], exec
	s_load_dwordx2 s[10:11], s[10:11], 0x0
	s_cselect_b32 s28, s30, 0
	s_and_b32 s30, s26, 14
	s_lshl_b32 s26, s26, 1
	s_add_i32 s31, s13, s28
	s_and_b32 s26, s26, 30
	s_and_b64 s[28:29], s[8:9], exec
	s_mulk_i32 s13, 0x4400
	s_cselect_b32 s26, s30, s26
	s_add_i32 s38, s13, 0
	s_lshl_b32 s30, s27, 11
	s_lshl_b32 s13, s27, 13
	s_waitcnt lgkmcnt(0)
	s_add_u32 s10, s10, s13
	s_addc_u32 s11, s11, 0
	s_lshl_b32 s26, s26, 6
	v_bfe_u32 v128, v66, 3, 3
	v_or_b32_e32 v130, s26, v128
	v_lshlrev_b64 v[2:3], s12, v[130:131]
	v_lshlrev_b32_e32 v4, 4, v66
	v_lshl_add_u64 v[2:3], v[2:3], 2, s[10:11]
	v_and_b32_e32 v130, 0x70, v4
	s_lshl_b32 s10, s31, 5
	v_lshl_add_u64 v[2:3], v[2:3], 0, v[130:131]
	s_ashr_i32 s11, s10, 31
	v_lshl_add_u64 v[142:143], s[10:11], 2, v[2:3]
	s_lshl_b64 s[28:29], 64, s12
	v_lshl_add_u64 v[140:141], s[28:29], 2, v[142:143]
	s_lshl_b64 s[28:29], 8, s12
	v_lshl_add_u64 v[144:145], s[28:29], 2, v[142:143]
	s_lshl_b64 s[28:29], 0x48, s12
	v_lshl_add_u64 v[146:147], s[28:29], 2, v[142:143]
	s_lshl_b64 s[28:29], 16, s12
	v_lshl_add_u64 v[148:149], s[28:29], 2, v[142:143]
	s_lshl_b64 s[28:29], 0x50, s12
	v_lshl_add_u64 v[150:151], s[28:29], 2, v[142:143]
	s_lshl_b64 s[28:29], 24, s12
	v_lshl_add_u64 v[152:153], s[28:29], 2, v[142:143]
	s_lshl_b64 s[28:29], 0x58, s12
	v_lshl_add_u64 v[154:155], s[28:29], 2, v[142:143]
	s_lshl_b64 s[28:29], 32, s12
	v_lshl_add_u64 v[156:157], s[28:29], 2, v[142:143]
	s_lshl_b64 s[28:29], 0x60, s12
	v_lshl_add_u64 v[158:159], s[28:29], 2, v[142:143]
	s_lshl_b64 s[28:29], 40, s12
	v_lshl_add_u64 v[160:161], s[28:29], 2, v[142:143]
	s_lshl_b64 s[28:29], 0x68, s12
	v_lshl_add_u64 v[162:163], s[28:29], 2, v[142:143]
	s_lshl_b64 s[28:29], 48, s12
	v_lshl_add_u64 v[164:165], s[28:29], 2, v[142:143]
	s_lshl_b64 s[28:29], 0x70, s12
	v_lshl_add_u64 v[166:167], s[28:29], 2, v[142:143]
	s_lshl_b64 s[28:29], 56, s12
	s_lshl_b64 s[12:13], 0x78, s12
	v_lshl_add_u64 v[168:169], s[28:29], 2, v[142:143]
	v_lshl_add_u64 v[170:171], s[12:13], 2, v[142:143]
	global_load_dwordx4 v[68:71], v[142:143], off nt
	global_load_dwordx4 v[72:75], v[140:141], off nt
	global_load_dwordx4 v[76:79], v[144:145], off nt
	global_load_dwordx4 v[80:83], v[146:147], off nt
	global_load_dwordx4 v[116:119], v[164:165], off nt
	global_load_dwordx4 v[120:123], v[166:167], off nt
	global_load_dwordx4 v[124:127], v[168:169], off nt
	global_load_dwordx4 v[132:135], v[170:171], off nt
	global_load_dwordx4 v[84:87], v[148:149], off nt
	global_load_dwordx4 v[88:91], v[150:151], off nt
	global_load_dwordx4 v[92:95], v[152:153], off nt
	global_load_dwordx4 v[96:99], v[154:155], off nt
	global_load_dwordx4 v[100:103], v[156:157], off nt
	global_load_dwordx4 v[104:107], v[158:159], off nt
	global_load_dwordx4 v[108:111], v[160:161], off nt
	global_load_dwordx4 v[112:115], v[162:163], off nt
	v_and_b32_e32 v129, 7, v66
	v_mul_u32_u24_e32 v66, 0x840, v129
	v_lshlrev_b32_e32 v67, 2, v128
	v_add3_u32 v174, s38, v66, v67
	v_add_u32_e32 v175, 0x400, v174
	v_add_u32_e32 v176, 0x600, v174
	global_load_dwordx4 v[50:53], v[142:143], off offset:1024 nt
	global_load_dwordx4 v[54:57], v[140:141], off offset:1024 nt
	global_load_dwordx4 v[58:61], v[144:145], off offset:1024 nt
	global_load_dwordx4 v[62:65], v[146:147], off offset:1024 nt
	global_load_dwordx4 v[34:37], v[148:149], off offset:1024 nt
	global_load_dwordx4 v[38:41], v[150:151], off offset:1024 nt
	global_load_dwordx4 v[42:45], v[152:153], off offset:1024 nt
	global_load_dwordx4 v[46:49], v[154:155], off offset:1024 nt
	global_load_dwordx4 v[18:21], v[156:157], off offset:1024 nt
	global_load_dwordx4 v[22:25], v[158:159], off offset:1024 nt
	global_load_dwordx4 v[26:29], v[160:161], off offset:1024 nt
	global_load_dwordx4 v[30:33], v[162:163], off offset:1024 nt
	global_load_dwordx4 v[2:5], v[164:165], off offset:1024 nt
	global_load_dwordx4 v[6:9], v[166:167], off offset:1024 nt
	global_load_dwordx4 v[10:13], v[168:169], off offset:1024 nt
	global_load_dwordx4 v[14:17], v[170:171], off offset:1024 nt
	v_lshlrev_b32_e32 v66, 6, v129
	v_mul_u32_u24_e32 v67, 0x210, v128
	v_add3_u32 v173, s38, v66, v67
	s_add_i32 s12, s10, 0x100
	s_ashr_i32 s13, s12, 31
	s_add_u32 s29, s19, s30
	s_addc_u32 s30, s20, 0
	s_lshl_b64 s[34:35], s[10:11], 10
	s_add_u32 s11, s29, s34
	s_addc_u32 s39, s30, s35
	s_lshl_b32 s27, s27, 12
	s_add_u32 s28, s21, s27
	s_addc_u32 s27, s22, 0
	s_waitcnt vmcnt(29)
	ds_write2_b32 v174, v68, v76 offset1:8
	s_waitcnt vmcnt(28)
	ds_write2_b32 v174, v72, v80 offset0:64 offset1:72
	ds_write2_b32 v174, v69, v77 offset0:132 offset1:140
	ds_write2_b32 v174, v73, v81 offset0:196 offset1:204
	ds_write2_b32 v175, v70, v78 offset0:8 offset1:16
	ds_write2_b32 v175, v74, v82 offset0:72 offset1:80
	ds_write2_b32 v175, v71, v79 offset0:140 offset1:148
	ds_write2_b32 v175, v75, v83 offset0:204 offset1:212
	s_waitcnt vmcnt(21)
	ds_write2_b32 v174, v84, v92 offset0:16 offset1:24
	s_waitcnt vmcnt(20)
	ds_write2_b32 v174, v88, v96 offset0:80 offset1:88
	ds_write2_b32 v174, v85, v93 offset0:148 offset1:156
	ds_write2_b32 v174, v89, v97 offset0:212 offset1:220
	ds_write2_b32 v175, v86, v94 offset0:24 offset1:32
	ds_write2_b32 v175, v90, v98 offset0:88 offset1:96
	ds_write2_b32 v175, v87, v95 offset0:156 offset1:164
	ds_write2_b32 v175, v91, v99 offset0:220 offset1:228
	s_waitcnt vmcnt(17)
	ds_write2_b32 v174, v100, v108 offset0:32 offset1:40
	s_waitcnt vmcnt(16)
	ds_write2_b32 v174, v104, v112 offset0:96 offset1:104
	ds_write2_b32 v174, v101, v109 offset0:164 offset1:172
	ds_write2_b32 v174, v105, v113 offset0:228 offset1:236
	ds_write2_b32 v175, v102, v110 offset0:40 offset1:48
	ds_write2_b32 v175, v106, v114 offset0:104 offset1:112
	ds_write2_b32 v175, v103, v111 offset0:172 offset1:180
	ds_write2_b32 v175, v107, v115 offset0:236 offset1:244
	ds_write2_b32 v174, v116, v124 offset0:48 offset1:56
	ds_write2_b32 v174, v120, v132 offset0:112 offset1:120
	ds_write2_b32 v174, v117, v125 offset0:180 offset1:188
	ds_write2_b32 v174, v121, v133 offset0:244 offset1:252
	ds_write2_b32 v175, v118, v126 offset0:56 offset1:64
	ds_write2_b32 v175, v122, v134 offset0:120 offset1:128
	ds_write2_b32 v175, v119, v127 offset0:188 offset1:196
	ds_write2_b32 v176, v123, v135 offset0:124 offset1:132
	s_waitcnt lgkmcnt(0)
	ds_read_b128 v[66:69], v173
	ds_read_b128 v[70:73], v173 offset:16
	ds_read_b128 v[74:77], v173 offset:32
	ds_read_b128 v[78:81], v173 offset:48
	s_lshl_b32 s31, s31, 6
	s_and_b32 s33, s31, 0xffffff00
	s_waitcnt lgkmcnt(2)
	v_mul_f32_e32 v70, v172, v70
	v_mul_f32_e32 v82, v172, v66
	v_mul_f32_e32 v67, v172, v67
	v_mov_b32_e32 v66, 0
	v_cvt_pk_fp8_f32 v66, v82, v67
	v_mul_f32_e32 v71, v172, v71
	v_mov_b32_e32 v67, 0
	v_cvt_pk_fp8_f32 v67, v70, v71
	v_mul_f32_e32 v68, v172, v68
	v_mul_f32_e32 v69, v172, v69
	v_cvt_pk_fp8_f32 v66, v68, v69 op_sel:[0,0,1]
	v_mul_f32_e32 v68, v172, v72
	v_mul_f32_e32 v69, v172, v73
	v_cvt_pk_fp8_f32 v67, v68, v69 op_sel:[0,0,1]
	s_waitcnt lgkmcnt(1)
	v_mul_f32_e32 v69, v172, v74
	v_mul_f32_e32 v70, v172, v75
	v_mov_b32_e32 v68, 0
	v_cvt_pk_fp8_f32 v68, v69, v70
	s_waitcnt lgkmcnt(0)
	v_mul_f32_e32 v72, v172, v78
	v_mul_f32_e32 v73, v172, v79
	v_mov_b32_e32 v69, 0
	s_lshl_b32 s31, s15, 7
	v_cvt_pk_fp8_f32 v69, v72, v73
	s_add_i32 s15, s33, s31
	s_and_b32 s33, s10, 0x60
	s_or_b32 s34, s15, s33
	v_mul_f32_e32 v70, v172, v76
	v_mul_f32_e32 v71, v172, v77
	s_ashr_i32 s35, s34, 31
	v_cvt_pk_fp8_f32 v68, v70, v71 op_sel:[0,0,1]
	v_mul_f32_e32 v70, v172, v80
	v_mul_f32_e32 v71, v172, v81
	s_lshl_b64 s[34:35], s[34:35], 11
	v_cvt_pk_fp8_f32 v69, v70, v71 op_sel:[0,0,1]
	ds_read_b128 v[70:73], v173 offset:4224
	ds_read_b128 v[74:77], v173 offset:4240
	s_add_u32 s15, s28, s34
	s_addc_u32 s48, s27, s35
	s_and_b64 s[34:35], s[8:9], exec
	s_cselect_b32 s11, s11, s15
	s_cselect_b32 s35, s39, s48
	s_add_u32 s34, s11, s26
	s_waitcnt lgkmcnt(1)
	v_mul_f32_e32 v83, v172, v70
	v_mul_f32_e32 v71, v172, v71
	v_mov_b32_e32 v70, 0
	v_lshlrev_b32_e32 v130, 4, v129
	s_addc_u32 s35, s35, 0
	v_cvt_pk_fp8_f32 v70, v83, v71
	v_lshl_add_u64 v[78:79], s[34:35], 0, v[130:131]
	v_lshlrev_b32_e32 v136, s14, v128
	v_mov_b32_e32 v137, v131
	v_lshl_add_u64 v[80:81], v[78:79], 0, v[136:137]
	global_store_dwordx4 v[80:81], v[66:69], off nt
	v_mov_b32_e32 v71, 0
	v_or_b32_e32 v82, 8, v128
	v_mul_f32_e32 v66, v172, v72
	v_mul_f32_e32 v67, v172, v73
	v_cvt_pk_fp8_f32 v70, v66, v67 op_sel:[0,0,1]
	s_waitcnt lgkmcnt(0)
	v_mul_f32_e32 v66, v172, v74
	v_mul_f32_e32 v67, v172, v75
	v_cvt_pk_fp8_f32 v71, v66, v67
	ds_read_b128 v[66:69], v173 offset:4256
	v_mul_f32_e32 v72, v172, v76
	v_mul_f32_e32 v73, v172, v77
	ds_read_b128 v[74:77], v173 offset:4272
	v_cvt_pk_fp8_f32 v71, v72, v73 op_sel:[0,0,1]
	s_waitcnt lgkmcnt(1)
	v_mul_f32_e32 v66, v172, v66
	v_mul_f32_e32 v67, v172, v67
	v_mov_b32_e32 v72, 0
	v_cvt_pk_fp8_f32 v72, v66, v67
	v_mul_f32_e32 v66, v172, v68
	v_mul_f32_e32 v67, v172, v69
	s_waitcnt lgkmcnt(0)
	v_mul_f32_e32 v68, v172, v74
	v_mul_f32_e32 v69, v172, v75
	v_mov_b32_e32 v73, 0
	v_cvt_pk_fp8_f32 v73, v68, v69
	v_cvt_pk_fp8_f32 v72, v66, v67 op_sel:[0,0,1]
	v_mul_f32_e32 v66, v172, v76
	v_mul_f32_e32 v67, v172, v77
	v_cvt_pk_fp8_f32 v73, v66, v67 op_sel:[0,0,1]
	ds_read_b128 v[66:69], v173 offset:8448
	v_lshlrev_b32_e32 v134, s14, v82
	v_mov_b32_e32 v135, v131
	v_lshl_add_u64 v[74:75], v[78:79], 0, v[134:135]
	global_store_dwordx4 v[74:75], v[70:73], off nt
	ds_read_b128 v[70:73], v173 offset:8464
	s_waitcnt lgkmcnt(1)
	v_mul_f32_e32 v74, v172, v66
	v_mul_f32_e32 v67, v172, v67
	v_mov_b32_e32 v66, 0
	v_cvt_pk_fp8_f32 v66, v74, v67
	v_mul_f32_e32 v67, v172, v68
	v_mul_f32_e32 v68, v172, v69
	s_waitcnt lgkmcnt(0)
	v_mul_f32_e32 v69, v172, v71
	v_cvt_pk_fp8_f32 v66, v67, v68 op_sel:[0,0,1]
	v_mul_f32_e32 v68, v172, v70
	v_mov_b32_e32 v67, 0
	v_cvt_pk_fp8_f32 v67, v68, v69
	ds_read_b128 v[68:71], v173 offset:8480
	v_mul_f32_e32 v72, v172, v72
	v_mul_f32_e32 v73, v172, v73
	v_cvt_pk_fp8_f32 v67, v72, v73 op_sel:[0,0,1]
	ds_read_b128 v[72:75], v173 offset:8496
	s_waitcnt lgkmcnt(1)
	v_mul_f32_e32 v77, v172, v68
	v_mul_f32_e32 v69, v172, v69
	v_mov_b32_e32 v68, 0
	v_cvt_pk_fp8_f32 v68, v77, v69
	s_waitcnt lgkmcnt(0)
	v_mul_f32_e32 v72, v172, v72
	v_mul_f32_e32 v73, v172, v73
	v_mov_b32_e32 v69, 0
	v_cvt_pk_fp8_f32 v69, v72, v73
	v_mul_f32_e32 v70, v172, v70
	v_mul_f32_e32 v71, v172, v71
	v_cvt_pk_fp8_f32 v68, v70, v71 op_sel:[0,0,1]
	v_mul_f32_e32 v70, v172, v74
	v_mul_f32_e32 v71, v172, v75
	v_cvt_pk_fp8_f32 v69, v70, v71 op_sel:[0,0,1]
	ds_read_b128 v[70:73], v173 offset:12672
	v_or_b32_e32 v76, 16, v128
	v_lshlrev_b32_e32 v132, s14, v76
	v_mov_b32_e32 v133, v131
	v_lshl_add_u64 v[74:75], v[78:79], 0, v[132:133]
	global_store_dwordx4 v[74:75], v[66:69], off nt
	ds_read_b128 v[66:69], v173 offset:12688
	s_waitcnt lgkmcnt(1)
	v_mul_f32_e32 v74, v172, v70
	v_mul_f32_e32 v71, v172, v71
	v_mov_b32_e32 v70, 0
	v_cvt_pk_fp8_f32 v70, v74, v71
	v_mul_f32_e32 v71, v172, v72
	v_mul_f32_e32 v72, v172, v73
	s_waitcnt lgkmcnt(0)
	v_mul_f32_e32 v66, v172, v66
	v_cvt_pk_fp8_f32 v70, v71, v72 op_sel:[0,0,1]
	v_mul_f32_e32 v67, v172, v67
	v_mov_b32_e32 v71, 0
	v_cvt_pk_fp8_f32 v71, v66, v67
	ds_read_b128 v[72:75], v173 offset:12704
	v_mul_f32_e32 v66, v172, v68
	v_mul_f32_e32 v67, v172, v69
	v_cvt_pk_fp8_f32 v71, v66, v67 op_sel:[0,0,1]
	ds_read_b128 v[66:69], v173 offset:12720
	s_waitcnt lgkmcnt(1)
	v_mul_f32_e32 v77, v172, v72
	v_mul_f32_e32 v73, v172, v73
	v_mov_b32_e32 v72, 0
	v_cvt_pk_fp8_f32 v72, v77, v73
	s_waitcnt lgkmcnt(0)
	v_mul_f32_e32 v66, v172, v66
	v_mul_f32_e32 v67, v172, v67
	v_mov_b32_e32 v73, 0
	v_cvt_pk_fp8_f32 v73, v66, v67
	v_mul_f32_e32 v74, v172, v74
	v_mul_f32_e32 v75, v172, v75
	v_mul_f32_e32 v66, v172, v68
	v_mul_f32_e32 v67, v172, v69
	v_cvt_pk_fp8_f32 v72, v74, v75 op_sel:[0,0,1]
	v_cvt_pk_fp8_f32 v73, v66, v67 op_sel:[0,0,1]
	v_or_b32_e32 v76, 24, v128
	v_lshlrev_b32_e32 v138, s14, v76
	v_mov_b32_e32 v139, v131
	v_lshl_add_u64 v[66:67], v[78:79], 0, v[138:139]
	global_store_dwordx4 v[66:67], v[70:73], off nt
	s_waitcnt lgkmcnt(0)
	global_load_dwordx4 v[114:117], v[142:143], off offset:2048 nt
	global_load_dwordx4 v[118:121], v[140:141], off offset:2048 nt
	global_load_dwordx4 v[122:125], v[144:145], off offset:2048 nt
	global_load_dwordx4 v[126:129], v[146:147], off offset:2048 nt
	global_load_dwordx4 v[98:101], v[148:149], off offset:2048 nt
	global_load_dwordx4 v[102:105], v[150:151], off offset:2048 nt
	global_load_dwordx4 v[106:109], v[152:153], off offset:2048 nt
	global_load_dwordx4 v[110:113], v[154:155], off offset:2048 nt
	global_load_dwordx4 v[82:85], v[156:157], off offset:2048 nt
	global_load_dwordx4 v[86:89], v[158:159], off offset:2048 nt
	global_load_dwordx4 v[90:93], v[160:161], off offset:2048 nt
	global_load_dwordx4 v[94:97], v[162:163], off offset:2048 nt
	global_load_dwordx4 v[66:69], v[164:165], off offset:2048 nt
	global_load_dwordx4 v[70:73], v[166:167], off offset:2048 nt
	global_load_dwordx4 v[74:77], v[168:169], off offset:2048 nt
	global_load_dwordx4 v[78:81], v[170:171], off offset:2048 nt
	s_waitcnt vmcnt(33)
	ds_write2_b32 v174, v50, v58 offset1:8
	s_waitcnt vmcnt(32)
	ds_write2_b32 v174, v54, v62 offset0:64 offset1:72
	ds_write2_b32 v174, v51, v59 offset0:132 offset1:140
	ds_write2_b32 v174, v55, v63 offset0:196 offset1:204
	ds_write2_b32 v175, v52, v60 offset0:8 offset1:16
	ds_write2_b32 v175, v56, v64 offset0:72 offset1:80
	ds_write2_b32 v175, v53, v61 offset0:140 offset1:148
	ds_write2_b32 v175, v57, v65 offset0:204 offset1:212
	s_waitcnt vmcnt(29)
	ds_write2_b32 v174, v34, v42 offset0:16 offset1:24
	s_waitcnt vmcnt(28)
	ds_write2_b32 v174, v38, v46 offset0:80 offset1:88
	ds_write2_b32 v174, v35, v43 offset0:148 offset1:156
	ds_write2_b32 v174, v39, v47 offset0:212 offset1:220
	ds_write2_b32 v175, v36, v44 offset0:24 offset1:32
	ds_write2_b32 v175, v40, v48 offset0:88 offset1:96
	ds_write2_b32 v175, v37, v45 offset0:156 offset1:164
	ds_write2_b32 v175, v41, v49 offset0:220 offset1:228
	s_waitcnt vmcnt(25)
	ds_write2_b32 v174, v18, v26 offset0:32 offset1:40
	s_waitcnt vmcnt(24)
	ds_write2_b32 v174, v22, v30 offset0:96 offset1:104
	ds_write2_b32 v174, v19, v27 offset0:164 offset1:172
	ds_write2_b32 v174, v23, v31 offset0:228 offset1:236
	ds_write2_b32 v175, v20, v28 offset0:40 offset1:48
	ds_write2_b32 v175, v24, v32 offset0:104 offset1:112
	ds_write2_b32 v175, v21, v29 offset0:172 offset1:180
	ds_write2_b32 v175, v25, v33 offset0:236 offset1:244
	s_waitcnt vmcnt(21)
	ds_write2_b32 v174, v2, v10 offset0:48 offset1:56
	s_waitcnt vmcnt(20)
	ds_write2_b32 v174, v6, v14 offset0:112 offset1:120
	ds_write2_b32 v174, v3, v11 offset0:180 offset1:188
	ds_write2_b32 v174, v7, v15 offset0:244 offset1:252
	ds_write2_b32 v175, v4, v12 offset0:56 offset1:64
	ds_write2_b32 v175, v8, v16 offset0:120 offset1:128
	ds_write2_b32 v175, v5, v13 offset0:188 offset1:196
	ds_write2_b32 v176, v9, v17 offset0:124 offset1:132
	s_waitcnt lgkmcnt(0)
	ds_read_b128 v[2:5], v173
	ds_read_b128 v[6:9], v173 offset:16
	ds_read_b128 v[10:13], v173 offset:32
	ds_read_b128 v[14:17], v173 offset:48
	s_add_i32 s14, s10, 0x200
	s_ashr_i32 s15, s14, 31
	s_waitcnt lgkmcnt(2)
	v_mul_f32_e32 v6, v172, v6
	v_mul_f32_e32 v18, v172, v2
	v_mul_f32_e32 v3, v172, v3
	v_mov_b32_e32 v2, 0
	v_cvt_pk_fp8_f32 v2, v18, v3
	v_mul_f32_e32 v7, v172, v7
	v_mov_b32_e32 v3, 0
	v_cvt_pk_fp8_f32 v3, v6, v7
	v_mul_f32_e32 v4, v172, v4
	v_mul_f32_e32 v5, v172, v5
	s_lshl_b64 s[34:35], s[12:13], 10
	v_cvt_pk_fp8_f32 v2, v4, v5 op_sel:[0,0,1]
	v_mul_f32_e32 v4, v172, v8
	v_mul_f32_e32 v5, v172, v9
	s_add_u32 s11, s29, s34
	v_cvt_pk_fp8_f32 v3, v4, v5 op_sel:[0,0,1]
	s_waitcnt lgkmcnt(1)
	v_mul_f32_e32 v5, v172, v10
	v_mul_f32_e32 v6, v172, v11
	v_mov_b32_e32 v4, 0
	s_addc_u32 s34, s30, s35
	s_lshl_b32 s12, s12, 1
	v_cvt_pk_fp8_f32 v4, v5, v6
	s_waitcnt lgkmcnt(0)
	v_mul_f32_e32 v8, v172, v14
	v_mul_f32_e32 v9, v172, v15
	v_mov_b32_e32 v5, 0
	s_and_b32 s12, s12, 0xffffff00
	v_cvt_pk_fp8_f32 v5, v8, v9
	s_add_i32 s12, s12, s31
	s_or_b32 s12, s12, s33
	v_mul_f32_e32 v6, v172, v12
	v_mul_f32_e32 v7, v172, v13
	s_ashr_i32 s13, s12, 31
	v_cvt_pk_fp8_f32 v4, v6, v7 op_sel:[0,0,1]
	v_mul_f32_e32 v6, v172, v16
	v_mul_f32_e32 v7, v172, v17
	s_lshl_b64 s[12:13], s[12:13], 11
	v_cvt_pk_fp8_f32 v5, v6, v7 op_sel:[0,0,1]
	ds_read_b128 v[6:9], v173 offset:4224
	ds_read_b128 v[10:13], v173 offset:4240
	s_add_u32 s35, s28, s12
	s_addc_u32 s38, s27, s13
	s_and_b64 s[12:13], s[8:9], exec
	s_cselect_b32 s11, s11, s35
	s_cselect_b32 s13, s34, s38
	s_add_u32 s12, s11, s26
	s_waitcnt lgkmcnt(1)
	v_mul_f32_e32 v18, v172, v6
	v_mul_f32_e32 v7, v172, v7
	v_mov_b32_e32 v6, 0
	s_addc_u32 s13, s13, 0
	v_cvt_pk_fp8_f32 v6, v18, v7
	v_lshl_add_u64 v[16:17], s[12:13], 0, v[130:131]
	v_lshl_add_u64 v[14:15], v[16:17], 0, v[136:137]
	global_store_dwordx4 v[14:15], v[2:5], off nt
	v_mov_b32_e32 v7, 0
	s_waitcnt lgkmcnt(0)
	v_mul_f32_e32 v14, v172, v13
	v_mul_f32_e32 v2, v172, v8
	v_mul_f32_e32 v3, v172, v9
	v_cvt_pk_fp8_f32 v6, v2, v3 op_sel:[0,0,1]
	ds_read_b128 v[2:5], v173 offset:4256
	v_mul_f32_e32 v8, v172, v10
	v_mul_f32_e32 v9, v172, v11
	v_cvt_pk_fp8_f32 v7, v8, v9
	v_mul_f32_e32 v9, v172, v12
	ds_read_b128 v[10:13], v173 offset:4272
	s_waitcnt lgkmcnt(1)
	v_mul_f32_e32 v2, v172, v2
	v_mul_f32_e32 v3, v172, v3
	v_mov_b32_e32 v8, 0
	v_cvt_pk_fp8_f32 v8, v2, v3
	v_mul_f32_e32 v2, v172, v4
	v_mul_f32_e32 v3, v172, v5
	v_cvt_pk_fp8_f32 v7, v9, v14 op_sel:[0,0,1]
	v_cvt_pk_fp8_f32 v8, v2, v3 op_sel:[0,0,1]
	s_waitcnt lgkmcnt(0)
	v_mul_f32_e32 v2, v172, v10
	v_mul_f32_e32 v3, v172, v11
	v_mov_b32_e32 v9, 0
	v_cvt_pk_fp8_f32 v9, v2, v3
	ds_read_b128 v[2:5], v173 offset:8448
	v_mul_f32_e32 v10, v172, v12
	v_mul_f32_e32 v11, v172, v13
	v_cvt_pk_fp8_f32 v9, v10, v11 op_sel:[0,0,1]
	ds_read_b128 v[10:13], v173 offset:8464
	s_waitcnt lgkmcnt(1)
	v_mul_f32_e32 v18, v172, v2
	v_mul_f32_e32 v3, v172, v3
	v_mov_b32_e32 v2, 0
	v_cvt_pk_fp8_f32 v2, v18, v3
	v_lshl_add_u64 v[14:15], v[16:17], 0, v[134:135]
	v_mul_f32_e32 v3, v172, v4
	v_mul_f32_e32 v4, v172, v5
	global_store_dwordx4 v[14:15], v[6:9], off nt
	v_cvt_pk_fp8_f32 v2, v3, v4 op_sel:[0,0,1]
	ds_read_b128 v[4:7], v173 offset:8480
	s_waitcnt lgkmcnt(1)
	v_mul_f32_e32 v8, v172, v10
	v_mul_f32_e32 v9, v172, v11
	v_mov_b32_e32 v3, 0
	v_cvt_pk_fp8_f32 v3, v8, v9
	ds_read_b128 v[8:11], v173 offset:8496
	s_waitcnt lgkmcnt(1)
	v_mul_f32_e32 v14, v172, v4
	v_mul_f32_e32 v5, v172, v5
	v_mov_b32_e32 v4, 0
	v_cvt_pk_fp8_f32 v4, v14, v5
	v_mul_f32_e32 v12, v172, v12
	v_mul_f32_e32 v13, v172, v13
	v_mul_f32_e32 v5, v172, v6
	v_mul_f32_e32 v6, v172, v7
	v_cvt_pk_fp8_f32 v3, v12, v13 op_sel:[0,0,1]
	v_cvt_pk_fp8_f32 v4, v5, v6 op_sel:[0,0,1]
	s_waitcnt lgkmcnt(0)
	v_mul_f32_e32 v12, v172, v8
	v_mul_f32_e32 v13, v172, v9
	ds_read_b128 v[6:9], v173 offset:12672
	v_mov_b32_e32 v5, 0
	v_cvt_pk_fp8_f32 v5, v12, v13
	v_mul_f32_e32 v14, v172, v10
	v_mul_f32_e32 v15, v172, v11
	ds_read_b128 v[10:13], v173 offset:12688
	s_waitcnt lgkmcnt(1)
	v_mul_f32_e32 v18, v172, v6
	v_mul_f32_e32 v7, v172, v7
	v_mov_b32_e32 v6, 0
	v_cvt_pk_fp8_f32 v6, v18, v7
	v_mul_f32_e32 v7, v172, v8
	v_mul_f32_e32 v8, v172, v9
	s_waitcnt lgkmcnt(0)
	v_mul_f32_e32 v9, v172, v11
	v_cvt_pk_fp8_f32 v6, v7, v8 op_sel:[0,0,1]
	v_mul_f32_e32 v8, v172, v10
	v_mov_b32_e32 v7, 0
	v_cvt_pk_fp8_f32 v7, v8, v9
	ds_read_b128 v[8:11], v173 offset:12704
	v_mul_f32_e32 v12, v172, v12
	v_mul_f32_e32 v13, v172, v13
	v_cvt_pk_fp8_f32 v5, v14, v15 op_sel:[0,0,1]
	v_cvt_pk_fp8_f32 v7, v12, v13 op_sel:[0,0,1]
	ds_read_b128 v[12:15], v173 offset:12720
	s_waitcnt lgkmcnt(1)
	v_mul_f32_e32 v18, v172, v8
	v_mul_f32_e32 v9, v172, v9
	v_mov_b32_e32 v8, 0
	v_cvt_pk_fp8_f32 v8, v18, v9
	s_waitcnt lgkmcnt(0)
	v_mul_f32_e32 v12, v172, v12
	v_mul_f32_e32 v13, v172, v13
	v_mov_b32_e32 v9, 0
	v_cvt_pk_fp8_f32 v9, v12, v13
	v_mul_f32_e32 v10, v172, v10
	v_mul_f32_e32 v11, v172, v11
	v_cvt_pk_fp8_f32 v8, v10, v11 op_sel:[0,0,1]
	v_mul_f32_e32 v10, v172, v14
	v_mul_f32_e32 v11, v172, v15
	v_cvt_pk_fp8_f32 v9, v10, v11 op_sel:[0,0,1]
	v_lshl_add_u64 v[10:11], v[16:17], 0, v[132:133]
	global_store_dwordx4 v[10:11], v[2:5], off nt
	s_addk_i32 s10, 0x300
	s_ashr_i32 s11, s10, 31
	v_lshl_add_u64 v[2:3], v[16:17], 0, v[138:139]
	global_store_dwordx4 v[2:3], v[6:9], off nt
	s_waitcnt lgkmcnt(0)
	global_load_dwordx4 v[42:45], v[142:143], off offset:3072 nt
	global_load_dwordx4 v[46:49], v[140:141], off offset:3072 nt
	global_load_dwordx4 v[58:61], v[144:145], off offset:3072 nt
	global_load_dwordx4 v[62:65], v[146:147], off offset:3072 nt
	global_load_dwordx4 v[34:37], v[148:149], off offset:3072 nt
	global_load_dwordx4 v[38:41], v[150:151], off offset:3072 nt
	global_load_dwordx4 v[50:53], v[152:153], off offset:3072 nt
	global_load_dwordx4 v[54:57], v[154:155], off offset:3072 nt
	global_load_dwordx4 v[18:21], v[156:157], off offset:3072 nt
	global_load_dwordx4 v[22:25], v[158:159], off offset:3072 nt
	global_load_dwordx4 v[26:29], v[160:161], off offset:3072 nt
	global_load_dwordx4 v[30:33], v[162:163], off offset:3072 nt
	global_load_dwordx4 v[2:5], v[164:165], off offset:3072 nt
	global_load_dwordx4 v[6:9], v[166:167], off offset:3072 nt
	global_load_dwordx4 v[10:13], v[168:169], off offset:3072 nt
	global_load_dwordx4 v[14:17], v[170:171], off offset:3072 nt
	s_waitcnt vmcnt(33)
	ds_write2_b32 v174, v114, v122 offset1:8
	s_waitcnt vmcnt(32)
	ds_write2_b32 v174, v118, v126 offset0:64 offset1:72
	ds_write2_b32 v174, v115, v123 offset0:132 offset1:140
	ds_write2_b32 v174, v119, v127 offset0:196 offset1:204
	ds_write2_b32 v175, v116, v124 offset0:8 offset1:16
	ds_write2_b32 v175, v120, v128 offset0:72 offset1:80
	ds_write2_b32 v175, v117, v125 offset0:140 offset1:148
	ds_write2_b32 v175, v121, v129 offset0:204 offset1:212
	s_waitcnt vmcnt(29)
	ds_write2_b32 v174, v98, v106 offset0:16 offset1:24
	s_waitcnt vmcnt(28)
	ds_write2_b32 v174, v102, v110 offset0:80 offset1:88
	ds_write2_b32 v174, v99, v107 offset0:148 offset1:156
	ds_write2_b32 v174, v103, v111 offset0:212 offset1:220
	ds_write2_b32 v175, v100, v108 offset0:24 offset1:32
	ds_write2_b32 v175, v104, v112 offset0:88 offset1:96
	ds_write2_b32 v175, v101, v109 offset0:156 offset1:164
	ds_write2_b32 v175, v105, v113 offset0:220 offset1:228
	s_waitcnt vmcnt(25)
	ds_write2_b32 v174, v82, v90 offset0:32 offset1:40
	s_waitcnt vmcnt(24)
	ds_write2_b32 v174, v86, v94 offset0:96 offset1:104
	ds_write2_b32 v174, v83, v91 offset0:164 offset1:172
	ds_write2_b32 v174, v87, v95 offset0:228 offset1:236
	ds_write2_b32 v175, v84, v92 offset0:40 offset1:48
	ds_write2_b32 v175, v88, v96 offset0:104 offset1:112
	ds_write2_b32 v175, v85, v93 offset0:172 offset1:180
	ds_write2_b32 v175, v89, v97 offset0:236 offset1:244
	s_waitcnt vmcnt(21)
	ds_write2_b32 v174, v66, v74 offset0:48 offset1:56
	s_waitcnt vmcnt(20)
	ds_write2_b32 v174, v70, v78 offset0:112 offset1:120
	ds_write2_b32 v174, v67, v75 offset0:180 offset1:188
	ds_write2_b32 v174, v71, v79 offset0:244 offset1:252
	ds_write2_b32 v175, v68, v76 offset0:56 offset1:64
	ds_write2_b32 v175, v72, v80 offset0:120 offset1:128
	ds_write2_b32 v175, v69, v77 offset0:188 offset1:196
	ds_write2_b32 v176, v73, v81 offset0:124 offset1:132
	s_waitcnt lgkmcnt(0)
	ds_read_b128 v[66:69], v173
	ds_read_b128 v[70:73], v173 offset:16
	ds_read_b128 v[74:77], v173 offset:32
	ds_read_b128 v[78:81], v173 offset:48
	s_lshl_b64 s[12:13], s[14:15], 10
	s_add_u32 s15, s29, s12
	s_waitcnt lgkmcnt(2)
	v_mul_f32_e32 v70, v172, v70
	v_mul_f32_e32 v82, v172, v66
	v_mul_f32_e32 v67, v172, v67
	v_mov_b32_e32 v66, 0
	v_cvt_pk_fp8_f32 v66, v82, v67
	v_mul_f32_e32 v71, v172, v71
	v_mov_b32_e32 v67, 0
	v_cvt_pk_fp8_f32 v67, v70, v71
	v_mul_f32_e32 v68, v172, v68
	v_mul_f32_e32 v69, v172, v69
	v_cvt_pk_fp8_f32 v66, v68, v69 op_sel:[0,0,1]
	v_mul_f32_e32 v68, v172, v72
	v_mul_f32_e32 v69, v172, v73
	v_cvt_pk_fp8_f32 v67, v68, v69 op_sel:[0,0,1]
	s_waitcnt lgkmcnt(1)
	v_mul_f32_e32 v69, v172, v74
	v_mul_f32_e32 v70, v172, v75
	v_mov_b32_e32 v68, 0
	s_addc_u32 s34, s30, s13
	s_lshl_b32 s12, s14, 1
	v_cvt_pk_fp8_f32 v68, v69, v70
	s_waitcnt lgkmcnt(0)
	v_mul_f32_e32 v72, v172, v78
	v_mul_f32_e32 v73, v172, v79
	v_mov_b32_e32 v69, 0
	s_and_b32 s12, s12, 0xffffff00
	v_cvt_pk_fp8_f32 v69, v72, v73
	s_add_i32 s12, s12, s31
	s_or_b32 s12, s12, s33
	v_mul_f32_e32 v70, v172, v76
	v_mul_f32_e32 v71, v172, v77
	s_ashr_i32 s13, s12, 31
	v_cvt_pk_fp8_f32 v68, v70, v71 op_sel:[0,0,1]
	v_mul_f32_e32 v70, v172, v80
	v_mul_f32_e32 v71, v172, v81
	s_lshl_b64 s[12:13], s[12:13], 11
	v_cvt_pk_fp8_f32 v69, v70, v71 op_sel:[0,0,1]
	ds_read_b128 v[70:73], v173 offset:4224
	ds_read_b128 v[74:77], v173 offset:4240
	s_add_u32 s14, s28, s12
	s_addc_u32 s35, s27, s13
	s_and_b64 s[12:13], s[8:9], exec
	s_cselect_b32 s12, s15, s14
	s_cselect_b32 s13, s34, s35
	s_add_u32 s12, s12, s26
	s_waitcnt lgkmcnt(1)
	v_mul_f32_e32 v82, v172, v70
	v_mul_f32_e32 v71, v172, v71
	v_mov_b32_e32 v70, 0
	s_addc_u32 s13, s13, 0
	v_cvt_pk_fp8_f32 v70, v82, v71
	v_lshl_add_u64 v[80:81], s[12:13], 0, v[130:131]
	v_lshl_add_u64 v[78:79], v[80:81], 0, v[136:137]
	global_store_dwordx4 v[78:79], v[66:69], off nt
	v_mov_b32_e32 v71, 0
	s_waitcnt lgkmcnt(0)
	v_mul_f32_e32 v78, v172, v77
	v_mul_f32_e32 v66, v172, v72
	v_mul_f32_e32 v67, v172, v73
	v_cvt_pk_fp8_f32 v70, v66, v67 op_sel:[0,0,1]
	ds_read_b128 v[66:69], v173 offset:4256
	v_mul_f32_e32 v72, v172, v74
	v_mul_f32_e32 v73, v172, v75
	v_cvt_pk_fp8_f32 v71, v72, v73
	v_mul_f32_e32 v73, v172, v76
	ds_read_b128 v[74:77], v173 offset:4272
	s_waitcnt lgkmcnt(1)
	v_mul_f32_e32 v66, v172, v66
	v_mul_f32_e32 v67, v172, v67
	v_mov_b32_e32 v72, 0
	v_cvt_pk_fp8_f32 v72, v66, v67
	v_mul_f32_e32 v66, v172, v68
	v_mul_f32_e32 v67, v172, v69
	v_cvt_pk_fp8_f32 v71, v73, v78 op_sel:[0,0,1]
	v_cvt_pk_fp8_f32 v72, v66, v67 op_sel:[0,0,1]
	s_waitcnt lgkmcnt(0)
	v_mul_f32_e32 v66, v172, v74
	v_mul_f32_e32 v67, v172, v75
	v_mov_b32_e32 v73, 0
	v_cvt_pk_fp8_f32 v73, v66, v67
	ds_read_b128 v[66:69], v173 offset:8448
	v_mul_f32_e32 v74, v172, v76
	v_mul_f32_e32 v75, v172, v77
	v_cvt_pk_fp8_f32 v73, v74, v75 op_sel:[0,0,1]
	ds_read_b128 v[74:77], v173 offset:8464
	s_waitcnt lgkmcnt(1)
	v_mul_f32_e32 v82, v172, v66
	v_mul_f32_e32 v67, v172, v67
	v_mov_b32_e32 v66, 0
	v_cvt_pk_fp8_f32 v66, v82, v67
	v_lshl_add_u64 v[78:79], v[80:81], 0, v[134:135]
	v_mul_f32_e32 v67, v172, v68
	v_mul_f32_e32 v68, v172, v69
	global_store_dwordx4 v[78:79], v[70:73], off nt
	v_cvt_pk_fp8_f32 v66, v67, v68 op_sel:[0,0,1]
	ds_read_b128 v[68:71], v173 offset:8480
	s_waitcnt lgkmcnt(1)
	v_mul_f32_e32 v72, v172, v74
	v_mul_f32_e32 v73, v172, v75
	v_mov_b32_e32 v67, 0
	v_cvt_pk_fp8_f32 v67, v72, v73
	ds_read_b128 v[72:75], v173 offset:8496
	s_waitcnt lgkmcnt(1)
	v_mul_f32_e32 v78, v172, v68
	v_mul_f32_e32 v69, v172, v69
	v_mov_b32_e32 v68, 0
	v_cvt_pk_fp8_f32 v68, v78, v69
	v_mul_f32_e32 v76, v172, v76
	v_mul_f32_e32 v77, v172, v77
	v_mul_f32_e32 v69, v172, v70
	v_mul_f32_e32 v70, v172, v71
	v_cvt_pk_fp8_f32 v67, v76, v77 op_sel:[0,0,1]
	v_cvt_pk_fp8_f32 v68, v69, v70 op_sel:[0,0,1]
	s_waitcnt lgkmcnt(0)
	v_mul_f32_e32 v76, v172, v72
	v_mul_f32_e32 v77, v172, v73
	ds_read_b128 v[70:73], v173 offset:12672
	v_mov_b32_e32 v69, 0
	v_cvt_pk_fp8_f32 v69, v76, v77
	v_mul_f32_e32 v78, v172, v74
	v_mul_f32_e32 v79, v172, v75
	ds_read_b128 v[74:77], v173 offset:12688
	s_waitcnt lgkmcnt(1)
	v_mul_f32_e32 v82, v172, v70
	v_mul_f32_e32 v71, v172, v71
	v_mov_b32_e32 v70, 0
	v_cvt_pk_fp8_f32 v70, v82, v71
	v_mul_f32_e32 v71, v172, v72
	v_mul_f32_e32 v72, v172, v73
	s_waitcnt lgkmcnt(0)
	v_mul_f32_e32 v73, v172, v75
	v_cvt_pk_fp8_f32 v70, v71, v72 op_sel:[0,0,1]
	v_mul_f32_e32 v72, v172, v74
	v_mov_b32_e32 v71, 0
	v_cvt_pk_fp8_f32 v71, v72, v73
	ds_read_b128 v[72:75], v173 offset:12704
	v_mul_f32_e32 v76, v172, v76
	v_mul_f32_e32 v77, v172, v77
	v_cvt_pk_fp8_f32 v69, v78, v79 op_sel:[0,0,1]
	v_cvt_pk_fp8_f32 v71, v76, v77 op_sel:[0,0,1]
	ds_read_b128 v[76:79], v173 offset:12720
	s_waitcnt lgkmcnt(1)
	v_mul_f32_e32 v82, v172, v72
	v_mul_f32_e32 v73, v172, v73
	v_mov_b32_e32 v72, 0
	v_cvt_pk_fp8_f32 v72, v82, v73
	s_waitcnt lgkmcnt(0)
	v_mul_f32_e32 v76, v172, v76
	v_mul_f32_e32 v77, v172, v77
	v_mov_b32_e32 v73, 0
	v_cvt_pk_fp8_f32 v73, v76, v77
	v_mul_f32_e32 v74, v172, v74
	v_mul_f32_e32 v75, v172, v75
	v_cvt_pk_fp8_f32 v72, v74, v75 op_sel:[0,0,1]
	v_mul_f32_e32 v74, v172, v78
	v_mul_f32_e32 v75, v172, v79
	v_cvt_pk_fp8_f32 v73, v74, v75 op_sel:[0,0,1]
	v_lshl_add_u64 v[74:75], v[80:81], 0, v[132:133]
	global_store_dwordx4 v[74:75], v[66:69], off nt
	s_lshl_b64 s[12:13], s[10:11], 10
	s_add_u32 s12, s29, s12
	v_lshl_add_u64 v[66:67], v[80:81], 0, v[138:139]
	global_store_dwordx4 v[66:67], v[70:73], off nt
	s_waitcnt lgkmcnt(0)
	s_waitcnt vmcnt(17)
	ds_write2_b32 v174, v42, v58 offset1:8
	s_waitcnt vmcnt(16)
	ds_write2_b32 v174, v46, v62 offset0:64 offset1:72
	ds_write2_b32 v174, v43, v59 offset0:132 offset1:140
	ds_write2_b32 v174, v47, v63 offset0:196 offset1:204
	ds_write2_b32 v175, v44, v60 offset0:8 offset1:16
	ds_write2_b32 v175, v48, v64 offset0:72 offset1:80
	ds_write2_b32 v175, v45, v61 offset0:140 offset1:148
	ds_write2_b32 v175, v49, v65 offset0:204 offset1:212
	s_waitcnt vmcnt(13)
	ds_write2_b32 v174, v34, v50 offset0:16 offset1:24
	s_waitcnt vmcnt(12)
	ds_write2_b32 v174, v38, v54 offset0:80 offset1:88
	ds_write2_b32 v174, v35, v51 offset0:148 offset1:156
	ds_write2_b32 v174, v39, v55 offset0:212 offset1:220
	ds_write2_b32 v175, v36, v52 offset0:24 offset1:32
	ds_write2_b32 v175, v40, v56 offset0:88 offset1:96
	ds_write2_b32 v175, v37, v53 offset0:156 offset1:164
	ds_write2_b32 v175, v41, v57 offset0:220 offset1:228
	s_waitcnt vmcnt(9)
	ds_write2_b32 v174, v18, v26 offset0:32 offset1:40
	s_waitcnt vmcnt(8)
	ds_write2_b32 v174, v22, v30 offset0:96 offset1:104
	ds_write2_b32 v174, v19, v27 offset0:164 offset1:172
	ds_write2_b32 v174, v23, v31 offset0:228 offset1:236
	ds_write2_b32 v175, v20, v28 offset0:40 offset1:48
	ds_write2_b32 v175, v24, v32 offset0:104 offset1:112
	ds_write2_b32 v175, v21, v29 offset0:172 offset1:180
	ds_write2_b32 v175, v25, v33 offset0:236 offset1:244
	s_waitcnt vmcnt(5)
	ds_write2_b32 v174, v2, v10 offset0:48 offset1:56
	s_waitcnt vmcnt(4)
	ds_write2_b32 v174, v6, v14 offset0:112 offset1:120
	ds_write2_b32 v174, v3, v11 offset0:180 offset1:188
	ds_write2_b32 v174, v7, v15 offset0:244 offset1:252
	ds_write2_b32 v175, v4, v12 offset0:56 offset1:64
	ds_write2_b32 v175, v8, v16 offset0:120 offset1:128
	ds_write2_b32 v175, v5, v13 offset0:188 offset1:196
	ds_write2_b32 v176, v9, v17 offset0:124 offset1:132
	s_waitcnt lgkmcnt(0)
	ds_read_b128 v[2:5], v173
	ds_read_b128 v[6:9], v173 offset:16
	ds_read_b128 v[10:13], v173 offset:32
	ds_read_b128 v[14:17], v173 offset:48
	s_addc_u32 s13, s30, s13
	s_lshl_b32 s10, s10, 1
	s_waitcnt lgkmcnt(2)
	v_mul_f32_e32 v6, v172, v6
	v_mul_f32_e32 v18, v172, v2
	v_mul_f32_e32 v3, v172, v3
	v_mov_b32_e32 v2, 0
	v_cvt_pk_fp8_f32 v2, v18, v3
	v_mul_f32_e32 v7, v172, v7
	v_mov_b32_e32 v3, 0
	v_cvt_pk_fp8_f32 v3, v6, v7
	v_mul_f32_e32 v4, v172, v4
	v_mul_f32_e32 v5, v172, v5
	v_cvt_pk_fp8_f32 v2, v4, v5 op_sel:[0,0,1]
	v_mul_f32_e32 v4, v172, v8
	v_mul_f32_e32 v5, v172, v9
	v_cvt_pk_fp8_f32 v3, v4, v5 op_sel:[0,0,1]
	s_waitcnt lgkmcnt(1)
	v_mul_f32_e32 v5, v172, v10
	v_mul_f32_e32 v6, v172, v11
	v_mov_b32_e32 v4, 0
	v_cvt_pk_fp8_f32 v4, v5, v6
	s_waitcnt lgkmcnt(0)
	v_mul_f32_e32 v8, v172, v14
	v_mul_f32_e32 v9, v172, v15
	v_mov_b32_e32 v5, 0
	s_and_b32 s10, s10, 0xffffff00
	v_cvt_pk_fp8_f32 v5, v8, v9
	s_add_i32 s10, s10, s31
	s_or_b32 s10, s10, s33
	v_mul_f32_e32 v6, v172, v12
	v_mul_f32_e32 v7, v172, v13
	s_ashr_i32 s11, s10, 31
	v_cvt_pk_fp8_f32 v4, v6, v7 op_sel:[0,0,1]
	v_mul_f32_e32 v6, v172, v16
	v_mul_f32_e32 v7, v172, v17
	s_lshl_b64 s[10:11], s[10:11], 11
	v_cvt_pk_fp8_f32 v5, v6, v7 op_sel:[0,0,1]
	ds_read_b128 v[6:9], v173 offset:4224
	ds_read_b128 v[10:13], v173 offset:4240
	s_add_u32 s10, s28, s10
	s_addc_u32 s11, s27, s11
	s_and_b64 s[8:9], s[8:9], exec
	s_cselect_b32 s8, s12, s10
	s_cselect_b32 s9, s13, s11
	s_add_u32 s8, s8, s26
	s_waitcnt lgkmcnt(1)
	v_mul_f32_e32 v18, v172, v6
	v_mul_f32_e32 v7, v172, v7
	v_mov_b32_e32 v6, 0
	s_addc_u32 s9, s9, 0
	v_cvt_pk_fp8_f32 v6, v18, v7
	v_lshl_add_u64 v[16:17], s[8:9], 0, v[130:131]
	v_lshl_add_u64 v[14:15], v[16:17], 0, v[136:137]
	global_store_dwordx4 v[14:15], v[2:5], off nt
	v_mov_b32_e32 v7, 0
	s_waitcnt lgkmcnt(0)
	v_mul_f32_e32 v14, v172, v13
	v_mul_f32_e32 v2, v172, v8
	v_mul_f32_e32 v3, v172, v9
	v_cvt_pk_fp8_f32 v6, v2, v3 op_sel:[0,0,1]
	ds_read_b128 v[2:5], v173 offset:4256
	v_mul_f32_e32 v8, v172, v10
	v_mul_f32_e32 v9, v172, v11
	v_cvt_pk_fp8_f32 v7, v8, v9
	v_mul_f32_e32 v9, v172, v12
	ds_read_b128 v[10:13], v173 offset:4272
	s_waitcnt lgkmcnt(1)
	v_mul_f32_e32 v2, v172, v2
	v_mul_f32_e32 v3, v172, v3
	v_mov_b32_e32 v8, 0
	v_cvt_pk_fp8_f32 v8, v2, v3
	v_mul_f32_e32 v2, v172, v4
	v_mul_f32_e32 v3, v172, v5
	v_cvt_pk_fp8_f32 v7, v9, v14 op_sel:[0,0,1]
	v_cvt_pk_fp8_f32 v8, v2, v3 op_sel:[0,0,1]
	s_waitcnt lgkmcnt(0)
	v_mul_f32_e32 v2, v172, v10
	v_mul_f32_e32 v3, v172, v11
	v_mov_b32_e32 v9, 0
	v_cvt_pk_fp8_f32 v9, v2, v3
	ds_read_b128 v[2:5], v173 offset:8448
	v_mul_f32_e32 v10, v172, v12
	v_mul_f32_e32 v11, v172, v13
	v_cvt_pk_fp8_f32 v9, v10, v11 op_sel:[0,0,1]
	ds_read_b128 v[10:13], v173 offset:8464
	s_waitcnt lgkmcnt(1)
	v_mul_f32_e32 v18, v172, v2
	v_mul_f32_e32 v3, v172, v3
	v_mov_b32_e32 v2, 0
	v_cvt_pk_fp8_f32 v2, v18, v3
	v_lshl_add_u64 v[14:15], v[16:17], 0, v[134:135]
	v_mul_f32_e32 v3, v172, v4
	v_mul_f32_e32 v4, v172, v5
	global_store_dwordx4 v[14:15], v[6:9], off nt
	v_cvt_pk_fp8_f32 v2, v3, v4 op_sel:[0,0,1]
	ds_read_b128 v[4:7], v173 offset:8480
	s_waitcnt lgkmcnt(1)
	v_mul_f32_e32 v8, v172, v10
	v_mul_f32_e32 v9, v172, v11
	v_mov_b32_e32 v3, 0
	v_cvt_pk_fp8_f32 v3, v8, v9
	ds_read_b128 v[8:11], v173 offset:8496
	s_waitcnt lgkmcnt(1)
	v_mul_f32_e32 v14, v172, v4
	v_mul_f32_e32 v5, v172, v5
	v_mov_b32_e32 v4, 0
	v_cvt_pk_fp8_f32 v4, v14, v5
	v_mul_f32_e32 v12, v172, v12
	v_mul_f32_e32 v13, v172, v13
	v_mul_f32_e32 v5, v172, v6
	v_mul_f32_e32 v6, v172, v7
	v_cvt_pk_fp8_f32 v3, v12, v13 op_sel:[0,0,1]
	v_cvt_pk_fp8_f32 v4, v5, v6 op_sel:[0,0,1]
	s_waitcnt lgkmcnt(0)
	v_mul_f32_e32 v12, v172, v8
	v_mul_f32_e32 v13, v172, v9
	ds_read_b128 v[6:9], v173 offset:12672
	v_mov_b32_e32 v5, 0
	v_cvt_pk_fp8_f32 v5, v12, v13
	v_mul_f32_e32 v14, v172, v10
	v_mul_f32_e32 v15, v172, v11
	ds_read_b128 v[10:13], v173 offset:12688
	s_waitcnt lgkmcnt(1)
	v_mul_f32_e32 v18, v172, v6
	v_mul_f32_e32 v7, v172, v7
	v_mov_b32_e32 v6, 0
	v_cvt_pk_fp8_f32 v6, v18, v7
	v_mul_f32_e32 v7, v172, v8
	v_mul_f32_e32 v8, v172, v9
	s_waitcnt lgkmcnt(0)
	v_mul_f32_e32 v9, v172, v11
	v_cvt_pk_fp8_f32 v6, v7, v8 op_sel:[0,0,1]
	v_mul_f32_e32 v8, v172, v10
	v_mov_b32_e32 v7, 0
	v_cvt_pk_fp8_f32 v7, v8, v9
	ds_read_b128 v[8:11], v173 offset:12704
	v_mul_f32_e32 v12, v172, v12
	v_mul_f32_e32 v13, v172, v13
	v_cvt_pk_fp8_f32 v5, v14, v15 op_sel:[0,0,1]
	v_cvt_pk_fp8_f32 v7, v12, v13 op_sel:[0,0,1]
	ds_read_b128 v[12:15], v173 offset:12720
	s_waitcnt lgkmcnt(1)
	v_mul_f32_e32 v18, v172, v8
	v_mul_f32_e32 v9, v172, v9
	v_mov_b32_e32 v8, 0
	v_cvt_pk_fp8_f32 v8, v18, v9
	s_waitcnt lgkmcnt(0)
	v_mul_f32_e32 v12, v172, v12
	v_mul_f32_e32 v13, v172, v13
	v_mov_b32_e32 v9, 0
	v_cvt_pk_fp8_f32 v9, v12, v13
	v_mul_f32_e32 v10, v172, v10
	v_mul_f32_e32 v11, v172, v11
	v_cvt_pk_fp8_f32 v8, v10, v11 op_sel:[0,0,1]
	v_mul_f32_e32 v10, v172, v14
	v_mul_f32_e32 v11, v172, v15
	v_cvt_pk_fp8_f32 v9, v10, v11 op_sel:[0,0,1]
	v_lshl_add_u64 v[10:11], v[16:17], 0, v[132:133]
	global_store_dwordx4 v[10:11], v[2:5], off nt
	s_nop 1
	v_lshl_add_u64 v[2:3], v[16:17], 0, v[138:139]
	global_store_dwordx4 v[2:3], v[6:9], off nt
	s_waitcnt lgkmcnt(0)
	s_barrier
	s_and_saveexec_b64 s[8:9], s[36:37]
	s_cbranch_execz .LBB0_2656
	v_mov_b32_e32 v2, s16
	s_waitcnt vmcnt(0)
	ds_write_b32 v2, v255
	s_branch .LBB0_2656

.LBB0_2676:
	v_mov_b32_e32 v102, 0
	s_and_saveexec_b64 s[4:5], s[36:37]
	s_cbranch_execz .LBB0_2680
	s_mov_b64 s[18:19], exec
	v_mbcnt_lo_u32_b32 v2, s18, 0
	v_mbcnt_hi_u32_b32 v2, s19, v2
	v_cmp_eq_u32_e32 vcc, 0, v2
	s_and_saveexec_b64 s[6:7], vcc
	s_cbranch_execz .LBB0_2679
	s_bcnt1_i32_b64 s8, s[18:19]
	v_mov_b32_e32 v3, s8
	global_atomic_add v255, v79, v3, s[48:49] sc0
.LBB0_2679:
	s_or_b64 exec, exec, s[6:7]
.LBB0_2680:
	s_or_b64 exec, exec, s[4:5]
	v_mov_b32 v85, v0
	s_ashr_i32 s20, s85, 1
	v_readfirstlane_b32 s8, v85
	s_ashr_i32 s8, s8, 2
	s_ashr_i32 s21, s20, 31
	s_and_b32 s22, s8, -16
	s_lshl_b64 s[20:21], s[20:21], 7
	s_ashr_i32 s23, s22, 31
	s_add_u32 s8, s20, s22
	s_addc_u32 s59, s21, s23
	s_mulk_i32 s59, 0x2100
	s_mul_hi_u32 s60, s8, 0x2100
	s_add_i32 s59, s60, s59
	s_mulk_i32 s8, 0x2100
	v_and_b32_e32 v103, 63, v85
	s_add_u32 s60, s10, s8
	s_addc_u32 s61, s11, s59
	v_lshlrev_b32_e32 v78, 4, v103
	s_and_b32 s8, s85, 1
	v_lshlrev_b32_e32 v4, 4, v85
	v_ashrrev_i32_e32 v83, 4, v85
	s_load_dwordx4 s[4:7], s[0:1], 0x68
	s_load_dwordx2 s[18:19], s[0:1], 0x80
	s_waitcnt lgkmcnt(0)
	s_barrier
	v_lshl_add_u64 v[18:19], s[60:61], 0, v[78:79]
	global_load_dwordx4 v[6:9], v78, s[60:61] offset:3584
	s_lshl_b32 s59, s8, 8
	v_and_b32_e32 v78, 0xf0, v4
	v_and_b32_e32 v4, 0xffffff80, v83
	v_bfe_u32 v82, v85, 4, 7
	v_add_u32_e32 v4, s59, v4
	v_add_co_u32_e32 v14, vcc, s27, v18
	v_or_b32_e32 v4, v4, v82
	s_nop 0
	v_addc_co_u32_e32 v15, vcc, 0, v19, vcc
	v_ashrrev_i32_e32 v5, 31, v4
	v_add_co_u32_e32 v2, vcc, s54, v18
	v_lshl_add_u64 v[20:21], s[14:15], 0, v[78:79]
	v_lshlrev_b64 v[4:5], 8, v[4:5]
	v_addc_co_u32_e32 v3, vcc, 0, v19, vcc
	v_lshl_add_u64 v[10:11], v[20:21], 0, v[4:5]
	global_load_dwordx4 v[2:5], v[2:3], off offset:3328
	s_nop 0
	global_load_dwordx4 v[10:13], v[10:11], off
	v_add_u32_e32 v84, 0x200, v85
	v_add_co_u32_e32 v16, vcc, s28, v18
	v_ashrrev_i32_e32 v86, 4, v84
	s_nop 0
	v_addc_co_u32_e32 v17, vcc, 0, v19, vcc
	global_load_dwordx4 v[74:77], v[14:15], off offset:3840
	global_load_dwordx4 v[70:73], v[16:17], off
	v_and_b32_e32 v15, 0xffffff80, v86
	v_bfe_u32 v14, v84, 4, 7
	v_add_u32_e32 v15, s59, v15
	v_or_b32_e32 v14, v15, v14
	v_ashrrev_i32_e32 v15, 31, v14
	v_lshlrev_b64 v[14:15], 8, v[14:15]
	v_lshl_add_u64 v[14:15], v[20:21], 0, v[14:15]
	global_load_dwordx4 v[14:17], v[14:15], off
	v_add_co_u32_e32 v22, vcc, s29, v18
	v_lshrrev_b32_e32 v111, 4, v85
	s_nop 0
	v_addc_co_u32_e32 v23, vcc, 0, v19, vcc
	v_add_co_u32_e32 v24, vcc, s30, v18
	v_add_u32_e32 v90, s55, v78
	s_nop 0
	v_addc_co_u32_e32 v25, vcc, 0, v19, vcc
	global_load_dwordx4 v[66:69], v[22:23], off offset:256
	global_load_dwordx4 v[62:65], v[24:25], off offset:512
	v_add_co_u32_e32 v22, vcc, s31, v18
	v_add_u32_e32 v137, 0xa00, v85
	s_nop 0
	v_addc_co_u32_e32 v23, vcc, 0, v19, vcc
	v_add_co_u32_e32 v24, vcc, s33, v18
	v_ashrrev_i32_e32 v138, 4, v137
	s_nop 0
	v_addc_co_u32_e32 v25, vcc, 0, v19, vcc
	global_load_dwordx4 v[58:61], v[22:23], off offset:768
	global_load_dwordx4 v[54:57], v[24:25], off offset:1024
	v_add_co_u32_e32 v22, vcc, s34, v18
	v_add_u32_e32 v139, 0xc00, v85
	s_nop 0
	v_addc_co_u32_e32 v23, vcc, 0, v19, vcc
	v_add_co_u32_e32 v24, vcc, s35, v18
	v_ashrrev_i32_e32 v140, 4, v139
	s_nop 0
	v_addc_co_u32_e32 v25, vcc, 0, v19, vcc
	global_load_dwordx4 v[50:53], v[22:23], off offset:1280
	global_load_dwordx4 v[46:49], v[24:25], off offset:1536
	v_add_co_u32_e32 v22, vcc, s38, v18
	v_add_u32_e32 v141, 0xe00, v85
	s_nop 0
	v_addc_co_u32_e32 v23, vcc, 0, v19, vcc
	v_add_co_u32_e32 v24, vcc, s39, v18
	v_ashrrev_i32_e32 v142, 4, v141
	s_nop 0
	v_addc_co_u32_e32 v25, vcc, 0, v19, vcc
	global_load_dwordx4 v[42:45], v[22:23], off offset:1792
	global_load_dwordx4 v[38:41], v[24:25], off offset:2048
	v_add_co_u32_e32 v22, vcc, s50, v18
	s_waitcnt vmcnt(13)
	v_lshlrev_b32_e32 v110, 16, v6
	v_addc_co_u32_e32 v23, vcc, 0, v19, vcc
	v_add_co_u32_e32 v24, vcc, s51, v18
	v_and_b32_e32 v109, 0xffff0000, v6
	s_nop 0
	v_addc_co_u32_e32 v25, vcc, 0, v19, vcc
	global_load_dwordx4 v[34:37], v[22:23], off offset:2304
	global_load_dwordx4 v[30:33], v[24:25], off offset:2560
	v_add_co_u32_e32 v22, vcc, s52, v18
	v_add_f32_e32 v6, 0, v110
	s_nop 0
	v_addc_co_u32_e32 v23, vcc, 0, v19, vcc
	v_add_co_u32_e32 v18, vcc, s53, v18
	v_lshlrev_b32_e32 v108, 16, v7
	s_nop 0
	v_addc_co_u32_e32 v19, vcc, 0, v19, vcc
	global_load_dwordx4 v[26:29], v[22:23], off offset:2816
	s_nop 0
	global_load_dwordx4 v[22:25], v[18:19], off offset:3072
	v_bfi_b32 v18, s56, v83, v111
	v_mad_u64_u32 v[18:19], s[60:61], v18, s57, v[90:91]
	s_waitcnt vmcnt(15)
	ds_write_b128 v18, v[10:13]
	v_lshrrev_b32_e32 v10, 4, v84
	v_bfi_b32 v10, s56, v86, v10
	v_mad_u64_u32 v[10:11], s[60:61], v10, s57, v[90:91]
	v_add_u32_e32 v11, 0x400, v85
	v_ashrrev_i32_e32 v18, 4, v11
	v_and_b32_e32 v13, 0xffffff80, v18
	v_bfe_u32 v12, v11, 4, 7
	v_add_u32_e32 v13, s59, v13
	v_or_b32_e32 v12, v13, v12
	v_ashrrev_i32_e32 v13, 31, v12
	v_lshlrev_b64 v[12:13], 8, v[12:13]
	v_lshl_add_u64 v[12:13], v[20:21], 0, v[12:13]
	global_load_dwordx4 v[86:89], v[12:13], off
	s_waitcnt vmcnt(13)
	ds_write_b128 v10, v[14:17]
	v_lshrrev_b32_e32 v10, 4, v11
	v_bfi_b32 v10, s56, v18, v10
	v_mad_u64_u32 v[132:133], s[60:61], v10, s57, v[90:91]
	v_add_u32_e32 v133, 0x600, v85
	v_ashrrev_i32_e32 v135, 4, v133
	v_add_u32_e32 v12, 0x800, v85
	v_and_b32_e32 v11, 0xffffff80, v135
	v_ashrrev_i32_e32 v136, 4, v12
	v_bfe_u32 v10, v133, 4, 7
	v_add_u32_e32 v11, s59, v11
	v_and_b32_e32 v12, 0xffffff80, v136
	v_or_b32_e32 v10, v11, v10
	v_add_u32_e32 v12, s59, v12
	v_ashrrev_i32_e32 v11, 31, v10
	v_or_b32_e32 v12, v12, v82
	v_lshlrev_b64 v[10:11], 8, v[10:11]
	v_ashrrev_i32_e32 v13, 31, v12
	v_lshl_add_u64 v[10:11], v[20:21], 0, v[10:11]
	v_lshlrev_b64 v[12:13], 8, v[12:13]
	v_lshl_add_u64 v[12:13], v[20:21], 0, v[12:13]
	global_load_dwordx4 v[112:115], v[10:11], off
	global_load_dwordx4 v[116:119], v[12:13], off
	v_and_b32_e32 v11, 0xffffff80, v138
	v_bfe_u32 v10, v137, 4, 7
	v_add_u32_e32 v11, s59, v11
	v_and_b32_e32 v13, 0xffffff80, v140
	v_or_b32_e32 v10, v11, v10
	v_bfe_u32 v12, v139, 4, 7
	v_add_u32_e32 v13, s59, v13
	v_ashrrev_i32_e32 v11, 31, v10
	v_or_b32_e32 v12, v13, v12
	v_lshlrev_b64 v[10:11], 8, v[10:11]
	v_ashrrev_i32_e32 v13, 31, v12
	v_lshl_add_u64 v[10:11], v[20:21], 0, v[10:11]
	v_lshlrev_b64 v[12:13], 8, v[12:13]
	v_lshl_add_u64 v[12:13], v[20:21], 0, v[12:13]
	global_load_dwordx4 v[120:123], v[10:11], off
	global_load_dwordx4 v[124:127], v[12:13], off
	v_and_b32_e32 v11, 0xffffff80, v142
	v_bfe_u32 v10, v141, 4, 7
	v_add_u32_e32 v11, s59, v11
	v_add_f32_e32 v6, v6, v109
	v_or_b32_e32 v10, v11, v10
	v_and_b32_e32 v107, 0xffff0000, v7
	v_add_f32_e32 v6, v6, v108
	v_ashrrev_i32_e32 v11, 31, v10
	v_lshlrev_b32_e32 v106, 16, v8
	v_add_f32_e32 v6, v6, v107
	v_lshlrev_b64 v[10:11], 8, v[10:11]
	v_and_b32_e32 v105, 0xffff0000, v8
	v_add_f32_e32 v6, v6, v106
	v_lshl_add_u64 v[10:11], v[20:21], 0, v[10:11]
	v_cmp_lt_i32_e32 vcc, v93, v92
	v_lshlrev_b32_e32 v104, 16, v9
	v_add_f32_e32 v6, v6, v105
	global_load_dwordx4 v[128:131], v[10:11], off
	v_cndmask_b32_e32 v11, v1, v93, vcc
	v_and_b32_e32 v91, 0xffff0000, v9
	v_add_f32_e32 v6, v6, v104
	v_lshlrev_b32_e32 v78, 2, v11
	v_add_f32_e32 v6, v6, v91
	ds_bpermute_b32 v7, v78, v6
	v_cmp_lt_i32_e32 vcc, v94, v92
	v_lshlrev_b32_e32 v10, 5, v103
	global_load_dwordx4 v[14:17], v10, s[4:5] offset:2048
	global_load_dwordx4 v[18:21], v10, s[6:7] offset:2048
	v_cndmask_b32_e32 v8, v1, v94, vcc
	v_lshlrev_b32_e32 v82, 2, v8
	s_waitcnt lgkmcnt(0)
	v_add_f32_e32 v84, v6, v7
	global_load_dwordx4 v[6:9], v10, s[4:5] offset:2064
	s_nop 0
	global_load_dwordx4 v[10:13], v10, s[6:7] offset:2064
	ds_bpermute_b32 v143, v82, v84
	v_cmp_lt_i32_e32 vcc, v95, v92
	v_lshlrev_b32_e32 v134, 3, v103
	s_waitcnt lgkmcnt(0)
	v_add_f32_e32 v143, v84, v143
	v_cndmask_b32_e32 v83, v1, v95, vcc
	v_lshlrev_b32_e32 v83, 2, v83
	ds_bpermute_b32 v144, v83, v143
	v_cmp_lt_i32_e32 vcc, v96, v92
	s_waitcnt vmcnt(9)
	ds_write_b128 v132, v[86:89]
	v_lshrrev_b32_e32 v89, 4, v133
	v_cndmask_b32_e32 v84, v1, v96, vcc
	v_lshlrev_b32_e32 v84, 2, v84
	s_waitcnt lgkmcnt(1)
	v_add_f32_e32 v87, v143, v144
	ds_bpermute_b32 v88, v84, v87
	v_cmp_lt_i32_e32 vcc, v97, v92
	v_bfi_b32 v89, s56, v135, v89
	s_waitcnt lgkmcnt(0)
	v_add_f32_e32 v88, v87, v88
	v_cndmask_b32_e32 v86, v1, v97, vcc
	v_lshlrev_b32_e32 v86, 2, v86
	ds_bpermute_b32 v132, v86, v88
	v_cmp_lt_i32_e32 vcc, v98, v92
	s_waitcnt lgkmcnt(0)
	v_add_f32_e32 v132, v88, v132
	v_cndmask_b32_e32 v87, v1, v98, vcc
	v_lshlrev_b32_e32 v87, 2, v87
	ds_bpermute_b32 v133, v87, v132
	v_mad_u64_u32 v[88:89], s[4:5], v89, s57, v[90:91]
	s_waitcnt vmcnt(8)
	ds_write_b128 v88, v[112:115]
	v_bfi_b32 v88, s56, v136, v111
	s_waitcnt lgkmcnt(1)
	v_add_f32_e32 v89, v132, v133
	v_fmac_f32_e32 v109, 0xbb000000, v89
	v_fmac_f32_e32 v110, 0xbb000000, v89
	v_mul_f32_e32 v111, v109, v109
	v_fmac_f32_e32 v111, v110, v110
	v_fmac_f32_e32 v108, 0xbb000000, v89
	v_fmac_f32_e32 v111, v108, v108
	v_fmac_f32_e32 v107, 0xbb000000, v89
	v_fmac_f32_e32 v111, v107, v107
	v_fmac_f32_e32 v106, 0xbb000000, v89
	v_fmac_f32_e32 v111, v106, v106
	v_fmac_f32_e32 v105, 0xbb000000, v89
	v_fmac_f32_e32 v111, v105, v105
	v_fmac_f32_e32 v104, 0xbb000000, v89
	v_fmac_f32_e32 v111, v104, v104
	v_fmac_f32_e32 v91, 0xbb000000, v89
	v_fmac_f32_e32 v111, v91, v91
	ds_bpermute_b32 v112, v78, v111
	v_mad_u64_u32 v[88:89], s[4:5], v88, s57, v[90:91]
	s_waitcnt vmcnt(7)
	ds_write_b128 v88, v[116:119]
	v_lshrrev_b32_e32 v88, 4, v137
	s_waitcnt lgkmcnt(1)
	v_add_f32_e32 v111, v111, v112
	ds_bpermute_b32 v112, v82, v111
	v_bfi_b32 v88, s56, v138, v88
	v_mad_u64_u32 v[88:89], s[4:5], v88, s57, v[90:91]
	s_waitcnt vmcnt(6)
	ds_write_b128 v88, v[120:123]
	s_waitcnt lgkmcnt(1)
	v_add_f32_e32 v111, v111, v112
	ds_bpermute_b32 v112, v83, v111
	v_lshrrev_b32_e32 v88, 4, v139
	v_bfi_b32 v88, s56, v140, v88
	v_mad_u64_u32 v[88:89], s[4:5], v88, s57, v[90:91]
	s_waitcnt lgkmcnt(0)
	v_add_f32_e32 v111, v111, v112
	ds_bpermute_b32 v112, v84, v111
	s_waitcnt vmcnt(5)
	ds_write_b128 v88, v[124:127]
	v_lshrrev_b32_e32 v88, 4, v141
	v_bfi_b32 v88, s56, v142, v88
	v_mad_u64_u32 v[88:89], s[4:5], v88, s57, v[90:91]
	s_waitcnt lgkmcnt(1)
	v_add_f32_e32 v89, v111, v112
	ds_bpermute_b32 v90, v86, v89
	s_waitcnt vmcnt(4)
	ds_write_b128 v88, v[128:131]
	v_bfe_u32 v88, v85, 5, 1
	v_cmp_eq_u32_e32 vcc, s8, v88
	v_subrev_u32_e32 v88, s59, v134
	s_waitcnt lgkmcnt(1)
	v_add_f32_e32 v111, v89, v90
	ds_bpermute_b32 v112, v87, v111
	v_add_u32_e32 v89, s22, v134
	v_and_b32_e32 v90, 0x78, v89
	v_mul_i32_i24_e32 v88, 0x110, v88
	v_lshlrev_b32_e32 v90, 1, v90
	s_and_saveexec_b64 s[6:7], vcc
	s_cbranch_execz .LBB0_2682
	s_waitcnt lgkmcnt(0)
	v_add_f32_e32 v111, v111, v112
	v_fmamk_f32 v111, v111, 0x3b000000, v99
	v_mul_f32_e32 v112, 0x4b800000, v111
	v_cmp_gt_f32_e64 s[4:5], s58, v111
	s_nop 1
	v_cndmask_b32_e64 v111, v111, v112, s[4:5]
	v_rsq_f32_e32 v111, v111
	v_add3_u32 v112, 0, v90, v88
	v_mul_f32_e32 v113, 0x45800000, v111
	v_cndmask_b32_e64 v111, v111, v113, s[4:5]
	v_mul_f32_e32 v110, v110, v111
	v_mul_f32_e32 v109, v109, v111
	v_mul_f32_e32 v108, v108, v111
	v_mul_f32_e32 v107, v107, v111
	v_mul_f32_e32 v106, v106, v111
	v_mul_f32_e32 v105, v105, v111
	v_mul_f32_e32 v104, v104, v111
	v_mul_f32_e32 v91, v91, v111
	s_waitcnt vmcnt(2)
	v_fma_f32 v110, v14, v110, v18
	v_fma_f32 v109, v15, v109, v19
	v_fma_f32 v108, v16, v108, v20
	v_fma_f32 v107, v17, v107, v21
	s_waitcnt vmcnt(0)
	v_fma_f32 v106, v6, v106, v10
	v_fma_f32 v105, v7, v105, v11
	v_fma_f32 v104, v8, v104, v12
	v_fma_f32 v91, v9, v91, v13
	v_cvt_pk_bf16_f32 v110, v110, s0
	v_cvt_pk_bf16_f32 v109, v109, s0
	v_cvt_pk_bf16_f32 v108, v108, s0
	v_cvt_pk_bf16_f32 v107, v107, s0
	v_cvt_pk_bf16_f32 v106, v106, s0
	v_cvt_pk_bf16_f32 v105, v105, s0
	v_cvt_pk_bf16_f32 v104, v104, s0
	v_cvt_pk_bf16_f32 v91, v91, s0
	ds_write_b16 v112, v110
	ds_write_b16 v112, v109 offset:272
	ds_write_b16 v112, v108 offset:544
	ds_write_b16 v112, v107 offset:816
	ds_write_b16 v112, v106 offset:1088
	ds_write_b16 v112, v105 offset:1360
	ds_write_b16 v112, v104 offset:1632
	ds_write_b16 v112, v91 offset:1904

.LBB0_2777:
	v_mov_b32_e32 v2, s24
	s_waitcnt vmcnt(0)
	ds_write_b32 v2, v255
	s_branch .LBB0_2675

.LBB0_2781:
	v_mov_b32_e32 v107, 0
	s_and_saveexec_b64 s[4:5], s[36:37]
	s_cbranch_execz .LBB0_2785
	s_mov_b64 s[8:9], exec
	v_mbcnt_lo_u32_b32 v2, s8, 0
	v_mbcnt_hi_u32_b32 v2, s9, v2
	v_cmp_eq_u32_e32 vcc, 0, v2
	s_and_saveexec_b64 s[6:7], vcc
	s_cbranch_execz .LBB0_2784
	s_bcnt1_i32_b64 s8, s[8:9]
	v_mov_b32_e32 v3, s8
	global_atomic_add v255, v67, v3, s[48:49] sc0
.LBB0_2784:
	s_or_b64 exec, exec, s[6:7]
.LBB0_2785:
	s_or_b64 exec, exec, s[4:5]
	v_mov_b32 v111, v0
	s_lshl_b32 s86, s85, 5
	v_readfirstlane_b32 s4, v111
	s_ashr_i32 s4, s4, 6
	s_and_b32 s87, s4, 3
	s_lshl_b32 s4, s4, 2
	s_and_b32 s4, s4, -16
	s_add_i32 s86, s86, s4
	v_and_b32_e32 v108, 15, v111
	s_add_i32 s85, s86, 0xffffe000
	s_barrier
	s_load_dwordx2 s[62:63], s[0:1], 0x60
	v_or_b32_e32 v68, s85, v108
	v_cmp_gt_i32_e32 vcc, s66, v68
	v_and_b32_e32 v112, 3, v111
	s_cmp_lt_i32 s87, 2
	v_cndmask_b32_e32 v2, v105, v106, vcc
	v_bitop3_b32 v109, v2, s85, v108 bitop3:0xe0
	v_lshrrev_b32_e32 v2, 1, v111
	v_cndmask_b32_e32 v110, v1, v104, vcc
	v_and_b32_e32 v66, 24, v2
	s_mov_b64 s[4:5], -1
	s_cbranch_scc1 .LBB0_2826
	v_add_u32_e32 v113, 3, v109
	s_mov_b64 s[6:7], -1
	s_cmp_gt_i32 s87, 2
	v_add_u32_e32 v114, 4, v109
	v_cmp_lt_u32_e64 s[4:5], v113, v110
	s_cbranch_scc0 .LBB0_2806
	v_subrev_co_u32_e32 v2, vcc, 8, v109
	v_add_u32_e32 v6, 8, v109
	v_max_i32_e32 v5, 0, v2
	v_min_u32_e32 v6, v6, v110
	v_sub_u32_e32 v5, v6, v5
	v_cvt_f32_i32_e32 v5, v5
	v_add_u32_e32 v3, -1, v110
	v_min_i32_e32 v4, v2, v3
	v_cndmask_b32_e64 v4, v4, 0, vcc
	v_div_scale_f32 v6, s[6:7], v5, v5, 1.0
	v_rcp_f32_e32 v7, v6
	v_add_u32_e32 v20, 6, v109
	v_add_u32_e32 v22, 7, v109
	v_min_u32_e32 v21, v20, v3
	v_fma_f32 v8, -v6, v7, 1.0
	v_fmac_f32_e32 v7, v8, v7
	v_div_scale_f32 v8, vcc, 1.0, v5, 1.0
	v_mul_f32_e32 v9, v8, v7
	v_fma_f32 v10, -v6, v9, v8
	v_fmac_f32_e32 v9, v10, v7
	v_fma_f32 v6, -v6, v9, v8
	v_div_fmas_f32 v6, v6, v7, v9
	v_div_fixup_f32 v69, v6, v5, 1.0
	v_subrev_co_u32_e32 v5, vcc, 7, v109
	v_min_i32_e32 v6, v5, v3
	s_nop 0
	v_cndmask_b32_e64 v6, v6, 0, vcc
	v_subrev_co_u32_e32 v7, vcc, 6, v109
	v_min_i32_e32 v8, v7, v3
	s_nop 0
	v_cndmask_b32_e64 v8, v8, 0, vcc
	v_subrev_co_u32_e32 v9, vcc, 5, v109
	v_min_i32_e32 v10, v9, v3
	s_nop 0
	v_cndmask_b32_e64 v10, v10, 0, vcc
	v_subrev_co_u32_e32 v11, vcc, 4, v109
	v_min_i32_e32 v12, v11, v3
	s_nop 0
	v_cndmask_b32_e64 v12, v12, 0, vcc
	v_subrev_co_u32_e32 v13, vcc, 3, v109
	v_min_i32_e32 v14, v13, v3
	s_nop 0
	v_cndmask_b32_e64 v14, v14, 0, vcc
	v_subrev_co_u32_e32 v15, vcc, 2, v109
	v_min_i32_e32 v16, v15, v3
	s_nop 0
	v_cndmask_b32_e64 v16, v16, 0, vcc
	v_subrev_co_u32_e32 v17, vcc, 1, v109
	v_min_i32_e32 v18, v17, v3
	s_nop 0
	v_cndmask_b32_e64 v18, v18, 0, vcc
	v_cmp_lt_u32_e32 vcc, v2, v110
	v_cmp_lt_u32_e64 s[10:11], v9, v110
	v_cmp_lt_u32_e64 s[18:19], v17, v110
	v_add_u32_e32 v2, 1, v109
	v_add_u32_e32 v9, 2, v109
	v_add_u32_e32 v17, 5, v109
	v_cmp_lt_u32_e64 s[6:7], v5, v110
	v_cmp_lt_u32_e64 s[8:9], v7, v110
	v_cmp_lt_u32_e64 s[12:13], v11, v110
	v_cmp_lt_u32_e64 s[14:15], v13, v110
	v_cmp_lt_u32_e64 s[16:17], v15, v110
	v_min_u32_e32 v5, v109, v3
	v_min_u32_e32 v7, v2, v3
	v_min_u32_e32 v11, v9, v3
	v_min_u32_e32 v13, v113, v3
	v_min_u32_e32 v15, v114, v3
	v_min_u32_e32 v19, v17, v3
	v_min_u32_e32 v23, v22, v3
	v_lshlrev_b32_e32 v3, 9, v111
	v_cmp_lt_u32_e64 s[22:23], v2, v110
	v_cmp_lt_u32_e64 s[24:25], v9, v110
	v_and_b32_e32 v9, 48, v111
	v_lshlrev_b32_e32 v2, 8, v112
	v_and_b32_e32 v3, 0x1800, v3
	v_or3_b32 v2, v3, v2, v9
	v_mov_b32_e32 v3, v67
	v_lshl_add_u64 v[70:71], s[40:41], 0, v[2:3]
	v_add3_u32 v2, v4, s86, v108
	v_sub_u32_e32 v2, v2, v109
	v_add_u32_e32 v2, 0xffffe000, v2
	v_mad_i64_i32 v[2:3], s[38:39], v2, s67, 0
	v_or_b32_e32 v2, v2, v9
	v_lshl_add_u64 v[72:73], s[54:55], 0, v[2:3]
	v_add3_u32 v2, v6, s86, v108
	v_sub_u32_e32 v2, v2, v109
	v_add_u32_e32 v2, 0xffffe000, v2
	v_mad_i64_i32 v[2:3], s[38:39], v2, s67, 0
	v_or_b32_e32 v2, v2, v9
	v_lshl_add_u64 v[74:75], s[54:55], 0, v[2:3]
	v_add3_u32 v2, v8, s86, v108
	v_sub_u32_e32 v2, v2, v109
	v_add_u32_e32 v2, 0xffffe000, v2
	v_mad_i64_i32 v[2:3], s[38:39], v2, s67, 0
	v_or_b32_e32 v2, v2, v9
	v_lshl_add_u64 v[76:77], s[54:55], 0, v[2:3]
	v_add3_u32 v2, v10, s86, v108
	v_sub_u32_e32 v2, v2, v109
	v_add_u32_e32 v2, 0xffffe000, v2
	v_mad_i64_i32 v[2:3], s[38:39], v2, s67, 0
	v_or_b32_e32 v2, v2, v9
	v_lshl_add_u64 v[78:79], s[54:55], 0, v[2:3]
	v_add3_u32 v2, v12, s86, v108
	v_sub_u32_e32 v2, v2, v109
	v_add_u32_e32 v2, 0xffffe000, v2
	v_mad_i64_i32 v[2:3], s[38:39], v2, s67, 0
	v_or_b32_e32 v2, v2, v9
	v_lshl_add_u64 v[80:81], s[54:55], 0, v[2:3]
	v_add3_u32 v2, v14, s86, v108
	v_sub_u32_e32 v2, v2, v109
	v_add_u32_e32 v2, 0xffffe000, v2
	v_mad_i64_i32 v[2:3], s[38:39], v2, s67, 0
	v_or_b32_e32 v2, v2, v9
	v_lshl_add_u64 v[82:83], s[54:55], 0, v[2:3]
	v_add3_u32 v2, v16, s86, v108
	v_sub_u32_e32 v2, v2, v109
	v_add_u32_e32 v2, 0xffffe000, v2
	v_mad_i64_i32 v[2:3], s[38:39], v2, s67, 0
	v_or_b32_e32 v2, v2, v9
	v_lshl_add_u64 v[84:85], s[54:55], 0, v[2:3]
	v_add3_u32 v2, v18, s86, v108
	v_sub_u32_e32 v2, v2, v109
	v_add_u32_e32 v2, 0xffffe000, v2
	v_mad_i64_i32 v[2:3], s[38:39], v2, s67, 0
	v_or_b32_e32 v2, v2, v9
	v_lshl_add_u64 v[86:87], s[54:55], 0, v[2:3]
	v_add3_u32 v2, v5, s86, v108
	v_sub_u32_e32 v2, v2, v109
	v_add_u32_e32 v2, 0xffffe000, v2
	v_mad_i64_i32 v[2:3], s[38:39], v2, s67, 0
	v_or_b32_e32 v2, v2, v9
	v_lshl_add_u64 v[88:89], s[54:55], 0, v[2:3]
	v_add3_u32 v2, v7, s86, v108
	v_sub_u32_e32 v2, v2, v109
	v_add_u32_e32 v2, 0xffffe000, v2
	v_mad_i64_i32 v[2:3], s[38:39], v2, s67, 0
	v_or_b32_e32 v2, v2, v9
	v_lshl_add_u64 v[90:91], s[54:55], 0, v[2:3]
	v_add3_u32 v2, v11, s86, v108
	v_sub_u32_e32 v2, v2, v109
	v_add_u32_e32 v2, 0xffffe000, v2
	v_mad_i64_i32 v[2:3], s[38:39], v2, s67, 0
	v_or_b32_e32 v2, v2, v9
	v_lshl_add_u64 v[92:93], s[54:55], 0, v[2:3]
	v_add3_u32 v2, v13, s86, v108
	v_sub_u32_e32 v2, v2, v109
	v_add_u32_e32 v2, 0xffffe000, v2
	v_mad_i64_i32 v[2:3], s[38:39], v2, s67, 0
	v_or_b32_e32 v2, v2, v9
	v_lshl_add_u64 v[94:95], s[54:55], 0, v[2:3]
	v_add3_u32 v2, v15, s86, v108
	v_sub_u32_e32 v2, v2, v109
	v_add_u32_e32 v2, 0xffffe000, v2
	v_mad_i64_i32 v[2:3], s[38:39], v2, s67, 0
	v_or_b32_e32 v2, v2, v9
	v_lshl_add_u64 v[96:97], s[54:55], 0, v[2:3]
	v_add3_u32 v2, v19, s86, v108
	v_sub_u32_e32 v2, v2, v109
	v_add_u32_e32 v2, 0xffffe000, v2
	v_mad_i64_i32 v[2:3], s[38:39], v2, s67, 0
	v_or_b32_e32 v2, v2, v9
	v_lshl_add_u64 v[98:99], s[54:55], 0, v[2:3]
	v_add3_u32 v2, v21, s86, v108
	v_sub_u32_e32 v2, v2, v109
	v_add_u32_e32 v2, 0xffffe000, v2
	v_mad_i64_i32 v[2:3], s[38:39], v2, s67, 0
	v_or_b32_e32 v2, v2, v9
	v_lshl_add_u64 v[100:101], s[54:55], 0, v[2:3]
	v_add3_u32 v2, v23, s86, v108
	v_sub_u32_e32 v2, v2, v109
	v_add_u32_e32 v2, 0xffffe000, v2
	v_mad_i64_i32 v[2:3], s[38:39], v2, s67, 0
	v_or_b32_e32 v2, v2, v9
	v_mov_b32_e32 v26, 0
	v_cmp_lt_u32_e64 s[20:21], v109, v110
	v_cmp_lt_u32_e64 s[26:27], v114, v110
	v_cmp_lt_u32_e64 s[28:29], v17, v110
	v_cmp_lt_u32_e64 s[30:31], v20, v110
	v_cmp_lt_u32_e64 s[34:35], v22, v110
	v_lshl_add_u64 v[102:103], s[54:55], 0, v[2:3]
	s_mov_b64 s[64:65], 0
	v_mov_b32_e32 v27, v26
	v_mov_b32_e32 v28, v26
	v_mov_b32_e32 v29, v26
	v_mov_b32_e32 v30, v26
	v_mov_b32_e32 v31, v26
	v_mov_b32_e32 v32, v26
	v_mov_b32_e32 v33, v26
	v_mov_b32_e32 v18, v26
	v_mov_b32_e32 v19, v26
	v_mov_b32_e32 v20, v26
	v_mov_b32_e32 v21, v26
	v_mov_b32_e32 v22, v26
	v_mov_b32_e32 v23, v26
	v_mov_b32_e32 v24, v26
	v_mov_b32_e32 v25, v26
	v_mov_b32_e32 v10, v26
	v_mov_b32_e32 v11, v26
	v_mov_b32_e32 v12, v26
	v_mov_b32_e32 v13, v26
	v_mov_b32_e32 v14, v26
	v_mov_b32_e32 v15, v26
	v_mov_b32_e32 v16, v26
	v_mov_b32_e32 v17, v26
	v_mov_b32_e32 v2, v26
	v_mov_b32_e32 v3, v26
	v_mov_b32_e32 v4, v26
	v_mov_b32_e32 v5, v26
	v_mov_b32_e32 v6, v26
	v_mov_b32_e32 v7, v26
	v_mov_b32_e32 v8, v26
	v_mov_b32_e32 v9, v26

.LBB0_2871:
	v_mov_b32_e32 v85, 0
	s_and_saveexec_b64 s[4:5], s[36:37]
	s_cbranch_execz .LBB0_2875
	s_mov_b64 s[26:27], exec
	v_mbcnt_lo_u32_b32 v2, s26, 0
	v_mbcnt_hi_u32_b32 v2, s27, v2
	v_cmp_eq_u32_e32 vcc, 0, v2
	s_and_saveexec_b64 s[6:7], vcc
	s_cbranch_execz .LBB0_2874
	s_bcnt1_i32_b64 s14, s[26:27]
	v_mov_b32_e32 v3, s14
	global_atomic_add v255, v75, v3, s[48:49] sc0
.LBB0_2874:
	s_or_b64 exec, exec, s[6:7]
.LBB0_2875:
	s_or_b64 exec, exec, s[4:5]
	s_add_i32 s4, s85, 0xfffffd00
	s_ashr_i32 s5, s4, 31
	s_lshr_b32 s5, s5, 25
	s_add_i32 s5, s4, s5
	s_and_b32 s6, s5, 0xffffff80
	s_ashr_i32 s72, s5, 7
	s_sub_i32 s74, s4, s6
	s_add_i32 s73, s74, 4
	s_ashr_i32 s4, s5, 9
	s_and_b32 s38, s72, 3
	s_cmp_lt_i32 s74, 0
	s_cselect_b64 s[6:7], -1, 0
	s_cmp_gt_i32 s74, -1
	s_cselect_b64 s[30:31], -1, 0
	s_ashr_i32 s5, s4, 31
	s_lshl_b32 s28, s4, 8
	s_lshl_b32 s14, s73, 6
	s_lshl_b64 s[26:27], s[4:5], 13
	s_ashr_i32 s29, s28, 31
	s_and_b64 s[4:5], s[6:7], exec
	s_cselect_b32 s4, s50, 0xffffff00
	s_cselect_b32 s5, s29, s27
	s_cselect_b32 s6, s28, s26
	s_add_i32 s14, s14, s4
	v_mov_b32 v87, v0
	s_add_u32 s28, s6, s14
	v_ashrrev_i32_e32 v18, 3, v87
	s_addc_u32 s29, s5, 0
	v_ashrrev_i32_e32 v19, 31, v18
	v_lshl_add_u64 v[2:3], s[28:29], 0, v[18:19]
	v_mad_u64_u32 v[4:5], s[4:5], v2, s51, v[76:77]
	v_and_b32_e32 v36, 7, v87
	v_mad_i32_i24 v5, v3, s51, v5
	s_lshl_b32 s14, s38, 7
	v_lshlrev_b32_e32 v74, 4, v36
	v_lshl_add_u64 v[2:3], v[4:5], 0, s[14:15]
	v_lshl_add_u64 v[2:3], v[2:3], 0, v[74:75]
	v_add_co_u32_e32 v2, vcc, s52, v2
	s_lshl_b32 s4, s38, 8
	s_nop 0
	v_addc_co_u32_e32 v3, vcc, 0, v3, vcc
	s_mov_b32 s5, s15
	global_load_dwordx4 v[14:17], v[2:3], off offset:512
	global_load_dwordx4 v[10:13], v[2:3], off offset:1024
	v_lshl_add_u64 v[2:3], v[4:5], 0, s[4:5]
	v_lshlrev_b32_e32 v74, 5, v36
	v_lshl_add_u64 v[2:3], v[2:3], 0, v[74:75]
	v_lshl_add_u64 v[4:5], v[2:3], 0, s[16:17]
	v_add_co_u32_e32 v2, vcc, 0x1000, v2
	v_readfirstlane_b32 s75, v87
	s_nop 0
	v_addc_co_u32_e32 v3, vcc, 0, v3, vcc
	global_load_dwordx4 v[6:9], v[2:3], off offset:1536
	s_nop 0
	global_load_dwordx4 v[2:5], v[4:5], off offset:16
	s_load_dwordx4 s[4:7], s[0:1], 0x88
	s_load_dwordx2 s[26:27], s[0:1], 0x98
	v_cmp_gt_i32_e32 vcc, s53, v87
	s_waitcnt lgkmcnt(0)
	s_barrier
	s_and_saveexec_b64 s[34:35], vcc
	s_cbranch_execz .LBB0_2877
	v_ashrrev_i32_e32 v24, 2, v87
	v_ashrrev_i32_e32 v25, 31, v24
	v_lshl_add_u64 v[20:21], s[28:29], 0, v[24:25]
	v_mad_u64_u32 v[22:23], s[76:77], v20, s51, v[76:77]
	v_mov_b32_e32 v20, v23
	v_lshlrev_b32_e32 v19, 3, v87
	v_mad_u64_u32 v[20:21], s[76:77], v21, s51, v[20:21]
	v_and_b32_e32 v19, 24, v19
	v_mov_b32_e32 v23, v20
	v_lshlrev_b32_e32 v74, 1, v19
	v_lshl_add_u64 v[20:21], v[22:23], 0, v[74:75]
	v_add_co_u32_e32 v20, vcc, s52, v20
	v_lshlrev_b32_e32 v24, 7, v24
	s_nop 0
	v_addc_co_u32_e32 v21, vcc, 0, v21, vcc
	global_load_dwordx4 v[20:23], v[20:21], off offset:3584
	v_lshlrev_b32_e32 v19, 2, v19
	v_add3_u32 v19, 0, v24, v19
	s_waitcnt vmcnt(0)
	v_lshlrev_b32_e32 v24, 16, v20
	v_and_b32_e32 v25, 0xffff0000, v20
	v_lshlrev_b32_e32 v26, 16, v21
	v_and_b32_e32 v27, 0xffff0000, v21
	v_lshlrev_b32_e32 v20, 16, v22
	v_and_b32_e32 v21, 0xffff0000, v22
	v_lshlrev_b32_e32 v22, 16, v23
	v_and_b32_e32 v23, 0xffff0000, v23
	ds_write_b128 v19, v[24:27] offset:32768
	ds_write_b128 v19, v[20:23] offset:32784

.LBB0_2942:
	s_and_saveexec_b64 s[4:5], s[36:37]
	s_cbranch_execz .LBB0_2870
	s_nop 0
	v_mov_b32_e32 v2, s70
	s_waitcnt vmcnt(0)
	ds_write_b32 v2, v255
	s_branch .LBB0_2870

.LBB0_2955:
	s_or_b64 exec, exec, s[10:11]
.LBB0_2956:
	s_or_b64 exec, exec, s[8:9]
	s_add_i32 s28, s26, 0x180
	s_lshl_b32 s8, s28, 6
	s_and_b32 s27, s8, 0x3c00
	s_bitset1_b32 s27, 14
	s_ashr_i32 s15, s28, 8
	s_lshr_b32 s12, s27, 10
	s_cmp_eq_u32 s15, 2
	s_cselect_b64 s[8:9], -1, 0
	s_cmp_lg_u32 s15, 2
	s_cselect_b64 s[10:11], -1, 0
	v_mov_b32 v66, v0
	s_and_b64 vcc, exec, s[10:11]
	v_readfirstlane_b32 s29, v66
	v_mov_b32_e32 v172, 0
	s_cbranch_vccnz .LBB0_2958
	s_lshl_b32 s13, s12, 2
	v_mov_b32_e32 v2, s13
	global_load_dword v2, v2, s[6:7] sc1
	s_waitcnt vmcnt(0)
	v_div_scale_f32 v3, s[30:31], v2, v2, s24
	v_rcp_f32_e32 v4, v3
	v_div_scale_f32 v5, vcc, s24, v2, s24
	v_fma_f32 v6, -v3, v4, 1.0
	v_fmac_f32_e32 v4, v6, v4
	v_mul_f32_e32 v6, v5, v4
	v_fma_f32 v7, -v3, v6, v5
	v_fmac_f32_e32 v6, v7, v4
	v_fma_f32 v3, -v3, v6, v5
	v_div_fmas_f32 v3, v3, v4, v6
	v_div_fixup_f32 v3, v3, v2, s24
	v_cmp_lt_f32_e32 vcc, 0, v2
	s_nop 1
	v_cndmask_b32_e32 v172, 0, v3, vcc

.LBB0_2961:
	s_ashr_i32 s13, s29, 6
	s_cmp_eq_u32 s15, 1
	s_cselect_b32 s10, s25, 0xd8
	s_cmpk_gt_u32 s28, 0xff
	s_cselect_b32 s10, s10, 0xc8
	s_add_u32 s10, s0, s10
	s_addc_u32 s11, s1, 0
	s_lshl_b32 s28, s26, 5
	s_and_b32 s30, s28, 32
	s_and_b64 s[28:29], s[8:9], exec
	s_load_dwordx2 s[10:11], s[10:11], 0x0
	s_cselect_b32 s28, s30, 0
	s_and_b32 s30, s26, 14
	s_lshl_b32 s26, s26, 1
	s_add_i32 s31, s13, s28
	s_and_b32 s26, s26, 30
	s_and_b64 s[28:29], s[8:9], exec
	s_mulk_i32 s13, 0x4400
	s_cselect_b32 s26, s30, s26
	s_add_i32 s38, s13, 0
	s_lshl_b32 s30, s27, 11
	s_lshl_b32 s13, s27, 13
	s_waitcnt lgkmcnt(0)
	s_add_u32 s10, s10, s13
	s_addc_u32 s11, s11, 0
	s_lshl_b32 s26, s26, 6
	v_bfe_u32 v128, v66, 3, 3
	v_or_b32_e32 v130, s26, v128
	v_lshlrev_b64 v[2:3], s12, v[130:131]
	v_lshlrev_b32_e32 v4, 4, v66
	v_lshl_add_u64 v[2:3], v[2:3], 2, s[10:11]
	v_and_b32_e32 v130, 0x70, v4
	s_lshl_b32 s10, s31, 5
	v_lshl_add_u64 v[2:3], v[2:3], 0, v[130:131]
	s_ashr_i32 s11, s10, 31
	v_lshl_add_u64 v[142:143], s[10:11], 2, v[2:3]
	s_lshl_b64 s[28:29], 64, s12
	v_lshl_add_u64 v[140:141], s[28:29], 2, v[142:143]
	s_lshl_b64 s[28:29], 8, s12
	v_lshl_add_u64 v[144:145], s[28:29], 2, v[142:143]
	s_lshl_b64 s[28:29], 0x48, s12
	v_lshl_add_u64 v[146:147], s[28:29], 2, v[142:143]
	s_lshl_b64 s[28:29], 16, s12
	v_lshl_add_u64 v[148:149], s[28:29], 2, v[142:143]
	s_lshl_b64 s[28:29], 0x50, s12
	v_lshl_add_u64 v[150:151], s[28:29], 2, v[142:143]
	s_lshl_b64 s[28:29], 24, s12
	v_lshl_add_u64 v[152:153], s[28:29], 2, v[142:143]
	s_lshl_b64 s[28:29], 0x58, s12
	v_lshl_add_u64 v[154:155], s[28:29], 2, v[142:143]
	s_lshl_b64 s[28:29], 32, s12
	v_lshl_add_u64 v[156:157], s[28:29], 2, v[142:143]
	s_lshl_b64 s[28:29], 0x60, s12
	v_lshl_add_u64 v[158:159], s[28:29], 2, v[142:143]
	s_lshl_b64 s[28:29], 40, s12
	v_lshl_add_u64 v[160:161], s[28:29], 2, v[142:143]
	s_lshl_b64 s[28:29], 0x68, s12
	v_lshl_add_u64 v[162:163], s[28:29], 2, v[142:143]
	s_lshl_b64 s[28:29], 48, s12
	v_lshl_add_u64 v[164:165], s[28:29], 2, v[142:143]
	s_lshl_b64 s[28:29], 0x70, s12
	v_lshl_add_u64 v[166:167], s[28:29], 2, v[142:143]
	s_lshl_b64 s[28:29], 56, s12
	s_lshl_b64 s[12:13], 0x78, s12
	v_lshl_add_u64 v[168:169], s[28:29], 2, v[142:143]
	v_lshl_add_u64 v[170:171], s[12:13], 2, v[142:143]
	global_load_dwordx4 v[68:71], v[142:143], off nt
	global_load_dwordx4 v[72:75], v[140:141], off nt
	global_load_dwordx4 v[76:79], v[144:145], off nt
	global_load_dwordx4 v[80:83], v[146:147], off nt
	global_load_dwordx4 v[116:119], v[164:165], off nt
	global_load_dwordx4 v[120:123], v[166:167], off nt
	global_load_dwordx4 v[124:127], v[168:169], off nt
	global_load_dwordx4 v[132:135], v[170:171], off nt
	global_load_dwordx4 v[84:87], v[148:149], off nt
	global_load_dwordx4 v[88:91], v[150:151], off nt
	global_load_dwordx4 v[92:95], v[152:153], off nt
	global_load_dwordx4 v[96:99], v[154:155], off nt
	global_load_dwordx4 v[100:103], v[156:157], off nt
	global_load_dwordx4 v[104:107], v[158:159], off nt
	global_load_dwordx4 v[108:111], v[160:161], off nt
	global_load_dwordx4 v[112:115], v[162:163], off nt
	v_and_b32_e32 v129, 7, v66
	v_mul_u32_u24_e32 v66, 0x840, v129
	v_lshlrev_b32_e32 v67, 2, v128
	v_add3_u32 v174, s38, v66, v67
	v_add_u32_e32 v175, 0x400, v174
	v_add_u32_e32 v176, 0x600, v174
	global_load_dwordx4 v[50:53], v[142:143], off offset:1024 nt
	global_load_dwordx4 v[54:57], v[140:141], off offset:1024 nt
	global_load_dwordx4 v[58:61], v[144:145], off offset:1024 nt
	global_load_dwordx4 v[62:65], v[146:147], off offset:1024 nt
	global_load_dwordx4 v[34:37], v[148:149], off offset:1024 nt
	global_load_dwordx4 v[38:41], v[150:151], off offset:1024 nt
	global_load_dwordx4 v[42:45], v[152:153], off offset:1024 nt
	global_load_dwordx4 v[46:49], v[154:155], off offset:1024 nt
	global_load_dwordx4 v[18:21], v[156:157], off offset:1024 nt
	global_load_dwordx4 v[22:25], v[158:159], off offset:1024 nt
	global_load_dwordx4 v[26:29], v[160:161], off offset:1024 nt
	global_load_dwordx4 v[30:33], v[162:163], off offset:1024 nt
	global_load_dwordx4 v[2:5], v[164:165], off offset:1024 nt
	global_load_dwordx4 v[6:9], v[166:167], off offset:1024 nt
	global_load_dwordx4 v[10:13], v[168:169], off offset:1024 nt
	global_load_dwordx4 v[14:17], v[170:171], off offset:1024 nt
	v_lshlrev_b32_e32 v66, 6, v129
	v_mul_u32_u24_e32 v67, 0x210, v128
	v_add3_u32 v173, s38, v66, v67
	s_add_i32 s12, s10, 0x100
	s_ashr_i32 s13, s12, 31
	s_add_u32 s29, s19, s30
	s_addc_u32 s30, s20, 0
	s_lshl_b64 s[34:35], s[10:11], 10
	s_add_u32 s11, s29, s34
	s_addc_u32 s39, s30, s35
	s_lshl_b32 s27, s27, 12
	s_add_u32 s28, s21, s27
	s_addc_u32 s27, s22, 0
	s_waitcnt vmcnt(29)
	ds_write2_b32 v174, v68, v76 offset1:8
	s_waitcnt vmcnt(28)
	ds_write2_b32 v174, v72, v80 offset0:64 offset1:72
	ds_write2_b32 v174, v69, v77 offset0:132 offset1:140
	ds_write2_b32 v174, v73, v81 offset0:196 offset1:204
	ds_write2_b32 v175, v70, v78 offset0:8 offset1:16
	ds_write2_b32 v175, v74, v82 offset0:72 offset1:80
	ds_write2_b32 v175, v71, v79 offset0:140 offset1:148
	ds_write2_b32 v175, v75, v83 offset0:204 offset1:212
	s_waitcnt vmcnt(21)
	ds_write2_b32 v174, v84, v92 offset0:16 offset1:24
	s_waitcnt vmcnt(20)
	ds_write2_b32 v174, v88, v96 offset0:80 offset1:88
	ds_write2_b32 v174, v85, v93 offset0:148 offset1:156
	ds_write2_b32 v174, v89, v97 offset0:212 offset1:220
	ds_write2_b32 v175, v86, v94 offset0:24 offset1:32
	ds_write2_b32 v175, v90, v98 offset0:88 offset1:96
	ds_write2_b32 v175, v87, v95 offset0:156 offset1:164
	ds_write2_b32 v175, v91, v99 offset0:220 offset1:228
	s_waitcnt vmcnt(17)
	ds_write2_b32 v174, v100, v108 offset0:32 offset1:40
	s_waitcnt vmcnt(16)
	ds_write2_b32 v174, v104, v112 offset0:96 offset1:104
	ds_write2_b32 v174, v101, v109 offset0:164 offset1:172
	ds_write2_b32 v174, v105, v113 offset0:228 offset1:236
	ds_write2_b32 v175, v102, v110 offset0:40 offset1:48
	ds_write2_b32 v175, v106, v114 offset0:104 offset1:112
	ds_write2_b32 v175, v103, v111 offset0:172 offset1:180
	ds_write2_b32 v175, v107, v115 offset0:236 offset1:244
	ds_write2_b32 v174, v116, v124 offset0:48 offset1:56
	ds_write2_b32 v174, v120, v132 offset0:112 offset1:120
	ds_write2_b32 v174, v117, v125 offset0:180 offset1:188
	ds_write2_b32 v174, v121, v133 offset0:244 offset1:252
	ds_write2_b32 v175, v118, v126 offset0:56 offset1:64
	ds_write2_b32 v175, v122, v134 offset0:120 offset1:128
	ds_write2_b32 v175, v119, v127 offset0:188 offset1:196
	ds_write2_b32 v176, v123, v135 offset0:124 offset1:132
	s_waitcnt lgkmcnt(0)
	ds_read_b128 v[66:69], v173
	ds_read_b128 v[70:73], v173 offset:16
	ds_read_b128 v[74:77], v173 offset:32
	ds_read_b128 v[78:81], v173 offset:48
	s_lshl_b32 s31, s31, 6
	s_and_b32 s33, s31, 0xffffff00
	s_waitcnt lgkmcnt(2)
	v_mul_f32_e32 v70, v172, v70
	v_mul_f32_e32 v82, v172, v66
	v_mul_f32_e32 v67, v172, v67
	v_mov_b32_e32 v66, 0
	v_cvt_pk_fp8_f32 v66, v82, v67
	v_mul_f32_e32 v71, v172, v71
	v_mov_b32_e32 v67, 0
	v_cvt_pk_fp8_f32 v67, v70, v71
	v_mul_f32_e32 v68, v172, v68
	v_mul_f32_e32 v69, v172, v69
	v_cvt_pk_fp8_f32 v66, v68, v69 op_sel:[0,0,1]
	v_mul_f32_e32 v68, v172, v72
	v_mul_f32_e32 v69, v172, v73
	v_cvt_pk_fp8_f32 v67, v68, v69 op_sel:[0,0,1]
	s_waitcnt lgkmcnt(1)
	v_mul_f32_e32 v69, v172, v74
	v_mul_f32_e32 v70, v172, v75
	v_mov_b32_e32 v68, 0
	v_cvt_pk_fp8_f32 v68, v69, v70
	s_waitcnt lgkmcnt(0)
	v_mul_f32_e32 v72, v172, v78
	v_mul_f32_e32 v73, v172, v79
	v_mov_b32_e32 v69, 0
	s_lshl_b32 s31, s15, 7
	v_cvt_pk_fp8_f32 v69, v72, v73
	s_add_i32 s15, s33, s31
	s_and_b32 s33, s10, 0x60
	s_or_b32 s34, s15, s33
	v_mul_f32_e32 v70, v172, v76
	v_mul_f32_e32 v71, v172, v77
	s_ashr_i32 s35, s34, 31
	v_cvt_pk_fp8_f32 v68, v70, v71 op_sel:[0,0,1]
	v_mul_f32_e32 v70, v172, v80
	v_mul_f32_e32 v71, v172, v81
	s_lshl_b64 s[34:35], s[34:35], 11
	v_cvt_pk_fp8_f32 v69, v70, v71 op_sel:[0,0,1]
	ds_read_b128 v[70:73], v173 offset:4224
	ds_read_b128 v[74:77], v173 offset:4240
	s_add_u32 s15, s28, s34
	s_addc_u32 s46, s27, s35
	s_and_b64 s[34:35], s[8:9], exec
	s_cselect_b32 s11, s11, s15
	s_cselect_b32 s35, s39, s46
	s_add_u32 s34, s11, s26
	s_waitcnt lgkmcnt(1)
	v_mul_f32_e32 v83, v172, v70
	v_mul_f32_e32 v71, v172, v71
	v_mov_b32_e32 v70, 0
	v_lshlrev_b32_e32 v130, 4, v129
	s_addc_u32 s35, s35, 0
	v_cvt_pk_fp8_f32 v70, v83, v71
	v_lshl_add_u64 v[78:79], s[34:35], 0, v[130:131]
	v_lshlrev_b32_e32 v136, s14, v128
	v_mov_b32_e32 v137, v131
	v_lshl_add_u64 v[80:81], v[78:79], 0, v[136:137]
	global_store_dwordx4 v[80:81], v[66:69], off nt
	v_mov_b32_e32 v71, 0
	v_or_b32_e32 v82, 8, v128
	v_mul_f32_e32 v66, v172, v72
	v_mul_f32_e32 v67, v172, v73
	v_cvt_pk_fp8_f32 v70, v66, v67 op_sel:[0,0,1]
	s_waitcnt lgkmcnt(0)
	v_mul_f32_e32 v66, v172, v74
	v_mul_f32_e32 v67, v172, v75
	v_cvt_pk_fp8_f32 v71, v66, v67
	ds_read_b128 v[66:69], v173 offset:4256
	v_mul_f32_e32 v72, v172, v76
	v_mul_f32_e32 v73, v172, v77
	ds_read_b128 v[74:77], v173 offset:4272
	v_cvt_pk_fp8_f32 v71, v72, v73 op_sel:[0,0,1]
	s_waitcnt lgkmcnt(1)
	v_mul_f32_e32 v66, v172, v66
	v_mul_f32_e32 v67, v172, v67
	v_mov_b32_e32 v72, 0
	v_cvt_pk_fp8_f32 v72, v66, v67
	v_mul_f32_e32 v66, v172, v68
	v_mul_f32_e32 v67, v172, v69
	s_waitcnt lgkmcnt(0)
	v_mul_f32_e32 v68, v172, v74
	v_mul_f32_e32 v69, v172, v75
	v_mov_b32_e32 v73, 0
	v_cvt_pk_fp8_f32 v73, v68, v69
	v_cvt_pk_fp8_f32 v72, v66, v67 op_sel:[0,0,1]
	v_mul_f32_e32 v66, v172, v76
	v_mul_f32_e32 v67, v172, v77
	v_cvt_pk_fp8_f32 v73, v66, v67 op_sel:[0,0,1]
	ds_read_b128 v[66:69], v173 offset:8448
	v_lshlrev_b32_e32 v134, s14, v82
	v_mov_b32_e32 v135, v131
	v_lshl_add_u64 v[74:75], v[78:79], 0, v[134:135]
	global_store_dwordx4 v[74:75], v[70:73], off nt
	ds_read_b128 v[70:73], v173 offset:8464
	s_waitcnt lgkmcnt(1)
	v_mul_f32_e32 v74, v172, v66
	v_mul_f32_e32 v67, v172, v67
	v_mov_b32_e32 v66, 0
	v_cvt_pk_fp8_f32 v66, v74, v67
	v_mul_f32_e32 v67, v172, v68
	v_mul_f32_e32 v68, v172, v69
	s_waitcnt lgkmcnt(0)
	v_mul_f32_e32 v69, v172, v71
	v_cvt_pk_fp8_f32 v66, v67, v68 op_sel:[0,0,1]
	v_mul_f32_e32 v68, v172, v70
	v_mov_b32_e32 v67, 0
	v_cvt_pk_fp8_f32 v67, v68, v69
	ds_read_b128 v[68:71], v173 offset:8480
	v_mul_f32_e32 v72, v172, v72
	v_mul_f32_e32 v73, v172, v73
	v_cvt_pk_fp8_f32 v67, v72, v73 op_sel:[0,0,1]
	ds_read_b128 v[72:75], v173 offset:8496
	s_waitcnt lgkmcnt(1)
	v_mul_f32_e32 v77, v172, v68
	v_mul_f32_e32 v69, v172, v69
	v_mov_b32_e32 v68, 0
	v_cvt_pk_fp8_f32 v68, v77, v69
	s_waitcnt lgkmcnt(0)
	v_mul_f32_e32 v72, v172, v72
	v_mul_f32_e32 v73, v172, v73
	v_mov_b32_e32 v69, 0
	v_cvt_pk_fp8_f32 v69, v72, v73
	v_mul_f32_e32 v70, v172, v70
	v_mul_f32_e32 v71, v172, v71
	v_cvt_pk_fp8_f32 v68, v70, v71 op_sel:[0,0,1]
	v_mul_f32_e32 v70, v172, v74
	v_mul_f32_e32 v71, v172, v75
	v_cvt_pk_fp8_f32 v69, v70, v71 op_sel:[0,0,1]
	ds_read_b128 v[70:73], v173 offset:12672
	v_or_b32_e32 v76, 16, v128
	v_lshlrev_b32_e32 v132, s14, v76
	v_mov_b32_e32 v133, v131
	v_lshl_add_u64 v[74:75], v[78:79], 0, v[132:133]
	global_store_dwordx4 v[74:75], v[66:69], off nt
	ds_read_b128 v[66:69], v173 offset:12688
	s_waitcnt lgkmcnt(1)
	v_mul_f32_e32 v74, v172, v70
	v_mul_f32_e32 v71, v172, v71
	v_mov_b32_e32 v70, 0
	v_cvt_pk_fp8_f32 v70, v74, v71
	v_mul_f32_e32 v71, v172, v72
	v_mul_f32_e32 v72, v172, v73
	s_waitcnt lgkmcnt(0)
	v_mul_f32_e32 v66, v172, v66
	v_cvt_pk_fp8_f32 v70, v71, v72 op_sel:[0,0,1]
	v_mul_f32_e32 v67, v172, v67
	v_mov_b32_e32 v71, 0
	v_cvt_pk_fp8_f32 v71, v66, v67
	ds_read_b128 v[72:75], v173 offset:12704
	v_mul_f32_e32 v66, v172, v68
	v_mul_f32_e32 v67, v172, v69
	v_cvt_pk_fp8_f32 v71, v66, v67 op_sel:[0,0,1]
	ds_read_b128 v[66:69], v173 offset:12720
	s_waitcnt lgkmcnt(1)
	v_mul_f32_e32 v77, v172, v72
	v_mul_f32_e32 v73, v172, v73
	v_mov_b32_e32 v72, 0
	v_cvt_pk_fp8_f32 v72, v77, v73
	s_waitcnt lgkmcnt(0)
	v_mul_f32_e32 v66, v172, v66
	v_mul_f32_e32 v67, v172, v67
	v_mov_b32_e32 v73, 0
	v_cvt_pk_fp8_f32 v73, v66, v67
	v_mul_f32_e32 v74, v172, v74
	v_mul_f32_e32 v75, v172, v75
	v_mul_f32_e32 v66, v172, v68
	v_mul_f32_e32 v67, v172, v69
	v_cvt_pk_fp8_f32 v72, v74, v75 op_sel:[0,0,1]
	v_cvt_pk_fp8_f32 v73, v66, v67 op_sel:[0,0,1]
	v_or_b32_e32 v76, 24, v128
	v_lshlrev_b32_e32 v138, s14, v76
	v_mov_b32_e32 v139, v131
	v_lshl_add_u64 v[66:67], v[78:79], 0, v[138:139]
	global_store_dwordx4 v[66:67], v[70:73], off nt
	s_waitcnt lgkmcnt(0)
	global_load_dwordx4 v[114:117], v[142:143], off offset:2048 nt
	global_load_dwordx4 v[118:121], v[140:141], off offset:2048 nt
	global_load_dwordx4 v[122:125], v[144:145], off offset:2048 nt
	global_load_dwordx4 v[126:129], v[146:147], off offset:2048 nt
	global_load_dwordx4 v[98:101], v[148:149], off offset:2048 nt
	global_load_dwordx4 v[102:105], v[150:151], off offset:2048 nt
	global_load_dwordx4 v[106:109], v[152:153], off offset:2048 nt
	global_load_dwordx4 v[110:113], v[154:155], off offset:2048 nt
	global_load_dwordx4 v[82:85], v[156:157], off offset:2048 nt
	global_load_dwordx4 v[86:89], v[158:159], off offset:2048 nt
	global_load_dwordx4 v[90:93], v[160:161], off offset:2048 nt
	global_load_dwordx4 v[94:97], v[162:163], off offset:2048 nt
	global_load_dwordx4 v[66:69], v[164:165], off offset:2048 nt
	global_load_dwordx4 v[70:73], v[166:167], off offset:2048 nt
	global_load_dwordx4 v[74:77], v[168:169], off offset:2048 nt
	global_load_dwordx4 v[78:81], v[170:171], off offset:2048 nt
	s_waitcnt vmcnt(33)
	ds_write2_b32 v174, v50, v58 offset1:8
	s_waitcnt vmcnt(32)
	ds_write2_b32 v174, v54, v62 offset0:64 offset1:72
	ds_write2_b32 v174, v51, v59 offset0:132 offset1:140
	ds_write2_b32 v174, v55, v63 offset0:196 offset1:204
	ds_write2_b32 v175, v52, v60 offset0:8 offset1:16
	ds_write2_b32 v175, v56, v64 offset0:72 offset1:80
	ds_write2_b32 v175, v53, v61 offset0:140 offset1:148
	ds_write2_b32 v175, v57, v65 offset0:204 offset1:212
	s_waitcnt vmcnt(29)
	ds_write2_b32 v174, v34, v42 offset0:16 offset1:24
	s_waitcnt vmcnt(28)
	ds_write2_b32 v174, v38, v46 offset0:80 offset1:88
	ds_write2_b32 v174, v35, v43 offset0:148 offset1:156
	ds_write2_b32 v174, v39, v47 offset0:212 offset1:220
	ds_write2_b32 v175, v36, v44 offset0:24 offset1:32
	ds_write2_b32 v175, v40, v48 offset0:88 offset1:96
	ds_write2_b32 v175, v37, v45 offset0:156 offset1:164
	ds_write2_b32 v175, v41, v49 offset0:220 offset1:228
	s_waitcnt vmcnt(25)
	ds_write2_b32 v174, v18, v26 offset0:32 offset1:40
	s_waitcnt vmcnt(24)
	ds_write2_b32 v174, v22, v30 offset0:96 offset1:104
	ds_write2_b32 v174, v19, v27 offset0:164 offset1:172
	ds_write2_b32 v174, v23, v31 offset0:228 offset1:236
	ds_write2_b32 v175, v20, v28 offset0:40 offset1:48
	ds_write2_b32 v175, v24, v32 offset0:104 offset1:112
	ds_write2_b32 v175, v21, v29 offset0:172 offset1:180
	ds_write2_b32 v175, v25, v33 offset0:236 offset1:244
	s_waitcnt vmcnt(21)
	ds_write2_b32 v174, v2, v10 offset0:48 offset1:56
	s_waitcnt vmcnt(20)
	ds_write2_b32 v174, v6, v14 offset0:112 offset1:120
	ds_write2_b32 v174, v3, v11 offset0:180 offset1:188
	ds_write2_b32 v174, v7, v15 offset0:244 offset1:252
	ds_write2_b32 v175, v4, v12 offset0:56 offset1:64
	ds_write2_b32 v175, v8, v16 offset0:120 offset1:128
	ds_write2_b32 v175, v5, v13 offset0:188 offset1:196
	ds_write2_b32 v176, v9, v17 offset0:124 offset1:132
	s_waitcnt lgkmcnt(0)
	ds_read_b128 v[2:5], v173
	ds_read_b128 v[6:9], v173 offset:16
	ds_read_b128 v[10:13], v173 offset:32
	ds_read_b128 v[14:17], v173 offset:48
	s_add_i32 s14, s10, 0x200
	s_ashr_i32 s15, s14, 31
	s_waitcnt lgkmcnt(2)
	v_mul_f32_e32 v6, v172, v6
	v_mul_f32_e32 v18, v172, v2
	v_mul_f32_e32 v3, v172, v3
	v_mov_b32_e32 v2, 0
	v_cvt_pk_fp8_f32 v2, v18, v3
	v_mul_f32_e32 v7, v172, v7
	v_mov_b32_e32 v3, 0
	v_cvt_pk_fp8_f32 v3, v6, v7
	v_mul_f32_e32 v4, v172, v4
	v_mul_f32_e32 v5, v172, v5
	s_lshl_b64 s[34:35], s[12:13], 10
	v_cvt_pk_fp8_f32 v2, v4, v5 op_sel:[0,0,1]
	v_mul_f32_e32 v4, v172, v8
	v_mul_f32_e32 v5, v172, v9
	s_add_u32 s11, s29, s34
	v_cvt_pk_fp8_f32 v3, v4, v5 op_sel:[0,0,1]
	s_waitcnt lgkmcnt(1)
	v_mul_f32_e32 v5, v172, v10
	v_mul_f32_e32 v6, v172, v11
	v_mov_b32_e32 v4, 0
	s_addc_u32 s34, s30, s35
	s_lshl_b32 s12, s12, 1
	v_cvt_pk_fp8_f32 v4, v5, v6
	s_waitcnt lgkmcnt(0)
	v_mul_f32_e32 v8, v172, v14
	v_mul_f32_e32 v9, v172, v15
	v_mov_b32_e32 v5, 0
	s_and_b32 s12, s12, 0xffffff00
	v_cvt_pk_fp8_f32 v5, v8, v9
	s_add_i32 s12, s12, s31
	s_or_b32 s12, s12, s33
	v_mul_f32_e32 v6, v172, v12
	v_mul_f32_e32 v7, v172, v13
	s_ashr_i32 s13, s12, 31
	v_cvt_pk_fp8_f32 v4, v6, v7 op_sel:[0,0,1]
	v_mul_f32_e32 v6, v172, v16
	v_mul_f32_e32 v7, v172, v17
	s_lshl_b64 s[12:13], s[12:13], 11
	v_cvt_pk_fp8_f32 v5, v6, v7 op_sel:[0,0,1]
	ds_read_b128 v[6:9], v173 offset:4224
	ds_read_b128 v[10:13], v173 offset:4240
	s_add_u32 s35, s28, s12
	s_addc_u32 s38, s27, s13
	s_and_b64 s[12:13], s[8:9], exec
	s_cselect_b32 s11, s11, s35
	s_cselect_b32 s13, s34, s38
	s_add_u32 s12, s11, s26
	s_waitcnt lgkmcnt(1)
	v_mul_f32_e32 v18, v172, v6
	v_mul_f32_e32 v7, v172, v7
	v_mov_b32_e32 v6, 0
	s_addc_u32 s13, s13, 0
	v_cvt_pk_fp8_f32 v6, v18, v7
	v_lshl_add_u64 v[16:17], s[12:13], 0, v[130:131]
	v_lshl_add_u64 v[14:15], v[16:17], 0, v[136:137]
	global_store_dwordx4 v[14:15], v[2:5], off nt
	v_mov_b32_e32 v7, 0
	s_waitcnt lgkmcnt(0)
	v_mul_f32_e32 v14, v172, v13
	v_mul_f32_e32 v2, v172, v8
	v_mul_f32_e32 v3, v172, v9
	v_cvt_pk_fp8_f32 v6, v2, v3 op_sel:[0,0,1]
	ds_read_b128 v[2:5], v173 offset:4256
	v_mul_f32_e32 v8, v172, v10
	v_mul_f32_e32 v9, v172, v11
	v_cvt_pk_fp8_f32 v7, v8, v9
	v_mul_f32_e32 v9, v172, v12
	ds_read_b128 v[10:13], v173 offset:4272
	s_waitcnt lgkmcnt(1)
	v_mul_f32_e32 v2, v172, v2
	v_mul_f32_e32 v3, v172, v3
	v_mov_b32_e32 v8, 0
	v_cvt_pk_fp8_f32 v8, v2, v3
	v_mul_f32_e32 v2, v172, v4
	v_mul_f32_e32 v3, v172, v5
	v_cvt_pk_fp8_f32 v7, v9, v14 op_sel:[0,0,1]
	v_cvt_pk_fp8_f32 v8, v2, v3 op_sel:[0,0,1]
	s_waitcnt lgkmcnt(0)
	v_mul_f32_e32 v2, v172, v10
	v_mul_f32_e32 v3, v172, v11
	v_mov_b32_e32 v9, 0
	v_cvt_pk_fp8_f32 v9, v2, v3
	ds_read_b128 v[2:5], v173 offset:8448
	v_mul_f32_e32 v10, v172, v12
	v_mul_f32_e32 v11, v172, v13
	v_cvt_pk_fp8_f32 v9, v10, v11 op_sel:[0,0,1]
	ds_read_b128 v[10:13], v173 offset:8464
	s_waitcnt lgkmcnt(1)
	v_mul_f32_e32 v18, v172, v2
	v_mul_f32_e32 v3, v172, v3
	v_mov_b32_e32 v2, 0
	v_cvt_pk_fp8_f32 v2, v18, v3
	v_lshl_add_u64 v[14:15], v[16:17], 0, v[134:135]
	v_mul_f32_e32 v3, v172, v4
	v_mul_f32_e32 v4, v172, v5
	global_store_dwordx4 v[14:15], v[6:9], off nt
	v_cvt_pk_fp8_f32 v2, v3, v4 op_sel:[0,0,1]
	ds_read_b128 v[4:7], v173 offset:8480
	s_waitcnt lgkmcnt(1)
	v_mul_f32_e32 v8, v172, v10
	v_mul_f32_e32 v9, v172, v11
	v_mov_b32_e32 v3, 0
	v_cvt_pk_fp8_f32 v3, v8, v9
	ds_read_b128 v[8:11], v173 offset:8496
	s_waitcnt lgkmcnt(1)
	v_mul_f32_e32 v14, v172, v4
	v_mul_f32_e32 v5, v172, v5
	v_mov_b32_e32 v4, 0
	v_cvt_pk_fp8_f32 v4, v14, v5
	v_mul_f32_e32 v12, v172, v12
	v_mul_f32_e32 v13, v172, v13
	v_mul_f32_e32 v5, v172, v6
	v_mul_f32_e32 v6, v172, v7
	v_cvt_pk_fp8_f32 v3, v12, v13 op_sel:[0,0,1]
	v_cvt_pk_fp8_f32 v4, v5, v6 op_sel:[0,0,1]
	s_waitcnt lgkmcnt(0)
	v_mul_f32_e32 v12, v172, v8
	v_mul_f32_e32 v13, v172, v9
	ds_read_b128 v[6:9], v173 offset:12672
	v_mov_b32_e32 v5, 0
	v_cvt_pk_fp8_f32 v5, v12, v13
	v_mul_f32_e32 v14, v172, v10
	v_mul_f32_e32 v15, v172, v11
	ds_read_b128 v[10:13], v173 offset:12688
	s_waitcnt lgkmcnt(1)
	v_mul_f32_e32 v18, v172, v6
	v_mul_f32_e32 v7, v172, v7
	v_mov_b32_e32 v6, 0
	v_cvt_pk_fp8_f32 v6, v18, v7
	v_mul_f32_e32 v7, v172, v8
	v_mul_f32_e32 v8, v172, v9
	s_waitcnt lgkmcnt(0)
	v_mul_f32_e32 v9, v172, v11
	v_cvt_pk_fp8_f32 v6, v7, v8 op_sel:[0,0,1]
	v_mul_f32_e32 v8, v172, v10
	v_mov_b32_e32 v7, 0
	v_cvt_pk_fp8_f32 v7, v8, v9
	ds_read_b128 v[8:11], v173 offset:12704
	v_mul_f32_e32 v12, v172, v12
	v_mul_f32_e32 v13, v172, v13
	v_cvt_pk_fp8_f32 v5, v14, v15 op_sel:[0,0,1]
	v_cvt_pk_fp8_f32 v7, v12, v13 op_sel:[0,0,1]
	ds_read_b128 v[12:15], v173 offset:12720
	s_waitcnt lgkmcnt(1)
	v_mul_f32_e32 v18, v172, v8
	v_mul_f32_e32 v9, v172, v9
	v_mov_b32_e32 v8, 0
	v_cvt_pk_fp8_f32 v8, v18, v9
	s_waitcnt lgkmcnt(0)
	v_mul_f32_e32 v12, v172, v12
	v_mul_f32_e32 v13, v172, v13
	v_mov_b32_e32 v9, 0
	v_cvt_pk_fp8_f32 v9, v12, v13
	v_mul_f32_e32 v10, v172, v10
	v_mul_f32_e32 v11, v172, v11
	v_cvt_pk_fp8_f32 v8, v10, v11 op_sel:[0,0,1]
	v_mul_f32_e32 v10, v172, v14
	v_mul_f32_e32 v11, v172, v15
	v_cvt_pk_fp8_f32 v9, v10, v11 op_sel:[0,0,1]
	v_lshl_add_u64 v[10:11], v[16:17], 0, v[132:133]
	global_store_dwordx4 v[10:11], v[2:5], off nt
	s_addk_i32 s10, 0x300
	s_ashr_i32 s11, s10, 31
	v_lshl_add_u64 v[2:3], v[16:17], 0, v[138:139]
	global_store_dwordx4 v[2:3], v[6:9], off nt
	s_waitcnt lgkmcnt(0)
	global_load_dwordx4 v[42:45], v[142:143], off offset:3072 nt
	global_load_dwordx4 v[46:49], v[140:141], off offset:3072 nt
	global_load_dwordx4 v[58:61], v[144:145], off offset:3072 nt
	global_load_dwordx4 v[62:65], v[146:147], off offset:3072 nt
	global_load_dwordx4 v[34:37], v[148:149], off offset:3072 nt
	global_load_dwordx4 v[38:41], v[150:151], off offset:3072 nt
	global_load_dwordx4 v[50:53], v[152:153], off offset:3072 nt
	global_load_dwordx4 v[54:57], v[154:155], off offset:3072 nt
	global_load_dwordx4 v[18:21], v[156:157], off offset:3072 nt
	global_load_dwordx4 v[22:25], v[158:159], off offset:3072 nt
	global_load_dwordx4 v[26:29], v[160:161], off offset:3072 nt
	global_load_dwordx4 v[30:33], v[162:163], off offset:3072 nt
	global_load_dwordx4 v[2:5], v[164:165], off offset:3072 nt
	global_load_dwordx4 v[6:9], v[166:167], off offset:3072 nt
	global_load_dwordx4 v[10:13], v[168:169], off offset:3072 nt
	global_load_dwordx4 v[14:17], v[170:171], off offset:3072 nt
	s_waitcnt vmcnt(33)
	ds_write2_b32 v174, v114, v122 offset1:8
	s_waitcnt vmcnt(32)
	ds_write2_b32 v174, v118, v126 offset0:64 offset1:72
	ds_write2_b32 v174, v115, v123 offset0:132 offset1:140
	ds_write2_b32 v174, v119, v127 offset0:196 offset1:204
	ds_write2_b32 v175, v116, v124 offset0:8 offset1:16
	ds_write2_b32 v175, v120, v128 offset0:72 offset1:80
	ds_write2_b32 v175, v117, v125 offset0:140 offset1:148
	ds_write2_b32 v175, v121, v129 offset0:204 offset1:212
	s_waitcnt vmcnt(29)
	ds_write2_b32 v174, v98, v106 offset0:16 offset1:24
	s_waitcnt vmcnt(28)
	ds_write2_b32 v174, v102, v110 offset0:80 offset1:88
	ds_write2_b32 v174, v99, v107 offset0:148 offset1:156
	ds_write2_b32 v174, v103, v111 offset0:212 offset1:220
	ds_write2_b32 v175, v100, v108 offset0:24 offset1:32
	ds_write2_b32 v175, v104, v112 offset0:88 offset1:96
	ds_write2_b32 v175, v101, v109 offset0:156 offset1:164
	ds_write2_b32 v175, v105, v113 offset0:220 offset1:228
	s_waitcnt vmcnt(25)
	ds_write2_b32 v174, v82, v90 offset0:32 offset1:40
	s_waitcnt vmcnt(24)
	ds_write2_b32 v174, v86, v94 offset0:96 offset1:104
	ds_write2_b32 v174, v83, v91 offset0:164 offset1:172
	ds_write2_b32 v174, v87, v95 offset0:228 offset1:236
	ds_write2_b32 v175, v84, v92 offset0:40 offset1:48
	ds_write2_b32 v175, v88, v96 offset0:104 offset1:112
	ds_write2_b32 v175, v85, v93 offset0:172 offset1:180
	ds_write2_b32 v175, v89, v97 offset0:236 offset1:244
	s_waitcnt vmcnt(21)
	ds_write2_b32 v174, v66, v74 offset0:48 offset1:56
	s_waitcnt vmcnt(20)
	ds_write2_b32 v174, v70, v78 offset0:112 offset1:120
	ds_write2_b32 v174, v67, v75 offset0:180 offset1:188
	ds_write2_b32 v174, v71, v79 offset0:244 offset1:252
	ds_write2_b32 v175, v68, v76 offset0:56 offset1:64
	ds_write2_b32 v175, v72, v80 offset0:120 offset1:128
	ds_write2_b32 v175, v69, v77 offset0:188 offset1:196
	ds_write2_b32 v176, v73, v81 offset0:124 offset1:132
	s_waitcnt lgkmcnt(0)
	ds_read_b128 v[66:69], v173
	ds_read_b128 v[70:73], v173 offset:16
	ds_read_b128 v[74:77], v173 offset:32
	ds_read_b128 v[78:81], v173 offset:48
	s_lshl_b64 s[12:13], s[14:15], 10
	s_add_u32 s15, s29, s12
	s_waitcnt lgkmcnt(2)
	v_mul_f32_e32 v70, v172, v70
	v_mul_f32_e32 v82, v172, v66
	v_mul_f32_e32 v67, v172, v67
	v_mov_b32_e32 v66, 0
	v_cvt_pk_fp8_f32 v66, v82, v67
	v_mul_f32_e32 v71, v172, v71
	v_mov_b32_e32 v67, 0
	v_cvt_pk_fp8_f32 v67, v70, v71
	v_mul_f32_e32 v68, v172, v68
	v_mul_f32_e32 v69, v172, v69
	v_cvt_pk_fp8_f32 v66, v68, v69 op_sel:[0,0,1]
	v_mul_f32_e32 v68, v172, v72
	v_mul_f32_e32 v69, v172, v73
	v_cvt_pk_fp8_f32 v67, v68, v69 op_sel:[0,0,1]
	s_waitcnt lgkmcnt(1)
	v_mul_f32_e32 v69, v172, v74
	v_mul_f32_e32 v70, v172, v75
	v_mov_b32_e32 v68, 0
	s_addc_u32 s34, s30, s13
	s_lshl_b32 s12, s14, 1
	v_cvt_pk_fp8_f32 v68, v69, v70
	s_waitcnt lgkmcnt(0)
	v_mul_f32_e32 v72, v172, v78
	v_mul_f32_e32 v73, v172, v79
	v_mov_b32_e32 v69, 0
	s_and_b32 s12, s12, 0xffffff00
	v_cvt_pk_fp8_f32 v69, v72, v73
	s_add_i32 s12, s12, s31
	s_or_b32 s12, s12, s33
	v_mul_f32_e32 v70, v172, v76
	v_mul_f32_e32 v71, v172, v77
	s_ashr_i32 s13, s12, 31
	v_cvt_pk_fp8_f32 v68, v70, v71 op_sel:[0,0,1]
	v_mul_f32_e32 v70, v172, v80
	v_mul_f32_e32 v71, v172, v81
	s_lshl_b64 s[12:13], s[12:13], 11
	v_cvt_pk_fp8_f32 v69, v70, v71 op_sel:[0,0,1]
	ds_read_b128 v[70:73], v173 offset:4224
	ds_read_b128 v[74:77], v173 offset:4240
	s_add_u32 s14, s28, s12
	s_addc_u32 s35, s27, s13
	s_and_b64 s[12:13], s[8:9], exec
	s_cselect_b32 s12, s15, s14
	s_cselect_b32 s13, s34, s35
	s_add_u32 s12, s12, s26
	s_waitcnt lgkmcnt(1)
	v_mul_f32_e32 v82, v172, v70
	v_mul_f32_e32 v71, v172, v71
	v_mov_b32_e32 v70, 0
	s_addc_u32 s13, s13, 0
	v_cvt_pk_fp8_f32 v70, v82, v71
	v_lshl_add_u64 v[80:81], s[12:13], 0, v[130:131]
	v_lshl_add_u64 v[78:79], v[80:81], 0, v[136:137]
	global_store_dwordx4 v[78:79], v[66:69], off nt
	v_mov_b32_e32 v71, 0
	s_waitcnt lgkmcnt(0)
	v_mul_f32_e32 v78, v172, v77
	v_mul_f32_e32 v66, v172, v72
	v_mul_f32_e32 v67, v172, v73
	v_cvt_pk_fp8_f32 v70, v66, v67 op_sel:[0,0,1]
	ds_read_b128 v[66:69], v173 offset:4256
	v_mul_f32_e32 v72, v172, v74
	v_mul_f32_e32 v73, v172, v75
	v_cvt_pk_fp8_f32 v71, v72, v73
	v_mul_f32_e32 v73, v172, v76
	ds_read_b128 v[74:77], v173 offset:4272
	s_waitcnt lgkmcnt(1)
	v_mul_f32_e32 v66, v172, v66
	v_mul_f32_e32 v67, v172, v67
	v_mov_b32_e32 v72, 0
	v_cvt_pk_fp8_f32 v72, v66, v67
	v_mul_f32_e32 v66, v172, v68
	v_mul_f32_e32 v67, v172, v69
	v_cvt_pk_fp8_f32 v71, v73, v78 op_sel:[0,0,1]
	v_cvt_pk_fp8_f32 v72, v66, v67 op_sel:[0,0,1]
	s_waitcnt lgkmcnt(0)
	v_mul_f32_e32 v66, v172, v74
	v_mul_f32_e32 v67, v172, v75
	v_mov_b32_e32 v73, 0
	v_cvt_pk_fp8_f32 v73, v66, v67
	ds_read_b128 v[66:69], v173 offset:8448
	v_mul_f32_e32 v74, v172, v76
	v_mul_f32_e32 v75, v172, v77
	v_cvt_pk_fp8_f32 v73, v74, v75 op_sel:[0,0,1]
	ds_read_b128 v[74:77], v173 offset:8464
	s_waitcnt lgkmcnt(1)
	v_mul_f32_e32 v82, v172, v66
	v_mul_f32_e32 v67, v172, v67
	v_mov_b32_e32 v66, 0
	v_cvt_pk_fp8_f32 v66, v82, v67
	v_lshl_add_u64 v[78:79], v[80:81], 0, v[134:135]
	v_mul_f32_e32 v67, v172, v68
	v_mul_f32_e32 v68, v172, v69
	global_store_dwordx4 v[78:79], v[70:73], off nt
	v_cvt_pk_fp8_f32 v66, v67, v68 op_sel:[0,0,1]
	ds_read_b128 v[68:71], v173 offset:8480
	s_waitcnt lgkmcnt(1)
	v_mul_f32_e32 v72, v172, v74
	v_mul_f32_e32 v73, v172, v75
	v_mov_b32_e32 v67, 0
	v_cvt_pk_fp8_f32 v67, v72, v73
	ds_read_b128 v[72:75], v173 offset:8496
	s_waitcnt lgkmcnt(1)
	v_mul_f32_e32 v78, v172, v68
	v_mul_f32_e32 v69, v172, v69
	v_mov_b32_e32 v68, 0
	v_cvt_pk_fp8_f32 v68, v78, v69
	v_mul_f32_e32 v76, v172, v76
	v_mul_f32_e32 v77, v172, v77
	v_mul_f32_e32 v69, v172, v70
	v_mul_f32_e32 v70, v172, v71
	v_cvt_pk_fp8_f32 v67, v76, v77 op_sel:[0,0,1]
	v_cvt_pk_fp8_f32 v68, v69, v70 op_sel:[0,0,1]
	s_waitcnt lgkmcnt(0)
	v_mul_f32_e32 v76, v172, v72
	v_mul_f32_e32 v77, v172, v73
	ds_read_b128 v[70:73], v173 offset:12672
	v_mov_b32_e32 v69, 0
	v_cvt_pk_fp8_f32 v69, v76, v77
	v_mul_f32_e32 v78, v172, v74
	v_mul_f32_e32 v79, v172, v75
	ds_read_b128 v[74:77], v173 offset:12688
	s_waitcnt lgkmcnt(1)
	v_mul_f32_e32 v82, v172, v70
	v_mul_f32_e32 v71, v172, v71
	v_mov_b32_e32 v70, 0
	v_cvt_pk_fp8_f32 v70, v82, v71
	v_mul_f32_e32 v71, v172, v72
	v_mul_f32_e32 v72, v172, v73
	s_waitcnt lgkmcnt(0)
	v_mul_f32_e32 v73, v172, v75
	v_cvt_pk_fp8_f32 v70, v71, v72 op_sel:[0,0,1]
	v_mul_f32_e32 v72, v172, v74
	v_mov_b32_e32 v71, 0
	v_cvt_pk_fp8_f32 v71, v72, v73
	ds_read_b128 v[72:75], v173 offset:12704
	v_mul_f32_e32 v76, v172, v76
	v_mul_f32_e32 v77, v172, v77
	v_cvt_pk_fp8_f32 v69, v78, v79 op_sel:[0,0,1]
	v_cvt_pk_fp8_f32 v71, v76, v77 op_sel:[0,0,1]
	ds_read_b128 v[76:79], v173 offset:12720
	s_waitcnt lgkmcnt(1)
	v_mul_f32_e32 v82, v172, v72
	v_mul_f32_e32 v73, v172, v73
	v_mov_b32_e32 v72, 0
	v_cvt_pk_fp8_f32 v72, v82, v73
	s_waitcnt lgkmcnt(0)
	v_mul_f32_e32 v76, v172, v76
	v_mul_f32_e32 v77, v172, v77
	v_mov_b32_e32 v73, 0
	v_cvt_pk_fp8_f32 v73, v76, v77
	v_mul_f32_e32 v74, v172, v74
	v_mul_f32_e32 v75, v172, v75
	v_cvt_pk_fp8_f32 v72, v74, v75 op_sel:[0,0,1]
	v_mul_f32_e32 v74, v172, v78
	v_mul_f32_e32 v75, v172, v79
	v_cvt_pk_fp8_f32 v73, v74, v75 op_sel:[0,0,1]
	v_lshl_add_u64 v[74:75], v[80:81], 0, v[132:133]
	global_store_dwordx4 v[74:75], v[66:69], off nt
	s_lshl_b64 s[12:13], s[10:11], 10
	s_add_u32 s12, s29, s12
	v_lshl_add_u64 v[66:67], v[80:81], 0, v[138:139]
	global_store_dwordx4 v[66:67], v[70:73], off nt
	s_waitcnt lgkmcnt(0)
	s_waitcnt vmcnt(17)
	ds_write2_b32 v174, v42, v58 offset1:8
	s_waitcnt vmcnt(16)
	ds_write2_b32 v174, v46, v62 offset0:64 offset1:72
	ds_write2_b32 v174, v43, v59 offset0:132 offset1:140
	ds_write2_b32 v174, v47, v63 offset0:196 offset1:204
	ds_write2_b32 v175, v44, v60 offset0:8 offset1:16
	ds_write2_b32 v175, v48, v64 offset0:72 offset1:80
	ds_write2_b32 v175, v45, v61 offset0:140 offset1:148
	ds_write2_b32 v175, v49, v65 offset0:204 offset1:212
	s_waitcnt vmcnt(13)
	ds_write2_b32 v174, v34, v50 offset0:16 offset1:24
	s_waitcnt vmcnt(12)
	ds_write2_b32 v174, v38, v54 offset0:80 offset1:88
	ds_write2_b32 v174, v35, v51 offset0:148 offset1:156
	ds_write2_b32 v174, v39, v55 offset0:212 offset1:220
	ds_write2_b32 v175, v36, v52 offset0:24 offset1:32
	ds_write2_b32 v175, v40, v56 offset0:88 offset1:96
	ds_write2_b32 v175, v37, v53 offset0:156 offset1:164
	ds_write2_b32 v175, v41, v57 offset0:220 offset1:228
	s_waitcnt vmcnt(9)
	ds_write2_b32 v174, v18, v26 offset0:32 offset1:40
	s_waitcnt vmcnt(8)
	ds_write2_b32 v174, v22, v30 offset0:96 offset1:104
	ds_write2_b32 v174, v19, v27 offset0:164 offset1:172
	ds_write2_b32 v174, v23, v31 offset0:228 offset1:236
	ds_write2_b32 v175, v20, v28 offset0:40 offset1:48
	ds_write2_b32 v175, v24, v32 offset0:104 offset1:112
	ds_write2_b32 v175, v21, v29 offset0:172 offset1:180
	ds_write2_b32 v175, v25, v33 offset0:236 offset1:244
	s_waitcnt vmcnt(5)
	ds_write2_b32 v174, v2, v10 offset0:48 offset1:56
	s_waitcnt vmcnt(4)
	ds_write2_b32 v174, v6, v14 offset0:112 offset1:120
	ds_write2_b32 v174, v3, v11 offset0:180 offset1:188
	ds_write2_b32 v174, v7, v15 offset0:244 offset1:252
	ds_write2_b32 v175, v4, v12 offset0:56 offset1:64
	ds_write2_b32 v175, v8, v16 offset0:120 offset1:128
	ds_write2_b32 v175, v5, v13 offset0:188 offset1:196
	ds_write2_b32 v176, v9, v17 offset0:124 offset1:132
	s_waitcnt lgkmcnt(0)
	ds_read_b128 v[2:5], v173
	ds_read_b128 v[6:9], v173 offset:16
	ds_read_b128 v[10:13], v173 offset:32
	ds_read_b128 v[14:17], v173 offset:48
	s_addc_u32 s13, s30, s13
	s_lshl_b32 s10, s10, 1
	s_waitcnt lgkmcnt(2)
	v_mul_f32_e32 v6, v172, v6
	v_mul_f32_e32 v18, v172, v2
	v_mul_f32_e32 v3, v172, v3
	v_mov_b32_e32 v2, 0
	v_cvt_pk_fp8_f32 v2, v18, v3
	v_mul_f32_e32 v7, v172, v7
	v_mov_b32_e32 v3, 0
	v_cvt_pk_fp8_f32 v3, v6, v7
	v_mul_f32_e32 v4, v172, v4
	v_mul_f32_e32 v5, v172, v5
	v_cvt_pk_fp8_f32 v2, v4, v5 op_sel:[0,0,1]
	v_mul_f32_e32 v4, v172, v8
	v_mul_f32_e32 v5, v172, v9
	v_cvt_pk_fp8_f32 v3, v4, v5 op_sel:[0,0,1]
	s_waitcnt lgkmcnt(1)
	v_mul_f32_e32 v5, v172, v10
	v_mul_f32_e32 v6, v172, v11
	v_mov_b32_e32 v4, 0
	v_cvt_pk_fp8_f32 v4, v5, v6
	s_waitcnt lgkmcnt(0)
	v_mul_f32_e32 v8, v172, v14
	v_mul_f32_e32 v9, v172, v15
	v_mov_b32_e32 v5, 0
	s_and_b32 s10, s10, 0xffffff00
	v_cvt_pk_fp8_f32 v5, v8, v9
	s_add_i32 s10, s10, s31
	s_or_b32 s10, s10, s33
	v_mul_f32_e32 v6, v172, v12
	v_mul_f32_e32 v7, v172, v13
	s_ashr_i32 s11, s10, 31
	v_cvt_pk_fp8_f32 v4, v6, v7 op_sel:[0,0,1]
	v_mul_f32_e32 v6, v172, v16
	v_mul_f32_e32 v7, v172, v17
	s_lshl_b64 s[10:11], s[10:11], 11
	v_cvt_pk_fp8_f32 v5, v6, v7 op_sel:[0,0,1]
	ds_read_b128 v[6:9], v173 offset:4224
	ds_read_b128 v[10:13], v173 offset:4240
	s_add_u32 s10, s28, s10
	s_addc_u32 s11, s27, s11
	s_and_b64 s[8:9], s[8:9], exec
	s_cselect_b32 s8, s12, s10
	s_cselect_b32 s9, s13, s11
	s_add_u32 s8, s8, s26
	s_waitcnt lgkmcnt(1)
	v_mul_f32_e32 v18, v172, v6
	v_mul_f32_e32 v7, v172, v7
	v_mov_b32_e32 v6, 0
	s_addc_u32 s9, s9, 0
	v_cvt_pk_fp8_f32 v6, v18, v7
	v_lshl_add_u64 v[16:17], s[8:9], 0, v[130:131]
	v_lshl_add_u64 v[14:15], v[16:17], 0, v[136:137]
	global_store_dwordx4 v[14:15], v[2:5], off nt
	v_mov_b32_e32 v7, 0
	s_waitcnt lgkmcnt(0)
	v_mul_f32_e32 v14, v172, v13
	v_mul_f32_e32 v2, v172, v8
	v_mul_f32_e32 v3, v172, v9
	v_cvt_pk_fp8_f32 v6, v2, v3 op_sel:[0,0,1]
	ds_read_b128 v[2:5], v173 offset:4256
	v_mul_f32_e32 v8, v172, v10
	v_mul_f32_e32 v9, v172, v11
	v_cvt_pk_fp8_f32 v7, v8, v9
	v_mul_f32_e32 v9, v172, v12
	ds_read_b128 v[10:13], v173 offset:4272
	s_waitcnt lgkmcnt(1)
	v_mul_f32_e32 v2, v172, v2
	v_mul_f32_e32 v3, v172, v3
	v_mov_b32_e32 v8, 0
	v_cvt_pk_fp8_f32 v8, v2, v3
	v_mul_f32_e32 v2, v172, v4
	v_mul_f32_e32 v3, v172, v5
	v_cvt_pk_fp8_f32 v7, v9, v14 op_sel:[0,0,1]
	v_cvt_pk_fp8_f32 v8, v2, v3 op_sel:[0,0,1]
	s_waitcnt lgkmcnt(0)
	v_mul_f32_e32 v2, v172, v10
	v_mul_f32_e32 v3, v172, v11
	v_mov_b32_e32 v9, 0
	v_cvt_pk_fp8_f32 v9, v2, v3
	ds_read_b128 v[2:5], v173 offset:8448
	v_mul_f32_e32 v10, v172, v12
	v_mul_f32_e32 v11, v172, v13
	v_cvt_pk_fp8_f32 v9, v10, v11 op_sel:[0,0,1]
	ds_read_b128 v[10:13], v173 offset:8464
	s_waitcnt lgkmcnt(1)
	v_mul_f32_e32 v18, v172, v2
	v_mul_f32_e32 v3, v172, v3
	v_mov_b32_e32 v2, 0
	v_cvt_pk_fp8_f32 v2, v18, v3
	v_lshl_add_u64 v[14:15], v[16:17], 0, v[134:135]
	v_mul_f32_e32 v3, v172, v4
	v_mul_f32_e32 v4, v172, v5
	global_store_dwordx4 v[14:15], v[6:9], off nt
	v_cvt_pk_fp8_f32 v2, v3, v4 op_sel:[0,0,1]
	ds_read_b128 v[4:7], v173 offset:8480
	s_waitcnt lgkmcnt(1)
	v_mul_f32_e32 v8, v172, v10
	v_mul_f32_e32 v9, v172, v11
	v_mov_b32_e32 v3, 0
	v_cvt_pk_fp8_f32 v3, v8, v9
	ds_read_b128 v[8:11], v173 offset:8496
	s_waitcnt lgkmcnt(1)
	v_mul_f32_e32 v14, v172, v4
	v_mul_f32_e32 v5, v172, v5
	v_mov_b32_e32 v4, 0
	v_cvt_pk_fp8_f32 v4, v14, v5
	v_mul_f32_e32 v12, v172, v12
	v_mul_f32_e32 v13, v172, v13
	v_mul_f32_e32 v5, v172, v6
	v_mul_f32_e32 v6, v172, v7
	v_cvt_pk_fp8_f32 v3, v12, v13 op_sel:[0,0,1]
	v_cvt_pk_fp8_f32 v4, v5, v6 op_sel:[0,0,1]
	s_waitcnt lgkmcnt(0)
	v_mul_f32_e32 v12, v172, v8
	v_mul_f32_e32 v13, v172, v9
	ds_read_b128 v[6:9], v173 offset:12672
	v_mov_b32_e32 v5, 0
	v_cvt_pk_fp8_f32 v5, v12, v13
	v_mul_f32_e32 v14, v172, v10
	v_mul_f32_e32 v15, v172, v11
	ds_read_b128 v[10:13], v173 offset:12688
	s_waitcnt lgkmcnt(1)
	v_mul_f32_e32 v18, v172, v6
	v_mul_f32_e32 v7, v172, v7
	v_mov_b32_e32 v6, 0
	v_cvt_pk_fp8_f32 v6, v18, v7
	v_mul_f32_e32 v7, v172, v8
	v_mul_f32_e32 v8, v172, v9
	s_waitcnt lgkmcnt(0)
	v_mul_f32_e32 v9, v172, v11
	v_cvt_pk_fp8_f32 v6, v7, v8 op_sel:[0,0,1]
	v_mul_f32_e32 v8, v172, v10
	v_mov_b32_e32 v7, 0
	v_cvt_pk_fp8_f32 v7, v8, v9
	ds_read_b128 v[8:11], v173 offset:12704
	v_mul_f32_e32 v12, v172, v12
	v_mul_f32_e32 v13, v172, v13
	v_cvt_pk_fp8_f32 v5, v14, v15 op_sel:[0,0,1]
	v_cvt_pk_fp8_f32 v7, v12, v13 op_sel:[0,0,1]
	ds_read_b128 v[12:15], v173 offset:12720
	s_waitcnt lgkmcnt(1)
	v_mul_f32_e32 v18, v172, v8
	v_mul_f32_e32 v9, v172, v9
	v_mov_b32_e32 v8, 0
	v_cvt_pk_fp8_f32 v8, v18, v9
	s_waitcnt lgkmcnt(0)
	v_mul_f32_e32 v12, v172, v12
	v_mul_f32_e32 v13, v172, v13
	v_mov_b32_e32 v9, 0
	v_cvt_pk_fp8_f32 v9, v12, v13
	v_mul_f32_e32 v10, v172, v10
	v_mul_f32_e32 v11, v172, v11
	v_cvt_pk_fp8_f32 v8, v10, v11 op_sel:[0,0,1]
	v_mul_f32_e32 v10, v172, v14
	v_mul_f32_e32 v11, v172, v15
	v_cvt_pk_fp8_f32 v9, v10, v11 op_sel:[0,0,1]
	v_lshl_add_u64 v[10:11], v[16:17], 0, v[132:133]
	global_store_dwordx4 v[10:11], v[2:5], off nt
	s_nop 1
	v_lshl_add_u64 v[2:3], v[16:17], 0, v[138:139]
	global_store_dwordx4 v[2:3], v[6:9], off nt
	s_waitcnt lgkmcnt(0)
	s_barrier
	s_and_saveexec_b64 s[8:9], s[36:37]
	s_cbranch_execz .LBB0_2951
	v_mov_b32_e32 v2, s16
	s_waitcnt vmcnt(0)
	ds_write_b32 v2, v255
	s_branch .LBB0_2951
